# all per-segment s_setprio flips of the GEMM loops deleted; one static s_setprio 1 for waves 4-7 at kernel start (whole kernel)
# baseline (speedup 1.0000x reference)
.LBB0_4:
	s_or_b64 exec, exec, s[2:3]
	s_load_dwordx2 s[36:37], s[0:1], 0x110
	s_load_dword s15, s[0:1], 0x118
	s_mov_b32 s80, 0
	s_waitcnt lgkmcnt(0)
	s_barrier
	s_cmp_gt_u32 s81, 0xff
	s_cbranch_scc0 .Lnoprio_g
	s_setprio 1
.Lnoprio_g:
	s_sub_i32 s0, s37, s36
	s_cmp_lt_i32 s0, 2
	s_cbranch_scc1 .LBB0_11
	s_getreg_b32 s0, hwreg(HW_REG_XCC_ID, 0, 4)
	s_and_b32 s33, s0, 15
	s_cmp_gt_u32 s81, 63
	s_cbranch_scc1 .LBB0_10
	v_mbcnt_lo_u32_b32 v0, -1, 0
	v_mbcnt_hi_u32_b32 v0, -1, v0
	v_cmp_eq_u32_e32 vcc, 0, v0
	s_and_saveexec_b64 s[0:1], vcc
	s_cbranch_execz .LBB0_9
	s_mov_b64 s[2:3], exec
	v_mbcnt_lo_u32_b32 v0, s2, 0
	v_mbcnt_hi_u32_b32 v0, s3, v0
	v_cmp_eq_u32_e32 vcc, 0, v0
	s_and_b64 s[4:5], exec, vcc
	s_mov_b64 exec, s[4:5]
	s_cbranch_execz .LBB0_9
	s_lshl_b32 s4, s33, 8
	s_bcnt1_i32_b64 s2, s[2:3]
	v_mov_b32_e32 v0, s4
	v_mov_b32_e32 v1, s2
	global_atomic_add v0, v1, s[34:35] offset:1024

.LBB0_243:
	ds_read_b128 v[8:11], v180
	ds_read_b128 v[12:15], v180 offset:1024
	s_waitcnt lgkmcnt(0)
	ds_read_b128 v[0:3], v180 offset:2048
	ds_read_b128 v[4:7], v180 offset:3072
	s_add_u32 s22, s4, 0xfffc0080
	s_addc_u32 s23, s5, -1
	s_cmp_eq_u32 s75, 12
	s_cselect_b32 s25, s69, s23
	s_cselect_b32 s24, s70, s22
	s_cselect_b32 s23, s71, s74
	s_cselect_b32 s22, s72, s73
	v_lshl_add_u64 v[166:167], s[4:5], 0, v[160:161]
	s_add_i32 m0, s39, 0xc000
	ds_read_b128 v[186:189], v181
	ds_read_b128 v[190:193], v181 offset:1024
	ds_read_b128 v[194:197], v181 offset:2048
	ds_read_b128 v[198:201], v181 offset:3072
	ds_read_b128 v[202:205], v181 offset:4096
	ds_read_b128 v[206:209], v181 offset:5120
	ds_read_b128 v[210:213], v181 offset:6144
	ds_read_b128 v[214:217], v181 offset:7168
	global_load_lds_dwordx4 v[166:167], off
	v_lshl_add_u64 v[166:167], s[4:5], 0, v[158:159]
	s_add_i32 m0, s39, 0xe000
	s_nop 0
	global_load_lds_dwordx4 v[166:167], off
	s_waitcnt lgkmcnt(8)
	s_barrier
	s_waitcnt lgkmcnt(0)
	s_waitcnt lgkmcnt(0)
	v_mfma_scale_f32_16x16x128_f8f6f4 v[140:143], v[8:15], v[186:193], v[140:143], v175, v175 op_sel_hi:[0,0,0]
	v_mfma_scale_f32_16x16x128_f8f6f4 v[136:139], v[0:7], v[186:193], v[136:139], v175, v175 op_sel_hi:[0,0,0]
	v_mfma_scale_f32_16x16x128_f8f6f4 v[124:127], v[8:15], v[194:201], v[124:127], v175, v175 op_sel_hi:[0,0,0]
	v_mfma_scale_f32_16x16x128_f8f6f4 v[120:123], v[0:7], v[194:201], v[120:123], v175, v175 op_sel_hi:[0,0,0]
	v_mfma_scale_f32_16x16x128_f8f6f4 v[108:111], v[8:15], v[202:209], v[108:111], v175, v175 op_sel_hi:[0,0,0]
	v_mfma_scale_f32_16x16x128_f8f6f4 v[104:107], v[0:7], v[202:209], v[104:107], v175, v175 op_sel_hi:[0,0,0]
	v_mfma_scale_f32_16x16x128_f8f6f4 v[92:95], v[8:15], v[210:217], v[92:95], v175, v175 op_sel_hi:[0,0,0]
	v_mfma_scale_f32_16x16x128_f8f6f4 v[88:91], v[0:7], v[210:217], v[88:91], v175, v175 op_sel_hi:[0,0,0]
	s_barrier
	s_add_i32 s76, s51, s38
	v_lshl_add_u64 v[166:167], s[22:23], 0, v[146:147]
	s_mov_b32 m0, s76
	ds_read_b128 v[224:227], v182
	ds_read_b128 v[228:231], v182 offset:1024
	ds_read_b128 v[232:235], v182 offset:2048
	ds_read_b128 v[236:239], v182 offset:3072
	global_load_lds_dwordx4 v[166:167], off
	v_lshl_add_u64 v[168:169], s[22:23], 0, v[150:151]
	s_add_i32 m0, s76, 0x2000
	s_nop 0
	global_load_lds_dwordx4 v[168:169], off
	s_barrier
	s_waitcnt lgkmcnt(0)
	s_waitcnt lgkmcnt(0)
	v_mfma_scale_f32_16x16x128_f8f6f4 v[132:135], v[224:231], v[186:193], v[132:135], v175, v175 op_sel_hi:[0,0,0]
	v_mfma_scale_f32_16x16x128_f8f6f4 v[128:131], v[232:239], v[186:193], v[128:131], v175, v175 op_sel_hi:[0,0,0]
	v_mfma_scale_f32_16x16x128_f8f6f4 v[116:119], v[224:231], v[194:201], v[116:119], v175, v175 op_sel_hi:[0,0,0]
	v_mfma_scale_f32_16x16x128_f8f6f4 v[112:115], v[232:239], v[194:201], v[112:115], v175, v175 op_sel_hi:[0,0,0]
	v_mfma_scale_f32_16x16x128_f8f6f4 v[100:103], v[224:231], v[202:209], v[100:103], v175, v175 op_sel_hi:[0,0,0]
	v_mfma_scale_f32_16x16x128_f8f6f4 v[96:99], v[232:239], v[202:209], v[96:99], v175, v175 op_sel_hi:[0,0,0]
	v_mfma_scale_f32_16x16x128_f8f6f4 v[84:87], v[224:231], v[210:217], v[84:87], v175, v175 op_sel_hi:[0,0,0]
	v_mfma_scale_f32_16x16x128_f8f6f4 v[80:83], v[232:239], v[210:217], v[80:83], v175, v175 op_sel_hi:[0,0,0]
	s_mov_b32 m0, s39
	v_lshl_add_u64 v[170:171], s[24:25], 0, v[144:145]
	s_barrier
	ds_read_b128 v[186:189], v181 offset:16384
	ds_read_b128 v[190:193], v181 offset:17408
	ds_read_b128 v[194:197], v181 offset:18432
	ds_read_b128 v[198:201], v181 offset:19456
	ds_read_b128 v[202:205], v181 offset:20480
	ds_read_b128 v[206:209], v181 offset:21504
	ds_read_b128 v[210:213], v181 offset:22528
	ds_read_b128 v[214:217], v181 offset:23552
	global_load_lds_dwordx4 v[170:171], off
	v_lshl_add_u64 v[172:173], s[24:25], 0, v[148:149]
	s_mov_b32 m0, s40
	s_nop 0
	global_load_lds_dwordx4 v[172:173], off
	s_barrier
	s_waitcnt lgkmcnt(0)
	s_waitcnt lgkmcnt(0)
	v_mfma_scale_f32_16x16x128_f8f6f4 v[76:79], v[8:15], v[186:193], v[76:79], v175, v175 op_sel_hi:[0,0,0]
	v_mfma_scale_f32_16x16x128_f8f6f4 v[72:75], v[0:7], v[186:193], v[72:75], v175, v175 op_sel_hi:[0,0,0]
	v_mfma_scale_f32_16x16x128_f8f6f4 v[60:63], v[8:15], v[194:201], v[60:63], v175, v175 op_sel_hi:[0,0,0]
	v_mfma_scale_f32_16x16x128_f8f6f4 v[56:59], v[0:7], v[194:201], v[56:59], v175, v175 op_sel_hi:[0,0,0]
	v_mfma_scale_f32_16x16x128_f8f6f4 v[44:47], v[8:15], v[202:209], v[44:47], v175, v175 op_sel_hi:[0,0,0]
	v_mfma_scale_f32_16x16x128_f8f6f4 v[40:43], v[0:7], v[202:209], v[40:43], v175, v175 op_sel_hi:[0,0,0]
	v_mfma_scale_f32_16x16x128_f8f6f4 v[28:31], v[8:15], v[210:217], v[28:31], v175, v175 op_sel_hi:[0,0,0]
	v_mfma_scale_f32_16x16x128_f8f6f4 v[24:27], v[0:7], v[210:217], v[24:27], v175, v175 op_sel_hi:[0,0,0]
	s_barrier
	s_add_u32 s76, s22, 0x40000
	s_addc_u32 s77, s23, 0
	s_add_i32 s78, s53, s38
	v_lshl_add_u64 v[0:1], s[76:77], 0, v[146:147]
	s_mov_b32 m0, s78
	s_nop 0
	global_load_lds_dwordx4 v[0:1], off
	v_lshl_add_u64 v[0:1], s[76:77], 0, v[150:151]
	s_add_i32 m0, s78, 0x2000
	s_nop 0
	global_load_lds_dwordx4 v[0:1], off
	s_waitcnt vmcnt(6)
	s_barrier
	v_mfma_scale_f32_16x16x128_f8f6f4 v[68:71], v[224:231], v[186:193], v[68:71], v175, v175 op_sel_hi:[0,0,0]
	v_mfma_scale_f32_16x16x128_f8f6f4 v[64:67], v[232:239], v[186:193], v[64:67], v175, v175 op_sel_hi:[0,0,0]
	v_mfma_scale_f32_16x16x128_f8f6f4 v[52:55], v[224:231], v[194:201], v[52:55], v175, v175 op_sel_hi:[0,0,0]
	v_mfma_scale_f32_16x16x128_f8f6f4 v[48:51], v[232:239], v[194:201], v[48:51], v175, v175 op_sel_hi:[0,0,0]
	v_mfma_scale_f32_16x16x128_f8f6f4 v[36:39], v[224:231], v[202:209], v[36:39], v175, v175 op_sel_hi:[0,0,0]
	v_mfma_scale_f32_16x16x128_f8f6f4 v[32:35], v[232:239], v[202:209], v[32:35], v175, v175 op_sel_hi:[0,0,0]
	v_mfma_scale_f32_16x16x128_f8f6f4 v[20:23], v[224:231], v[210:217], v[20:23], v175, v175 op_sel_hi:[0,0,0]
	v_mfma_scale_f32_16x16x128_f8f6f4 v[16:19], v[232:239], v[210:217], v[16:19], v175, v175 op_sel_hi:[0,0,0]
	s_add_i32 s76, 0, 0x18000
	v_add_u32_e32 v12, s76, v179
	s_barrier
	ds_read_b128 v[0:3], v12
	ds_read_b128 v[4:7], v12 offset:1024
	ds_read_b128 v[8:11], v12 offset:2048
	ds_read_b128 v[12:15], v12 offset:3072
	s_add_u32 s24, s24, 0x40000
	s_addc_u32 s25, s25, 0
	s_mov_b32 m0, s41
	v_lshl_add_u64 v[218:219], s[24:25], 0, v[144:145]
	ds_read_b128 v[186:189], v181 offset:32768
	ds_read_b128 v[190:193], v181 offset:33792
	ds_read_b128 v[194:197], v181 offset:34816
	ds_read_b128 v[198:201], v181 offset:35840
	ds_read_b128 v[202:205], v181 offset:36864
	ds_read_b128 v[206:209], v181 offset:37888
	ds_read_b128 v[210:213], v181 offset:38912
	ds_read_b128 v[214:217], v181 offset:39936
	global_load_lds_dwordx4 v[218:219], off
	v_lshl_add_u64 v[218:219], s[24:25], 0, v[148:149]
	s_mov_b32 m0, s42
	s_nop 0
	global_load_lds_dwordx4 v[218:219], off
	s_waitcnt lgkmcnt(8)
	s_barrier
	s_waitcnt lgkmcnt(0)
	s_waitcnt lgkmcnt(0)
	v_mfma_scale_f32_16x16x128_f8f6f4 v[140:143], v[0:7], v[186:193], v[140:143], v175, v175 op_sel_hi:[0,0,0]
	v_mfma_scale_f32_16x16x128_f8f6f4 v[136:139], v[8:15], v[186:193], v[136:139], v175, v175 op_sel_hi:[0,0,0]
	v_mfma_scale_f32_16x16x128_f8f6f4 v[124:127], v[0:7], v[194:201], v[124:127], v175, v175 op_sel_hi:[0,0,0]
	v_mfma_scale_f32_16x16x128_f8f6f4 v[120:123], v[8:15], v[194:201], v[120:123], v175, v175 op_sel_hi:[0,0,0]
	v_mfma_scale_f32_16x16x128_f8f6f4 v[108:111], v[0:7], v[202:209], v[108:111], v175, v175 op_sel_hi:[0,0,0]
	v_mfma_scale_f32_16x16x128_f8f6f4 v[104:107], v[8:15], v[202:209], v[104:107], v175, v175 op_sel_hi:[0,0,0]
	v_mfma_scale_f32_16x16x128_f8f6f4 v[92:95], v[0:7], v[210:217], v[92:95], v175, v175 op_sel_hi:[0,0,0]
	v_mfma_scale_f32_16x16x128_f8f6f4 v[88:91], v[8:15], v[210:217], v[88:91], v175, v175 op_sel_hi:[0,0,0]
	s_barrier
	s_add_i32 s24, 0, 0x1c000
	s_add_i32 s25, s76, s38
	v_add_u32_e32 v152, s24, v179
	v_lshl_add_u64 v[166:167], v[166:167], 0, s[12:13]
	s_mov_b32 m0, s25
	ds_read_b128 v[224:227], v152
	ds_read_b128 v[228:231], v152 offset:1024
	ds_read_b128 v[232:235], v152 offset:2048
	ds_read_b128 v[236:239], v152 offset:3072
	global_load_lds_dwordx4 v[166:167], off
	v_lshl_add_u64 v[166:167], v[168:169], 0, s[12:13]
	s_add_i32 m0, s25, 0x2000
	s_nop 0
	global_load_lds_dwordx4 v[166:167], off
	s_barrier
	s_waitcnt lgkmcnt(0)
	s_waitcnt lgkmcnt(0)
	v_mfma_scale_f32_16x16x128_f8f6f4 v[132:135], v[224:231], v[186:193], v[132:135], v175, v175 op_sel_hi:[0,0,0]
	v_mfma_scale_f32_16x16x128_f8f6f4 v[128:131], v[232:239], v[186:193], v[128:131], v175, v175 op_sel_hi:[0,0,0]
	v_mfma_scale_f32_16x16x128_f8f6f4 v[116:119], v[224:231], v[194:201], v[116:119], v175, v175 op_sel_hi:[0,0,0]
	v_mfma_scale_f32_16x16x128_f8f6f4 v[112:115], v[232:239], v[194:201], v[112:115], v175, v175 op_sel_hi:[0,0,0]
	v_mfma_scale_f32_16x16x128_f8f6f4 v[100:103], v[224:231], v[202:209], v[100:103], v175, v175 op_sel_hi:[0,0,0]
	v_mfma_scale_f32_16x16x128_f8f6f4 v[96:99], v[232:239], v[202:209], v[96:99], v175, v175 op_sel_hi:[0,0,0]
	v_mfma_scale_f32_16x16x128_f8f6f4 v[84:87], v[224:231], v[210:217], v[84:87], v175, v175 op_sel_hi:[0,0,0]
	v_mfma_scale_f32_16x16x128_f8f6f4 v[80:83], v[232:239], v[210:217], v[80:83], v175, v175 op_sel_hi:[0,0,0]
	s_mov_b32 m0, s46
	v_lshl_add_u64 v[166:167], v[170:171], 0, s[12:13]
	s_barrier
	ds_read_b128 v[186:189], v181 offset:49152
	ds_read_b128 v[190:193], v181 offset:50176
	ds_read_b128 v[194:197], v181 offset:51200
	ds_read_b128 v[198:201], v181 offset:52224
	ds_read_b128 v[202:205], v181 offset:53248
	ds_read_b128 v[206:209], v181 offset:54272
	ds_read_b128 v[210:213], v181 offset:55296
	ds_read_b128 v[214:217], v181 offset:56320
	global_load_lds_dwordx4 v[166:167], off
	v_lshl_add_u64 v[166:167], v[172:173], 0, s[12:13]
	s_mov_b32 m0, s47
	s_nop 0
	global_load_lds_dwordx4 v[166:167], off
	s_barrier
	s_waitcnt lgkmcnt(0)
	s_waitcnt lgkmcnt(0)
	v_mfma_scale_f32_16x16x128_f8f6f4 v[76:79], v[0:7], v[186:193], v[76:79], v175, v175 op_sel_hi:[0,0,0]
	v_mfma_scale_f32_16x16x128_f8f6f4 v[72:75], v[8:15], v[186:193], v[72:75], v175, v175 op_sel_hi:[0,0,0]
	v_mfma_scale_f32_16x16x128_f8f6f4 v[60:63], v[0:7], v[194:201], v[60:63], v175, v175 op_sel_hi:[0,0,0]
	v_mfma_scale_f32_16x16x128_f8f6f4 v[56:59], v[8:15], v[194:201], v[56:59], v175, v175 op_sel_hi:[0,0,0]
	v_mfma_scale_f32_16x16x128_f8f6f4 v[44:47], v[0:7], v[202:209], v[44:47], v175, v175 op_sel_hi:[0,0,0]
	v_mfma_scale_f32_16x16x128_f8f6f4 v[40:43], v[8:15], v[202:209], v[40:43], v175, v175 op_sel_hi:[0,0,0]
	v_mfma_scale_f32_16x16x128_f8f6f4 v[28:31], v[0:7], v[210:217], v[28:31], v175, v175 op_sel_hi:[0,0,0]
	v_mfma_scale_f32_16x16x128_f8f6f4 v[24:27], v[8:15], v[210:217], v[24:27], v175, v175 op_sel_hi:[0,0,0]
	s_barrier
	s_add_u32 s22, s22, 0x40080
	s_addc_u32 s23, s23, 0
	s_add_i32 s24, s24, s38
	v_lshl_add_u64 v[0:1], s[22:23], 0, v[146:147]
	s_mov_b32 m0, s24
	s_nop 0
	global_load_lds_dwordx4 v[0:1], off
	v_lshl_add_u64 v[0:1], s[22:23], 0, v[150:151]
	s_add_i32 m0, s24, 0x2000
	s_nop 0
	global_load_lds_dwordx4 v[0:1], off
	s_waitcnt vmcnt(6)
	s_barrier
	v_mfma_scale_f32_16x16x128_f8f6f4 v[68:71], v[224:231], v[186:193], v[68:71], v175, v175 op_sel_hi:[0,0,0]
	v_mfma_scale_f32_16x16x128_f8f6f4 v[64:67], v[232:239], v[186:193], v[64:67], v175, v175 op_sel_hi:[0,0,0]
	v_mfma_scale_f32_16x16x128_f8f6f4 v[52:55], v[224:231], v[194:201], v[52:55], v175, v175 op_sel_hi:[0,0,0]
	v_mfma_scale_f32_16x16x128_f8f6f4 v[48:51], v[232:239], v[194:201], v[48:51], v175, v175 op_sel_hi:[0,0,0]
	v_mfma_scale_f32_16x16x128_f8f6f4 v[36:39], v[224:231], v[202:209], v[36:39], v175, v175 op_sel_hi:[0,0,0]
	v_mfma_scale_f32_16x16x128_f8f6f4 v[32:35], v[232:239], v[202:209], v[32:35], v175, v175 op_sel_hi:[0,0,0]
	v_mfma_scale_f32_16x16x128_f8f6f4 v[20:23], v[224:231], v[210:217], v[20:23], v175, v175 op_sel_hi:[0,0,0]
	v_mfma_scale_f32_16x16x128_f8f6f4 v[16:19], v[232:239], v[210:217], v[16:19], v175, v175 op_sel_hi:[0,0,0]
	s_add_i32 s75, s75, 2
	s_add_u32 s73, s73, 0x100
	s_addc_u32 s74, s74, 0
	s_add_u32 s4, s4, 0x100
	s_addc_u32 s5, s5, 0
	s_cmp_gt_u32 s75, 13
	s_barrier
	s_cbranch_scc0 .LBB0_243
	s_nop 7
	s_nop 7
	s_nop 7
	s_cmp_gt_i32 s67, 3
	s_cselect_b64 s[4:5], -1, 0
	v_lshl_add_u32 v0, s68, 8, v178
	s_and_b64 vcc, exec, s[4:5]
	s_cbranch_vccz .LBB0_247
	s_mov_b64 s[22:23], -1
	s_and_b64 vcc, exec, s[4:5]
	s_cbranch_vccnz .LBB0_264

.LBB0_365:
	ds_read_b128 v[12:15], v176
	ds_read_b128 v[16:19], v176 offset:1024
	ds_read_b128 v[28:31], v176 offset:2048
	ds_read_b128 v[32:35], v176 offset:3072
	s_add_u32 s18, s29, s57
	v_cmp_lt_i64_e32 vcc, s[6:7], v[144:145]
	s_addc_u32 s19, s30, 0
	s_and_b64 s[2:3], vcc, exec
	s_cselect_b32 s25, s19, s23
	s_cselect_b32 s24, s18, s22
	s_add_u32 s20, s31, s58
	s_addc_u32 s21, s38, 0
	s_and_b64 s[2:3], vcc, exec
	s_cselect_b32 s3, s21, s27
	s_cselect_b32 s2, s20, s26
	s_add_u32 s62, s22, 0x20080
	s_addc_u32 s63, s23, 0
	s_add_i32 s67, s40, 0xc000
	v_lshl_add_u64 v[44:45], s[62:63], 0, v[136:137]
	s_mov_b32 m0, s67
	s_add_i32 s61, s40, 0xe000
	ds_read_b128 v[4:7], v177
	ds_read_b128 v[8:11], v177 offset:1024
	ds_read_b128 v[20:23], v177 offset:2048
	ds_read_b128 v[24:27], v177 offset:3072
	ds_read_b128 v[36:39], v177 offset:4096
	ds_read_b128 v[40:43], v177 offset:5120
	ds_read_b128 v[52:55], v177 offset:6144
	ds_read_b128 v[56:59], v177 offset:7168
	global_load_lds_dwordx4 v[44:45], off
	v_lshl_add_u64 v[44:45], s[62:63], 0, v[140:141]
	s_mov_b32 m0, s61
	s_nop 0
	global_load_lds_dwordx4 v[44:45], off
	s_waitcnt lgkmcnt(8)
	s_barrier
	s_waitcnt lgkmcnt(0)
	v_mov_b64_e32 v[110:111], v[2:3]
	v_mov_b64_e32 v[114:115], v[2:3]
	v_mov_b64_e32 v[106:107], v[2:3]
	v_mov_b64_e32 v[102:103], v[2:3]
	v_mov_b64_e32 v[82:83], v[2:3]
	v_mov_b64_e32 v[78:79], v[2:3]
	v_mov_b64_e32 v[50:51], v[2:3]
	v_mov_b64_e32 v[46:47], v[2:3]
	v_mov_b64_e32 v[108:109], v[0:1]
	v_mov_b64_e32 v[112:113], v[0:1]
	v_mov_b64_e32 v[104:105], v[0:1]
	v_mov_b64_e32 v[100:101], v[0:1]
	v_mov_b64_e32 v[80:81], v[0:1]
	v_mov_b64_e32 v[76:77], v[0:1]
	v_mov_b64_e32 v[48:49], v[0:1]
	v_mov_b64_e32 v[44:45], v[0:1]
	s_waitcnt lgkmcnt(0)
	v_mfma_scale_f32_16x16x128_f8f6f4 v[108:111], v[12:19], v[4:11], v[108:111], v171, v171 op_sel_hi:[0,0,0]
	v_mfma_scale_f32_16x16x128_f8f6f4 v[112:115], v[28:35], v[4:11], v[112:115], v171, v171 op_sel_hi:[0,0,0]
	v_mfma_scale_f32_16x16x128_f8f6f4 v[104:107], v[12:19], v[20:27], v[104:107], v171, v171 op_sel_hi:[0,0,0]
	v_mfma_scale_f32_16x16x128_f8f6f4 v[100:103], v[28:35], v[20:27], v[100:103], v171, v171 op_sel_hi:[0,0,0]
	v_mfma_scale_f32_16x16x128_f8f6f4 v[80:83], v[12:19], v[36:43], v[80:83], v171, v171 op_sel_hi:[0,0,0]
	v_mfma_scale_f32_16x16x128_f8f6f4 v[76:79], v[28:35], v[36:43], v[76:79], v171, v171 op_sel_hi:[0,0,0]
	v_mfma_scale_f32_16x16x128_f8f6f4 v[48:51], v[12:19], v[52:59], v[48:51], v171, v171 op_sel_hi:[0,0,0]
	v_mfma_scale_f32_16x16x128_f8f6f4 v[44:47], v[28:35], v[52:59], v[44:47], v171, v171 op_sel_hi:[0,0,0]
	s_barrier
	v_lshl_add_u64 v[132:133], s[26:27], 0, v[138:139]
	s_add_i32 s64, s50, s39
	v_lshl_add_u64 v[60:61], v[132:133], 0, s[10:11]
	s_mov_b32 m0, s64
	v_lshl_add_u64 v[134:135], s[26:27], 0, v[142:143]
	s_add_i32 s62, s64, 0x2000
	ds_read_b128 v[154:157], v178
	ds_read_b128 v[158:161], v178 offset:1024
	ds_read_b128 v[180:183], v178 offset:2048
	ds_read_b128 v[184:187], v178 offset:3072
	global_load_lds_dwordx4 v[60:61], off
	v_lshl_add_u64 v[60:61], v[134:135], 0, s[10:11]
	s_mov_b32 m0, s62
	s_nop 0
	global_load_lds_dwordx4 v[60:61], off
	s_barrier
	s_waitcnt lgkmcnt(0)
	v_mov_b64_e32 v[126:127], v[2:3]
	v_mov_b64_e32 v[130:131], v[2:3]
	v_mov_b64_e32 v[122:123], v[2:3]
	v_mov_b64_e32 v[118:119], v[2:3]
	v_mov_b64_e32 v[98:99], v[2:3]
	v_mov_b64_e32 v[94:95], v[2:3]
	v_mov_b64_e32 v[66:67], v[2:3]
	v_mov_b64_e32 v[62:63], v[2:3]
	v_mov_b64_e32 v[124:125], v[0:1]
	v_mov_b64_e32 v[128:129], v[0:1]
	v_mov_b64_e32 v[120:121], v[0:1]
	v_mov_b64_e32 v[116:117], v[0:1]
	v_mov_b64_e32 v[96:97], v[0:1]
	v_mov_b64_e32 v[92:93], v[0:1]
	v_mov_b64_e32 v[64:65], v[0:1]
	v_mov_b64_e32 v[60:61], v[0:1]
	s_waitcnt lgkmcnt(0)
	v_mfma_scale_f32_16x16x128_f8f6f4 v[124:127], v[154:161], v[4:11], v[124:127], v171, v171 op_sel_hi:[0,0,0]
	v_mfma_scale_f32_16x16x128_f8f6f4 v[128:131], v[180:187], v[4:11], v[128:131], v171, v171 op_sel_hi:[0,0,0]
	v_mfma_scale_f32_16x16x128_f8f6f4 v[120:123], v[154:161], v[20:27], v[120:123], v171, v171 op_sel_hi:[0,0,0]
	v_mfma_scale_f32_16x16x128_f8f6f4 v[116:119], v[180:187], v[20:27], v[116:119], v171, v171 op_sel_hi:[0,0,0]
	v_mfma_scale_f32_16x16x128_f8f6f4 v[96:99], v[154:161], v[36:43], v[96:99], v171, v171 op_sel_hi:[0,0,0]
	v_mfma_scale_f32_16x16x128_f8f6f4 v[92:95], v[180:187], v[36:43], v[92:95], v171, v171 op_sel_hi:[0,0,0]
	v_mfma_scale_f32_16x16x128_f8f6f4 v[64:67], v[154:161], v[52:59], v[64:67], v171, v171 op_sel_hi:[0,0,0]
	v_mfma_scale_f32_16x16x128_f8f6f4 v[60:63], v[180:187], v[52:59], v[60:63], v171, v171 op_sel_hi:[0,0,0]
	v_lshl_add_u64 v[150:151], s[22:23], 0, v[136:137]
	s_mov_b32 m0, s40
	v_lshl_add_u64 v[4:5], v[150:151], 0, s[10:11]
	v_lshl_add_u64 v[152:153], s[22:23], 0, v[140:141]
	s_barrier
	ds_read_b128 v[52:55], v177 offset:16384
	ds_read_b128 v[56:59], v177 offset:17408
	ds_read_b128 v[188:191], v177 offset:18432
	ds_read_b128 v[192:195], v177 offset:19456
	ds_read_b128 v[196:199], v177 offset:20480
	ds_read_b128 v[200:203], v177 offset:21504
	ds_read_b128 v[204:207], v177 offset:22528
	ds_read_b128 v[208:211], v177 offset:23552
	global_load_lds_dwordx4 v[4:5], off
	v_lshl_add_u64 v[4:5], v[152:153], 0, s[10:11]
	s_mov_b32 m0, s41
	s_nop 0
	global_load_lds_dwordx4 v[4:5], off
	s_barrier
	s_waitcnt lgkmcnt(0)
	v_mov_b64_e32 v[74:75], v[2:3]
	v_mov_b64_e32 v[70:71], v[2:3]
	v_mov_b64_e32 v[42:43], v[2:3]
	v_mov_b64_e32 v[38:39], v[2:3]
	v_mov_b64_e32 v[26:27], v[2:3]
	v_mov_b64_e32 v[22:23], v[2:3]
	v_mov_b64_e32 v[10:11], v[2:3]
	v_mov_b64_e32 v[6:7], v[2:3]
	v_mov_b64_e32 v[72:73], v[0:1]
	v_mov_b64_e32 v[68:69], v[0:1]
	v_mov_b64_e32 v[40:41], v[0:1]
	v_mov_b64_e32 v[36:37], v[0:1]
	v_mov_b64_e32 v[24:25], v[0:1]
	v_mov_b64_e32 v[20:21], v[0:1]
	v_mov_b64_e32 v[8:9], v[0:1]
	v_mov_b64_e32 v[4:5], v[0:1]
	s_waitcnt lgkmcnt(0)
	v_mfma_scale_f32_16x16x128_f8f6f4 v[72:75], v[12:19], v[52:59], v[72:75], v171, v171 op_sel_hi:[0,0,0]
	v_mfma_scale_f32_16x16x128_f8f6f4 v[68:71], v[28:35], v[52:59], v[68:71], v171, v171 op_sel_hi:[0,0,0]
	v_mfma_scale_f32_16x16x128_f8f6f4 v[40:43], v[12:19], v[188:195], v[40:43], v171, v171 op_sel_hi:[0,0,0]
	v_mfma_scale_f32_16x16x128_f8f6f4 v[36:39], v[28:35], v[188:195], v[36:39], v171, v171 op_sel_hi:[0,0,0]
	v_mfma_scale_f32_16x16x128_f8f6f4 v[24:27], v[12:19], v[196:203], v[24:27], v171, v171 op_sel_hi:[0,0,0]
	v_mfma_scale_f32_16x16x128_f8f6f4 v[20:23], v[28:35], v[196:203], v[20:23], v171, v171 op_sel_hi:[0,0,0]
	v_mfma_scale_f32_16x16x128_f8f6f4 v[8:11], v[12:19], v[204:211], v[8:11], v171, v171 op_sel_hi:[0,0,0]
	v_mfma_scale_f32_16x16x128_f8f6f4 v[4:7], v[28:35], v[204:211], v[4:7], v171, v171 op_sel_hi:[0,0,0]
	s_barrier
	s_add_u32 s68, s26, 0x10100
	s_addc_u32 s69, s27, 0
	s_add_i32 s65, s51, s39
	v_lshl_add_u64 v[12:13], s[68:69], 0, v[138:139]
	s_mov_b32 m0, s65
	s_add_i32 s63, s65, 0x2000
	global_load_lds_dwordx4 v[12:13], off
	v_lshl_add_u64 v[12:13], s[68:69], 0, v[142:143]
	s_mov_b32 m0, s63
	s_nop 0
	global_load_lds_dwordx4 v[12:13], off
	s_waitcnt vmcnt(6)
	s_barrier
	v_mov_b64_e32 v[90:91], v[2:3]
	v_mov_b64_e32 v[86:87], v[2:3]
	v_mov_b64_e32 v[88:89], v[0:1]
	v_mov_b64_e32 v[84:85], v[0:1]
	v_mfma_scale_f32_16x16x128_f8f6f4 v[88:91], v[154:161], v[52:59], v[88:91], v171, v171 op_sel_hi:[0,0,0]
	v_mfma_scale_f32_16x16x128_f8f6f4 v[84:87], v[180:187], v[52:59], v[84:87], v171, v171 op_sel_hi:[0,0,0]
	v_mov_b64_e32 v[58:59], v[2:3]
	v_mov_b64_e32 v[54:55], v[2:3]
	v_mov_b64_e32 v[34:35], v[2:3]
	v_mov_b64_e32 v[30:31], v[2:3]
	v_mov_b64_e32 v[18:19], v[2:3]
	v_mov_b64_e32 v[14:15], v[2:3]
	v_mov_b64_e32 v[56:57], v[0:1]
	v_mov_b64_e32 v[52:53], v[0:1]
	v_mov_b64_e32 v[32:33], v[0:1]
	v_mov_b64_e32 v[28:29], v[0:1]
	v_mov_b64_e32 v[16:17], v[0:1]
	v_mov_b64_e32 v[12:13], v[0:1]
	v_mfma_scale_f32_16x16x128_f8f6f4 v[56:59], v[154:161], v[188:195], v[56:59], v171, v171 op_sel_hi:[0,0,0]
	v_mfma_scale_f32_16x16x128_f8f6f4 v[52:55], v[180:187], v[188:195], v[52:55], v171, v171 op_sel_hi:[0,0,0]
	v_mfma_scale_f32_16x16x128_f8f6f4 v[32:35], v[154:161], v[196:203], v[32:35], v171, v171 op_sel_hi:[0,0,0]
	v_mfma_scale_f32_16x16x128_f8f6f4 v[28:31], v[180:187], v[196:203], v[28:31], v171, v171 op_sel_hi:[0,0,0]
	v_mfma_scale_f32_16x16x128_f8f6f4 v[16:19], v[154:161], v[204:211], v[16:19], v171, v171 op_sel_hi:[0,0,0]
	v_mfma_scale_f32_16x16x128_f8f6f4 v[12:15], v[180:187], v[204:211], v[12:15], v171, v171 op_sel_hi:[0,0,0]
	s_add_i32 s66, 0, 0x18000
	v_add_u32_e32 v154, s66, v174
	s_barrier
	ds_read_b128 v[156:159], v154
	ds_read_b128 v[160:163], v154 offset:1024
	ds_read_b128 v[180:183], v154 offset:2048
	ds_read_b128 v[184:187], v154 offset:3072
	s_add_u32 s68, s22, 0x20100
	s_addc_u32 s69, s23, 0
	s_mov_b32 m0, s42
	v_lshl_add_u64 v[164:165], s[68:69], 0, v[136:137]
	ds_read_b128 v[188:191], v177 offset:32768
	ds_read_b128 v[192:195], v177 offset:33792
	ds_read_b128 v[196:199], v177 offset:34816
	ds_read_b128 v[200:203], v177 offset:35840
	ds_read_b128 v[204:207], v177 offset:36864
	ds_read_b128 v[208:211], v177 offset:37888
	ds_read_b128 v[212:215], v177 offset:38912
	ds_read_b128 v[216:219], v177 offset:39936
	global_load_lds_dwordx4 v[164:165], off
	v_lshl_add_u64 v[164:165], s[68:69], 0, v[140:141]
	s_mov_b32 m0, s43
	s_nop 0
	global_load_lds_dwordx4 v[164:165], off
	s_waitcnt lgkmcnt(8)
	s_barrier
	s_waitcnt lgkmcnt(0)
	s_waitcnt lgkmcnt(0)
	v_mfma_scale_f32_16x16x128_f8f6f4 v[108:111], v[156:163], v[188:195], v[108:111], v171, v171 op_sel_hi:[0,0,0]
	v_mfma_scale_f32_16x16x128_f8f6f4 v[112:115], v[180:187], v[188:195], v[112:115], v171, v171 op_sel_hi:[0,0,0]
	v_mfma_scale_f32_16x16x128_f8f6f4 v[104:107], v[156:163], v[196:203], v[104:107], v171, v171 op_sel_hi:[0,0,0]
	v_mfma_scale_f32_16x16x128_f8f6f4 v[100:103], v[180:187], v[196:203], v[100:103], v171, v171 op_sel_hi:[0,0,0]
	v_mfma_scale_f32_16x16x128_f8f6f4 v[80:83], v[156:163], v[204:211], v[80:83], v171, v171 op_sel_hi:[0,0,0]
	v_mfma_scale_f32_16x16x128_f8f6f4 v[76:79], v[180:187], v[204:211], v[76:79], v171, v171 op_sel_hi:[0,0,0]
	v_mfma_scale_f32_16x16x128_f8f6f4 v[48:51], v[156:163], v[212:219], v[48:51], v171, v171 op_sel_hi:[0,0,0]
	v_mfma_scale_f32_16x16x128_f8f6f4 v[44:47], v[180:187], v[212:219], v[44:47], v171, v171 op_sel_hi:[0,0,0]
	s_barrier
	s_add_i32 s69, 0, 0x1c000
	s_add_i32 s68, s66, s39
	v_add_u32_e32 v155, s69, v174
	v_lshl_add_u64 v[132:133], v[132:133], 0, s[12:13]
	s_mov_b32 m0, s68
	s_add_i32 s66, s68, 0x2000
	ds_read_b128 v[224:227], v155
	ds_read_b128 v[228:231], v155 offset:1024
	ds_read_b128 v[232:235], v155 offset:2048
	ds_read_b128 v[236:239], v155 offset:3072
	global_load_lds_dwordx4 v[132:133], off
	v_lshl_add_u64 v[132:133], v[134:135], 0, s[12:13]
	s_mov_b32 m0, s66
	s_nop 0
	global_load_lds_dwordx4 v[132:133], off
	s_barrier
	s_waitcnt lgkmcnt(0)
	s_waitcnt lgkmcnt(0)
	v_mfma_scale_f32_16x16x128_f8f6f4 v[124:127], v[224:231], v[188:195], v[124:127], v171, v171 op_sel_hi:[0,0,0]
	v_mfma_scale_f32_16x16x128_f8f6f4 v[128:131], v[232:239], v[188:195], v[128:131], v171, v171 op_sel_hi:[0,0,0]
	v_mfma_scale_f32_16x16x128_f8f6f4 v[120:123], v[224:231], v[196:203], v[120:123], v171, v171 op_sel_hi:[0,0,0]
	v_mfma_scale_f32_16x16x128_f8f6f4 v[116:119], v[232:239], v[196:203], v[116:119], v171, v171 op_sel_hi:[0,0,0]
	v_mfma_scale_f32_16x16x128_f8f6f4 v[96:99], v[224:231], v[204:211], v[96:99], v171, v171 op_sel_hi:[0,0,0]
	v_mfma_scale_f32_16x16x128_f8f6f4 v[92:95], v[232:239], v[204:211], v[92:95], v171, v171 op_sel_hi:[0,0,0]
	v_mfma_scale_f32_16x16x128_f8f6f4 v[64:67], v[224:231], v[212:219], v[64:67], v171, v171 op_sel_hi:[0,0,0]
	v_mfma_scale_f32_16x16x128_f8f6f4 v[60:63], v[232:239], v[212:219], v[60:63], v171, v171 op_sel_hi:[0,0,0]
	s_mov_b32 m0, s46
	v_lshl_add_u64 v[132:133], v[150:151], 0, s[12:13]
	s_barrier
	ds_read_b128 v[188:191], v177 offset:49152
	ds_read_b128 v[192:195], v177 offset:50176
	ds_read_b128 v[196:199], v177 offset:51200
	ds_read_b128 v[200:203], v177 offset:52224
	ds_read_b128 v[204:207], v177 offset:53248
	ds_read_b128 v[208:211], v177 offset:54272
	ds_read_b128 v[212:215], v177 offset:55296
	ds_read_b128 v[216:219], v177 offset:56320
	global_load_lds_dwordx4 v[132:133], off
	v_lshl_add_u64 v[132:133], v[152:153], 0, s[12:13]
	s_mov_b32 m0, s47
	s_nop 0
	global_load_lds_dwordx4 v[132:133], off
	s_barrier
	s_waitcnt lgkmcnt(0)
	s_waitcnt lgkmcnt(0)
	v_mfma_scale_f32_16x16x128_f8f6f4 v[72:75], v[156:163], v[188:195], v[72:75], v171, v171 op_sel_hi:[0,0,0]
	v_mfma_scale_f32_16x16x128_f8f6f4 v[68:71], v[180:187], v[188:195], v[68:71], v171, v171 op_sel_hi:[0,0,0]
	v_mfma_scale_f32_16x16x128_f8f6f4 v[40:43], v[156:163], v[196:203], v[40:43], v171, v171 op_sel_hi:[0,0,0]
	v_mfma_scale_f32_16x16x128_f8f6f4 v[36:39], v[180:187], v[196:203], v[36:39], v171, v171 op_sel_hi:[0,0,0]
	v_mfma_scale_f32_16x16x128_f8f6f4 v[24:27], v[156:163], v[204:211], v[24:27], v171, v171 op_sel_hi:[0,0,0]
	v_mfma_scale_f32_16x16x128_f8f6f4 v[20:23], v[180:187], v[204:211], v[20:23], v171, v171 op_sel_hi:[0,0,0]
	v_mfma_scale_f32_16x16x128_f8f6f4 v[8:11], v[156:163], v[212:219], v[8:11], v171, v171 op_sel_hi:[0,0,0]
	v_mfma_scale_f32_16x16x128_f8f6f4 v[4:7], v[180:187], v[212:219], v[4:7], v171, v171 op_sel_hi:[0,0,0]
	s_barrier
	s_add_u32 s70, s26, 0x10180
	s_addc_u32 s71, s27, 0
	s_add_i32 s27, s69, s39
	v_lshl_add_u64 v[132:133], s[70:71], 0, v[138:139]
	s_mov_b32 m0, s27
	s_add_i32 s26, s27, 0x2000
	global_load_lds_dwordx4 v[132:133], off
	v_lshl_add_u64 v[132:133], s[70:71], 0, v[142:143]
	s_mov_b32 m0, s26
	s_nop 0
	global_load_lds_dwordx4 v[132:133], off
	s_waitcnt vmcnt(6)
	s_barrier
	v_mfma_scale_f32_16x16x128_f8f6f4 v[88:91], v[224:231], v[188:195], v[88:91], v171, v171 op_sel_hi:[0,0,0]
	v_mfma_scale_f32_16x16x128_f8f6f4 v[84:87], v[232:239], v[188:195], v[84:87], v171, v171 op_sel_hi:[0,0,0]
	v_mfma_scale_f32_16x16x128_f8f6f4 v[56:59], v[224:231], v[196:203], v[56:59], v171, v171 op_sel_hi:[0,0,0]
	v_mfma_scale_f32_16x16x128_f8f6f4 v[52:55], v[232:239], v[196:203], v[52:55], v171, v171 op_sel_hi:[0,0,0]
	v_mfma_scale_f32_16x16x128_f8f6f4 v[32:35], v[224:231], v[204:211], v[32:35], v171, v171 op_sel_hi:[0,0,0]
	v_mfma_scale_f32_16x16x128_f8f6f4 v[28:31], v[232:239], v[204:211], v[28:31], v171, v171 op_sel_hi:[0,0,0]
	v_mfma_scale_f32_16x16x128_f8f6f4 v[16:19], v[224:231], v[212:219], v[16:19], v171, v171 op_sel_hi:[0,0,0]
	v_mfma_scale_f32_16x16x128_f8f6f4 v[12:15], v[232:239], v[212:219], v[12:15], v171, v171 op_sel_hi:[0,0,0]
	s_barrier
	ds_read_b128 v[156:159], v176
	ds_read_b128 v[160:163], v176 offset:1024
	ds_read_b128 v[180:183], v176 offset:2048
	ds_read_b128 v[184:187], v176 offset:3072
	s_add_u32 s22, s22, 0x20180
	s_addc_u32 s23, s23, 0
	s_mov_b32 m0, s67
	v_lshl_add_u64 v[132:133], s[22:23], 0, v[136:137]
	ds_read_b128 v[188:191], v177
	ds_read_b128 v[192:195], v177 offset:1024
	ds_read_b128 v[196:199], v177 offset:2048
	ds_read_b128 v[200:203], v177 offset:3072
	ds_read_b128 v[204:207], v177 offset:4096
	ds_read_b128 v[208:211], v177 offset:5120
	ds_read_b128 v[212:215], v177 offset:6144
	ds_read_b128 v[216:219], v177 offset:7168
	global_load_lds_dwordx4 v[132:133], off
	v_lshl_add_u64 v[132:133], s[22:23], 0, v[140:141]
	s_mov_b32 m0, s61
	s_nop 0
	global_load_lds_dwordx4 v[132:133], off
	s_waitcnt lgkmcnt(8)
	s_barrier
	s_waitcnt lgkmcnt(0)
	s_waitcnt lgkmcnt(0)
	v_mfma_scale_f32_16x16x128_f8f6f4 v[108:111], v[156:163], v[188:195], v[108:111], v171, v171 op_sel_hi:[0,0,0]
	v_mfma_scale_f32_16x16x128_f8f6f4 v[112:115], v[180:187], v[188:195], v[112:115], v171, v171 op_sel_hi:[0,0,0]
	v_mfma_scale_f32_16x16x128_f8f6f4 v[104:107], v[156:163], v[196:203], v[104:107], v171, v171 op_sel_hi:[0,0,0]
	v_mfma_scale_f32_16x16x128_f8f6f4 v[100:103], v[180:187], v[196:203], v[100:103], v171, v171 op_sel_hi:[0,0,0]
	v_mfma_scale_f32_16x16x128_f8f6f4 v[80:83], v[156:163], v[204:211], v[80:83], v171, v171 op_sel_hi:[0,0,0]
	v_mfma_scale_f32_16x16x128_f8f6f4 v[76:79], v[180:187], v[204:211], v[76:79], v171, v171 op_sel_hi:[0,0,0]
	v_mfma_scale_f32_16x16x128_f8f6f4 v[48:51], v[156:163], v[212:219], v[48:51], v171, v171 op_sel_hi:[0,0,0]
	v_mfma_scale_f32_16x16x128_f8f6f4 v[44:47], v[180:187], v[212:219], v[44:47], v171, v171 op_sel_hi:[0,0,0]
	s_barrier
	s_mov_b32 m0, s64
	v_lshl_add_u64 v[132:133], s[2:3], 0, v[138:139]
	ds_read_b128 v[224:227], v178
	ds_read_b128 v[228:231], v178 offset:1024
	ds_read_b128 v[232:235], v178 offset:2048
	ds_read_b128 v[236:239], v178 offset:3072
	global_load_lds_dwordx4 v[132:133], off
	v_lshl_add_u64 v[134:135], s[2:3], 0, v[142:143]
	s_mov_b32 m0, s62
	s_nop 0
	global_load_lds_dwordx4 v[134:135], off
	s_barrier
	s_waitcnt lgkmcnt(0)
	s_waitcnt lgkmcnt(0)
	v_mfma_scale_f32_16x16x128_f8f6f4 v[124:127], v[224:231], v[188:195], v[124:127], v171, v171 op_sel_hi:[0,0,0]
	v_mfma_scale_f32_16x16x128_f8f6f4 v[128:131], v[232:239], v[188:195], v[128:131], v171, v171 op_sel_hi:[0,0,0]
	v_mfma_scale_f32_16x16x128_f8f6f4 v[120:123], v[224:231], v[196:203], v[120:123], v171, v171 op_sel_hi:[0,0,0]
	v_mfma_scale_f32_16x16x128_f8f6f4 v[116:119], v[232:239], v[196:203], v[116:119], v171, v171 op_sel_hi:[0,0,0]
	v_mfma_scale_f32_16x16x128_f8f6f4 v[96:99], v[224:231], v[204:211], v[96:99], v171, v171 op_sel_hi:[0,0,0]
	v_mfma_scale_f32_16x16x128_f8f6f4 v[92:95], v[232:239], v[204:211], v[92:95], v171, v171 op_sel_hi:[0,0,0]
	v_mfma_scale_f32_16x16x128_f8f6f4 v[64:67], v[224:231], v[212:219], v[64:67], v171, v171 op_sel_hi:[0,0,0]
	v_mfma_scale_f32_16x16x128_f8f6f4 v[60:63], v[232:239], v[212:219], v[60:63], v171, v171 op_sel_hi:[0,0,0]
	s_mov_b32 m0, s40
	v_lshl_add_u64 v[150:151], s[24:25], 0, v[136:137]
	s_barrier
	ds_read_b128 v[188:191], v177 offset:16384
	ds_read_b128 v[192:195], v177 offset:17408
	ds_read_b128 v[196:199], v177 offset:18432
	ds_read_b128 v[200:203], v177 offset:19456
	ds_read_b128 v[204:207], v177 offset:20480
	ds_read_b128 v[208:211], v177 offset:21504
	ds_read_b128 v[212:215], v177 offset:22528
	ds_read_b128 v[216:219], v177 offset:23552
	global_load_lds_dwordx4 v[150:151], off
	v_lshl_add_u64 v[152:153], s[24:25], 0, v[140:141]
	s_mov_b32 m0, s41
	s_nop 0
	global_load_lds_dwordx4 v[152:153], off
	s_barrier
	s_waitcnt lgkmcnt(0)
	s_waitcnt lgkmcnt(0)
	v_mfma_scale_f32_16x16x128_f8f6f4 v[72:75], v[156:163], v[188:195], v[72:75], v171, v171 op_sel_hi:[0,0,0]
	v_mfma_scale_f32_16x16x128_f8f6f4 v[68:71], v[180:187], v[188:195], v[68:71], v171, v171 op_sel_hi:[0,0,0]
	v_mfma_scale_f32_16x16x128_f8f6f4 v[40:43], v[156:163], v[196:203], v[40:43], v171, v171 op_sel_hi:[0,0,0]
	v_mfma_scale_f32_16x16x128_f8f6f4 v[36:39], v[180:187], v[196:203], v[36:39], v171, v171 op_sel_hi:[0,0,0]
	v_mfma_scale_f32_16x16x128_f8f6f4 v[24:27], v[156:163], v[204:211], v[24:27], v171, v171 op_sel_hi:[0,0,0]
	v_mfma_scale_f32_16x16x128_f8f6f4 v[20:23], v[180:187], v[204:211], v[20:23], v171, v171 op_sel_hi:[0,0,0]
	v_mfma_scale_f32_16x16x128_f8f6f4 v[8:11], v[156:163], v[212:219], v[8:11], v171, v171 op_sel_hi:[0,0,0]
	v_mfma_scale_f32_16x16x128_f8f6f4 v[4:7], v[180:187], v[212:219], v[4:7], v171, v171 op_sel_hi:[0,0,0]
	s_barrier
	s_add_u32 s22, s2, 0x10000
	s_addc_u32 s23, s3, 0
	s_mov_b32 m0, s65
	v_lshl_add_u64 v[156:157], s[22:23], 0, v[138:139]
	global_load_lds_dwordx4 v[156:157], off
	v_lshl_add_u64 v[156:157], s[22:23], 0, v[142:143]
	s_mov_b32 m0, s63
	s_nop 0
	global_load_lds_dwordx4 v[156:157], off
	s_waitcnt vmcnt(6)
	s_barrier
	v_mfma_scale_f32_16x16x128_f8f6f4 v[88:91], v[224:231], v[188:195], v[88:91], v171, v171 op_sel_hi:[0,0,0]
	v_mfma_scale_f32_16x16x128_f8f6f4 v[84:87], v[232:239], v[188:195], v[84:87], v171, v171 op_sel_hi:[0,0,0]
	v_mfma_scale_f32_16x16x128_f8f6f4 v[56:59], v[224:231], v[196:203], v[56:59], v171, v171 op_sel_hi:[0,0,0]
	v_mfma_scale_f32_16x16x128_f8f6f4 v[52:55], v[232:239], v[196:203], v[52:55], v171, v171 op_sel_hi:[0,0,0]
	v_mfma_scale_f32_16x16x128_f8f6f4 v[32:35], v[224:231], v[204:211], v[32:35], v171, v171 op_sel_hi:[0,0,0]
	v_mfma_scale_f32_16x16x128_f8f6f4 v[28:31], v[232:239], v[204:211], v[28:31], v171, v171 op_sel_hi:[0,0,0]
	v_mfma_scale_f32_16x16x128_f8f6f4 v[16:19], v[224:231], v[212:219], v[16:19], v171, v171 op_sel_hi:[0,0,0]
	v_mfma_scale_f32_16x16x128_f8f6f4 v[12:15], v[232:239], v[212:219], v[12:15], v171, v171 op_sel_hi:[0,0,0]
	s_barrier
	ds_read_b128 v[156:159], v154
	ds_read_b128 v[160:163], v154 offset:1024
	ds_read_b128 v[180:183], v154 offset:2048
	ds_read_b128 v[184:187], v154 offset:3072
	s_add_u32 s22, s24, 0x20000
	s_addc_u32 s23, s25, 0
	s_mov_b32 m0, s42
	v_lshl_add_u64 v[164:165], s[22:23], 0, v[136:137]
	ds_read_b128 v[188:191], v177 offset:32768
	ds_read_b128 v[192:195], v177 offset:33792
	ds_read_b128 v[196:199], v177 offset:34816
	ds_read_b128 v[200:203], v177 offset:35840
	ds_read_b128 v[204:207], v177 offset:36864
	ds_read_b128 v[208:211], v177 offset:37888
	ds_read_b128 v[212:215], v177 offset:38912
	ds_read_b128 v[216:219], v177 offset:39936
	global_load_lds_dwordx4 v[164:165], off
	v_lshl_add_u64 v[164:165], s[22:23], 0, v[140:141]
	s_mov_b32 m0, s43
	s_nop 0
	global_load_lds_dwordx4 v[164:165], off
	s_waitcnt lgkmcnt(8)
	s_barrier
	s_waitcnt lgkmcnt(0)
	s_waitcnt lgkmcnt(0)
	v_mfma_scale_f32_16x16x128_f8f6f4 v[108:111], v[156:163], v[188:195], v[108:111], v171, v171 op_sel_hi:[0,0,0]
	v_mfma_scale_f32_16x16x128_f8f6f4 v[112:115], v[180:187], v[188:195], v[112:115], v171, v171 op_sel_hi:[0,0,0]
	v_mfma_scale_f32_16x16x128_f8f6f4 v[104:107], v[156:163], v[196:203], v[104:107], v171, v171 op_sel_hi:[0,0,0]
	v_mfma_scale_f32_16x16x128_f8f6f4 v[100:103], v[180:187], v[196:203], v[100:103], v171, v171 op_sel_hi:[0,0,0]
	v_mfma_scale_f32_16x16x128_f8f6f4 v[80:83], v[156:163], v[204:211], v[80:83], v171, v171 op_sel_hi:[0,0,0]
	v_mfma_scale_f32_16x16x128_f8f6f4 v[76:79], v[180:187], v[204:211], v[76:79], v171, v171 op_sel_hi:[0,0,0]
	v_mfma_scale_f32_16x16x128_f8f6f4 v[48:51], v[156:163], v[212:219], v[48:51], v171, v171 op_sel_hi:[0,0,0]
	v_mfma_scale_f32_16x16x128_f8f6f4 v[44:47], v[180:187], v[212:219], v[44:47], v171, v171 op_sel_hi:[0,0,0]
	s_barrier
	s_mov_b32 m0, s68
	v_lshl_add_u64 v[132:133], v[132:133], 0, s[8:9]
	ds_read_b128 v[224:227], v155
	ds_read_b128 v[228:231], v155 offset:1024
	ds_read_b128 v[232:235], v155 offset:2048
	ds_read_b128 v[236:239], v155 offset:3072
	global_load_lds_dwordx4 v[132:133], off
	v_lshl_add_u64 v[132:133], v[134:135], 0, s[8:9]
	s_mov_b32 m0, s66
	s_nop 0
	global_load_lds_dwordx4 v[132:133], off
	s_barrier
	s_waitcnt lgkmcnt(0)
	s_waitcnt lgkmcnt(0)
	v_mfma_scale_f32_16x16x128_f8f6f4 v[124:127], v[224:231], v[188:195], v[124:127], v171, v171 op_sel_hi:[0,0,0]
	v_mfma_scale_f32_16x16x128_f8f6f4 v[128:131], v[232:239], v[188:195], v[128:131], v171, v171 op_sel_hi:[0,0,0]
	v_mfma_scale_f32_16x16x128_f8f6f4 v[120:123], v[224:231], v[196:203], v[120:123], v171, v171 op_sel_hi:[0,0,0]
	v_mfma_scale_f32_16x16x128_f8f6f4 v[116:119], v[232:239], v[196:203], v[116:119], v171, v171 op_sel_hi:[0,0,0]
	v_mfma_scale_f32_16x16x128_f8f6f4 v[96:99], v[224:231], v[204:211], v[96:99], v171, v171 op_sel_hi:[0,0,0]
	v_mfma_scale_f32_16x16x128_f8f6f4 v[92:95], v[232:239], v[204:211], v[92:95], v171, v171 op_sel_hi:[0,0,0]
	v_mfma_scale_f32_16x16x128_f8f6f4 v[64:67], v[224:231], v[212:219], v[64:67], v171, v171 op_sel_hi:[0,0,0]
	v_mfma_scale_f32_16x16x128_f8f6f4 v[60:63], v[232:239], v[212:219], v[60:63], v171, v171 op_sel_hi:[0,0,0]
	s_mov_b32 m0, s46
	v_lshl_add_u64 v[132:133], v[150:151], 0, s[8:9]
	s_barrier
	ds_read_b128 v[188:191], v177 offset:49152
	ds_read_b128 v[192:195], v177 offset:50176
	ds_read_b128 v[196:199], v177 offset:51200
	ds_read_b128 v[200:203], v177 offset:52224
	ds_read_b128 v[204:207], v177 offset:53248
	ds_read_b128 v[208:211], v177 offset:54272
	ds_read_b128 v[212:215], v177 offset:55296
	ds_read_b128 v[216:219], v177 offset:56320
	global_load_lds_dwordx4 v[132:133], off
	v_lshl_add_u64 v[132:133], v[152:153], 0, s[8:9]
	s_mov_b32 m0, s47
	s_nop 0
	global_load_lds_dwordx4 v[132:133], off
	s_barrier
	s_waitcnt lgkmcnt(0)
	s_waitcnt lgkmcnt(0)
	v_mfma_scale_f32_16x16x128_f8f6f4 v[72:75], v[156:163], v[188:195], v[72:75], v171, v171 op_sel_hi:[0,0,0]
	v_mfma_scale_f32_16x16x128_f8f6f4 v[68:71], v[180:187], v[188:195], v[68:71], v171, v171 op_sel_hi:[0,0,0]
	v_mfma_scale_f32_16x16x128_f8f6f4 v[40:43], v[156:163], v[196:203], v[40:43], v171, v171 op_sel_hi:[0,0,0]
	v_mfma_scale_f32_16x16x128_f8f6f4 v[36:39], v[180:187], v[196:203], v[36:39], v171, v171 op_sel_hi:[0,0,0]
	v_mfma_scale_f32_16x16x128_f8f6f4 v[24:27], v[156:163], v[204:211], v[24:27], v171, v171 op_sel_hi:[0,0,0]
	v_mfma_scale_f32_16x16x128_f8f6f4 v[20:23], v[180:187], v[204:211], v[20:23], v171, v171 op_sel_hi:[0,0,0]
	v_mfma_scale_f32_16x16x128_f8f6f4 v[8:11], v[156:163], v[212:219], v[8:11], v171, v171 op_sel_hi:[0,0,0]
	v_mfma_scale_f32_16x16x128_f8f6f4 v[4:7], v[180:187], v[212:219], v[4:7], v171, v171 op_sel_hi:[0,0,0]
	s_barrier
	s_add_u32 s2, s2, 0x10080
	s_addc_u32 s3, s3, 0
	s_mov_b32 m0, s27
	v_lshl_add_u64 v[132:133], s[2:3], 0, v[138:139]
	global_load_lds_dwordx4 v[132:133], off
	v_lshl_add_u64 v[132:133], s[2:3], 0, v[142:143]
	s_mov_b32 m0, s26
	s_nop 0
	global_load_lds_dwordx4 v[132:133], off
	s_waitcnt vmcnt(6)
	s_barrier
	v_mfma_scale_f32_16x16x128_f8f6f4 v[88:91], v[224:231], v[188:195], v[88:91], v171, v171 op_sel_hi:[0,0,0]
	v_mfma_scale_f32_16x16x128_f8f6f4 v[84:87], v[232:239], v[188:195], v[84:87], v171, v171 op_sel_hi:[0,0,0]
	v_mfma_scale_f32_16x16x128_f8f6f4 v[56:59], v[224:231], v[196:203], v[56:59], v171, v171 op_sel_hi:[0,0,0]
	v_mfma_scale_f32_16x16x128_f8f6f4 v[52:55], v[232:239], v[196:203], v[52:55], v171, v171 op_sel_hi:[0,0,0]
	v_mfma_scale_f32_16x16x128_f8f6f4 v[32:35], v[224:231], v[204:211], v[32:35], v171, v171 op_sel_hi:[0,0,0]
	v_mfma_scale_f32_16x16x128_f8f6f4 v[28:31], v[232:239], v[204:211], v[28:31], v171, v171 op_sel_hi:[0,0,0]
	v_mfma_scale_f32_16x16x128_f8f6f4 v[16:19], v[224:231], v[212:219], v[16:19], v171, v171 op_sel_hi:[0,0,0]
	v_mfma_scale_f32_16x16x128_f8f6f4 v[12:15], v[232:239], v[212:219], v[12:15], v171, v171 op_sel_hi:[0,0,0]
	v_lshl_add_u32 v164, s60, 8, v173
	s_cmp_lt_i32 s59, 6
	s_cselect_b32 s2, 0, 32
	v_or_b32_e32 v162, 16, v164
	s_cselect_b32 s24, s52, 0x47b1c000
	s_cselect_b32 s22, s53, 0x800
	s_cselect_b32 s23, 0, -6
	s_add_u32 s2, s44, s2
	v_ashrrev_i32_e32 v165, 31, v164
	v_ashrrev_i32_e32 v163, 31, v162
	s_addc_u32 s3, s45, 0
	v_lshlrev_b64 v[132:133], 6, v[164:165]
	v_lshlrev_b64 v[150:151], 6, v[162:163]
	s_barrier
	s_nop 7
	s_nop 7
	s_nop 7
	v_lshl_add_u64 v[132:133], s[2:3], 0, v[132:133]
	v_lshl_add_u64 v[150:151], s[2:3], 0, v[150:151]
	global_load_dwordx4 v[180:183], v[132:133], off
	s_nop 0
	global_load_dwordx4 v[132:135], v[132:133], off offset:16
	s_nop 0
	global_load_dwordx4 v[184:187], v[150:151], off
	global_load_dwordx4 v[188:191], v[150:151], off offset:16
	v_or_b32_e32 v160, 32, v164
	v_ashrrev_i32_e32 v161, 31, v160
	v_lshlrev_b64 v[150:151], 6, v[160:161]
	v_or_b32_e32 v158, 48, v164
	v_lshl_add_u64 v[150:151], s[2:3], 0, v[150:151]
	v_ashrrev_i32_e32 v159, 31, v158
	global_load_dwordx4 v[192:195], v[150:151], off
	global_load_dwordx4 v[196:199], v[150:151], off offset:16
	v_lshlrev_b64 v[150:151], 6, v[158:159]
	v_lshl_add_u64 v[150:151], s[2:3], 0, v[150:151]
	global_load_dwordx4 v[200:203], v[150:151], off
	global_load_dwordx4 v[204:207], v[150:151], off offset:16
	v_add_u32_e32 v156, 0x80, v164
	v_add_u32_e32 v152, 0xa0, v164
	v_add_u32_e32 v150, 0xb0, v164
	v_add_u32_e32 v154, 0x90, v164
	v_ashrrev_i32_e32 v157, 31, v156
	v_ashrrev_i32_e32 v153, 31, v152
	v_ashrrev_i32_e32 v151, 31, v150
	v_ashrrev_i32_e32 v155, 31, v154
	v_lshlrev_b64 v[208:209], 6, v[156:157]
	v_lshlrev_b64 v[212:213], 6, v[152:153]
	v_lshlrev_b64 v[214:215], 6, v[150:151]
	v_lshlrev_b64 v[210:211], 6, v[154:155]
	v_lshl_add_u64 v[216:217], s[2:3], 0, v[208:209]
	v_lshl_add_u64 v[232:233], s[2:3], 0, v[212:213]
	v_lshl_add_u64 v[240:241], s[2:3], 0, v[214:215]
	v_lshl_add_u64 v[220:221], s[2:3], 0, v[210:211]
	global_load_dwordx4 v[208:211], v[216:217], off
	global_load_dwordx4 v[212:215], v[216:217], off offset:16
	s_nop 0
	global_load_dwordx4 v[216:219], v[220:221], off
	global_load_dwordx4 v[224:227], v[220:221], off offset:16
	global_load_dwordx4 v[228:231], v[232:233], off
	s_nop 0
	global_load_dwordx4 v[232:235], v[232:233], off offset:16
	s_nop 0
	global_load_dwordx4 v[236:239], v[240:241], off
	s_nop 0
	global_load_dwordx4 v[240:243], v[240:241], off offset:16
	s_mov_b32 s60, s56
	s_mov_b64 s[26:27], s[20:21]
	s_waitcnt vmcnt(0)
	v_mov_b32_e32 v220, v180
	v_mov_b32_e32 v221, v132
	v_mov_b32_e32 v132, v181
	v_mov_b32_e32 v180, v182
	v_mov_b32_e32 v181, v134
	v_mov_b32_e32 v134, v183
	v_mov_b32_e32 v182, v184
	v_mov_b32_e32 v183, v188
	v_mov_b32_e32 v188, v185
	v_mov_b32_e32 v184, v186
	v_mov_b32_e32 v185, v190
	v_mov_b32_e32 v190, v187
	v_pk_add_f32 v[132:133], v[220:221], v[132:133]
	v_pk_add_f32 v[134:135], v[180:181], v[134:135]
	v_pk_add_f32 v[180:181], v[182:183], v[188:189]
	v_pk_add_f32 v[182:183], v[184:185], v[190:191]
	v_pk_add_f32 v[132:133], v[132:133], v[134:135]
	v_pk_add_f32 v[134:135], v[180:181], v[182:183]
	v_mov_b32_e32 v181, v132
	v_mov_b32_e32 v180, v134
	v_mov_b32_e32 v132, v135
	v_pk_add_f32 v[132:133], v[180:181], v[132:133]
	v_mov_b32_e32 v186, v192
	v_pk_fma_f32 v[132:133], v[132:133], s[16:17], v[148:149] op_sel_hi:[1,0,0]
	v_mov_b32_e32 v187, v196
	v_mul_f32_e32 v134, 0x4b800000, v133
	v_mul_f32_e32 v135, 0x4b800000, v132
	v_cmp_gt_f32_e32 vcc, s54, v133
	v_cmp_gt_f32_e64 s[2:3], s54, v132
	v_mov_b32_e32 v196, v193
	v_cndmask_b32_e32 v133, v133, v134, vcc
	v_cndmask_b32_e64 v132, v132, v135, s[2:3]
	v_rsq_f32_e32 v134, v133
	v_rsq_f32_e32 v135, v132
	v_mov_b32_e32 v192, v194
	v_mov_b32_e32 v193, v198
	v_mul_f32_e32 v151, 0x45800000, v134
	v_mul_f32_e32 v153, 0x45800000, v135
	v_cndmask_b32_e32 v134, v134, v151, vcc
	v_cndmask_b32_e64 v135, v135, v153, s[2:3]
	v_mov_b32_e32 v198, v195
	v_pk_add_f32 v[132:133], v[186:187], v[196:197]
	v_mul_f32_e32 v180, 0x3c800000, v134
	v_mul_f32_e32 v182, 0x3c800000, v135
	v_pk_add_f32 v[134:135], v[192:193], v[198:199]
	v_mov_b32_e32 v184, v202
	v_pk_add_f32 v[132:133], v[132:133], v[134:135]
	v_mov_b32_e32 v134, v200
	v_mov_b32_e32 v135, v204
	v_mov_b32_e32 v204, v201
	v_mov_b32_e32 v185, v206
	v_mov_b32_e32 v206, v203
	v_pk_add_f32 v[134:135], v[134:135], v[204:205]
	v_pk_add_f32 v[184:185], v[184:185], v[206:207]
	v_mov_b32_e32 v186, v218
	v_pk_add_f32 v[134:135], v[134:135], v[184:185]
	v_mov_b32_e32 v185, v132
	v_mov_b32_e32 v184, v134
	v_mov_b32_e32 v132, v135
	v_pk_add_f32 v[132:133], v[184:185], v[132:133]
	v_mov_b32_e32 v135, v214
	v_pk_fma_f32 v[132:133], v[132:133], s[16:17], v[148:149] op_sel_hi:[1,0,0]
	v_mov_b32_e32 v214, v211
	v_mul_f32_e32 v134, 0x4b800000, v133
	v_cmp_gt_f32_e32 vcc, s54, v133
	v_cmp_gt_f32_e64 s[2:3], s54, v132
	v_mov_b32_e32 v187, v226
	v_cndmask_b32_e32 v133, v133, v134, vcc
	v_rsq_f32_e32 v133, v133
	v_mul_f32_e32 v134, 0x4b800000, v132
	v_cndmask_b32_e64 v132, v132, v134, s[2:3]
	v_rsq_f32_e32 v132, v132
	v_mul_f32_e32 v134, 0x45800000, v133
	v_cndmask_b32_e32 v133, v133, v134, vcc
	v_mul_f32_e32 v184, 0x3c800000, v133
	v_mul_f32_e32 v133, 0x45800000, v132
	v_cndmask_b32_e64 v132, v132, v133, s[2:3]
	v_mul_f32_e32 v172, 0x3c800000, v132
	v_mov_b32_e32 v132, v208
	v_mov_b32_e32 v133, v212
	v_mov_b32_e32 v212, v209
	v_mov_b32_e32 v134, v210
	v_pk_add_f32 v[132:133], v[132:133], v[212:213]
	v_pk_add_f32 v[134:135], v[134:135], v[214:215]
	v_mov_b32_e32 v226, v219
	v_pk_add_f32 v[132:133], v[132:133], v[134:135]
	v_mov_b32_e32 v134, v216
	v_mov_b32_e32 v135, v224
	v_mov_b32_e32 v224, v217
	v_pk_add_f32 v[134:135], v[134:135], v[224:225]
	v_pk_add_f32 v[186:187], v[186:187], v[226:227]
	v_pk_mul_f32 v[108:109], v[108:109], v[180:181] op_sel_hi:[1,0]
	v_pk_add_f32 v[134:135], v[134:135], v[186:187]
	v_mov_b32_e32 v187, v132
	v_mov_b32_e32 v186, v134
	v_mov_b32_e32 v132, v135
	v_pk_add_f32 v[132:133], v[186:187], v[132:133]
	v_mov_b32_e32 v135, v234
	v_pk_fma_f32 v[132:133], v[132:133], s[16:17], v[148:149] op_sel_hi:[1,0,0]
	v_mov_b32_e32 v234, v231
	v_mul_f32_e32 v134, 0x4b800000, v133
	v_cmp_gt_f32_e32 vcc, s54, v133
	v_cmp_gt_f32_e64 s[2:3], s54, v132
	v_mov_b32_e32 v186, v238
	v_cndmask_b32_e32 v133, v133, v134, vcc
	v_rsq_f32_e32 v133, v133
	v_mul_f32_e32 v134, 0x4b800000, v132
	v_cndmask_b32_e64 v132, v132, v134, s[2:3]
	v_rsq_f32_e32 v132, v132
	v_mul_f32_e32 v134, 0x45800000, v133
	v_cndmask_b32_e32 v133, v133, v134, vcc
	v_mul_f32_e32 v170, 0x3c800000, v133
	v_mul_f32_e32 v133, 0x45800000, v132
	v_cndmask_b32_e64 v132, v132, v133, s[2:3]
	v_mul_f32_e32 v168, 0x3c800000, v132
	v_mov_b32_e32 v132, v228
	v_mov_b32_e32 v133, v232
	v_mov_b32_e32 v232, v229
	v_mov_b32_e32 v134, v230
	v_pk_add_f32 v[132:133], v[132:133], v[232:233]
	v_pk_add_f32 v[134:135], v[134:135], v[234:235]
	v_mov_b32_e32 v187, v242
	v_pk_add_f32 v[132:133], v[132:133], v[134:135]
	v_mov_b32_e32 v134, v236
	v_mov_b32_e32 v135, v240
	v_mov_b32_e32 v240, v237
	v_mov_b32_e32 v242, v239
	v_pk_add_f32 v[134:135], v[134:135], v[240:241]
	v_pk_add_f32 v[186:187], v[186:187], v[242:243]
	v_pk_mul_f32 v[110:111], v[110:111], v[180:181] op_sel_hi:[1,0]
	v_pk_add_f32 v[134:135], v[134:135], v[186:187]
	v_mov_b32_e32 v187, v132
	v_mov_b32_e32 v186, v134
	v_mov_b32_e32 v132, v135
	v_pk_add_f32 v[132:133], v[186:187], v[132:133]
	v_cvt_pk_bf16_f32 v108, v108, v109
	v_cvt_pk_bf16_f32 v109, v110, v111
	v_pk_mul_f32 v[114:115], v[114:115], v[180:181] op_sel_hi:[1,0]
	v_pk_fma_f32 v[132:133], v[132:133], s[16:17], v[148:149] op_sel_hi:[1,0,0]
	v_pk_mul_f32 v[112:113], v[112:113], v[180:181] op_sel_hi:[1,0]
	v_mul_f32_e32 v134, 0x4b800000, v133
	v_cmp_gt_f32_e32 vcc, s54, v133
	v_cmp_gt_f32_e64 s[2:3], s54, v132
	v_cvt_pk_bf16_f32 v110, v112, v113
	v_cvt_pk_bf16_f32 v111, v114, v115
	v_pk_mul_f32 v[112:113], v[130:131], v[180:181] op_sel_hi:[1,0]
	v_cndmask_b32_e32 v133, v133, v134, vcc
	v_rsq_f32_e32 v133, v133
	v_mul_f32_e32 v134, 0x4b800000, v132
	v_cndmask_b32_e64 v132, v132, v134, s[2:3]
	v_rsq_f32_e32 v132, v132
	v_mul_f32_e32 v134, 0x45800000, v133
	v_cndmask_b32_e32 v133, v133, v134, vcc
	v_mul_f32_e32 v166, 0x3c800000, v133
	v_mul_f32_e32 v133, 0x45800000, v132
	v_cndmask_b32_e64 v132, v132, v133, s[2:3]
	s_add_u32 s2, s4, s24
	s_addc_u32 s3, s5, 0
	s_add_i32 s23, s23, s59
	v_lshl_or_b32 v134, s23, 8, v175
	v_ashrrev_i32_e32 v135, 31, v134
	v_lshl_add_u64 v[134:135], v[134:135], 1, s[2:3]
	v_mad_i64_i32 v[164:165], s[2:3], s22, v164, 0
	v_lshl_add_u64 v[164:165], v[164:165], 1, v[134:135]
	global_store_dwordx4 v[164:165], v[108:111], off
	v_pk_mul_f32 v[114:115], v[128:129], v[180:181] op_sel_hi:[1,0]
	v_pk_mul_f32 v[106:107], v[106:107], v[182:183] op_sel_hi:[1,0]
	v_pk_mul_f32 v[108:109], v[124:125], v[180:181] op_sel_hi:[1,0]
	v_pk_mul_f32 v[110:111], v[126:127], v[180:181] op_sel_hi:[1,0]
	v_cvt_pk_bf16_f32 v108, v108, v109
	v_pk_mul_f32 v[104:105], v[104:105], v[182:183] op_sel_hi:[1,0]
	v_cvt_pk_bf16_f32 v109, v110, v111
	v_cvt_pk_bf16_f32 v110, v114, v115
	v_cvt_pk_bf16_f32 v111, v112, v113
	global_store_dwordx4 v[164:165], v[108:111], off offset:256
	v_pk_mul_f32 v[82:83], v[82:83], v[184:185] op_sel_hi:[1,0]
	v_pk_mul_f32 v[80:81], v[80:81], v[184:185] op_sel_hi:[1,0]
	v_mad_i64_i32 v[108:109], s[2:3], s22, v162, 0
	v_lshl_add_u64 v[108:109], v[108:109], 1, v[134:135]
	v_pk_mul_f32 v[110:111], v[102:103], v[182:183] op_sel_hi:[1,0]
	v_pk_mul_f32 v[102:103], v[100:101], v[182:183] op_sel_hi:[1,0]
	v_cvt_pk_bf16_f32 v100, v104, v105
	v_cvt_pk_bf16_f32 v101, v106, v107
	v_pk_mul_f32 v[104:105], v[118:119], v[182:183] op_sel_hi:[1,0]
	v_cvt_pk_bf16_f32 v102, v102, v103
	v_cvt_pk_bf16_f32 v103, v110, v111
	global_store_dwordx4 v[108:109], v[100:103], off
	v_pk_mul_f32 v[106:107], v[116:117], v[182:183] op_sel_hi:[1,0]
	v_pk_mul_f32 v[50:51], v[50:51], v[172:173] op_sel_hi:[1,0]
	v_pk_mul_f32 v[100:101], v[120:121], v[182:183] op_sel_hi:[1,0]
	v_pk_mul_f32 v[102:103], v[122:123], v[182:183] op_sel_hi:[1,0]
	v_cvt_pk_bf16_f32 v100, v100, v101
	v_pk_mul_f32 v[48:49], v[48:49], v[172:173] op_sel_hi:[1,0]
	v_cvt_pk_bf16_f32 v101, v102, v103
	v_cvt_pk_bf16_f32 v102, v106, v107
	v_cvt_pk_bf16_f32 v103, v104, v105
	global_store_dwordx4 v[108:109], v[100:103], off offset:256
	v_pk_mul_f32 v[42:43], v[42:43], v[168:169] op_sel_hi:[1,0]
	v_pk_mul_f32 v[40:41], v[40:41], v[168:169] op_sel_hi:[1,0]
	v_mad_i64_i32 v[100:101], s[2:3], s22, v160, 0
	v_lshl_add_u64 v[100:101], v[100:101], 1, v[134:135]
	v_pk_mul_f32 v[102:103], v[78:79], v[184:185] op_sel_hi:[1,0]
	v_pk_mul_f32 v[78:79], v[76:77], v[184:185] op_sel_hi:[1,0]
	v_cvt_pk_bf16_f32 v76, v80, v81
	v_cvt_pk_bf16_f32 v77, v82, v83
	v_pk_mul_f32 v[80:81], v[94:95], v[184:185] op_sel_hi:[1,0]
	v_cvt_pk_bf16_f32 v78, v78, v79
	v_cvt_pk_bf16_f32 v79, v102, v103
	global_store_dwordx4 v[100:101], v[76:79], off
	v_pk_mul_f32 v[82:83], v[92:93], v[184:185] op_sel_hi:[1,0]
	v_pk_mul_f32 v[26:27], v[26:27], v[166:167] op_sel_hi:[1,0]
	v_pk_mul_f32 v[76:77], v[96:97], v[184:185] op_sel_hi:[1,0]
	v_pk_mul_f32 v[78:79], v[98:99], v[184:185] op_sel_hi:[1,0]
	v_cvt_pk_bf16_f32 v76, v76, v77
	v_pk_mul_f32 v[24:25], v[24:25], v[166:167] op_sel_hi:[1,0]
	v_cvt_pk_bf16_f32 v77, v78, v79
	v_cvt_pk_bf16_f32 v78, v82, v83
	v_cvt_pk_bf16_f32 v79, v80, v81
	global_store_dwordx4 v[100:101], v[76:79], off offset:256
	v_mul_f32_e32 v132, 0x3c800000, v132
	v_pk_mul_f32 v[10:11], v[10:11], v[132:133] op_sel_hi:[1,0]
	v_mad_i64_i32 v[76:77], s[2:3], s22, v158, 0
	v_lshl_add_u64 v[76:77], v[76:77], 1, v[134:135]
	v_pk_mul_f32 v[78:79], v[46:47], v[172:173] op_sel_hi:[1,0]
	v_pk_mul_f32 v[46:47], v[44:45], v[172:173] op_sel_hi:[1,0]
	v_cvt_pk_bf16_f32 v44, v48, v49
	v_cvt_pk_bf16_f32 v45, v50, v51
	v_pk_mul_f32 v[48:49], v[62:63], v[172:173] op_sel_hi:[1,0]
	v_cvt_pk_bf16_f32 v46, v46, v47
	v_cvt_pk_bf16_f32 v47, v78, v79
	global_store_dwordx4 v[76:77], v[44:47], off
	v_pk_mul_f32 v[50:51], v[60:61], v[172:173] op_sel_hi:[1,0]
	v_pk_mul_f32 v[60:61], v[68:69], v[170:171] op_sel_hi:[1,0]
	v_pk_mul_f32 v[44:45], v[64:65], v[172:173] op_sel_hi:[1,0]
	v_pk_mul_f32 v[46:47], v[66:67], v[172:173] op_sel_hi:[1,0]
	v_cvt_pk_bf16_f32 v44, v44, v45
	v_pk_mul_f32 v[8:9], v[8:9], v[132:133] op_sel_hi:[1,0]
	v_cvt_pk_bf16_f32 v45, v46, v47
	v_cvt_pk_bf16_f32 v46, v50, v51
	v_cvt_pk_bf16_f32 v47, v48, v49
	global_store_dwordx4 v[76:77], v[44:47], off offset:256
	v_pk_mul_f32 v[50:51], v[70:71], v[170:171] op_sel_hi:[1,0]
	s_add_i32 s49, s49, s17
	v_mad_i64_i32 v[44:45], s[2:3], s22, v156, 0
	v_lshl_add_u64 v[48:49], v[44:45], 1, v[134:135]
	v_pk_mul_f32 v[46:47], v[74:75], v[170:171] op_sel_hi:[1,0]
	v_pk_mul_f32 v[44:45], v[72:73], v[170:171] op_sel_hi:[1,0]
	s_andn2_b64 vcc, exec, s[0:1]
	v_cvt_pk_bf16_f32 v44, v44, v45
	v_cvt_pk_bf16_f32 v45, v46, v47
	v_cvt_pk_bf16_f32 v46, v60, v61
	v_cvt_pk_bf16_f32 v47, v50, v51
	global_store_dwordx4 v[48:49], v[44:47], off
	v_pk_mul_f32 v[50:51], v[86:87], v[170:171] op_sel_hi:[1,0]
	v_pk_mul_f32 v[60:61], v[84:85], v[170:171] op_sel_hi:[1,0]
	v_pk_mul_f32 v[46:47], v[90:91], v[170:171] op_sel_hi:[1,0]
	v_pk_mul_f32 v[44:45], v[88:89], v[170:171] op_sel_hi:[1,0]
	s_mov_b32 s59, s55
	v_cvt_pk_bf16_f32 v44, v44, v45
	v_cvt_pk_bf16_f32 v45, v46, v47
	v_cvt_pk_bf16_f32 v46, v60, v61
	v_cvt_pk_bf16_f32 v47, v50, v51
	global_store_dwordx4 v[48:49], v[44:47], off offset:256
	s_nop 1
	v_mad_i64_i32 v[44:45], s[2:3], s22, v154, 0
	v_pk_mul_f32 v[46:47], v[38:39], v[168:169] op_sel_hi:[1,0]
	v_pk_mul_f32 v[38:39], v[36:37], v[168:169] op_sel_hi:[1,0]
	v_lshl_add_u64 v[44:45], v[44:45], 1, v[134:135]
	v_cvt_pk_bf16_f32 v36, v40, v41
	v_cvt_pk_bf16_f32 v37, v42, v43
	v_cvt_pk_bf16_f32 v38, v38, v39
	v_cvt_pk_bf16_f32 v39, v46, v47
	global_store_dwordx4 v[44:45], v[36:39], off
	v_pk_mul_f32 v[40:41], v[54:55], v[168:169] op_sel_hi:[1,0]
	v_pk_mul_f32 v[42:43], v[52:53], v[168:169] op_sel_hi:[1,0]
	v_pk_mul_f32 v[38:39], v[58:59], v[168:169] op_sel_hi:[1,0]
	v_pk_mul_f32 v[36:37], v[56:57], v[168:169] op_sel_hi:[1,0]
	s_nop 0
	v_cvt_pk_bf16_f32 v36, v36, v37
	v_cvt_pk_bf16_f32 v37, v38, v39
	v_cvt_pk_bf16_f32 v38, v42, v43
	v_cvt_pk_bf16_f32 v39, v40, v41
	global_store_dwordx4 v[44:45], v[36:39], off offset:256
	s_nop 1
	v_mad_i64_i32 v[36:37], s[2:3], s22, v152, 0
	v_pk_mul_f32 v[38:39], v[22:23], v[166:167] op_sel_hi:[1,0]
	v_pk_mul_f32 v[22:23], v[20:21], v[166:167] op_sel_hi:[1,0]
	v_lshl_add_u64 v[36:37], v[36:37], 1, v[134:135]
	v_cvt_pk_bf16_f32 v20, v24, v25
	v_cvt_pk_bf16_f32 v21, v26, v27
	v_cvt_pk_bf16_f32 v22, v22, v23
	v_cvt_pk_bf16_f32 v23, v38, v39
	global_store_dwordx4 v[36:37], v[20:23], off
	v_pk_mul_f32 v[24:25], v[30:31], v[166:167] op_sel_hi:[1,0]
	v_pk_mul_f32 v[26:27], v[28:29], v[166:167] op_sel_hi:[1,0]
	v_pk_mul_f32 v[22:23], v[34:35], v[166:167] op_sel_hi:[1,0]
	v_pk_mul_f32 v[20:21], v[32:33], v[166:167] op_sel_hi:[1,0]
	s_nop 0
	v_cvt_pk_bf16_f32 v20, v20, v21
	v_cvt_pk_bf16_f32 v21, v22, v23
	v_cvt_pk_bf16_f32 v22, v26, v27
	v_cvt_pk_bf16_f32 v23, v24, v25
	global_store_dwordx4 v[36:37], v[20:23], off offset:256
	s_nop 1
	v_mad_i64_i32 v[20:21], s[2:3], s22, v150, 0
	v_pk_mul_f32 v[22:23], v[6:7], v[132:133] op_sel_hi:[1,0]
	v_pk_mul_f32 v[6:7], v[4:5], v[132:133] op_sel_hi:[1,0]
	v_lshl_add_u64 v[20:21], v[20:21], 1, v[134:135]
	v_cvt_pk_bf16_f32 v4, v8, v9
	v_cvt_pk_bf16_f32 v5, v10, v11
	v_cvt_pk_bf16_f32 v6, v6, v7
	v_cvt_pk_bf16_f32 v7, v22, v23
	global_store_dwordx4 v[20:21], v[4:7], off
	s_mov_b64 s[22:23], s[18:19]
	v_pk_mul_f32 v[8:9], v[14:15], v[132:133] op_sel_hi:[1,0]
	v_pk_mul_f32 v[6:7], v[18:19], v[132:133] op_sel_hi:[1,0]
	v_pk_mul_f32 v[4:5], v[16:17], v[132:133] op_sel_hi:[1,0]
	v_pk_mul_f32 v[10:11], v[12:13], v[132:133] op_sel_hi:[1,0]
	v_cvt_pk_bf16_f32 v4, v4, v5
	v_cvt_pk_bf16_f32 v5, v6, v7
	s_nop 0
	v_cvt_pk_bf16_f32 v6, v10, v11
	v_cvt_pk_bf16_f32 v7, v8, v9
	global_store_dwordx4 v[20:21], v[4:7], off offset:256
	s_cbranch_vccz .LBB0_371

.LBB0_911:
	ds_read_b128 v[8:11], v231
	ds_read_b128 v[12:15], v231 offset:1024
	ds_read_b128 v[0:3], v231 offset:2048
	ds_read_b128 v[4:7], v231 offset:3072
	v_lshl_add_u64 v[172:173], v[170:171], 0, s[2:3]
	s_add_i32 s94, s73, 0xc000
	v_lshl_add_u64 v[174:175], v[172:173], 0, s[10:11]
	s_mov_b32 m0, s94
	ds_read_b128 v[180:183], v228
	ds_read_b128 v[184:187], v228 offset:1024
	ds_read_b128 v[188:191], v228 offset:2048
	ds_read_b128 v[192:195], v228 offset:3072
	ds_read_b128 v[196:199], v228 offset:4096
	ds_read_b128 v[200:203], v228 offset:5120
	ds_read_b128 v[204:207], v228 offset:6144
	ds_read_b128 v[208:211], v228 offset:7168
	global_load_lds_dwordx4 v[174:175], off
	v_lshl_add_u64 v[174:175], v[168:169], 0, s[2:3]
	s_add_i32 s93, s73, 0xe000
	v_lshl_add_u64 v[176:177], v[174:175], 0, s[10:11]
	s_mov_b32 m0, s93
	s_nop 0
	global_load_lds_dwordx4 v[176:177], off
	s_waitcnt lgkmcnt(8)
	s_barrier
	s_waitcnt lgkmcnt(0)
	s_waitcnt lgkmcnt(0)
	v_mfma_scale_f32_16x16x128_f8f6f4 v[16:19], v[8:15], v[180:187], v[16:19], v225, v225 op_sel_hi:[0,0,0]
	v_mfma_scale_f32_16x16x128_f8f6f4 v[20:23], v[0:7], v[180:187], v[20:23], v225, v225 op_sel_hi:[0,0,0]
	v_mfma_scale_f32_16x16x128_f8f6f4 v[24:27], v[8:15], v[188:195], v[24:27], v225, v225 op_sel_hi:[0,0,0]
	v_mfma_scale_f32_16x16x128_f8f6f4 v[28:31], v[0:7], v[188:195], v[28:31], v225, v225 op_sel_hi:[0,0,0]
	v_mfma_scale_f32_16x16x128_f8f6f4 v[32:35], v[8:15], v[196:203], v[32:35], v225, v225 op_sel_hi:[0,0,0]
	v_mfma_scale_f32_16x16x128_f8f6f4 v[36:39], v[0:7], v[196:203], v[36:39], v225, v225 op_sel_hi:[0,0,0]
	v_mfma_scale_f32_16x16x128_f8f6f4 v[40:43], v[8:15], v[204:211], v[40:43], v225, v225 op_sel_hi:[0,0,0]
	v_mfma_scale_f32_16x16x128_f8f6f4 v[44:47], v[0:7], v[204:211], v[44:47], v225, v225 op_sel_hi:[0,0,0]
	s_barrier
	v_lshl_add_u64 v[176:177], v[146:147], 0, s[2:3]
	s_add_i32 s96, s83, s72
	v_lshl_add_u64 v[178:179], v[176:177], 0, s[12:13]
	s_mov_b32 m0, s96
	ds_read_b128 v[212:215], v232
	ds_read_b128 v[216:219], v232 offset:1024
	ds_read_b128 v[234:237], v232 offset:2048
	ds_read_b128 v[238:241], v232 offset:3072
	global_load_lds_dwordx4 v[178:179], off
	v_lshl_add_u64 v[178:179], v[144:145], 0, s[2:3]
	s_add_i32 s95, s96, 0x2000
	v_lshl_add_u64 v[220:221], v[178:179], 0, s[12:13]
	s_mov_b32 m0, s95
	s_nop 0
	global_load_lds_dwordx4 v[220:221], off
	s_barrier
	s_waitcnt lgkmcnt(0)
	s_waitcnt lgkmcnt(0)
	v_mfma_scale_f32_16x16x128_f8f6f4 v[48:51], v[212:219], v[180:187], v[48:51], v225, v225 op_sel_hi:[0,0,0]
	v_mfma_scale_f32_16x16x128_f8f6f4 v[52:55], v[234:241], v[180:187], v[52:55], v225, v225 op_sel_hi:[0,0,0]
	v_mfma_scale_f32_16x16x128_f8f6f4 v[56:59], v[212:219], v[188:195], v[56:59], v225, v225 op_sel_hi:[0,0,0]
	v_mfma_scale_f32_16x16x128_f8f6f4 v[60:63], v[234:241], v[188:195], v[60:63], v225, v225 op_sel_hi:[0,0,0]
	v_mfma_scale_f32_16x16x128_f8f6f4 v[64:67], v[212:219], v[196:203], v[64:67], v225, v225 op_sel_hi:[0,0,0]
	v_mfma_scale_f32_16x16x128_f8f6f4 v[68:71], v[234:241], v[196:203], v[68:71], v225, v225 op_sel_hi:[0,0,0]
	v_mfma_scale_f32_16x16x128_f8f6f4 v[72:75], v[212:219], v[204:211], v[72:75], v225, v225 op_sel_hi:[0,0,0]
	v_mfma_scale_f32_16x16x128_f8f6f4 v[76:79], v[234:241], v[204:211], v[76:79], v225, v225 op_sel_hi:[0,0,0]
	s_mov_b32 m0, s73
	v_lshl_add_u64 v[220:221], v[172:173], 0, s[12:13]
	s_barrier
	ds_read_b128 v[180:183], v228 offset:16384
	ds_read_b128 v[184:187], v228 offset:17408
	ds_read_b128 v[188:191], v228 offset:18432
	ds_read_b128 v[192:195], v228 offset:19456
	ds_read_b128 v[196:199], v228 offset:20480
	ds_read_b128 v[200:203], v228 offset:21504
	ds_read_b128 v[204:207], v228 offset:22528
	ds_read_b128 v[208:211], v228 offset:23552
	global_load_lds_dwordx4 v[220:221], off
	v_lshl_add_u64 v[220:221], v[174:175], 0, s[12:13]
	s_mov_b32 m0, s74
	s_nop 0
	global_load_lds_dwordx4 v[220:221], off
	s_barrier
	s_waitcnt lgkmcnt(0)
	s_waitcnt lgkmcnt(0)
	v_mfma_scale_f32_16x16x128_f8f6f4 v[80:83], v[8:15], v[180:187], v[80:83], v225, v225 op_sel_hi:[0,0,0]
	v_mfma_scale_f32_16x16x128_f8f6f4 v[84:87], v[0:7], v[180:187], v[84:87], v225, v225 op_sel_hi:[0,0,0]
	v_mfma_scale_f32_16x16x128_f8f6f4 v[88:91], v[8:15], v[188:195], v[88:91], v225, v225 op_sel_hi:[0,0,0]
	v_mfma_scale_f32_16x16x128_f8f6f4 v[92:95], v[0:7], v[188:195], v[92:95], v225, v225 op_sel_hi:[0,0,0]
	v_mfma_scale_f32_16x16x128_f8f6f4 v[96:99], v[8:15], v[196:203], v[96:99], v225, v225 op_sel_hi:[0,0,0]
	v_mfma_scale_f32_16x16x128_f8f6f4 v[100:103], v[0:7], v[196:203], v[100:103], v225, v225 op_sel_hi:[0,0,0]
	v_mfma_scale_f32_16x16x128_f8f6f4 v[104:107], v[8:15], v[204:211], v[104:107], v225, v225 op_sel_hi:[0,0,0]
	v_mfma_scale_f32_16x16x128_f8f6f4 v[108:111], v[0:7], v[204:211], v[108:111], v225, v225 op_sel_hi:[0,0,0]
	s_barrier
	s_add_i32 s97, s84, s72
	v_lshl_add_u64 v[0:1], v[176:177], 0, s[16:17]
	s_mov_b32 m0, s97
	s_add_i32 s52, s97, 0x2000
	global_load_lds_dwordx4 v[0:1], off
	v_lshl_add_u64 v[0:1], v[178:179], 0, s[16:17]
	s_mov_b32 m0, s52
	s_nop 0
	global_load_lds_dwordx4 v[0:1], off
	s_waitcnt vmcnt(6)
	s_barrier
	v_mfma_scale_f32_16x16x128_f8f6f4 v[112:115], v[212:219], v[180:187], v[112:115], v225, v225 op_sel_hi:[0,0,0]
	v_mfma_scale_f32_16x16x128_f8f6f4 v[116:119], v[234:241], v[180:187], v[116:119], v225, v225 op_sel_hi:[0,0,0]
	v_mfma_scale_f32_16x16x128_f8f6f4 v[120:123], v[212:219], v[188:195], v[120:123], v225, v225 op_sel_hi:[0,0,0]
	v_mfma_scale_f32_16x16x128_f8f6f4 v[124:127], v[234:241], v[188:195], v[124:127], v225, v225 op_sel_hi:[0,0,0]
	v_mfma_scale_f32_16x16x128_f8f6f4 v[128:131], v[212:219], v[196:203], v[128:131], v225, v225 op_sel_hi:[0,0,0]
	v_mfma_scale_f32_16x16x128_f8f6f4 v[132:135], v[234:241], v[196:203], v[132:135], v225, v225 op_sel_hi:[0,0,0]
	v_mfma_scale_f32_16x16x128_f8f6f4 v[136:139], v[212:219], v[204:211], v[136:139], v225, v225 op_sel_hi:[0,0,0]
	v_mfma_scale_f32_16x16x128_f8f6f4 v[140:143], v[234:241], v[204:211], v[140:143], v225, v225 op_sel_hi:[0,0,0]
	s_add_i32 s62, 0, 0x18000
	v_add_u32_e32 v235, s62, v227
	s_barrier
	ds_read_b128 v[0:3], v235
	ds_read_b128 v[4:7], v235 offset:1024
	ds_read_b128 v[8:11], v235 offset:2048
	ds_read_b128 v[12:15], v235 offset:3072
	s_mov_b32 m0, s75
	v_lshl_add_u64 v[212:213], v[172:173], 0, s[16:17]
	ds_read_b128 v[180:183], v228 offset:32768
	ds_read_b128 v[184:187], v228 offset:33792
	ds_read_b128 v[188:191], v228 offset:34816
	ds_read_b128 v[192:195], v228 offset:35840
	ds_read_b128 v[196:199], v228 offset:36864
	ds_read_b128 v[200:203], v228 offset:37888
	ds_read_b128 v[204:207], v228 offset:38912
	ds_read_b128 v[208:211], v228 offset:39936
	global_load_lds_dwordx4 v[212:213], off
	v_lshl_add_u64 v[212:213], v[174:175], 0, s[16:17]
	s_mov_b32 m0, s76
	s_nop 0
	global_load_lds_dwordx4 v[212:213], off
	s_waitcnt lgkmcnt(8)
	s_barrier
	s_waitcnt lgkmcnt(0)
	s_waitcnt lgkmcnt(0)
	v_mfma_scale_f32_16x16x128_f8f6f4 v[16:19], v[0:7], v[180:187], v[16:19], v225, v225 op_sel_hi:[0,0,0]
	v_mfma_scale_f32_16x16x128_f8f6f4 v[20:23], v[8:15], v[180:187], v[20:23], v225, v225 op_sel_hi:[0,0,0]
	v_mfma_scale_f32_16x16x128_f8f6f4 v[24:27], v[0:7], v[188:195], v[24:27], v225, v225 op_sel_hi:[0,0,0]
	v_mfma_scale_f32_16x16x128_f8f6f4 v[28:31], v[8:15], v[188:195], v[28:31], v225, v225 op_sel_hi:[0,0,0]
	v_mfma_scale_f32_16x16x128_f8f6f4 v[32:35], v[0:7], v[196:203], v[32:35], v225, v225 op_sel_hi:[0,0,0]
	v_mfma_scale_f32_16x16x128_f8f6f4 v[36:39], v[8:15], v[196:203], v[36:39], v225, v225 op_sel_hi:[0,0,0]
	v_mfma_scale_f32_16x16x128_f8f6f4 v[40:43], v[0:7], v[204:211], v[40:43], v225, v225 op_sel_hi:[0,0,0]
	v_mfma_scale_f32_16x16x128_f8f6f4 v[44:47], v[8:15], v[204:211], v[44:47], v225, v225 op_sel_hi:[0,0,0]
	s_barrier
	s_add_i32 s53, 0, 0x1c000
	s_add_i32 s62, s62, s72
	v_add_u32_e32 v234, s53, v227
	v_lshl_add_u64 v[220:221], v[176:177], 0, s[18:19]
	s_mov_b32 m0, s62
	s_add_i32 s63, s62, 0x2000
	ds_read_b128 v[212:215], v234
	ds_read_b128 v[216:219], v234 offset:1024
	ds_read_b128 v[236:239], v234 offset:2048
	ds_read_b128 v[240:243], v234 offset:3072
	global_load_lds_dwordx4 v[220:221], off
	v_lshl_add_u64 v[220:221], v[178:179], 0, s[18:19]
	s_mov_b32 m0, s63
	s_nop 0
	global_load_lds_dwordx4 v[220:221], off
	s_barrier
	s_waitcnt lgkmcnt(0)
	s_waitcnt lgkmcnt(0)
	v_mfma_scale_f32_16x16x128_f8f6f4 v[48:51], v[212:219], v[180:187], v[48:51], v225, v225 op_sel_hi:[0,0,0]
	v_mfma_scale_f32_16x16x128_f8f6f4 v[52:55], v[236:243], v[180:187], v[52:55], v225, v225 op_sel_hi:[0,0,0]
	v_mfma_scale_f32_16x16x128_f8f6f4 v[56:59], v[212:219], v[188:195], v[56:59], v225, v225 op_sel_hi:[0,0,0]
	v_mfma_scale_f32_16x16x128_f8f6f4 v[60:63], v[236:243], v[188:195], v[60:63], v225, v225 op_sel_hi:[0,0,0]
	v_mfma_scale_f32_16x16x128_f8f6f4 v[64:67], v[212:219], v[196:203], v[64:67], v225, v225 op_sel_hi:[0,0,0]
	v_mfma_scale_f32_16x16x128_f8f6f4 v[68:71], v[236:243], v[196:203], v[68:71], v225, v225 op_sel_hi:[0,0,0]
	v_mfma_scale_f32_16x16x128_f8f6f4 v[72:75], v[212:219], v[204:211], v[72:75], v225, v225 op_sel_hi:[0,0,0]
	v_mfma_scale_f32_16x16x128_f8f6f4 v[76:79], v[236:243], v[204:211], v[76:79], v225, v225 op_sel_hi:[0,0,0]
	s_mov_b32 m0, s80
	v_lshl_add_u64 v[172:173], v[172:173], 0, s[18:19]
	s_barrier
	ds_read_b128 v[180:183], v228 offset:49152
	ds_read_b128 v[184:187], v228 offset:50176
	ds_read_b128 v[188:191], v228 offset:51200
	ds_read_b128 v[192:195], v228 offset:52224
	ds_read_b128 v[196:199], v228 offset:53248
	ds_read_b128 v[200:203], v228 offset:54272
	ds_read_b128 v[204:207], v228 offset:55296
	ds_read_b128 v[208:211], v228 offset:56320
	global_load_lds_dwordx4 v[172:173], off
	v_lshl_add_u64 v[172:173], v[174:175], 0, s[18:19]
	s_mov_b32 m0, s81
	s_nop 0
	global_load_lds_dwordx4 v[172:173], off
	s_barrier
	s_waitcnt lgkmcnt(0)
	s_waitcnt lgkmcnt(0)
	v_mfma_scale_f32_16x16x128_f8f6f4 v[80:83], v[0:7], v[180:187], v[80:83], v225, v225 op_sel_hi:[0,0,0]
	v_mfma_scale_f32_16x16x128_f8f6f4 v[84:87], v[8:15], v[180:187], v[84:87], v225, v225 op_sel_hi:[0,0,0]
	v_mfma_scale_f32_16x16x128_f8f6f4 v[88:91], v[0:7], v[188:195], v[88:91], v225, v225 op_sel_hi:[0,0,0]
	v_mfma_scale_f32_16x16x128_f8f6f4 v[92:95], v[8:15], v[188:195], v[92:95], v225, v225 op_sel_hi:[0,0,0]
	v_mfma_scale_f32_16x16x128_f8f6f4 v[96:99], v[0:7], v[196:203], v[96:99], v225, v225 op_sel_hi:[0,0,0]
	v_mfma_scale_f32_16x16x128_f8f6f4 v[100:103], v[8:15], v[196:203], v[100:103], v225, v225 op_sel_hi:[0,0,0]
	v_mfma_scale_f32_16x16x128_f8f6f4 v[104:107], v[0:7], v[204:211], v[104:107], v225, v225 op_sel_hi:[0,0,0]
	v_mfma_scale_f32_16x16x128_f8f6f4 v[108:111], v[8:15], v[204:211], v[108:111], v225, v225 op_sel_hi:[0,0,0]
	s_barrier
	s_add_i32 s53, s53, s72
	v_lshl_add_u64 v[0:1], v[176:177], 0, s[20:21]
	s_mov_b32 m0, s53
	s_add_i32 s64, s53, 0x2000
	global_load_lds_dwordx4 v[0:1], off
	v_lshl_add_u64 v[0:1], v[178:179], 0, s[20:21]
	s_mov_b32 m0, s64
	s_nop 0
	global_load_lds_dwordx4 v[0:1], off
	s_waitcnt vmcnt(6)
	s_barrier
	v_mfma_scale_f32_16x16x128_f8f6f4 v[112:115], v[212:219], v[180:187], v[112:115], v225, v225 op_sel_hi:[0,0,0]
	v_mfma_scale_f32_16x16x128_f8f6f4 v[116:119], v[236:243], v[180:187], v[116:119], v225, v225 op_sel_hi:[0,0,0]
	v_mfma_scale_f32_16x16x128_f8f6f4 v[120:123], v[212:219], v[188:195], v[120:123], v225, v225 op_sel_hi:[0,0,0]
	v_mfma_scale_f32_16x16x128_f8f6f4 v[124:127], v[236:243], v[188:195], v[124:127], v225, v225 op_sel_hi:[0,0,0]
	v_mfma_scale_f32_16x16x128_f8f6f4 v[128:131], v[212:219], v[196:203], v[128:131], v225, v225 op_sel_hi:[0,0,0]
	v_mfma_scale_f32_16x16x128_f8f6f4 v[132:135], v[236:243], v[196:203], v[132:135], v225, v225 op_sel_hi:[0,0,0]
	v_mfma_scale_f32_16x16x128_f8f6f4 v[136:139], v[212:219], v[204:211], v[136:139], v225, v225 op_sel_hi:[0,0,0]
	v_mfma_scale_f32_16x16x128_f8f6f4 v[140:143], v[236:243], v[204:211], v[140:143], v225, v225 op_sel_hi:[0,0,0]
	s_add_i32 s44, s44, 2
	s_add_u32 s2, s2, 0x100
	s_addc_u32 s3, s3, 0
	s_cmp_gt_u32 s44, 5
	s_barrier
	s_cbranch_scc0 .LBB0_911
	s_add_u32 s44, s65, s89
	s_addc_u32 s45, s66, 0
	s_add_u32 s46, s70, s90
	s_addc_u32 s47, s71, 0
	s_and_b64 s[2:3], vcc, exec
	s_mul_i32 s2, s92, 24
	s_cselect_b32 s55, s45, s49
	s_cselect_b32 s54, s44, s48
	s_add_i32 s58, s2, s91
	s_ashr_i32 s59, s58, 31
	s_lshl_b64 s[2:3], s[58:59], 16
	s_add_u32 s2, s78, s2
	s_addc_u32 s3, s79, s3
	s_add_i32 s56, s58, 8
	s_ashr_i32 s57, s56, 31
	v_mov_b32_e32 v156, v230
	s_lshl_b64 s[56:57], s[56:57], 16
	s_nop 7
	s_nop 7
	s_nop 7
	s_add_u32 s56, s78, s56
	s_addc_u32 s57, s79, s57
	global_load_dwordx2 v[210:211], v156, s[2:3]
	global_load_dwordx2 v[216:217], v156, s[56:57]
	global_load_dwordx2 v[206:207], v156, s[2:3] offset:512
	global_load_dwordx2 v[208:209], v156, s[56:57] offset:512
	global_load_dwordx2 v[202:203], v156, s[2:3] offset:1024
	global_load_dwordx2 v[204:205], v156, s[56:57] offset:1024
	global_load_dwordx2 v[198:199], v156, s[2:3] offset:1536
	global_load_dwordx2 v[200:201], v156, s[56:57] offset:1536
	global_load_dwordx2 v[194:195], v156, s[2:3] offset:2048
	global_load_dwordx2 v[196:197], v156, s[56:57] offset:2048
	global_load_dwordx2 v[190:191], v156, s[2:3] offset:2560
	global_load_dwordx2 v[192:193], v156, s[56:57] offset:2560
	global_load_dwordx2 v[186:187], v156, s[2:3] offset:3072
	global_load_dwordx2 v[188:189], v156, s[56:57] offset:3072
	global_load_dwordx2 v[182:183], v156, s[2:3] offset:3584
	global_load_dwordx2 v[184:185], v156, s[56:57] offset:3584
	v_lshl_add_u64 v[0:1], s[2:3], 0, v[156:157]
	v_lshl_add_u64 v[2:3], s[56:57], 0, v[156:157]
	v_add_co_u32_e64 v0, s[2:3], s85, v0
	s_waitcnt vmcnt(0)
	v_cvt_f32_ubyte3_e32 v237, v210
	v_cvt_f32_ubyte0_e32 v156, v216
	v_add_f32_e32 v156, 0.5, v156
	v_rcp_f32_e32 v218, v156
	v_cvt_f32_ubyte0_e32 v156, v217
	v_add_f32_e32 v156, 0.5, v156
	v_rcp_f32_e32 v212, v156
	v_cvt_f32_ubyte1_e32 v156, v216
	v_add_f32_e32 v156, 0.5, v156
	v_rcp_f32_e32 v219, v156
	v_cvt_f32_ubyte1_e32 v156, v217
	v_add_f32_e32 v156, 0.5, v156
	v_rcp_f32_e32 v213, v156
	v_cvt_f32_ubyte2_e32 v156, v216
	v_add_f32_e32 v156, 0.5, v156
	v_rcp_f32_e32 v220, v156
	v_cvt_f32_ubyte2_e32 v156, v217
	v_add_f32_e32 v156, 0.5, v156
	v_rcp_f32_e32 v214, v156
	v_cvt_f32_ubyte3_e32 v156, v216
	v_add_f32_e32 v156, 0.5, v156
	v_rcp_f32_e32 v221, v156
	v_cvt_f32_ubyte3_e32 v156, v217
	v_add_f32_e32 v156, 0.5, v156
	v_cvt_f32_ubyte1_e32 v217, v210
	v_cvt_f32_ubyte0_e32 v216, v210
	v_cvt_f32_ubyte2_e32 v236, v210
	v_rcp_f32_e32 v215, v156
	v_pk_add_f32 v[236:237], v[236:237], 0.5 op_sel_hi:[1,0]
	v_pk_add_f32 v[216:217], v[216:217], 0.5 op_sel_hi:[1,0]
	v_cvt_f32_ubyte0_e32 v156, v208
	v_pk_mul_f32 v[216:217], v[216:217], v[218:219]
	v_pk_mul_f32 v[218:219], v[236:237], v[220:221]
	v_pk_mul_f32 v[16:17], v[16:17], v[216:217]
	v_pk_mul_f32 v[18:19], v[18:19], v[218:219]
	v_cvt_f32_ubyte3_e32 v219, v211
	v_cvt_f32_ubyte2_e32 v218, v211
	v_cvt_f32_ubyte1_e32 v217, v211
	v_cvt_f32_ubyte0_e32 v216, v211
	v_pk_add_f32 v[210:211], v[218:219], 0.5 op_sel_hi:[1,0]
	v_add_f32_e32 v156, 0.5, v156
	v_pk_mul_f32 v[210:211], v[210:211], v[214:215]
	v_pk_add_f32 v[216:217], v[216:217], 0.5 op_sel_hi:[1,0]
	v_pk_mul_f32 v[22:23], v[22:23], v[210:211]
	v_rcp_f32_e32 v210, v156
	v_cvt_f32_ubyte0_e32 v156, v209
	v_pk_mul_f32 v[212:213], v[216:217], v[212:213]
	v_add_f32_e32 v156, 0.5, v156
	v_pk_mul_f32 v[20:21], v[20:21], v[212:213]
	v_rcp_f32_e32 v212, v156
	v_cvt_f32_ubyte1_e32 v156, v208
	v_add_f32_e32 v156, 0.5, v156
	v_rcp_f32_e32 v211, v156
	v_cvt_f32_ubyte1_e32 v156, v209
	v_add_f32_e32 v156, 0.5, v156
	v_rcp_f32_e32 v213, v156
	v_cvt_f32_ubyte2_e32 v156, v208
	v_add_f32_e32 v156, 0.5, v156
	v_rcp_f32_e32 v214, v156
	v_cvt_f32_ubyte2_e32 v156, v209
	v_add_f32_e32 v156, 0.5, v156
	v_rcp_f32_e32 v216, v156
	v_cvt_f32_ubyte3_e32 v156, v208
	v_add_f32_e32 v156, 0.5, v156
	v_rcp_f32_e32 v215, v156
	v_cvt_f32_ubyte3_e32 v156, v209
	v_add_f32_e32 v156, 0.5, v156
	v_cvt_f32_ubyte1_e32 v209, v206
	v_cvt_f32_ubyte0_e32 v208, v206
	v_cvt_f32_ubyte3_e32 v219, v206
	v_cvt_f32_ubyte2_e32 v218, v206
	v_rcp_f32_e32 v217, v156
	v_pk_add_f32 v[218:219], v[218:219], 0.5 op_sel_hi:[1,0]
	v_pk_add_f32 v[208:209], v[208:209], 0.5 op_sel_hi:[1,0]
	v_cvt_f32_ubyte0_e32 v156, v204
	v_pk_mul_f32 v[208:209], v[208:209], v[210:211]
	v_pk_mul_f32 v[210:211], v[218:219], v[214:215]
	v_pk_mul_f32 v[48:49], v[48:49], v[208:209]
	v_pk_mul_f32 v[50:51], v[50:51], v[210:211]
	v_cvt_f32_ubyte3_e32 v211, v207
	v_cvt_f32_ubyte2_e32 v210, v207
	v_cvt_f32_ubyte1_e32 v209, v207
	v_cvt_f32_ubyte0_e32 v208, v207
	v_pk_add_f32 v[206:207], v[210:211], 0.5 op_sel_hi:[1,0]
	v_add_f32_e32 v156, 0.5, v156
	v_pk_mul_f32 v[206:207], v[206:207], v[216:217]
	v_pk_add_f32 v[208:209], v[208:209], 0.5 op_sel_hi:[1,0]
	v_pk_mul_f32 v[54:55], v[54:55], v[206:207]
	v_rcp_f32_e32 v206, v156
	v_cvt_f32_ubyte0_e32 v156, v205
	v_pk_mul_f32 v[208:209], v[208:209], v[212:213]
	v_add_f32_e32 v156, 0.5, v156
	v_pk_mul_f32 v[52:53], v[52:53], v[208:209]
	v_rcp_f32_e32 v208, v156
	v_cvt_f32_ubyte1_e32 v156, v204
	v_add_f32_e32 v156, 0.5, v156
	v_rcp_f32_e32 v207, v156
	v_cvt_f32_ubyte1_e32 v156, v205
	v_add_f32_e32 v156, 0.5, v156
	v_rcp_f32_e32 v209, v156
	v_cvt_f32_ubyte2_e32 v156, v204
	v_add_f32_e32 v156, 0.5, v156
	v_rcp_f32_e32 v210, v156
	v_cvt_f32_ubyte2_e32 v156, v205
	v_add_f32_e32 v156, 0.5, v156
	v_rcp_f32_e32 v212, v156
	v_cvt_f32_ubyte3_e32 v156, v204
	v_add_f32_e32 v156, 0.5, v156
	v_rcp_f32_e32 v211, v156
	v_cvt_f32_ubyte3_e32 v156, v205
	v_add_f32_e32 v156, 0.5, v156
	v_cvt_f32_ubyte1_e32 v205, v202
	v_cvt_f32_ubyte0_e32 v204, v202
	v_cvt_f32_ubyte3_e32 v215, v202
	v_cvt_f32_ubyte2_e32 v214, v202
	v_rcp_f32_e32 v213, v156
	v_pk_add_f32 v[214:215], v[214:215], 0.5 op_sel_hi:[1,0]
	v_pk_add_f32 v[204:205], v[204:205], 0.5 op_sel_hi:[1,0]
	v_cvt_f32_ubyte0_e32 v156, v200
	v_pk_mul_f32 v[204:205], v[204:205], v[206:207]
	v_pk_mul_f32 v[206:207], v[214:215], v[210:211]
	v_pk_mul_f32 v[24:25], v[24:25], v[204:205]
	v_pk_mul_f32 v[26:27], v[26:27], v[206:207]
	v_cvt_f32_ubyte3_e32 v207, v203
	v_cvt_f32_ubyte2_e32 v206, v203
	v_cvt_f32_ubyte1_e32 v205, v203
	v_cvt_f32_ubyte0_e32 v204, v203
	v_pk_add_f32 v[202:203], v[206:207], 0.5 op_sel_hi:[1,0]
	v_add_f32_e32 v156, 0.5, v156
	v_pk_mul_f32 v[202:203], v[202:203], v[212:213]
	v_pk_add_f32 v[204:205], v[204:205], 0.5 op_sel_hi:[1,0]
	v_pk_mul_f32 v[30:31], v[30:31], v[202:203]
	v_rcp_f32_e32 v202, v156
	v_cvt_f32_ubyte0_e32 v156, v201
	v_pk_mul_f32 v[204:205], v[204:205], v[208:209]
	v_add_f32_e32 v156, 0.5, v156
	v_pk_mul_f32 v[28:29], v[28:29], v[204:205]
	v_rcp_f32_e32 v204, v156
	v_cvt_f32_ubyte1_e32 v156, v200
	v_add_f32_e32 v156, 0.5, v156
	v_rcp_f32_e32 v203, v156
	v_cvt_f32_ubyte1_e32 v156, v201
	v_add_f32_e32 v156, 0.5, v156
	v_rcp_f32_e32 v205, v156
	v_cvt_f32_ubyte2_e32 v156, v200
	v_add_f32_e32 v156, 0.5, v156
	v_rcp_f32_e32 v206, v156
	v_cvt_f32_ubyte2_e32 v156, v201
	v_add_f32_e32 v156, 0.5, v156
	v_rcp_f32_e32 v208, v156
	v_cvt_f32_ubyte3_e32 v156, v200
	v_add_f32_e32 v156, 0.5, v156
	v_rcp_f32_e32 v207, v156
	v_cvt_f32_ubyte3_e32 v156, v201
	v_add_f32_e32 v156, 0.5, v156
	v_cvt_f32_ubyte1_e32 v201, v198
	v_cvt_f32_ubyte0_e32 v200, v198
	v_cvt_f32_ubyte3_e32 v211, v198
	v_cvt_f32_ubyte2_e32 v210, v198
	v_rcp_f32_e32 v209, v156
	v_pk_add_f32 v[210:211], v[210:211], 0.5 op_sel_hi:[1,0]
	v_pk_add_f32 v[200:201], v[200:201], 0.5 op_sel_hi:[1,0]
	v_cvt_f32_ubyte0_e32 v156, v196
	v_pk_mul_f32 v[200:201], v[200:201], v[202:203]
	v_pk_mul_f32 v[202:203], v[210:211], v[206:207]
	v_pk_mul_f32 v[56:57], v[56:57], v[200:201]
	v_pk_mul_f32 v[58:59], v[58:59], v[202:203]
	v_cvt_f32_ubyte3_e32 v203, v199
	v_cvt_f32_ubyte2_e32 v202, v199
	v_cvt_f32_ubyte1_e32 v201, v199
	v_cvt_f32_ubyte0_e32 v200, v199
	v_pk_add_f32 v[198:199], v[202:203], 0.5 op_sel_hi:[1,0]
	v_add_f32_e32 v156, 0.5, v156
	v_pk_mul_f32 v[198:199], v[198:199], v[208:209]
	v_pk_add_f32 v[200:201], v[200:201], 0.5 op_sel_hi:[1,0]
	v_pk_mul_f32 v[62:63], v[62:63], v[198:199]
	v_rcp_f32_e32 v198, v156
	v_cvt_f32_ubyte0_e32 v156, v197
	v_pk_mul_f32 v[200:201], v[200:201], v[204:205]
	v_add_f32_e32 v156, 0.5, v156
	v_pk_mul_f32 v[60:61], v[60:61], v[200:201]
	v_rcp_f32_e32 v200, v156
	v_cvt_f32_ubyte1_e32 v156, v196
	v_add_f32_e32 v156, 0.5, v156
	v_rcp_f32_e32 v199, v156
	v_cvt_f32_ubyte1_e32 v156, v197
	v_add_f32_e32 v156, 0.5, v156
	v_rcp_f32_e32 v201, v156
	v_cvt_f32_ubyte2_e32 v156, v196
	v_add_f32_e32 v156, 0.5, v156
	v_rcp_f32_e32 v202, v156
	v_cvt_f32_ubyte2_e32 v156, v197
	v_addc_co_u32_e64 v1, s[2:3], 0, v1, s[2:3]
	v_add_f32_e32 v156, 0.5, v156
	v_add_co_u32_e64 v6, s[2:3], s85, v2
	v_rcp_f32_e32 v204, v156
	v_cvt_f32_ubyte3_e32 v156, v196
	v_addc_co_u32_e64 v7, s[2:3], 0, v3, s[2:3]
	v_add_f32_e32 v156, 0.5, v156
	global_load_dwordx2 v[178:179], v[0:1], off
	global_load_dwordx2 v[180:181], v[6:7], off
	global_load_dwordx2 v[174:175], v[0:1], off offset:512
	global_load_dwordx2 v[176:177], v[6:7], off offset:512
	global_load_dwordx2 v[170:171], v[0:1], off offset:1024
	global_load_dwordx2 v[172:173], v[6:7], off offset:1024
	global_load_dwordx2 v[144:145], v[0:1], off offset:1536
	global_load_dwordx2 v[146:147], v[6:7], off offset:1536
	global_load_dwordx2 v[12:13], v[0:1], off offset:2048
	global_load_dwordx2 v[14:15], v[6:7], off offset:2048
	global_load_dwordx2 v[8:9], v[0:1], off offset:2560
	global_load_dwordx2 v[10:11], v[6:7], off offset:2560
	global_load_dwordx2 v[2:3], v[0:1], off offset:3072
	global_load_dwordx2 v[4:5], v[6:7], off offset:3072
	s_nop 0
	global_load_dwordx2 v[0:1], v[0:1], off offset:3584
	s_nop 0
	global_load_dwordx2 v[6:7], v[6:7], off offset:3584
	v_rcp_f32_e32 v203, v156
	v_cvt_f32_ubyte3_e32 v156, v197
	v_add_f32_e32 v156, 0.5, v156
	v_cvt_f32_ubyte1_e32 v197, v194
	v_cvt_f32_ubyte0_e32 v196, v194
	v_cvt_f32_ubyte3_e32 v207, v194
	v_cvt_f32_ubyte2_e32 v206, v194
	v_rcp_f32_e32 v205, v156
	v_pk_add_f32 v[206:207], v[206:207], 0.5 op_sel_hi:[1,0]
	v_pk_add_f32 v[196:197], v[196:197], 0.5 op_sel_hi:[1,0]
	v_cvt_f32_ubyte0_e32 v156, v192
	v_pk_mul_f32 v[196:197], v[196:197], v[198:199]
	v_pk_mul_f32 v[198:199], v[206:207], v[202:203]
	v_pk_mul_f32 v[32:33], v[32:33], v[196:197]
	v_pk_mul_f32 v[34:35], v[34:35], v[198:199]
	v_cvt_f32_ubyte3_e32 v199, v195
	v_cvt_f32_ubyte2_e32 v198, v195
	v_cvt_f32_ubyte1_e32 v197, v195
	v_cvt_f32_ubyte0_e32 v196, v195
	v_pk_add_f32 v[194:195], v[198:199], 0.5 op_sel_hi:[1,0]
	v_add_f32_e32 v156, 0.5, v156
	v_pk_mul_f32 v[194:195], v[194:195], v[204:205]
	v_pk_add_f32 v[196:197], v[196:197], 0.5 op_sel_hi:[1,0]
	v_pk_mul_f32 v[38:39], v[38:39], v[194:195]
	v_rcp_f32_e32 v194, v156
	v_cvt_f32_ubyte0_e32 v156, v193
	v_pk_mul_f32 v[196:197], v[196:197], v[200:201]
	v_add_f32_e32 v156, 0.5, v156
	v_pk_mul_f32 v[36:37], v[36:37], v[196:197]
	v_rcp_f32_e32 v196, v156
	v_cvt_f32_ubyte1_e32 v156, v192
	v_add_f32_e32 v156, 0.5, v156
	v_rcp_f32_e32 v195, v156
	v_cvt_f32_ubyte1_e32 v156, v193
	v_add_f32_e32 v156, 0.5, v156
	v_rcp_f32_e32 v197, v156
	v_cvt_f32_ubyte2_e32 v156, v192
	v_add_f32_e32 v156, 0.5, v156
	v_rcp_f32_e32 v198, v156
	v_cvt_f32_ubyte2_e32 v156, v193
	v_add_f32_e32 v156, 0.5, v156
	v_rcp_f32_e32 v200, v156
	v_cvt_f32_ubyte3_e32 v156, v192
	v_add_f32_e32 v156, 0.5, v156
	v_rcp_f32_e32 v199, v156
	v_cvt_f32_ubyte3_e32 v156, v193
	v_add_f32_e32 v156, 0.5, v156
	v_cvt_f32_ubyte1_e32 v193, v190
	v_cvt_f32_ubyte0_e32 v192, v190
	v_cvt_f32_ubyte3_e32 v203, v190
	v_cvt_f32_ubyte2_e32 v202, v190
	v_rcp_f32_e32 v201, v156
	v_pk_add_f32 v[202:203], v[202:203], 0.5 op_sel_hi:[1,0]
	v_pk_add_f32 v[192:193], v[192:193], 0.5 op_sel_hi:[1,0]
	v_cvt_f32_ubyte0_e32 v156, v188
	v_pk_mul_f32 v[192:193], v[192:193], v[194:195]
	v_pk_mul_f32 v[194:195], v[202:203], v[198:199]
	v_pk_mul_f32 v[64:65], v[64:65], v[192:193]
	v_pk_mul_f32 v[66:67], v[66:67], v[194:195]
	v_cvt_f32_ubyte3_e32 v195, v191
	v_cvt_f32_ubyte2_e32 v194, v191
	v_cvt_f32_ubyte1_e32 v193, v191
	v_cvt_f32_ubyte0_e32 v192, v191
	v_pk_add_f32 v[190:191], v[194:195], 0.5 op_sel_hi:[1,0]
	v_add_f32_e32 v156, 0.5, v156
	v_pk_mul_f32 v[190:191], v[190:191], v[200:201]
	v_pk_add_f32 v[192:193], v[192:193], 0.5 op_sel_hi:[1,0]
	v_pk_mul_f32 v[70:71], v[70:71], v[190:191]
	v_rcp_f32_e32 v190, v156
	v_cvt_f32_ubyte0_e32 v156, v189
	v_pk_mul_f32 v[192:193], v[192:193], v[196:197]
	v_add_f32_e32 v156, 0.5, v156
	v_pk_mul_f32 v[68:69], v[68:69], v[192:193]
	v_rcp_f32_e32 v192, v156
	v_cvt_f32_ubyte1_e32 v156, v188
	v_add_f32_e32 v156, 0.5, v156
	v_rcp_f32_e32 v191, v156
	v_cvt_f32_ubyte1_e32 v156, v189
	v_add_f32_e32 v156, 0.5, v156
	v_rcp_f32_e32 v193, v156
	v_cvt_f32_ubyte2_e32 v156, v188
	v_add_f32_e32 v156, 0.5, v156
	v_rcp_f32_e32 v194, v156
	v_cvt_f32_ubyte2_e32 v156, v189
	v_add_f32_e32 v156, 0.5, v156
	v_rcp_f32_e32 v196, v156
	v_cvt_f32_ubyte3_e32 v156, v188
	v_add_f32_e32 v156, 0.5, v156
	v_rcp_f32_e32 v195, v156
	v_cvt_f32_ubyte3_e32 v156, v189
	v_add_f32_e32 v156, 0.5, v156
	v_cvt_f32_ubyte1_e32 v189, v186
	v_cvt_f32_ubyte0_e32 v188, v186
	v_cvt_f32_ubyte3_e32 v199, v186
	v_cvt_f32_ubyte2_e32 v198, v186
	v_rcp_f32_e32 v197, v156
	v_pk_add_f32 v[198:199], v[198:199], 0.5 op_sel_hi:[1,0]
	v_pk_add_f32 v[188:189], v[188:189], 0.5 op_sel_hi:[1,0]
	v_cvt_f32_ubyte0_e32 v156, v184
	v_pk_mul_f32 v[188:189], v[188:189], v[190:191]
	v_pk_mul_f32 v[190:191], v[198:199], v[194:195]
	v_pk_mul_f32 v[40:41], v[40:41], v[188:189]
	v_pk_mul_f32 v[42:43], v[42:43], v[190:191]
	v_cvt_f32_ubyte3_e32 v191, v187
	v_cvt_f32_ubyte2_e32 v190, v187
	v_cvt_f32_ubyte1_e32 v189, v187
	v_cvt_f32_ubyte0_e32 v188, v187
	v_pk_add_f32 v[186:187], v[190:191], 0.5 op_sel_hi:[1,0]
	v_add_f32_e32 v156, 0.5, v156
	v_pk_mul_f32 v[186:187], v[186:187], v[196:197]
	v_pk_add_f32 v[188:189], v[188:189], 0.5 op_sel_hi:[1,0]
	v_pk_mul_f32 v[46:47], v[46:47], v[186:187]
	v_rcp_f32_e32 v186, v156
	v_cvt_f32_ubyte0_e32 v156, v185
	v_pk_mul_f32 v[188:189], v[188:189], v[192:193]
	v_add_f32_e32 v156, 0.5, v156
	v_pk_mul_f32 v[44:45], v[44:45], v[188:189]
	v_rcp_f32_e32 v188, v156
	v_cvt_f32_ubyte1_e32 v156, v184
	v_add_f32_e32 v156, 0.5, v156
	v_rcp_f32_e32 v187, v156
	v_cvt_f32_ubyte1_e32 v156, v185
	v_add_f32_e32 v156, 0.5, v156
	v_rcp_f32_e32 v189, v156
	v_cvt_f32_ubyte2_e32 v156, v184
	v_add_f32_e32 v156, 0.5, v156
	v_rcp_f32_e32 v190, v156
	v_cvt_f32_ubyte2_e32 v156, v185
	v_add_f32_e32 v156, 0.5, v156
	v_rcp_f32_e32 v192, v156
	v_cvt_f32_ubyte3_e32 v156, v184
	v_add_f32_e32 v156, 0.5, v156
	v_rcp_f32_e32 v191, v156
	v_cvt_f32_ubyte3_e32 v156, v185
	v_add_f32_e32 v156, 0.5, v156
	v_cvt_f32_ubyte1_e32 v185, v182
	v_cvt_f32_ubyte0_e32 v184, v182
	v_cvt_f32_ubyte3_e32 v195, v182
	v_cvt_f32_ubyte2_e32 v194, v182
	v_rcp_f32_e32 v193, v156
	v_pk_add_f32 v[194:195], v[194:195], 0.5 op_sel_hi:[1,0]
	v_pk_add_f32 v[184:185], v[184:185], 0.5 op_sel_hi:[1,0]
	s_waitcnt vmcnt(0)
	v_cvt_f32_ubyte0_e32 v156, v180
	v_pk_mul_f32 v[184:185], v[184:185], v[186:187]
	v_pk_mul_f32 v[186:187], v[194:195], v[190:191]
	v_pk_mul_f32 v[72:73], v[72:73], v[184:185]
	v_pk_mul_f32 v[74:75], v[74:75], v[186:187]
	v_cvt_f32_ubyte3_e32 v187, v183
	v_cvt_f32_ubyte2_e32 v186, v183
	v_cvt_f32_ubyte1_e32 v185, v183
	v_cvt_f32_ubyte0_e32 v184, v183
	v_pk_add_f32 v[182:183], v[186:187], 0.5 op_sel_hi:[1,0]
	v_add_f32_e32 v156, 0.5, v156
	v_pk_mul_f32 v[182:183], v[182:183], v[192:193]
	v_pk_add_f32 v[184:185], v[184:185], 0.5 op_sel_hi:[1,0]
	v_pk_mul_f32 v[78:79], v[78:79], v[182:183]
	v_rcp_f32_e32 v182, v156
	v_cvt_f32_ubyte0_e32 v156, v181
	v_pk_mul_f32 v[184:185], v[184:185], v[188:189]
	v_add_f32_e32 v156, 0.5, v156
	v_pk_mul_f32 v[76:77], v[76:77], v[184:185]
	v_rcp_f32_e32 v184, v156
	v_cvt_f32_ubyte1_e32 v156, v180
	v_add_f32_e32 v156, 0.5, v156
	v_rcp_f32_e32 v183, v156
	v_cvt_f32_ubyte1_e32 v156, v181
	v_add_f32_e32 v156, 0.5, v156
	v_rcp_f32_e32 v185, v156
	v_cvt_f32_ubyte2_e32 v156, v180
	v_add_f32_e32 v156, 0.5, v156
	v_rcp_f32_e32 v186, v156
	v_cvt_f32_ubyte2_e32 v156, v181
	v_add_f32_e32 v156, 0.5, v156
	v_rcp_f32_e32 v188, v156
	v_cvt_f32_ubyte3_e32 v156, v180
	v_add_f32_e32 v156, 0.5, v156
	v_rcp_f32_e32 v187, v156
	v_cvt_f32_ubyte3_e32 v156, v181
	v_add_f32_e32 v156, 0.5, v156
	v_cvt_f32_ubyte1_e32 v181, v178
	v_cvt_f32_ubyte0_e32 v180, v178
	v_cvt_f32_ubyte3_e32 v191, v178
	v_cvt_f32_ubyte2_e32 v190, v178
	v_rcp_f32_e32 v189, v156
	v_pk_add_f32 v[190:191], v[190:191], 0.5 op_sel_hi:[1,0]
	v_pk_add_f32 v[180:181], v[180:181], 0.5 op_sel_hi:[1,0]
	v_cvt_f32_ubyte0_e32 v156, v176
	v_pk_mul_f32 v[180:181], v[180:181], v[182:183]
	v_pk_mul_f32 v[182:183], v[190:191], v[186:187]
	v_pk_mul_f32 v[80:81], v[80:81], v[180:181]
	v_pk_mul_f32 v[82:83], v[82:83], v[182:183]
	v_cvt_f32_ubyte3_e32 v183, v179
	v_cvt_f32_ubyte2_e32 v182, v179
	v_cvt_f32_ubyte1_e32 v181, v179
	v_cvt_f32_ubyte0_e32 v180, v179
	v_pk_add_f32 v[178:179], v[182:183], 0.5 op_sel_hi:[1,0]
	v_add_f32_e32 v156, 0.5, v156
	v_pk_mul_f32 v[178:179], v[178:179], v[188:189]
	v_pk_add_f32 v[180:181], v[180:181], 0.5 op_sel_hi:[1,0]
	v_pk_mul_f32 v[86:87], v[86:87], v[178:179]
	v_rcp_f32_e32 v178, v156
	v_cvt_f32_ubyte0_e32 v156, v177
	v_pk_mul_f32 v[180:181], v[180:181], v[184:185]
	v_add_f32_e32 v156, 0.5, v156
	v_pk_mul_f32 v[84:85], v[84:85], v[180:181]
	v_rcp_f32_e32 v180, v156
	v_cvt_f32_ubyte1_e32 v156, v176
	v_add_f32_e32 v156, 0.5, v156
	v_rcp_f32_e32 v179, v156
	v_cvt_f32_ubyte1_e32 v156, v177
	v_add_f32_e32 v156, 0.5, v156
	v_rcp_f32_e32 v181, v156
	v_cvt_f32_ubyte2_e32 v156, v176
	v_add_f32_e32 v156, 0.5, v156
	v_rcp_f32_e32 v182, v156
	v_cvt_f32_ubyte2_e32 v156, v177
	v_add_f32_e32 v156, 0.5, v156
	v_rcp_f32_e32 v184, v156
	v_cvt_f32_ubyte3_e32 v156, v176
	v_add_f32_e32 v156, 0.5, v156
	v_rcp_f32_e32 v183, v156
	v_cvt_f32_ubyte3_e32 v156, v177
	v_add_f32_e32 v156, 0.5, v156
	v_cvt_f32_ubyte1_e32 v177, v174
	v_cvt_f32_ubyte0_e32 v176, v174
	v_cvt_f32_ubyte3_e32 v187, v174
	v_cvt_f32_ubyte2_e32 v186, v174
	v_rcp_f32_e32 v185, v156
	v_pk_add_f32 v[186:187], v[186:187], 0.5 op_sel_hi:[1,0]
	v_pk_add_f32 v[176:177], v[176:177], 0.5 op_sel_hi:[1,0]
	v_cvt_f32_ubyte0_e32 v156, v172
	v_pk_mul_f32 v[176:177], v[176:177], v[178:179]
	v_pk_mul_f32 v[178:179], v[186:187], v[182:183]
	v_pk_mul_f32 v[112:113], v[112:113], v[176:177]
	v_pk_mul_f32 v[114:115], v[114:115], v[178:179]
	v_cvt_f32_ubyte3_e32 v179, v175
	v_cvt_f32_ubyte2_e32 v178, v175
	v_cvt_f32_ubyte1_e32 v177, v175
	v_cvt_f32_ubyte0_e32 v176, v175
	v_pk_add_f32 v[174:175], v[178:179], 0.5 op_sel_hi:[1,0]
	v_add_f32_e32 v156, 0.5, v156
	v_pk_mul_f32 v[174:175], v[174:175], v[184:185]
	v_pk_add_f32 v[176:177], v[176:177], 0.5 op_sel_hi:[1,0]
	v_pk_mul_f32 v[118:119], v[118:119], v[174:175]
	v_rcp_f32_e32 v174, v156
	v_cvt_f32_ubyte0_e32 v156, v173
	v_pk_mul_f32 v[176:177], v[176:177], v[180:181]
	v_add_f32_e32 v156, 0.5, v156
	v_pk_mul_f32 v[116:117], v[116:117], v[176:177]
	v_rcp_f32_e32 v176, v156
	v_cvt_f32_ubyte1_e32 v156, v172
	v_add_f32_e32 v156, 0.5, v156
	v_rcp_f32_e32 v175, v156
	v_cvt_f32_ubyte1_e32 v156, v173
	v_add_f32_e32 v156, 0.5, v156
	v_rcp_f32_e32 v177, v156
	v_cvt_f32_ubyte2_e32 v156, v172
	v_add_f32_e32 v156, 0.5, v156
	v_rcp_f32_e32 v178, v156
	v_cvt_f32_ubyte2_e32 v156, v173
	v_add_f32_e32 v156, 0.5, v156
	v_rcp_f32_e32 v180, v156
	v_cvt_f32_ubyte3_e32 v156, v172
	v_add_f32_e32 v156, 0.5, v156
	v_rcp_f32_e32 v179, v156
	v_cvt_f32_ubyte3_e32 v156, v173
	v_add_f32_e32 v156, 0.5, v156
	v_cvt_f32_ubyte1_e32 v173, v170
	v_cvt_f32_ubyte0_e32 v172, v170
	v_cvt_f32_ubyte3_e32 v183, v170
	v_cvt_f32_ubyte2_e32 v182, v170
	v_rcp_f32_e32 v181, v156
	v_pk_add_f32 v[182:183], v[182:183], 0.5 op_sel_hi:[1,0]
	v_pk_add_f32 v[172:173], v[172:173], 0.5 op_sel_hi:[1,0]
	v_cvt_f32_ubyte0_e32 v156, v146
	v_pk_mul_f32 v[172:173], v[172:173], v[174:175]
	v_pk_mul_f32 v[174:175], v[182:183], v[178:179]
	v_pk_mul_f32 v[88:89], v[88:89], v[172:173]
	v_pk_mul_f32 v[90:91], v[90:91], v[174:175]
	v_cvt_f32_ubyte3_e32 v175, v171
	v_cvt_f32_ubyte2_e32 v174, v171
	v_cvt_f32_ubyte1_e32 v173, v171
	v_cvt_f32_ubyte0_e32 v172, v171
	v_pk_add_f32 v[170:171], v[174:175], 0.5 op_sel_hi:[1,0]
	v_add_f32_e32 v156, 0.5, v156
	v_pk_mul_f32 v[170:171], v[170:171], v[180:181]
	v_pk_add_f32 v[172:173], v[172:173], 0.5 op_sel_hi:[1,0]
	v_pk_mul_f32 v[94:95], v[94:95], v[170:171]
	v_rcp_f32_e32 v170, v156
	v_cvt_f32_ubyte0_e32 v156, v147
	v_pk_mul_f32 v[172:173], v[172:173], v[176:177]
	v_add_f32_e32 v156, 0.5, v156
	v_pk_mul_f32 v[92:93], v[92:93], v[172:173]
	v_rcp_f32_e32 v172, v156
	v_cvt_f32_ubyte1_e32 v156, v146
	v_add_f32_e32 v156, 0.5, v156
	v_rcp_f32_e32 v171, v156
	v_cvt_f32_ubyte1_e32 v156, v147
	v_add_f32_e32 v156, 0.5, v156
	v_rcp_f32_e32 v173, v156
	v_cvt_f32_ubyte2_e32 v156, v146
	v_cvt_f32_ubyte3_e32 v146, v146
	v_add_f32_e32 v156, 0.5, v156
	v_add_f32_e32 v146, 0.5, v146
	v_rcp_f32_e32 v174, v156
	v_rcp_f32_e32 v175, v146
	v_cvt_f32_ubyte3_e32 v146, v147
	v_cvt_f32_ubyte2_e32 v156, v147
	v_add_f32_e32 v146, 0.5, v146
	v_add_f32_e32 v156, 0.5, v156
	v_rcp_f32_e32 v177, v146
	v_cvt_f32_ubyte1_e32 v147, v144
	v_cvt_f32_ubyte0_e32 v146, v144
	v_cvt_f32_ubyte3_e32 v179, v144
	v_cvt_f32_ubyte2_e32 v178, v144
	v_rcp_f32_e32 v176, v156
	v_pk_add_f32 v[178:179], v[178:179], 0.5 op_sel_hi:[1,0]
	v_pk_add_f32 v[146:147], v[146:147], 0.5 op_sel_hi:[1,0]
	v_cvt_f32_ubyte2_e32 v156, v14
	v_pk_mul_f32 v[146:147], v[146:147], v[170:171]
	v_pk_mul_f32 v[170:171], v[178:179], v[174:175]
	v_pk_mul_f32 v[120:121], v[120:121], v[146:147]
	v_pk_mul_f32 v[122:123], v[122:123], v[170:171]
	v_cvt_f32_ubyte3_e32 v171, v145
	v_cvt_f32_ubyte2_e32 v170, v145
	v_cvt_f32_ubyte1_e32 v147, v145
	v_cvt_f32_ubyte0_e32 v146, v145
	v_pk_add_f32 v[144:145], v[170:171], 0.5 op_sel_hi:[1,0]
	v_pk_add_f32 v[146:147], v[146:147], 0.5 op_sel_hi:[1,0]
	v_pk_mul_f32 v[144:145], v[144:145], v[176:177]
	v_pk_mul_f32 v[146:147], v[146:147], v[172:173]
	v_pk_mul_f32 v[126:127], v[126:127], v[144:145]
	v_cvt_f32_ubyte0_e32 v145, v15
	v_add_f32_e32 v145, 0.5, v145
	v_pk_mul_f32 v[124:125], v[124:125], v[146:147]
	v_cvt_f32_ubyte0_e32 v144, v14
	v_rcp_f32_e32 v146, v145
	v_cvt_f32_ubyte1_e32 v145, v14
	v_cvt_f32_ubyte3_e32 v14, v14
	v_add_f32_e32 v144, 0.5, v144
	v_add_f32_e32 v145, 0.5, v145
	v_add_f32_e32 v156, 0.5, v156
	v_add_f32_e32 v14, 0.5, v14
	v_rcp_f32_e32 v144, v144
	v_rcp_f32_e32 v145, v145
	v_rcp_f32_e32 v170, v156
	v_rcp_f32_e32 v171, v14
	v_cvt_f32_ubyte3_e32 v14, v15
	v_cvt_f32_ubyte2_e32 v156, v15
	v_add_f32_e32 v14, 0.5, v14
	v_cvt_f32_ubyte1_e32 v147, v15
	v_add_f32_e32 v156, 0.5, v156
	v_rcp_f32_e32 v173, v14
	v_cvt_f32_ubyte1_e32 v15, v12
	v_cvt_f32_ubyte0_e32 v14, v12
	v_cvt_f32_ubyte3_e32 v175, v12
	v_cvt_f32_ubyte2_e32 v174, v12
	v_rcp_f32_e32 v172, v156
	v_pk_add_f32 v[174:175], v[174:175], 0.5 op_sel_hi:[1,0]
	v_pk_add_f32 v[14:15], v[14:15], 0.5 op_sel_hi:[1,0]
	v_add_f32_e32 v147, 0.5, v147
	v_pk_mul_f32 v[14:15], v[14:15], v[144:145]
	v_pk_mul_f32 v[144:145], v[174:175], v[170:171]
	v_rcp_f32_e32 v147, v147
	v_pk_mul_f32 v[98:99], v[98:99], v[144:145]
	v_cvt_f32_ubyte3_e32 v145, v13
	v_cvt_f32_ubyte2_e32 v144, v13
	v_pk_mul_f32 v[96:97], v[96:97], v[14:15]
	v_cvt_f32_ubyte1_e32 v15, v13
	v_cvt_f32_ubyte0_e32 v14, v13
	v_pk_add_f32 v[12:13], v[144:145], 0.5 op_sel_hi:[1,0]
	v_pk_add_f32 v[14:15], v[14:15], 0.5 op_sel_hi:[1,0]
	v_pk_mul_f32 v[12:13], v[12:13], v[172:173]
	v_pk_mul_f32 v[14:15], v[14:15], v[146:147]
	v_pk_mul_f32 v[102:103], v[102:103], v[12:13]
	v_cvt_f32_ubyte0_e32 v13, v11
	v_add_f32_e32 v13, 0.5, v13
	v_pk_mul_f32 v[100:101], v[100:101], v[14:15]
	v_cvt_f32_ubyte0_e32 v12, v10
	v_rcp_f32_e32 v14, v13
	v_cvt_f32_ubyte1_e32 v13, v10
	v_cvt_f32_ubyte2_e32 v144, v10
	v_cvt_f32_ubyte2_e32 v145, v11
	v_cvt_f32_ubyte3_e32 v10, v10
	v_add_f32_e32 v12, 0.5, v12
	v_add_f32_e32 v13, 0.5, v13
	v_add_f32_e32 v144, 0.5, v144
	v_add_f32_e32 v145, 0.5, v145
	v_add_f32_e32 v10, 0.5, v10
	v_rcp_f32_e32 v12, v12
	v_rcp_f32_e32 v13, v13
	v_rcp_f32_e32 v144, v144
	v_rcp_f32_e32 v146, v145
	v_rcp_f32_e32 v145, v10
	v_cvt_f32_ubyte3_e32 v10, v11
	v_add_f32_e32 v10, 0.5, v10
	v_cvt_f32_ubyte1_e32 v15, v11
	v_rcp_f32_e32 v147, v10
	v_cvt_f32_ubyte1_e32 v11, v8
	v_cvt_f32_ubyte0_e32 v10, v8
	v_cvt_f32_ubyte3_e32 v171, v8
	v_cvt_f32_ubyte2_e32 v170, v8
	v_pk_add_f32 v[170:171], v[170:171], 0.5 op_sel_hi:[1,0]
	v_pk_add_f32 v[10:11], v[10:11], 0.5 op_sel_hi:[1,0]
	v_add_f32_e32 v15, 0.5, v15
	v_pk_mul_f32 v[10:11], v[10:11], v[12:13]
	v_pk_mul_f32 v[12:13], v[170:171], v[144:145]
	v_rcp_f32_e32 v15, v15
	v_pk_mul_f32 v[130:131], v[130:131], v[12:13]
	v_cvt_f32_ubyte3_e32 v13, v9
	v_cvt_f32_ubyte2_e32 v12, v9
	v_pk_mul_f32 v[128:129], v[128:129], v[10:11]
	v_cvt_f32_ubyte1_e32 v11, v9
	v_cvt_f32_ubyte0_e32 v10, v9
	v_pk_add_f32 v[8:9], v[12:13], 0.5 op_sel_hi:[1,0]
	v_pk_add_f32 v[10:11], v[10:11], 0.5 op_sel_hi:[1,0]
	v_pk_mul_f32 v[8:9], v[8:9], v[146:147]
	v_pk_mul_f32 v[10:11], v[10:11], v[14:15]
	v_pk_mul_f32 v[134:135], v[134:135], v[8:9]
	v_cvt_f32_ubyte0_e32 v9, v5
	v_add_f32_e32 v9, 0.5, v9
	v_pk_mul_f32 v[132:133], v[132:133], v[10:11]
	v_cvt_f32_ubyte0_e32 v8, v4
	v_rcp_f32_e32 v10, v9
	v_cvt_f32_ubyte1_e32 v9, v4
	v_cvt_f32_ubyte2_e32 v12, v4
	v_cvt_f32_ubyte2_e32 v13, v5
	v_cvt_f32_ubyte3_e32 v4, v4
	v_add_f32_e32 v8, 0.5, v8
	v_add_f32_e32 v9, 0.5, v9
	v_add_f32_e32 v12, 0.5, v12
	v_add_f32_e32 v13, 0.5, v13
	v_add_f32_e32 v4, 0.5, v4
	v_rcp_f32_e32 v8, v8
	v_rcp_f32_e32 v9, v9
	v_rcp_f32_e32 v12, v12
	v_rcp_f32_e32 v14, v13
	v_rcp_f32_e32 v13, v4
	v_cvt_f32_ubyte3_e32 v4, v5
	v_add_f32_e32 v4, 0.5, v4
	v_cvt_f32_ubyte1_e32 v11, v5
	v_rcp_f32_e32 v15, v4
	v_cvt_f32_ubyte1_e32 v5, v2
	v_cvt_f32_ubyte0_e32 v4, v2
	v_cvt_f32_ubyte3_e32 v145, v2
	v_cvt_f32_ubyte2_e32 v144, v2
	v_pk_add_f32 v[144:145], v[144:145], 0.5 op_sel_hi:[1,0]
	v_pk_add_f32 v[4:5], v[4:5], 0.5 op_sel_hi:[1,0]
	v_add_f32_e32 v11, 0.5, v11
	v_pk_mul_f32 v[4:5], v[4:5], v[8:9]
	v_pk_mul_f32 v[8:9], v[144:145], v[12:13]
	v_rcp_f32_e32 v11, v11
	v_pk_mul_f32 v[106:107], v[106:107], v[8:9]
	v_cvt_f32_ubyte3_e32 v9, v3
	v_cvt_f32_ubyte2_e32 v8, v3
	v_pk_mul_f32 v[104:105], v[104:105], v[4:5]
	v_cvt_f32_ubyte1_e32 v5, v3
	v_cvt_f32_ubyte0_e32 v4, v3
	v_pk_add_f32 v[2:3], v[8:9], 0.5 op_sel_hi:[1,0]
	v_pk_add_f32 v[4:5], v[4:5], 0.5 op_sel_hi:[1,0]
	v_pk_mul_f32 v[2:3], v[2:3], v[14:15]
	v_pk_mul_f32 v[4:5], v[4:5], v[10:11]
	v_pk_mul_f32 v[110:111], v[110:111], v[2:3]
	v_cvt_f32_ubyte0_e32 v3, v7
	v_add_f32_e32 v3, 0.5, v3
	v_pk_mul_f32 v[108:109], v[108:109], v[4:5]
	v_cvt_f32_ubyte0_e32 v2, v6
	v_rcp_f32_e32 v4, v3
	v_cvt_f32_ubyte1_e32 v3, v6
	v_cvt_f32_ubyte2_e32 v8, v6
	v_cvt_f32_ubyte2_e32 v9, v7
	v_cvt_f32_ubyte3_e32 v6, v6
	v_add_f32_e32 v2, 0.5, v2
	v_add_f32_e32 v3, 0.5, v3
	v_add_f32_e32 v8, 0.5, v8
	v_add_f32_e32 v9, 0.5, v9
	v_add_f32_e32 v6, 0.5, v6
	v_rcp_f32_e32 v2, v2
	v_rcp_f32_e32 v3, v3
	v_rcp_f32_e32 v8, v8
	v_rcp_f32_e32 v10, v9
	v_rcp_f32_e32 v9, v6
	v_cvt_f32_ubyte3_e32 v6, v7
	v_cvt_f32_ubyte1_e32 v5, v7
	v_add_f32_e32 v6, 0.5, v6
	v_add_f32_e32 v5, 0.5, v5
	v_rcp_f32_e32 v11, v6
	v_cvt_f32_ubyte1_e32 v7, v0
	v_cvt_f32_ubyte0_e32 v6, v0
	v_cvt_f32_ubyte3_e32 v13, v0
	v_cvt_f32_ubyte2_e32 v12, v0
	v_rcp_f32_e32 v5, v5
	v_pk_add_f32 v[12:13], v[12:13], 0.5 op_sel_hi:[1,0]
	v_pk_add_f32 v[6:7], v[6:7], 0.5 op_sel_hi:[1,0]
	s_nop 0
	v_pk_mul_f32 v[2:3], v[6:7], v[2:3]
	v_pk_mul_f32 v[6:7], v[12:13], v[8:9]
	v_pk_mul_f32 v[136:137], v[136:137], v[2:3]
	v_pk_mul_f32 v[138:139], v[138:139], v[6:7]
	v_cvt_f32_ubyte1_e32 v3, v1
	v_cvt_f32_ubyte0_e32 v2, v1
	v_cvt_f32_ubyte3_e32 v7, v1
	v_cvt_f32_ubyte2_e32 v6, v1
	v_pk_add_f32 v[0:1], v[6:7], 0.5 op_sel_hi:[1,0]
	v_pk_add_f32 v[2:3], v[2:3], 0.5 op_sel_hi:[1,0]
	v_pk_mul_f32 v[0:1], v[0:1], v[10:11]
	v_pk_mul_f32 v[2:3], v[2:3], v[4:5]
	v_pk_mul_f32 v[142:143], v[142:143], v[0:1]
	v_pk_mul_f32 v[140:141], v[140:141], v[2:3]
	ds_read_b128 v[8:11], v231
	ds_read_b128 v[12:15], v231 offset:1024
	ds_read_b128 v[0:3], v231 offset:2048
	ds_read_b128 v[4:7], v231 offset:3072
	s_add_u32 s2, s48, 0x40480
	s_addc_u32 s3, s49, 0
	s_mov_b32 m0, s94
	v_lshl_add_u64 v[144:145], s[2:3], 0, v[148:149]
	ds_read_b128 v[174:177], v228
	ds_read_b128 v[178:181], v228 offset:1024
	ds_read_b128 v[182:185], v228 offset:2048
	ds_read_b128 v[186:189], v228 offset:3072
	ds_read_b128 v[190:193], v228 offset:4096
	ds_read_b128 v[194:197], v228 offset:5120
	ds_read_b128 v[198:201], v228 offset:6144
	ds_read_b128 v[202:205], v228 offset:7168
	global_load_lds_dwordx4 v[144:145], off
	v_lshl_add_u64 v[144:145], s[2:3], 0, v[152:153]
	s_mov_b32 m0, s93
	s_nop 0
	global_load_lds_dwordx4 v[144:145], off
	s_waitcnt lgkmcnt(8)
	s_barrier
	s_waitcnt lgkmcnt(0)
	s_waitcnt lgkmcnt(0)
	v_mfma_scale_f32_16x16x128_f8f6f4 v[16:19], v[8:15], v[174:181], v[16:19], v225, v225 op_sel_hi:[0,0,0]
	v_mfma_scale_f32_16x16x128_f8f6f4 v[20:23], v[0:7], v[174:181], v[20:23], v225, v225 op_sel_hi:[0,0,0]
	v_mfma_scale_f32_16x16x128_f8f6f4 v[24:27], v[8:15], v[182:189], v[24:27], v225, v225 op_sel_hi:[0,0,0]
	v_mfma_scale_f32_16x16x128_f8f6f4 v[28:31], v[0:7], v[182:189], v[28:31], v225, v225 op_sel_hi:[0,0,0]
	v_mfma_scale_f32_16x16x128_f8f6f4 v[32:35], v[8:15], v[190:197], v[32:35], v225, v225 op_sel_hi:[0,0,0]
	v_mfma_scale_f32_16x16x128_f8f6f4 v[36:39], v[0:7], v[190:197], v[36:39], v225, v225 op_sel_hi:[0,0,0]
	v_mfma_scale_f32_16x16x128_f8f6f4 v[40:43], v[8:15], v[198:205], v[40:43], v225, v225 op_sel_hi:[0,0,0]
	v_mfma_scale_f32_16x16x128_f8f6f4 v[44:47], v[0:7], v[198:205], v[44:47], v225, v225 op_sel_hi:[0,0,0]
	s_barrier
	v_lshl_add_u64 v[170:171], s[50:51], 0, v[150:151]
	s_mov_b32 m0, s96
	v_lshl_add_u64 v[144:145], v[170:171], 0, s[22:23]
	v_lshl_add_u64 v[172:173], s[50:51], 0, v[154:155]
	ds_read_b128 v[206:209], v232
	ds_read_b128 v[210:213], v232 offset:1024
	ds_read_b128 v[214:217], v232 offset:2048
	ds_read_b128 v[218:221], v232 offset:3072
	global_load_lds_dwordx4 v[144:145], off
	v_lshl_add_u64 v[144:145], v[172:173], 0, s[22:23]
	s_mov_b32 m0, s95
	s_nop 0
	global_load_lds_dwordx4 v[144:145], off
	s_barrier
	s_waitcnt lgkmcnt(0)
	s_waitcnt lgkmcnt(0)
	v_mfma_scale_f32_16x16x128_f8f6f4 v[48:51], v[206:213], v[174:181], v[48:51], v225, v225 op_sel_hi:[0,0,0]
	v_mfma_scale_f32_16x16x128_f8f6f4 v[52:55], v[214:221], v[174:181], v[52:55], v225, v225 op_sel_hi:[0,0,0]
	v_mfma_scale_f32_16x16x128_f8f6f4 v[56:59], v[206:213], v[182:189], v[56:59], v225, v225 op_sel_hi:[0,0,0]
	v_mfma_scale_f32_16x16x128_f8f6f4 v[60:63], v[214:221], v[182:189], v[60:63], v225, v225 op_sel_hi:[0,0,0]
	v_mfma_scale_f32_16x16x128_f8f6f4 v[64:67], v[206:213], v[190:197], v[64:67], v225, v225 op_sel_hi:[0,0,0]
	v_mfma_scale_f32_16x16x128_f8f6f4 v[68:71], v[214:221], v[190:197], v[68:71], v225, v225 op_sel_hi:[0,0,0]
	v_mfma_scale_f32_16x16x128_f8f6f4 v[72:75], v[206:213], v[198:205], v[72:75], v225, v225 op_sel_hi:[0,0,0]
	v_mfma_scale_f32_16x16x128_f8f6f4 v[76:79], v[214:221], v[198:205], v[76:79], v225, v225 op_sel_hi:[0,0,0]
	v_lshl_add_u64 v[174:175], s[48:49], 0, v[148:149]
	s_mov_b32 m0, s73
	v_lshl_add_u64 v[144:145], v[174:175], 0, s[22:23]
	s_barrier
	ds_read_b128 v[176:179], v228 offset:16384
	ds_read_b128 v[180:183], v228 offset:17408
	ds_read_b128 v[184:187], v228 offset:18432
	ds_read_b128 v[188:191], v228 offset:19456
	ds_read_b128 v[192:195], v228 offset:20480
	ds_read_b128 v[196:199], v228 offset:21504
	ds_read_b128 v[236:239], v228 offset:22528
	ds_read_b128 v[240:243], v228 offset:23552
	global_load_lds_dwordx4 v[144:145], off
	v_lshl_add_u64 v[144:145], v[168:169], 0, s[22:23]
	s_mov_b32 m0, s74
	s_nop 0
	global_load_lds_dwordx4 v[144:145], off
	s_barrier
	s_waitcnt lgkmcnt(0)
	s_waitcnt lgkmcnt(0)
	v_mfma_scale_f32_16x16x128_f8f6f4 v[80:83], v[8:15], v[176:183], v[80:83], v225, v225 op_sel_hi:[0,0,0]
	v_mfma_scale_f32_16x16x128_f8f6f4 v[84:87], v[0:7], v[176:183], v[84:87], v225, v225 op_sel_hi:[0,0,0]
	v_mfma_scale_f32_16x16x128_f8f6f4 v[88:91], v[8:15], v[184:191], v[88:91], v225, v225 op_sel_hi:[0,0,0]
	v_mfma_scale_f32_16x16x128_f8f6f4 v[92:95], v[0:7], v[184:191], v[92:95], v225, v225 op_sel_hi:[0,0,0]
	v_mfma_scale_f32_16x16x128_f8f6f4 v[96:99], v[8:15], v[192:199], v[96:99], v225, v225 op_sel_hi:[0,0,0]
	v_mfma_scale_f32_16x16x128_f8f6f4 v[100:103], v[0:7], v[192:199], v[100:103], v225, v225 op_sel_hi:[0,0,0]
	v_mfma_scale_f32_16x16x128_f8f6f4 v[104:107], v[8:15], v[236:243], v[104:107], v225, v225 op_sel_hi:[0,0,0]
	v_mfma_scale_f32_16x16x128_f8f6f4 v[108:111], v[0:7], v[236:243], v[108:111], v225, v225 op_sel_hi:[0,0,0]
	s_barrier
	s_add_u32 s2, s50, 0x40500
	s_addc_u32 s3, s51, 0
	s_mov_b32 m0, s97
	v_lshl_add_u64 v[0:1], s[2:3], 0, v[150:151]
	global_load_lds_dwordx4 v[0:1], off
	v_lshl_add_u64 v[0:1], s[2:3], 0, v[154:155]
	s_mov_b32 m0, s52
	s_nop 0
	global_load_lds_dwordx4 v[0:1], off
	s_waitcnt vmcnt(6)
	s_barrier
	v_mfma_scale_f32_16x16x128_f8f6f4 v[112:115], v[206:213], v[176:183], v[112:115], v225, v225 op_sel_hi:[0,0,0]
	v_mfma_scale_f32_16x16x128_f8f6f4 v[116:119], v[214:221], v[176:183], v[116:119], v225, v225 op_sel_hi:[0,0,0]
	v_mfma_scale_f32_16x16x128_f8f6f4 v[120:123], v[206:213], v[184:191], v[120:123], v225, v225 op_sel_hi:[0,0,0]
	v_mfma_scale_f32_16x16x128_f8f6f4 v[124:127], v[214:221], v[184:191], v[124:127], v225, v225 op_sel_hi:[0,0,0]
	v_mfma_scale_f32_16x16x128_f8f6f4 v[128:131], v[206:213], v[192:199], v[128:131], v225, v225 op_sel_hi:[0,0,0]
	v_mfma_scale_f32_16x16x128_f8f6f4 v[132:135], v[214:221], v[192:199], v[132:135], v225, v225 op_sel_hi:[0,0,0]
	v_mfma_scale_f32_16x16x128_f8f6f4 v[136:139], v[206:213], v[236:243], v[136:139], v225, v225 op_sel_hi:[0,0,0]
	v_mfma_scale_f32_16x16x128_f8f6f4 v[140:143], v[214:221], v[236:243], v[140:143], v225, v225 op_sel_hi:[0,0,0]
	s_barrier
	ds_read_b128 v[0:3], v235
	ds_read_b128 v[4:7], v235 offset:1024
	ds_read_b128 v[8:11], v235 offset:2048
	ds_read_b128 v[12:15], v235 offset:3072
	s_add_u32 s2, s48, 0x40500
	s_addc_u32 s3, s49, 0
	s_mov_b32 m0, s75
	v_lshl_add_u64 v[144:145], s[2:3], 0, v[148:149]
	ds_read_b128 v[176:179], v228 offset:32768
	ds_read_b128 v[180:183], v228 offset:33792
	ds_read_b128 v[184:187], v228 offset:34816
	ds_read_b128 v[188:191], v228 offset:35840
	ds_read_b128 v[192:195], v228 offset:36864
	ds_read_b128 v[196:199], v228 offset:37888
	ds_read_b128 v[200:203], v228 offset:38912
	ds_read_b128 v[204:207], v228 offset:39936
	global_load_lds_dwordx4 v[144:145], off
	v_lshl_add_u64 v[144:145], s[2:3], 0, v[152:153]
	s_mov_b32 m0, s76
	s_nop 0
	global_load_lds_dwordx4 v[144:145], off
	s_waitcnt lgkmcnt(8)
	s_barrier
	s_waitcnt lgkmcnt(0)
	s_waitcnt lgkmcnt(0)
	v_mfma_scale_f32_16x16x128_f8f6f4 v[16:19], v[0:7], v[176:183], v[16:19], v225, v225 op_sel_hi:[0,0,0]
	v_mfma_scale_f32_16x16x128_f8f6f4 v[20:23], v[8:15], v[176:183], v[20:23], v225, v225 op_sel_hi:[0,0,0]
	v_mfma_scale_f32_16x16x128_f8f6f4 v[24:27], v[0:7], v[184:191], v[24:27], v225, v225 op_sel_hi:[0,0,0]
	v_mfma_scale_f32_16x16x128_f8f6f4 v[28:31], v[8:15], v[184:191], v[28:31], v225, v225 op_sel_hi:[0,0,0]
	v_mfma_scale_f32_16x16x128_f8f6f4 v[32:35], v[0:7], v[192:199], v[32:35], v225, v225 op_sel_hi:[0,0,0]
	v_mfma_scale_f32_16x16x128_f8f6f4 v[36:39], v[8:15], v[192:199], v[36:39], v225, v225 op_sel_hi:[0,0,0]
	v_mfma_scale_f32_16x16x128_f8f6f4 v[40:43], v[0:7], v[200:207], v[40:43], v225, v225 op_sel_hi:[0,0,0]
	v_mfma_scale_f32_16x16x128_f8f6f4 v[44:47], v[8:15], v[200:207], v[44:47], v225, v225 op_sel_hi:[0,0,0]
	s_barrier
	s_mov_b32 m0, s62
	v_lshl_add_u64 v[144:145], v[170:171], 0, s[24:25]
	ds_read_b128 v[208:211], v234
	ds_read_b128 v[212:215], v234 offset:1024
	ds_read_b128 v[236:239], v234 offset:2048
	ds_read_b128 v[240:243], v234 offset:3072
	global_load_lds_dwordx4 v[144:145], off
	v_lshl_add_u64 v[144:145], v[172:173], 0, s[24:25]
	s_mov_b32 m0, s63
	s_nop 0
	global_load_lds_dwordx4 v[144:145], off
	s_barrier
	s_waitcnt lgkmcnt(0)
	s_waitcnt lgkmcnt(0)
	v_mfma_scale_f32_16x16x128_f8f6f4 v[48:51], v[208:215], v[176:183], v[48:51], v225, v225 op_sel_hi:[0,0,0]
	v_mfma_scale_f32_16x16x128_f8f6f4 v[52:55], v[236:243], v[176:183], v[52:55], v225, v225 op_sel_hi:[0,0,0]
	v_mfma_scale_f32_16x16x128_f8f6f4 v[56:59], v[208:215], v[184:191], v[56:59], v225, v225 op_sel_hi:[0,0,0]
	v_mfma_scale_f32_16x16x128_f8f6f4 v[60:63], v[236:243], v[184:191], v[60:63], v225, v225 op_sel_hi:[0,0,0]
	v_mfma_scale_f32_16x16x128_f8f6f4 v[64:67], v[208:215], v[192:199], v[64:67], v225, v225 op_sel_hi:[0,0,0]
	v_mfma_scale_f32_16x16x128_f8f6f4 v[68:71], v[236:243], v[192:199], v[68:71], v225, v225 op_sel_hi:[0,0,0]
	v_mfma_scale_f32_16x16x128_f8f6f4 v[72:75], v[208:215], v[200:207], v[72:75], v225, v225 op_sel_hi:[0,0,0]
	v_mfma_scale_f32_16x16x128_f8f6f4 v[76:79], v[236:243], v[200:207], v[76:79], v225, v225 op_sel_hi:[0,0,0]
	s_mov_b32 m0, s80
	v_lshl_add_u64 v[144:145], v[174:175], 0, s[24:25]
	s_barrier
	ds_read_b128 v[176:179], v228 offset:49152
	ds_read_b128 v[180:183], v228 offset:50176
	ds_read_b128 v[184:187], v228 offset:51200
	ds_read_b128 v[188:191], v228 offset:52224
	ds_read_b128 v[192:195], v228 offset:53248
	ds_read_b128 v[196:199], v228 offset:54272
	ds_read_b128 v[200:203], v228 offset:55296
	ds_read_b128 v[204:207], v228 offset:56320
	global_load_lds_dwordx4 v[144:145], off
	v_lshl_add_u64 v[144:145], v[168:169], 0, s[24:25]
	s_mov_b32 m0, s81
	s_nop 0
	global_load_lds_dwordx4 v[144:145], off
	s_barrier
	s_waitcnt lgkmcnt(0)
	s_waitcnt lgkmcnt(0)
	v_mfma_scale_f32_16x16x128_f8f6f4 v[80:83], v[0:7], v[176:183], v[80:83], v225, v225 op_sel_hi:[0,0,0]
	v_mfma_scale_f32_16x16x128_f8f6f4 v[84:87], v[8:15], v[176:183], v[84:87], v225, v225 op_sel_hi:[0,0,0]
	v_mfma_scale_f32_16x16x128_f8f6f4 v[88:91], v[0:7], v[184:191], v[88:91], v225, v225 op_sel_hi:[0,0,0]
	v_mfma_scale_f32_16x16x128_f8f6f4 v[92:95], v[8:15], v[184:191], v[92:95], v225, v225 op_sel_hi:[0,0,0]
	v_mfma_scale_f32_16x16x128_f8f6f4 v[96:99], v[0:7], v[192:199], v[96:99], v225, v225 op_sel_hi:[0,0,0]
	v_mfma_scale_f32_16x16x128_f8f6f4 v[100:103], v[8:15], v[192:199], v[100:103], v225, v225 op_sel_hi:[0,0,0]
	v_mfma_scale_f32_16x16x128_f8f6f4 v[104:107], v[0:7], v[200:207], v[104:107], v225, v225 op_sel_hi:[0,0,0]
	v_mfma_scale_f32_16x16x128_f8f6f4 v[108:111], v[8:15], v[200:207], v[108:111], v225, v225 op_sel_hi:[0,0,0]
	s_barrier
	s_add_u32 s2, s50, 0x40580
	s_addc_u32 s3, s51, 0
	s_mov_b32 m0, s53
	v_lshl_add_u64 v[0:1], s[2:3], 0, v[150:151]
	global_load_lds_dwordx4 v[0:1], off
	v_lshl_add_u64 v[0:1], s[2:3], 0, v[154:155]
	s_mov_b32 m0, s64
	s_nop 0
	global_load_lds_dwordx4 v[0:1], off
	s_waitcnt vmcnt(6)
	s_barrier
	v_mfma_scale_f32_16x16x128_f8f6f4 v[112:115], v[208:215], v[176:183], v[112:115], v225, v225 op_sel_hi:[0,0,0]
	v_mfma_scale_f32_16x16x128_f8f6f4 v[116:119], v[236:243], v[176:183], v[116:119], v225, v225 op_sel_hi:[0,0,0]
	v_mfma_scale_f32_16x16x128_f8f6f4 v[120:123], v[208:215], v[184:191], v[120:123], v225, v225 op_sel_hi:[0,0,0]
	v_mfma_scale_f32_16x16x128_f8f6f4 v[124:127], v[236:243], v[184:191], v[124:127], v225, v225 op_sel_hi:[0,0,0]
	v_mfma_scale_f32_16x16x128_f8f6f4 v[128:131], v[208:215], v[192:199], v[128:131], v225, v225 op_sel_hi:[0,0,0]
	v_mfma_scale_f32_16x16x128_f8f6f4 v[132:135], v[236:243], v[192:199], v[132:135], v225, v225 op_sel_hi:[0,0,0]
	v_mfma_scale_f32_16x16x128_f8f6f4 v[136:139], v[208:215], v[200:207], v[136:139], v225, v225 op_sel_hi:[0,0,0]
	v_mfma_scale_f32_16x16x128_f8f6f4 v[140:143], v[236:243], v[200:207], v[140:143], v225, v225 op_sel_hi:[0,0,0]
	s_barrier
	ds_read_b128 v[0:3], v231
	ds_read_b128 v[4:7], v231 offset:1024
	ds_read_b128 v[8:11], v231 offset:2048
	ds_read_b128 v[12:15], v231 offset:3072
	s_add_u32 s2, s48, 0x40580
	s_addc_u32 s3, s49, 0
	s_mov_b32 m0, s94
	v_lshl_add_u64 v[144:145], s[2:3], 0, v[148:149]
	ds_read_b128 v[176:179], v228
	ds_read_b128 v[180:183], v228 offset:1024
	ds_read_b128 v[184:187], v228 offset:2048
	ds_read_b128 v[188:191], v228 offset:3072
	ds_read_b128 v[192:195], v228 offset:4096
	ds_read_b128 v[196:199], v228 offset:5120
	ds_read_b128 v[200:203], v228 offset:6144
	ds_read_b128 v[204:207], v228 offset:7168
	global_load_lds_dwordx4 v[144:145], off
	v_lshl_add_u64 v[144:145], s[2:3], 0, v[152:153]
	s_mov_b32 m0, s93
	s_nop 0
	global_load_lds_dwordx4 v[144:145], off
	s_waitcnt lgkmcnt(8)
	s_barrier
	s_waitcnt lgkmcnt(0)
	s_waitcnt lgkmcnt(0)
	v_mfma_scale_f32_16x16x128_f8f6f4 v[16:19], v[0:7], v[176:183], v[16:19], v225, v225 op_sel_hi:[0,0,0]
	v_mfma_scale_f32_16x16x128_f8f6f4 v[20:23], v[8:15], v[176:183], v[20:23], v225, v225 op_sel_hi:[0,0,0]
	v_mfma_scale_f32_16x16x128_f8f6f4 v[24:27], v[0:7], v[184:191], v[24:27], v225, v225 op_sel_hi:[0,0,0]
	v_mfma_scale_f32_16x16x128_f8f6f4 v[28:31], v[8:15], v[184:191], v[28:31], v225, v225 op_sel_hi:[0,0,0]
	v_mfma_scale_f32_16x16x128_f8f6f4 v[32:35], v[0:7], v[192:199], v[32:35], v225, v225 op_sel_hi:[0,0,0]
	v_mfma_scale_f32_16x16x128_f8f6f4 v[36:39], v[8:15], v[192:199], v[36:39], v225, v225 op_sel_hi:[0,0,0]
	v_mfma_scale_f32_16x16x128_f8f6f4 v[40:43], v[0:7], v[200:207], v[40:43], v225, v225 op_sel_hi:[0,0,0]
	v_mfma_scale_f32_16x16x128_f8f6f4 v[44:47], v[8:15], v[200:207], v[44:47], v225, v225 op_sel_hi:[0,0,0]
	s_barrier
	s_mov_b32 m0, s96
	v_lshl_add_u64 v[144:145], v[170:171], 0, s[26:27]
	ds_read_b128 v[208:211], v232
	ds_read_b128 v[212:215], v232 offset:1024
	ds_read_b128 v[236:239], v232 offset:2048
	ds_read_b128 v[240:243], v232 offset:3072
	global_load_lds_dwordx4 v[144:145], off
	v_lshl_add_u64 v[144:145], v[172:173], 0, s[26:27]
	s_mov_b32 m0, s95
	s_nop 0
	global_load_lds_dwordx4 v[144:145], off
	s_barrier
	s_waitcnt lgkmcnt(0)
	s_waitcnt lgkmcnt(0)
	v_mfma_scale_f32_16x16x128_f8f6f4 v[48:51], v[208:215], v[176:183], v[48:51], v225, v225 op_sel_hi:[0,0,0]
	v_mfma_scale_f32_16x16x128_f8f6f4 v[52:55], v[236:243], v[176:183], v[52:55], v225, v225 op_sel_hi:[0,0,0]
	v_mfma_scale_f32_16x16x128_f8f6f4 v[56:59], v[208:215], v[184:191], v[56:59], v225, v225 op_sel_hi:[0,0,0]
	v_mfma_scale_f32_16x16x128_f8f6f4 v[60:63], v[236:243], v[184:191], v[60:63], v225, v225 op_sel_hi:[0,0,0]
	v_mfma_scale_f32_16x16x128_f8f6f4 v[64:67], v[208:215], v[192:199], v[64:67], v225, v225 op_sel_hi:[0,0,0]
	v_mfma_scale_f32_16x16x128_f8f6f4 v[68:71], v[236:243], v[192:199], v[68:71], v225, v225 op_sel_hi:[0,0,0]
	v_mfma_scale_f32_16x16x128_f8f6f4 v[72:75], v[208:215], v[200:207], v[72:75], v225, v225 op_sel_hi:[0,0,0]
	v_mfma_scale_f32_16x16x128_f8f6f4 v[76:79], v[236:243], v[200:207], v[76:79], v225, v225 op_sel_hi:[0,0,0]
	s_mov_b32 m0, s73
	v_lshl_add_u64 v[144:145], v[174:175], 0, s[26:27]
	s_barrier
	ds_read_b128 v[176:179], v228 offset:16384
	ds_read_b128 v[180:183], v228 offset:17408
	ds_read_b128 v[184:187], v228 offset:18432
	ds_read_b128 v[188:191], v228 offset:19456
	ds_read_b128 v[192:195], v228 offset:20480
	ds_read_b128 v[196:199], v228 offset:21504
	ds_read_b128 v[200:203], v228 offset:22528
	ds_read_b128 v[204:207], v228 offset:23552
	global_load_lds_dwordx4 v[144:145], off
	v_lshl_add_u64 v[144:145], v[168:169], 0, s[26:27]
	s_mov_b32 m0, s74
	s_nop 0
	global_load_lds_dwordx4 v[144:145], off
	s_barrier
	s_waitcnt lgkmcnt(0)
	s_waitcnt lgkmcnt(0)
	v_mfma_scale_f32_16x16x128_f8f6f4 v[80:83], v[0:7], v[176:183], v[80:83], v225, v225 op_sel_hi:[0,0,0]
	v_mfma_scale_f32_16x16x128_f8f6f4 v[84:87], v[8:15], v[176:183], v[84:87], v225, v225 op_sel_hi:[0,0,0]
	v_mfma_scale_f32_16x16x128_f8f6f4 v[88:91], v[0:7], v[184:191], v[88:91], v225, v225 op_sel_hi:[0,0,0]
	v_mfma_scale_f32_16x16x128_f8f6f4 v[92:95], v[8:15], v[184:191], v[92:95], v225, v225 op_sel_hi:[0,0,0]
	v_mfma_scale_f32_16x16x128_f8f6f4 v[96:99], v[0:7], v[192:199], v[96:99], v225, v225 op_sel_hi:[0,0,0]
	v_mfma_scale_f32_16x16x128_f8f6f4 v[100:103], v[8:15], v[192:199], v[100:103], v225, v225 op_sel_hi:[0,0,0]
	v_mfma_scale_f32_16x16x128_f8f6f4 v[104:107], v[0:7], v[200:207], v[104:107], v225, v225 op_sel_hi:[0,0,0]
	v_mfma_scale_f32_16x16x128_f8f6f4 v[108:111], v[8:15], v[200:207], v[108:111], v225, v225 op_sel_hi:[0,0,0]
	s_barrier
	s_add_u32 s2, s50, 0x40600
	s_addc_u32 s3, s51, 0
	s_mov_b32 m0, s97
	v_lshl_add_u64 v[0:1], s[2:3], 0, v[150:151]
	global_load_lds_dwordx4 v[0:1], off
	v_lshl_add_u64 v[0:1], s[2:3], 0, v[154:155]
	s_mov_b32 m0, s52
	s_nop 0
	global_load_lds_dwordx4 v[0:1], off
	s_waitcnt vmcnt(6)
	s_barrier
	v_mfma_scale_f32_16x16x128_f8f6f4 v[112:115], v[208:215], v[176:183], v[112:115], v225, v225 op_sel_hi:[0,0,0]
	v_mfma_scale_f32_16x16x128_f8f6f4 v[116:119], v[236:243], v[176:183], v[116:119], v225, v225 op_sel_hi:[0,0,0]
	v_mfma_scale_f32_16x16x128_f8f6f4 v[120:123], v[208:215], v[184:191], v[120:123], v225, v225 op_sel_hi:[0,0,0]
	v_mfma_scale_f32_16x16x128_f8f6f4 v[124:127], v[236:243], v[184:191], v[124:127], v225, v225 op_sel_hi:[0,0,0]
	v_mfma_scale_f32_16x16x128_f8f6f4 v[128:131], v[208:215], v[192:199], v[128:131], v225, v225 op_sel_hi:[0,0,0]
	v_mfma_scale_f32_16x16x128_f8f6f4 v[132:135], v[236:243], v[192:199], v[132:135], v225, v225 op_sel_hi:[0,0,0]
	v_mfma_scale_f32_16x16x128_f8f6f4 v[136:139], v[208:215], v[200:207], v[136:139], v225, v225 op_sel_hi:[0,0,0]
	v_mfma_scale_f32_16x16x128_f8f6f4 v[140:143], v[236:243], v[200:207], v[140:143], v225, v225 op_sel_hi:[0,0,0]
	s_barrier
	ds_read_b128 v[0:3], v235
	ds_read_b128 v[4:7], v235 offset:1024
	ds_read_b128 v[8:11], v235 offset:2048
	ds_read_b128 v[12:15], v235 offset:3072
	s_add_u32 s2, s48, 0x40600
	s_addc_u32 s3, s49, 0
	s_mov_b32 m0, s75
	v_lshl_add_u64 v[144:145], s[2:3], 0, v[148:149]
	ds_read_b128 v[176:179], v228 offset:32768
	ds_read_b128 v[180:183], v228 offset:33792
	ds_read_b128 v[184:187], v228 offset:34816
	ds_read_b128 v[188:191], v228 offset:35840
	ds_read_b128 v[192:195], v228 offset:36864
	ds_read_b128 v[196:199], v228 offset:37888
	ds_read_b128 v[200:203], v228 offset:38912
	ds_read_b128 v[204:207], v228 offset:39936
	global_load_lds_dwordx4 v[144:145], off
	v_lshl_add_u64 v[144:145], s[2:3], 0, v[152:153]
	s_mov_b32 m0, s76
	s_nop 0
	global_load_lds_dwordx4 v[144:145], off
	s_waitcnt lgkmcnt(8)
	s_barrier
	s_waitcnt lgkmcnt(0)
	s_waitcnt lgkmcnt(0)
	v_mfma_scale_f32_16x16x128_f8f6f4 v[16:19], v[0:7], v[176:183], v[16:19], v225, v225 op_sel_hi:[0,0,0]
	v_mfma_scale_f32_16x16x128_f8f6f4 v[20:23], v[8:15], v[176:183], v[20:23], v225, v225 op_sel_hi:[0,0,0]
	v_mfma_scale_f32_16x16x128_f8f6f4 v[24:27], v[0:7], v[184:191], v[24:27], v225, v225 op_sel_hi:[0,0,0]
	v_mfma_scale_f32_16x16x128_f8f6f4 v[28:31], v[8:15], v[184:191], v[28:31], v225, v225 op_sel_hi:[0,0,0]
	v_mfma_scale_f32_16x16x128_f8f6f4 v[32:35], v[0:7], v[192:199], v[32:35], v225, v225 op_sel_hi:[0,0,0]
	v_mfma_scale_f32_16x16x128_f8f6f4 v[36:39], v[8:15], v[192:199], v[36:39], v225, v225 op_sel_hi:[0,0,0]
	v_mfma_scale_f32_16x16x128_f8f6f4 v[40:43], v[0:7], v[200:207], v[40:43], v225, v225 op_sel_hi:[0,0,0]
	v_mfma_scale_f32_16x16x128_f8f6f4 v[44:47], v[8:15], v[200:207], v[44:47], v225, v225 op_sel_hi:[0,0,0]
	s_barrier
	s_mov_b32 m0, s62
	v_lshl_add_u64 v[144:145], v[170:171], 0, s[28:29]
	ds_read_b128 v[208:211], v234
	ds_read_b128 v[212:215], v234 offset:1024
	ds_read_b128 v[236:239], v234 offset:2048
	ds_read_b128 v[240:243], v234 offset:3072
	global_load_lds_dwordx4 v[144:145], off
	v_lshl_add_u64 v[144:145], v[172:173], 0, s[28:29]
	s_mov_b32 m0, s63
	s_nop 0
	global_load_lds_dwordx4 v[144:145], off
	s_barrier
	s_waitcnt lgkmcnt(0)
	s_waitcnt lgkmcnt(0)
	v_mfma_scale_f32_16x16x128_f8f6f4 v[48:51], v[208:215], v[176:183], v[48:51], v225, v225 op_sel_hi:[0,0,0]
	v_mfma_scale_f32_16x16x128_f8f6f4 v[52:55], v[236:243], v[176:183], v[52:55], v225, v225 op_sel_hi:[0,0,0]
	v_mfma_scale_f32_16x16x128_f8f6f4 v[56:59], v[208:215], v[184:191], v[56:59], v225, v225 op_sel_hi:[0,0,0]
	v_mfma_scale_f32_16x16x128_f8f6f4 v[60:63], v[236:243], v[184:191], v[60:63], v225, v225 op_sel_hi:[0,0,0]
	v_mfma_scale_f32_16x16x128_f8f6f4 v[64:67], v[208:215], v[192:199], v[64:67], v225, v225 op_sel_hi:[0,0,0]
	v_mfma_scale_f32_16x16x128_f8f6f4 v[68:71], v[236:243], v[192:199], v[68:71], v225, v225 op_sel_hi:[0,0,0]
	v_mfma_scale_f32_16x16x128_f8f6f4 v[72:75], v[208:215], v[200:207], v[72:75], v225, v225 op_sel_hi:[0,0,0]
	v_mfma_scale_f32_16x16x128_f8f6f4 v[76:79], v[236:243], v[200:207], v[76:79], v225, v225 op_sel_hi:[0,0,0]
	s_mov_b32 m0, s80
	v_lshl_add_u64 v[144:145], v[174:175], 0, s[28:29]
	s_barrier
	ds_read_b128 v[176:179], v228 offset:49152
	ds_read_b128 v[180:183], v228 offset:50176
	ds_read_b128 v[184:187], v228 offset:51200
	ds_read_b128 v[188:191], v228 offset:52224
	ds_read_b128 v[192:195], v228 offset:53248
	ds_read_b128 v[196:199], v228 offset:54272
	ds_read_b128 v[200:203], v228 offset:55296
	ds_read_b128 v[204:207], v228 offset:56320
	global_load_lds_dwordx4 v[144:145], off
	v_lshl_add_u64 v[144:145], v[168:169], 0, s[28:29]
	s_mov_b32 m0, s81
	s_nop 0
	global_load_lds_dwordx4 v[144:145], off
	s_barrier
	s_waitcnt lgkmcnt(0)
	s_waitcnt lgkmcnt(0)
	v_mfma_scale_f32_16x16x128_f8f6f4 v[80:83], v[0:7], v[176:183], v[80:83], v225, v225 op_sel_hi:[0,0,0]
	v_mfma_scale_f32_16x16x128_f8f6f4 v[84:87], v[8:15], v[176:183], v[84:87], v225, v225 op_sel_hi:[0,0,0]
	v_mfma_scale_f32_16x16x128_f8f6f4 v[88:91], v[0:7], v[184:191], v[88:91], v225, v225 op_sel_hi:[0,0,0]
	v_mfma_scale_f32_16x16x128_f8f6f4 v[92:95], v[8:15], v[184:191], v[92:95], v225, v225 op_sel_hi:[0,0,0]
	v_mfma_scale_f32_16x16x128_f8f6f4 v[96:99], v[0:7], v[192:199], v[96:99], v225, v225 op_sel_hi:[0,0,0]
	v_mfma_scale_f32_16x16x128_f8f6f4 v[100:103], v[8:15], v[192:199], v[100:103], v225, v225 op_sel_hi:[0,0,0]
	v_mfma_scale_f32_16x16x128_f8f6f4 v[104:107], v[0:7], v[200:207], v[104:107], v225, v225 op_sel_hi:[0,0,0]
	v_mfma_scale_f32_16x16x128_f8f6f4 v[108:111], v[8:15], v[200:207], v[108:111], v225, v225 op_sel_hi:[0,0,0]
	s_barrier
	s_add_u32 s2, s50, 0x40680
	s_addc_u32 s3, s51, 0
	s_mov_b32 m0, s53
	v_lshl_add_u64 v[0:1], s[2:3], 0, v[150:151]
	global_load_lds_dwordx4 v[0:1], off
	v_lshl_add_u64 v[0:1], s[2:3], 0, v[154:155]
	s_mov_b32 m0, s64
	s_nop 0
	global_load_lds_dwordx4 v[0:1], off
	s_waitcnt vmcnt(6)
	s_barrier
	v_mfma_scale_f32_16x16x128_f8f6f4 v[112:115], v[208:215], v[176:183], v[112:115], v225, v225 op_sel_hi:[0,0,0]
	v_mfma_scale_f32_16x16x128_f8f6f4 v[116:119], v[236:243], v[176:183], v[116:119], v225, v225 op_sel_hi:[0,0,0]
	v_mfma_scale_f32_16x16x128_f8f6f4 v[120:123], v[208:215], v[184:191], v[120:123], v225, v225 op_sel_hi:[0,0,0]
	v_mfma_scale_f32_16x16x128_f8f6f4 v[124:127], v[236:243], v[184:191], v[124:127], v225, v225 op_sel_hi:[0,0,0]
	v_mfma_scale_f32_16x16x128_f8f6f4 v[128:131], v[208:215], v[192:199], v[128:131], v225, v225 op_sel_hi:[0,0,0]
	v_mfma_scale_f32_16x16x128_f8f6f4 v[132:135], v[236:243], v[192:199], v[132:135], v225, v225 op_sel_hi:[0,0,0]
	v_mfma_scale_f32_16x16x128_f8f6f4 v[136:139], v[208:215], v[200:207], v[136:139], v225, v225 op_sel_hi:[0,0,0]
	v_mfma_scale_f32_16x16x128_f8f6f4 v[140:143], v[236:243], v[200:207], v[140:143], v225, v225 op_sel_hi:[0,0,0]
	s_and_b64 s[2:3], vcc, exec
	s_cselect_b32 s61, s47, s51
	s_cselect_b32 s60, s46, s50
	s_add_i32 s2, s58, 16
	s_ashr_i32 s3, s2, 31
	v_mov_b32_e32 v156, v230
	s_lshl_b64 s[2:3], s[2:3], 16
	s_barrier
	s_nop 7
	s_nop 7
	s_nop 7
	s_add_u32 s2, s78, s2
	s_addc_u32 s3, s79, s3
	global_load_dwordx2 v[216:217], v156, s[56:57]
	global_load_dwordx2 v[236:237], v156, s[2:3]
	global_load_dwordx2 v[212:213], v156, s[56:57] offset:512
	global_load_dwordx2 v[214:215], v156, s[2:3] offset:512
	global_load_dwordx2 v[208:209], v156, s[56:57] offset:1024
	global_load_dwordx2 v[210:211], v156, s[2:3] offset:1024
	global_load_dwordx2 v[204:205], v156, s[56:57] offset:1536
	global_load_dwordx2 v[206:207], v156, s[2:3] offset:1536
	global_load_dwordx2 v[200:201], v156, s[56:57] offset:2048
	global_load_dwordx2 v[202:203], v156, s[2:3] offset:2048
	global_load_dwordx2 v[196:197], v156, s[56:57] offset:2560
	global_load_dwordx2 v[198:199], v156, s[2:3] offset:2560
	global_load_dwordx2 v[192:193], v156, s[56:57] offset:3072
	global_load_dwordx2 v[194:195], v156, s[2:3] offset:3072
	global_load_dwordx2 v[188:189], v156, s[56:57] offset:3584
	global_load_dwordx2 v[190:191], v156, s[2:3] offset:3584
	v_lshl_add_u64 v[0:1], s[56:57], 0, v[156:157]
	v_lshl_add_u64 v[2:3], s[2:3], 0, v[156:157]
	v_add_co_u32_e32 v0, vcc, s85, v0
	s_waitcnt vmcnt(0)
	v_cvt_f32_ubyte3_e32 v243, v216
	v_cvt_f32_ubyte0_e32 v156, v236
	v_add_f32_e32 v156, 0.5, v156
	v_rcp_f32_e32 v238, v156
	v_cvt_f32_ubyte0_e32 v156, v237
	v_add_f32_e32 v156, 0.5, v156
	v_rcp_f32_e32 v218, v156
	v_cvt_f32_ubyte1_e32 v156, v236
	v_add_f32_e32 v156, 0.5, v156
	v_rcp_f32_e32 v239, v156
	v_cvt_f32_ubyte1_e32 v156, v237
	v_add_f32_e32 v156, 0.5, v156
	v_rcp_f32_e32 v219, v156
	v_cvt_f32_ubyte2_e32 v156, v236
	v_add_f32_e32 v156, 0.5, v156
	v_rcp_f32_e32 v240, v156
	v_cvt_f32_ubyte2_e32 v156, v237
	v_add_f32_e32 v156, 0.5, v156
	v_rcp_f32_e32 v220, v156
	v_cvt_f32_ubyte3_e32 v156, v236
	v_add_f32_e32 v156, 0.5, v156
	v_rcp_f32_e32 v241, v156
	v_cvt_f32_ubyte3_e32 v156, v237
	v_add_f32_e32 v156, 0.5, v156
	v_cvt_f32_ubyte1_e32 v237, v216
	v_cvt_f32_ubyte0_e32 v236, v216
	v_cvt_f32_ubyte2_e32 v242, v216
	v_rcp_f32_e32 v221, v156
	v_pk_add_f32 v[242:243], v[242:243], 0.5 op_sel_hi:[1,0]
	v_pk_add_f32 v[236:237], v[236:237], 0.5 op_sel_hi:[1,0]
	v_cvt_f32_ubyte0_e32 v156, v214
	v_pk_mul_f32 v[236:237], v[236:237], v[238:239]
	v_pk_mul_f32 v[238:239], v[242:243], v[240:241]
	v_pk_mul_f32 v[16:17], v[16:17], v[236:237]
	v_pk_mul_f32 v[18:19], v[18:19], v[238:239]
	v_cvt_f32_ubyte3_e32 v239, v217
	v_cvt_f32_ubyte2_e32 v238, v217
	v_cvt_f32_ubyte1_e32 v237, v217
	v_cvt_f32_ubyte0_e32 v236, v217
	v_pk_add_f32 v[216:217], v[238:239], 0.5 op_sel_hi:[1,0]
	v_add_f32_e32 v156, 0.5, v156
	v_pk_mul_f32 v[216:217], v[216:217], v[220:221]
	v_pk_add_f32 v[236:237], v[236:237], 0.5 op_sel_hi:[1,0]
	v_pk_mul_f32 v[22:23], v[22:23], v[216:217]
	v_rcp_f32_e32 v216, v156
	v_cvt_f32_ubyte0_e32 v156, v215
	v_pk_mul_f32 v[218:219], v[236:237], v[218:219]
	v_add_f32_e32 v156, 0.5, v156
	v_pk_mul_f32 v[20:21], v[20:21], v[218:219]
	v_rcp_f32_e32 v218, v156
	v_cvt_f32_ubyte1_e32 v156, v214
	v_add_f32_e32 v156, 0.5, v156
	v_rcp_f32_e32 v217, v156
	v_cvt_f32_ubyte1_e32 v156, v215
	v_add_f32_e32 v156, 0.5, v156
	v_rcp_f32_e32 v219, v156
	v_cvt_f32_ubyte2_e32 v156, v214
	v_add_f32_e32 v156, 0.5, v156
	v_rcp_f32_e32 v220, v156
	v_cvt_f32_ubyte2_e32 v156, v215
	v_add_f32_e32 v156, 0.5, v156
	v_rcp_f32_e32 v236, v156
	v_cvt_f32_ubyte3_e32 v156, v214
	v_add_f32_e32 v156, 0.5, v156
	v_rcp_f32_e32 v221, v156
	v_cvt_f32_ubyte3_e32 v156, v215
	v_add_f32_e32 v156, 0.5, v156
	v_cvt_f32_ubyte1_e32 v215, v212
	v_cvt_f32_ubyte0_e32 v214, v212
	v_cvt_f32_ubyte3_e32 v239, v212
	v_cvt_f32_ubyte2_e32 v238, v212
	v_rcp_f32_e32 v237, v156
	v_pk_add_f32 v[238:239], v[238:239], 0.5 op_sel_hi:[1,0]
	v_pk_add_f32 v[214:215], v[214:215], 0.5 op_sel_hi:[1,0]
	v_cvt_f32_ubyte0_e32 v156, v210
	v_pk_mul_f32 v[214:215], v[214:215], v[216:217]
	v_pk_mul_f32 v[216:217], v[238:239], v[220:221]
	v_pk_mul_f32 v[48:49], v[48:49], v[214:215]
	v_pk_mul_f32 v[50:51], v[50:51], v[216:217]
	v_cvt_f32_ubyte3_e32 v217, v213
	v_cvt_f32_ubyte2_e32 v216, v213
	v_cvt_f32_ubyte1_e32 v215, v213
	v_cvt_f32_ubyte0_e32 v214, v213
	v_pk_add_f32 v[212:213], v[216:217], 0.5 op_sel_hi:[1,0]
	v_add_f32_e32 v156, 0.5, v156
	v_pk_mul_f32 v[212:213], v[212:213], v[236:237]
	v_pk_add_f32 v[214:215], v[214:215], 0.5 op_sel_hi:[1,0]
	v_pk_mul_f32 v[54:55], v[54:55], v[212:213]
	v_rcp_f32_e32 v212, v156
	v_cvt_f32_ubyte0_e32 v156, v211
	v_pk_mul_f32 v[214:215], v[214:215], v[218:219]
	v_add_f32_e32 v156, 0.5, v156
	v_pk_mul_f32 v[52:53], v[52:53], v[214:215]
	v_rcp_f32_e32 v214, v156
	v_cvt_f32_ubyte1_e32 v156, v210
	v_add_f32_e32 v156, 0.5, v156
	v_rcp_f32_e32 v213, v156
	v_cvt_f32_ubyte1_e32 v156, v211
	v_add_f32_e32 v156, 0.5, v156
	v_rcp_f32_e32 v215, v156
	v_cvt_f32_ubyte2_e32 v156, v210
	v_add_f32_e32 v156, 0.5, v156
	v_rcp_f32_e32 v216, v156
	v_cvt_f32_ubyte2_e32 v156, v211
	v_add_f32_e32 v156, 0.5, v156
	v_rcp_f32_e32 v218, v156
	v_cvt_f32_ubyte3_e32 v156, v210
	v_add_f32_e32 v156, 0.5, v156
	v_rcp_f32_e32 v217, v156
	v_cvt_f32_ubyte3_e32 v156, v211
	v_add_f32_e32 v156, 0.5, v156
	v_cvt_f32_ubyte1_e32 v211, v208
	v_cvt_f32_ubyte0_e32 v210, v208
	v_cvt_f32_ubyte3_e32 v221, v208
	v_cvt_f32_ubyte2_e32 v220, v208
	v_rcp_f32_e32 v219, v156
	v_pk_add_f32 v[220:221], v[220:221], 0.5 op_sel_hi:[1,0]
	v_pk_add_f32 v[210:211], v[210:211], 0.5 op_sel_hi:[1,0]
	v_cvt_f32_ubyte0_e32 v156, v206
	v_pk_mul_f32 v[210:211], v[210:211], v[212:213]
	v_pk_mul_f32 v[212:213], v[220:221], v[216:217]
	v_pk_mul_f32 v[24:25], v[24:25], v[210:211]
	v_pk_mul_f32 v[26:27], v[26:27], v[212:213]
	v_cvt_f32_ubyte3_e32 v213, v209
	v_cvt_f32_ubyte2_e32 v212, v209
	v_cvt_f32_ubyte1_e32 v211, v209
	v_cvt_f32_ubyte0_e32 v210, v209
	v_pk_add_f32 v[208:209], v[212:213], 0.5 op_sel_hi:[1,0]
	v_add_f32_e32 v156, 0.5, v156
	v_pk_mul_f32 v[208:209], v[208:209], v[218:219]
	v_pk_add_f32 v[210:211], v[210:211], 0.5 op_sel_hi:[1,0]
	v_pk_mul_f32 v[30:31], v[30:31], v[208:209]
	v_rcp_f32_e32 v208, v156
	v_cvt_f32_ubyte0_e32 v156, v207
	v_pk_mul_f32 v[210:211], v[210:211], v[214:215]
	v_add_f32_e32 v156, 0.5, v156
	v_pk_mul_f32 v[28:29], v[28:29], v[210:211]
	v_rcp_f32_e32 v210, v156
	v_cvt_f32_ubyte1_e32 v156, v206
	v_add_f32_e32 v156, 0.5, v156
	v_rcp_f32_e32 v209, v156
	v_cvt_f32_ubyte1_e32 v156, v207
	v_add_f32_e32 v156, 0.5, v156
	v_rcp_f32_e32 v211, v156
	v_cvt_f32_ubyte2_e32 v156, v206
	v_add_f32_e32 v156, 0.5, v156
	v_rcp_f32_e32 v212, v156
	v_cvt_f32_ubyte2_e32 v156, v207
	v_add_f32_e32 v156, 0.5, v156
	v_rcp_f32_e32 v214, v156
	v_cvt_f32_ubyte3_e32 v156, v206
	v_add_f32_e32 v156, 0.5, v156
	v_rcp_f32_e32 v213, v156
	v_cvt_f32_ubyte3_e32 v156, v207
	v_add_f32_e32 v156, 0.5, v156
	v_cvt_f32_ubyte1_e32 v207, v204
	v_cvt_f32_ubyte0_e32 v206, v204
	v_cvt_f32_ubyte3_e32 v217, v204
	v_cvt_f32_ubyte2_e32 v216, v204
	v_rcp_f32_e32 v215, v156
	v_pk_add_f32 v[216:217], v[216:217], 0.5 op_sel_hi:[1,0]
	v_pk_add_f32 v[206:207], v[206:207], 0.5 op_sel_hi:[1,0]
	v_cvt_f32_ubyte0_e32 v156, v202
	v_pk_mul_f32 v[206:207], v[206:207], v[208:209]
	v_pk_mul_f32 v[208:209], v[216:217], v[212:213]
	v_pk_mul_f32 v[56:57], v[56:57], v[206:207]
	v_pk_mul_f32 v[58:59], v[58:59], v[208:209]
	v_cvt_f32_ubyte3_e32 v209, v205
	v_cvt_f32_ubyte2_e32 v208, v205
	v_cvt_f32_ubyte1_e32 v207, v205
	v_cvt_f32_ubyte0_e32 v206, v205
	v_pk_add_f32 v[204:205], v[208:209], 0.5 op_sel_hi:[1,0]
	v_add_f32_e32 v156, 0.5, v156
	v_pk_mul_f32 v[204:205], v[204:205], v[214:215]
	v_pk_add_f32 v[206:207], v[206:207], 0.5 op_sel_hi:[1,0]
	v_pk_mul_f32 v[62:63], v[62:63], v[204:205]
	v_rcp_f32_e32 v204, v156
	v_cvt_f32_ubyte0_e32 v156, v203
	v_pk_mul_f32 v[206:207], v[206:207], v[210:211]
	v_add_f32_e32 v156, 0.5, v156
	v_pk_mul_f32 v[60:61], v[60:61], v[206:207]
	v_rcp_f32_e32 v206, v156
	v_cvt_f32_ubyte1_e32 v156, v202
	v_add_f32_e32 v156, 0.5, v156
	v_rcp_f32_e32 v205, v156
	v_cvt_f32_ubyte1_e32 v156, v203
	v_add_f32_e32 v156, 0.5, v156
	v_rcp_f32_e32 v207, v156
	v_cvt_f32_ubyte2_e32 v156, v202
	v_add_f32_e32 v156, 0.5, v156
	v_rcp_f32_e32 v208, v156
	v_cvt_f32_ubyte2_e32 v156, v203
	v_addc_co_u32_e32 v1, vcc, 0, v1, vcc
	v_add_f32_e32 v156, 0.5, v156
	v_add_co_u32_e32 v6, vcc, s85, v2
	v_rcp_f32_e32 v210, v156
	v_cvt_f32_ubyte3_e32 v156, v202
	v_addc_co_u32_e32 v7, vcc, 0, v3, vcc
	v_add_f32_e32 v156, 0.5, v156
	global_load_dwordx2 v[184:185], v[0:1], off
	global_load_dwordx2 v[186:187], v[6:7], off
	global_load_dwordx2 v[180:181], v[0:1], off offset:512
	global_load_dwordx2 v[182:183], v[6:7], off offset:512
	global_load_dwordx2 v[176:177], v[0:1], off offset:1024
	global_load_dwordx2 v[178:179], v[6:7], off offset:1024
	global_load_dwordx2 v[144:145], v[0:1], off offset:1536
	global_load_dwordx2 v[146:147], v[6:7], off offset:1536
	global_load_dwordx2 v[12:13], v[0:1], off offset:2048
	global_load_dwordx2 v[14:15], v[6:7], off offset:2048
	global_load_dwordx2 v[8:9], v[0:1], off offset:2560
	global_load_dwordx2 v[10:11], v[6:7], off offset:2560
	global_load_dwordx2 v[2:3], v[0:1], off offset:3072
	global_load_dwordx2 v[4:5], v[6:7], off offset:3072
	s_nop 0
	global_load_dwordx2 v[0:1], v[0:1], off offset:3584
	s_nop 0
	global_load_dwordx2 v[6:7], v[6:7], off offset:3584
	v_rcp_f32_e32 v209, v156
	v_cvt_f32_ubyte3_e32 v156, v203
	v_add_f32_e32 v156, 0.5, v156
	v_cvt_f32_ubyte1_e32 v203, v200
	v_cvt_f32_ubyte0_e32 v202, v200
	v_cvt_f32_ubyte3_e32 v213, v200
	v_cvt_f32_ubyte2_e32 v212, v200
	v_rcp_f32_e32 v211, v156
	v_pk_add_f32 v[212:213], v[212:213], 0.5 op_sel_hi:[1,0]
	v_pk_add_f32 v[202:203], v[202:203], 0.5 op_sel_hi:[1,0]
	v_cvt_f32_ubyte0_e32 v156, v198
	v_pk_mul_f32 v[202:203], v[202:203], v[204:205]
	v_pk_mul_f32 v[204:205], v[212:213], v[208:209]
	v_pk_mul_f32 v[32:33], v[32:33], v[202:203]
	v_pk_mul_f32 v[34:35], v[34:35], v[204:205]
	v_cvt_f32_ubyte3_e32 v205, v201
	v_cvt_f32_ubyte2_e32 v204, v201
	v_cvt_f32_ubyte1_e32 v203, v201
	v_cvt_f32_ubyte0_e32 v202, v201
	v_pk_add_f32 v[200:201], v[204:205], 0.5 op_sel_hi:[1,0]
	v_add_f32_e32 v156, 0.5, v156
	v_pk_mul_f32 v[200:201], v[200:201], v[210:211]
	v_pk_add_f32 v[202:203], v[202:203], 0.5 op_sel_hi:[1,0]
	v_pk_mul_f32 v[38:39], v[38:39], v[200:201]
	v_rcp_f32_e32 v200, v156
	v_cvt_f32_ubyte0_e32 v156, v199
	v_pk_mul_f32 v[202:203], v[202:203], v[206:207]
	v_add_f32_e32 v156, 0.5, v156
	v_pk_mul_f32 v[36:37], v[36:37], v[202:203]
	v_rcp_f32_e32 v202, v156
	v_cvt_f32_ubyte1_e32 v156, v198
	v_add_f32_e32 v156, 0.5, v156
	v_rcp_f32_e32 v201, v156
	v_cvt_f32_ubyte1_e32 v156, v199
	v_add_f32_e32 v156, 0.5, v156
	v_rcp_f32_e32 v203, v156
	v_cvt_f32_ubyte2_e32 v156, v198
	v_add_f32_e32 v156, 0.5, v156
	v_rcp_f32_e32 v204, v156
	v_cvt_f32_ubyte2_e32 v156, v199
	v_add_f32_e32 v156, 0.5, v156
	v_rcp_f32_e32 v206, v156
	v_cvt_f32_ubyte3_e32 v156, v198
	v_add_f32_e32 v156, 0.5, v156
	v_rcp_f32_e32 v205, v156
	v_cvt_f32_ubyte3_e32 v156, v199
	v_add_f32_e32 v156, 0.5, v156
	v_cvt_f32_ubyte1_e32 v199, v196
	v_cvt_f32_ubyte0_e32 v198, v196
	v_cvt_f32_ubyte3_e32 v209, v196
	v_cvt_f32_ubyte2_e32 v208, v196
	v_rcp_f32_e32 v207, v156
	v_pk_add_f32 v[208:209], v[208:209], 0.5 op_sel_hi:[1,0]
	v_pk_add_f32 v[198:199], v[198:199], 0.5 op_sel_hi:[1,0]
	v_cvt_f32_ubyte0_e32 v156, v194
	v_pk_mul_f32 v[198:199], v[198:199], v[200:201]
	v_pk_mul_f32 v[200:201], v[208:209], v[204:205]
	v_pk_mul_f32 v[64:65], v[64:65], v[198:199]
	v_pk_mul_f32 v[66:67], v[66:67], v[200:201]
	v_cvt_f32_ubyte3_e32 v201, v197
	v_cvt_f32_ubyte2_e32 v200, v197
	v_cvt_f32_ubyte1_e32 v199, v197
	v_cvt_f32_ubyte0_e32 v198, v197
	v_pk_add_f32 v[196:197], v[200:201], 0.5 op_sel_hi:[1,0]
	v_add_f32_e32 v156, 0.5, v156
	v_pk_mul_f32 v[196:197], v[196:197], v[206:207]
	v_pk_add_f32 v[198:199], v[198:199], 0.5 op_sel_hi:[1,0]
	v_pk_mul_f32 v[70:71], v[70:71], v[196:197]
	v_rcp_f32_e32 v196, v156
	v_cvt_f32_ubyte0_e32 v156, v195
	v_pk_mul_f32 v[198:199], v[198:199], v[202:203]
	v_add_f32_e32 v156, 0.5, v156
	v_pk_mul_f32 v[68:69], v[68:69], v[198:199]
	v_rcp_f32_e32 v198, v156
	v_cvt_f32_ubyte1_e32 v156, v194
	v_add_f32_e32 v156, 0.5, v156
	v_rcp_f32_e32 v197, v156
	v_cvt_f32_ubyte1_e32 v156, v195
	v_add_f32_e32 v156, 0.5, v156
	v_rcp_f32_e32 v199, v156
	v_cvt_f32_ubyte2_e32 v156, v194
	v_add_f32_e32 v156, 0.5, v156
	v_rcp_f32_e32 v200, v156
	v_cvt_f32_ubyte2_e32 v156, v195
	v_add_f32_e32 v156, 0.5, v156
	v_rcp_f32_e32 v202, v156
	v_cvt_f32_ubyte3_e32 v156, v194
	v_add_f32_e32 v156, 0.5, v156
	v_rcp_f32_e32 v201, v156
	v_cvt_f32_ubyte3_e32 v156, v195
	v_add_f32_e32 v156, 0.5, v156
	v_cvt_f32_ubyte1_e32 v195, v192
	v_cvt_f32_ubyte0_e32 v194, v192
	v_cvt_f32_ubyte3_e32 v205, v192
	v_cvt_f32_ubyte2_e32 v204, v192
	v_rcp_f32_e32 v203, v156
	v_pk_add_f32 v[204:205], v[204:205], 0.5 op_sel_hi:[1,0]
	v_pk_add_f32 v[194:195], v[194:195], 0.5 op_sel_hi:[1,0]
	v_cvt_f32_ubyte0_e32 v156, v190
	v_pk_mul_f32 v[194:195], v[194:195], v[196:197]
	v_pk_mul_f32 v[196:197], v[204:205], v[200:201]
	v_pk_mul_f32 v[40:41], v[40:41], v[194:195]
	v_pk_mul_f32 v[42:43], v[42:43], v[196:197]
	v_cvt_f32_ubyte3_e32 v197, v193
	v_cvt_f32_ubyte2_e32 v196, v193
	v_cvt_f32_ubyte1_e32 v195, v193
	v_cvt_f32_ubyte0_e32 v194, v193
	v_pk_add_f32 v[192:193], v[196:197], 0.5 op_sel_hi:[1,0]
	v_add_f32_e32 v156, 0.5, v156
	v_pk_mul_f32 v[192:193], v[192:193], v[202:203]
	v_pk_add_f32 v[194:195], v[194:195], 0.5 op_sel_hi:[1,0]
	v_pk_mul_f32 v[46:47], v[46:47], v[192:193]
	v_rcp_f32_e32 v192, v156
	v_cvt_f32_ubyte0_e32 v156, v191
	v_pk_mul_f32 v[194:195], v[194:195], v[198:199]
	v_add_f32_e32 v156, 0.5, v156
	v_pk_mul_f32 v[44:45], v[44:45], v[194:195]
	v_rcp_f32_e32 v194, v156
	v_cvt_f32_ubyte1_e32 v156, v190
	v_add_f32_e32 v156, 0.5, v156
	v_rcp_f32_e32 v193, v156
	v_cvt_f32_ubyte1_e32 v156, v191
	v_add_f32_e32 v156, 0.5, v156
	v_rcp_f32_e32 v195, v156
	v_cvt_f32_ubyte2_e32 v156, v190
	v_add_f32_e32 v156, 0.5, v156
	v_rcp_f32_e32 v196, v156
	v_cvt_f32_ubyte2_e32 v156, v191
	v_add_f32_e32 v156, 0.5, v156
	v_rcp_f32_e32 v198, v156
	v_cvt_f32_ubyte3_e32 v156, v190
	v_add_f32_e32 v156, 0.5, v156
	v_rcp_f32_e32 v197, v156
	v_cvt_f32_ubyte3_e32 v156, v191
	v_add_f32_e32 v156, 0.5, v156
	v_cvt_f32_ubyte1_e32 v191, v188
	v_cvt_f32_ubyte0_e32 v190, v188
	v_cvt_f32_ubyte3_e32 v201, v188
	v_cvt_f32_ubyte2_e32 v200, v188
	v_rcp_f32_e32 v199, v156
	v_pk_add_f32 v[200:201], v[200:201], 0.5 op_sel_hi:[1,0]
	v_pk_add_f32 v[190:191], v[190:191], 0.5 op_sel_hi:[1,0]
	s_waitcnt vmcnt(0)
	v_cvt_f32_ubyte0_e32 v156, v186
	v_pk_mul_f32 v[190:191], v[190:191], v[192:193]
	v_pk_mul_f32 v[192:193], v[200:201], v[196:197]
	v_pk_mul_f32 v[72:73], v[72:73], v[190:191]
	v_pk_mul_f32 v[74:75], v[74:75], v[192:193]
	v_cvt_f32_ubyte3_e32 v193, v189
	v_cvt_f32_ubyte2_e32 v192, v189
	v_cvt_f32_ubyte1_e32 v191, v189
	v_cvt_f32_ubyte0_e32 v190, v189
	v_pk_add_f32 v[188:189], v[192:193], 0.5 op_sel_hi:[1,0]
	v_add_f32_e32 v156, 0.5, v156
	v_pk_mul_f32 v[188:189], v[188:189], v[198:199]
	v_pk_add_f32 v[190:191], v[190:191], 0.5 op_sel_hi:[1,0]
	v_pk_mul_f32 v[78:79], v[78:79], v[188:189]
	v_rcp_f32_e32 v188, v156
	v_cvt_f32_ubyte0_e32 v156, v187
	v_pk_mul_f32 v[190:191], v[190:191], v[194:195]
	v_add_f32_e32 v156, 0.5, v156
	v_pk_mul_f32 v[76:77], v[76:77], v[190:191]
	v_rcp_f32_e32 v190, v156
	v_cvt_f32_ubyte1_e32 v156, v186
	v_add_f32_e32 v156, 0.5, v156
	v_rcp_f32_e32 v189, v156
	v_cvt_f32_ubyte1_e32 v156, v187
	v_add_f32_e32 v156, 0.5, v156
	v_rcp_f32_e32 v191, v156
	v_cvt_f32_ubyte2_e32 v156, v186
	v_add_f32_e32 v156, 0.5, v156
	v_rcp_f32_e32 v192, v156
	v_cvt_f32_ubyte2_e32 v156, v187
	v_add_f32_e32 v156, 0.5, v156
	v_rcp_f32_e32 v194, v156
	v_cvt_f32_ubyte3_e32 v156, v186
	v_add_f32_e32 v156, 0.5, v156
	v_rcp_f32_e32 v193, v156
	v_cvt_f32_ubyte3_e32 v156, v187
	v_add_f32_e32 v156, 0.5, v156
	v_cvt_f32_ubyte1_e32 v187, v184
	v_cvt_f32_ubyte0_e32 v186, v184
	v_cvt_f32_ubyte3_e32 v197, v184
	v_cvt_f32_ubyte2_e32 v196, v184
	v_rcp_f32_e32 v195, v156
	v_pk_add_f32 v[196:197], v[196:197], 0.5 op_sel_hi:[1,0]
	v_pk_add_f32 v[186:187], v[186:187], 0.5 op_sel_hi:[1,0]
	v_cvt_f32_ubyte0_e32 v156, v182
	v_pk_mul_f32 v[186:187], v[186:187], v[188:189]
	v_pk_mul_f32 v[188:189], v[196:197], v[192:193]
	v_pk_mul_f32 v[80:81], v[80:81], v[186:187]
	v_pk_mul_f32 v[82:83], v[82:83], v[188:189]
	v_cvt_f32_ubyte3_e32 v189, v185
	v_cvt_f32_ubyte2_e32 v188, v185
	v_cvt_f32_ubyte1_e32 v187, v185
	v_cvt_f32_ubyte0_e32 v186, v185
	v_pk_add_f32 v[184:185], v[188:189], 0.5 op_sel_hi:[1,0]
	v_add_f32_e32 v156, 0.5, v156
	v_pk_mul_f32 v[184:185], v[184:185], v[194:195]
	v_pk_add_f32 v[186:187], v[186:187], 0.5 op_sel_hi:[1,0]
	v_pk_mul_f32 v[86:87], v[86:87], v[184:185]
	v_rcp_f32_e32 v184, v156
	v_cvt_f32_ubyte0_e32 v156, v183
	v_pk_mul_f32 v[186:187], v[186:187], v[190:191]
	v_add_f32_e32 v156, 0.5, v156
	v_pk_mul_f32 v[84:85], v[84:85], v[186:187]
	v_rcp_f32_e32 v186, v156
	v_cvt_f32_ubyte1_e32 v156, v182
	v_add_f32_e32 v156, 0.5, v156
	v_rcp_f32_e32 v185, v156
	v_cvt_f32_ubyte1_e32 v156, v183
	v_add_f32_e32 v156, 0.5, v156
	v_rcp_f32_e32 v187, v156
	v_cvt_f32_ubyte2_e32 v156, v182
	v_add_f32_e32 v156, 0.5, v156
	v_rcp_f32_e32 v188, v156
	v_cvt_f32_ubyte2_e32 v156, v183
	v_add_f32_e32 v156, 0.5, v156
	v_rcp_f32_e32 v190, v156
	v_cvt_f32_ubyte3_e32 v156, v182
	v_add_f32_e32 v156, 0.5, v156
	v_rcp_f32_e32 v189, v156
	v_cvt_f32_ubyte3_e32 v156, v183
	v_add_f32_e32 v156, 0.5, v156
	v_cvt_f32_ubyte1_e32 v183, v180
	v_cvt_f32_ubyte0_e32 v182, v180
	v_cvt_f32_ubyte3_e32 v193, v180
	v_cvt_f32_ubyte2_e32 v192, v180
	v_rcp_f32_e32 v191, v156
	v_pk_add_f32 v[192:193], v[192:193], 0.5 op_sel_hi:[1,0]
	v_pk_add_f32 v[182:183], v[182:183], 0.5 op_sel_hi:[1,0]
	v_cvt_f32_ubyte0_e32 v156, v178
	v_pk_mul_f32 v[182:183], v[182:183], v[184:185]
	v_pk_mul_f32 v[184:185], v[192:193], v[188:189]
	v_pk_mul_f32 v[112:113], v[112:113], v[182:183]
	v_pk_mul_f32 v[114:115], v[114:115], v[184:185]
	v_cvt_f32_ubyte3_e32 v185, v181
	v_cvt_f32_ubyte2_e32 v184, v181
	v_cvt_f32_ubyte1_e32 v183, v181
	v_cvt_f32_ubyte0_e32 v182, v181
	v_pk_add_f32 v[180:181], v[184:185], 0.5 op_sel_hi:[1,0]
	v_add_f32_e32 v156, 0.5, v156
	v_pk_mul_f32 v[180:181], v[180:181], v[190:191]
	v_pk_add_f32 v[182:183], v[182:183], 0.5 op_sel_hi:[1,0]
	v_pk_mul_f32 v[118:119], v[118:119], v[180:181]
	v_rcp_f32_e32 v180, v156
	v_cvt_f32_ubyte0_e32 v156, v179
	v_pk_mul_f32 v[182:183], v[182:183], v[186:187]
	v_add_f32_e32 v156, 0.5, v156
	v_pk_mul_f32 v[116:117], v[116:117], v[182:183]
	v_rcp_f32_e32 v182, v156
	v_cvt_f32_ubyte1_e32 v156, v178
	v_add_f32_e32 v156, 0.5, v156
	v_rcp_f32_e32 v181, v156
	v_cvt_f32_ubyte1_e32 v156, v179
	v_add_f32_e32 v156, 0.5, v156
	v_rcp_f32_e32 v183, v156
	v_cvt_f32_ubyte2_e32 v156, v178
	v_add_f32_e32 v156, 0.5, v156
	v_rcp_f32_e32 v184, v156
	v_cvt_f32_ubyte2_e32 v156, v179
	v_add_f32_e32 v156, 0.5, v156
	v_rcp_f32_e32 v186, v156
	v_cvt_f32_ubyte3_e32 v156, v178
	v_add_f32_e32 v156, 0.5, v156
	v_rcp_f32_e32 v185, v156
	v_cvt_f32_ubyte3_e32 v156, v179
	v_add_f32_e32 v156, 0.5, v156
	v_cvt_f32_ubyte1_e32 v179, v176
	v_cvt_f32_ubyte0_e32 v178, v176
	v_cvt_f32_ubyte3_e32 v189, v176
	v_cvt_f32_ubyte2_e32 v188, v176
	v_rcp_f32_e32 v187, v156
	v_pk_add_f32 v[188:189], v[188:189], 0.5 op_sel_hi:[1,0]
	v_pk_add_f32 v[178:179], v[178:179], 0.5 op_sel_hi:[1,0]
	v_cvt_f32_ubyte0_e32 v156, v146
	v_pk_mul_f32 v[178:179], v[178:179], v[180:181]
	v_pk_mul_f32 v[180:181], v[188:189], v[184:185]
	v_pk_mul_f32 v[88:89], v[88:89], v[178:179]
	v_pk_mul_f32 v[90:91], v[90:91], v[180:181]
	v_cvt_f32_ubyte3_e32 v181, v177
	v_cvt_f32_ubyte2_e32 v180, v177
	v_cvt_f32_ubyte1_e32 v179, v177
	v_cvt_f32_ubyte0_e32 v178, v177
	v_pk_add_f32 v[176:177], v[180:181], 0.5 op_sel_hi:[1,0]
	v_add_f32_e32 v156, 0.5, v156
	v_pk_mul_f32 v[176:177], v[176:177], v[186:187]
	v_pk_add_f32 v[178:179], v[178:179], 0.5 op_sel_hi:[1,0]
	v_pk_mul_f32 v[94:95], v[94:95], v[176:177]
	v_rcp_f32_e32 v176, v156
	v_cvt_f32_ubyte0_e32 v156, v147
	v_pk_mul_f32 v[178:179], v[178:179], v[182:183]
	v_add_f32_e32 v156, 0.5, v156
	v_pk_mul_f32 v[92:93], v[92:93], v[178:179]
	v_rcp_f32_e32 v178, v156
	v_cvt_f32_ubyte1_e32 v156, v146
	v_add_f32_e32 v156, 0.5, v156
	v_rcp_f32_e32 v177, v156
	v_cvt_f32_ubyte1_e32 v156, v147
	v_add_f32_e32 v156, 0.5, v156
	v_rcp_f32_e32 v179, v156
	v_cvt_f32_ubyte2_e32 v156, v146
	v_cvt_f32_ubyte3_e32 v146, v146
	v_add_f32_e32 v156, 0.5, v156
	v_add_f32_e32 v146, 0.5, v146
	v_rcp_f32_e32 v180, v156
	v_rcp_f32_e32 v181, v146
	v_cvt_f32_ubyte3_e32 v146, v147
	v_cvt_f32_ubyte2_e32 v156, v147
	v_add_f32_e32 v146, 0.5, v146
	v_add_f32_e32 v156, 0.5, v156
	v_rcp_f32_e32 v183, v146
	v_cvt_f32_ubyte1_e32 v147, v144
	v_cvt_f32_ubyte0_e32 v146, v144
	v_cvt_f32_ubyte3_e32 v185, v144
	v_cvt_f32_ubyte2_e32 v184, v144
	v_rcp_f32_e32 v182, v156
	v_pk_add_f32 v[184:185], v[184:185], 0.5 op_sel_hi:[1,0]
	v_pk_add_f32 v[146:147], v[146:147], 0.5 op_sel_hi:[1,0]
	v_cvt_f32_ubyte2_e32 v156, v14
	v_pk_mul_f32 v[146:147], v[146:147], v[176:177]
	v_pk_mul_f32 v[176:177], v[184:185], v[180:181]
	v_pk_mul_f32 v[120:121], v[120:121], v[146:147]
	v_pk_mul_f32 v[122:123], v[122:123], v[176:177]
	v_cvt_f32_ubyte3_e32 v177, v145
	v_cvt_f32_ubyte2_e32 v176, v145
	v_cvt_f32_ubyte1_e32 v147, v145
	v_cvt_f32_ubyte0_e32 v146, v145
	v_pk_add_f32 v[144:145], v[176:177], 0.5 op_sel_hi:[1,0]
	v_pk_add_f32 v[146:147], v[146:147], 0.5 op_sel_hi:[1,0]
	v_pk_mul_f32 v[144:145], v[144:145], v[182:183]
	v_pk_mul_f32 v[146:147], v[146:147], v[178:179]
	v_pk_mul_f32 v[126:127], v[126:127], v[144:145]
	v_cvt_f32_ubyte0_e32 v145, v15
	v_add_f32_e32 v145, 0.5, v145
	v_pk_mul_f32 v[124:125], v[124:125], v[146:147]
	v_cvt_f32_ubyte0_e32 v144, v14
	v_rcp_f32_e32 v146, v145
	v_cvt_f32_ubyte1_e32 v145, v14
	v_cvt_f32_ubyte3_e32 v14, v14
	v_add_f32_e32 v144, 0.5, v144
	v_add_f32_e32 v145, 0.5, v145
	v_add_f32_e32 v156, 0.5, v156
	v_add_f32_e32 v14, 0.5, v14
	v_rcp_f32_e32 v144, v144
	v_rcp_f32_e32 v145, v145
	v_rcp_f32_e32 v176, v156
	v_rcp_f32_e32 v177, v14
	v_cvt_f32_ubyte3_e32 v14, v15
	v_cvt_f32_ubyte2_e32 v156, v15
	v_add_f32_e32 v14, 0.5, v14
	v_cvt_f32_ubyte1_e32 v147, v15
	v_add_f32_e32 v156, 0.5, v156
	v_rcp_f32_e32 v179, v14
	v_cvt_f32_ubyte1_e32 v15, v12
	v_cvt_f32_ubyte0_e32 v14, v12
	v_cvt_f32_ubyte3_e32 v181, v12
	v_cvt_f32_ubyte2_e32 v180, v12
	v_rcp_f32_e32 v178, v156
	v_pk_add_f32 v[180:181], v[180:181], 0.5 op_sel_hi:[1,0]
	v_pk_add_f32 v[14:15], v[14:15], 0.5 op_sel_hi:[1,0]
	v_add_f32_e32 v147, 0.5, v147
	v_pk_mul_f32 v[14:15], v[14:15], v[144:145]
	v_pk_mul_f32 v[144:145], v[180:181], v[176:177]
	v_rcp_f32_e32 v147, v147
	v_pk_mul_f32 v[98:99], v[98:99], v[144:145]
	v_cvt_f32_ubyte3_e32 v145, v13
	v_cvt_f32_ubyte2_e32 v144, v13
	v_pk_mul_f32 v[96:97], v[96:97], v[14:15]
	v_cvt_f32_ubyte1_e32 v15, v13
	v_cvt_f32_ubyte0_e32 v14, v13
	v_pk_add_f32 v[12:13], v[144:145], 0.5 op_sel_hi:[1,0]
	v_pk_add_f32 v[14:15], v[14:15], 0.5 op_sel_hi:[1,0]
	v_pk_mul_f32 v[12:13], v[12:13], v[178:179]
	v_pk_mul_f32 v[14:15], v[14:15], v[146:147]
	v_pk_mul_f32 v[102:103], v[102:103], v[12:13]
	v_cvt_f32_ubyte0_e32 v13, v11
	v_add_f32_e32 v13, 0.5, v13
	v_pk_mul_f32 v[100:101], v[100:101], v[14:15]
	v_cvt_f32_ubyte0_e32 v12, v10
	v_rcp_f32_e32 v14, v13
	v_cvt_f32_ubyte1_e32 v13, v10
	v_cvt_f32_ubyte2_e32 v144, v10
	v_cvt_f32_ubyte2_e32 v145, v11
	v_cvt_f32_ubyte3_e32 v10, v10
	v_add_f32_e32 v12, 0.5, v12
	v_add_f32_e32 v13, 0.5, v13
	v_add_f32_e32 v144, 0.5, v144
	v_add_f32_e32 v145, 0.5, v145
	v_add_f32_e32 v10, 0.5, v10
	v_rcp_f32_e32 v12, v12
	v_rcp_f32_e32 v13, v13
	v_rcp_f32_e32 v144, v144
	v_rcp_f32_e32 v146, v145
	v_rcp_f32_e32 v145, v10
	v_cvt_f32_ubyte3_e32 v10, v11
	v_add_f32_e32 v10, 0.5, v10
	v_cvt_f32_ubyte1_e32 v15, v11
	v_rcp_f32_e32 v147, v10
	v_cvt_f32_ubyte1_e32 v11, v8
	v_cvt_f32_ubyte0_e32 v10, v8
	v_cvt_f32_ubyte3_e32 v177, v8
	v_cvt_f32_ubyte2_e32 v176, v8
	v_pk_add_f32 v[176:177], v[176:177], 0.5 op_sel_hi:[1,0]
	v_pk_add_f32 v[10:11], v[10:11], 0.5 op_sel_hi:[1,0]
	v_add_f32_e32 v15, 0.5, v15
	v_pk_mul_f32 v[10:11], v[10:11], v[12:13]
	v_pk_mul_f32 v[12:13], v[176:177], v[144:145]
	v_rcp_f32_e32 v15, v15
	v_pk_mul_f32 v[130:131], v[130:131], v[12:13]
	v_cvt_f32_ubyte3_e32 v13, v9
	v_cvt_f32_ubyte2_e32 v12, v9
	v_pk_mul_f32 v[128:129], v[128:129], v[10:11]
	v_cvt_f32_ubyte1_e32 v11, v9
	v_cvt_f32_ubyte0_e32 v10, v9
	v_pk_add_f32 v[8:9], v[12:13], 0.5 op_sel_hi:[1,0]
	v_pk_add_f32 v[10:11], v[10:11], 0.5 op_sel_hi:[1,0]
	v_pk_mul_f32 v[8:9], v[8:9], v[146:147]
	v_pk_mul_f32 v[10:11], v[10:11], v[14:15]
	v_pk_mul_f32 v[134:135], v[134:135], v[8:9]
	v_cvt_f32_ubyte0_e32 v9, v5
	v_add_f32_e32 v9, 0.5, v9
	v_pk_mul_f32 v[132:133], v[132:133], v[10:11]
	v_cvt_f32_ubyte0_e32 v8, v4
	v_rcp_f32_e32 v10, v9
	v_cvt_f32_ubyte1_e32 v9, v4
	v_cvt_f32_ubyte2_e32 v12, v4
	v_cvt_f32_ubyte2_e32 v13, v5
	v_cvt_f32_ubyte3_e32 v4, v4
	v_add_f32_e32 v8, 0.5, v8
	v_add_f32_e32 v9, 0.5, v9
	v_add_f32_e32 v12, 0.5, v12
	v_add_f32_e32 v13, 0.5, v13
	v_add_f32_e32 v4, 0.5, v4
	v_rcp_f32_e32 v8, v8
	v_rcp_f32_e32 v9, v9
	v_rcp_f32_e32 v12, v12
	v_rcp_f32_e32 v14, v13
	v_rcp_f32_e32 v13, v4
	v_cvt_f32_ubyte3_e32 v4, v5
	v_add_f32_e32 v4, 0.5, v4
	v_cvt_f32_ubyte1_e32 v11, v5
	v_rcp_f32_e32 v15, v4
	v_cvt_f32_ubyte1_e32 v5, v2
	v_cvt_f32_ubyte0_e32 v4, v2
	v_cvt_f32_ubyte3_e32 v145, v2
	v_cvt_f32_ubyte2_e32 v144, v2
	v_pk_add_f32 v[144:145], v[144:145], 0.5 op_sel_hi:[1,0]
	v_pk_add_f32 v[4:5], v[4:5], 0.5 op_sel_hi:[1,0]
	v_add_f32_e32 v11, 0.5, v11
	v_pk_mul_f32 v[4:5], v[4:5], v[8:9]
	v_pk_mul_f32 v[8:9], v[144:145], v[12:13]
	v_rcp_f32_e32 v11, v11
	v_pk_mul_f32 v[106:107], v[106:107], v[8:9]
	v_cvt_f32_ubyte3_e32 v9, v3
	v_cvt_f32_ubyte2_e32 v8, v3
	v_pk_mul_f32 v[104:105], v[104:105], v[4:5]
	v_cvt_f32_ubyte1_e32 v5, v3
	v_cvt_f32_ubyte0_e32 v4, v3
	v_pk_add_f32 v[2:3], v[8:9], 0.5 op_sel_hi:[1,0]
	v_pk_add_f32 v[4:5], v[4:5], 0.5 op_sel_hi:[1,0]
	v_pk_mul_f32 v[2:3], v[2:3], v[14:15]
	v_pk_mul_f32 v[4:5], v[4:5], v[10:11]
	v_pk_mul_f32 v[110:111], v[110:111], v[2:3]
	v_cvt_f32_ubyte0_e32 v3, v7
	v_add_f32_e32 v3, 0.5, v3
	v_pk_mul_f32 v[108:109], v[108:109], v[4:5]
	v_cvt_f32_ubyte0_e32 v2, v6
	v_rcp_f32_e32 v4, v3
	v_cvt_f32_ubyte1_e32 v3, v6
	v_cvt_f32_ubyte2_e32 v8, v6
	v_cvt_f32_ubyte2_e32 v9, v7
	v_cvt_f32_ubyte3_e32 v6, v6
	v_add_f32_e32 v2, 0.5, v2
	v_add_f32_e32 v3, 0.5, v3
	v_add_f32_e32 v8, 0.5, v8
	v_add_f32_e32 v9, 0.5, v9
	v_add_f32_e32 v6, 0.5, v6
	v_rcp_f32_e32 v2, v2
	v_rcp_f32_e32 v3, v3
	v_rcp_f32_e32 v8, v8
	v_rcp_f32_e32 v10, v9
	v_rcp_f32_e32 v9, v6
	v_cvt_f32_ubyte3_e32 v6, v7
	v_cvt_f32_ubyte1_e32 v5, v7
	v_add_f32_e32 v6, 0.5, v6
	v_add_f32_e32 v5, 0.5, v5
	v_rcp_f32_e32 v11, v6
	v_cvt_f32_ubyte1_e32 v7, v0
	v_cvt_f32_ubyte0_e32 v6, v0
	v_cvt_f32_ubyte3_e32 v13, v0
	v_cvt_f32_ubyte2_e32 v12, v0
	v_rcp_f32_e32 v5, v5
	v_pk_add_f32 v[12:13], v[12:13], 0.5 op_sel_hi:[1,0]
	v_pk_add_f32 v[6:7], v[6:7], 0.5 op_sel_hi:[1,0]
	s_nop 0
	v_pk_mul_f32 v[2:3], v[6:7], v[2:3]
	v_pk_mul_f32 v[6:7], v[12:13], v[8:9]
	v_pk_mul_f32 v[144:145], v[136:137], v[2:3]
	v_pk_mul_f32 v[146:147], v[138:139], v[6:7]
	v_cvt_f32_ubyte1_e32 v3, v1
	v_cvt_f32_ubyte0_e32 v2, v1
	v_cvt_f32_ubyte3_e32 v7, v1
	v_cvt_f32_ubyte2_e32 v6, v1
	v_pk_add_f32 v[0:1], v[6:7], 0.5 op_sel_hi:[1,0]
	v_pk_add_f32 v[2:3], v[2:3], 0.5 op_sel_hi:[1,0]
	v_pk_mul_f32 v[0:1], v[0:1], v[10:11]
	v_pk_mul_f32 v[2:3], v[2:3], v[4:5]
	v_pk_mul_f32 v[138:139], v[142:143], v[0:1]
	v_pk_mul_f32 v[136:137], v[140:141], v[2:3]
	ds_read_b128 v[8:11], v231
	ds_read_b128 v[12:15], v231 offset:1024
	ds_read_b128 v[0:3], v231 offset:2048
	ds_read_b128 v[4:7], v231 offset:3072
	s_add_u32 s56, s48, 0x40680
	s_addc_u32 s57, s49, 0
	s_mov_b32 m0, s94
	v_lshl_add_u64 v[140:141], s[56:57], 0, v[148:149]
	ds_read_b128 v[176:179], v228
	ds_read_b128 v[180:183], v228 offset:1024
	ds_read_b128 v[184:187], v228 offset:2048
	ds_read_b128 v[188:191], v228 offset:3072
	ds_read_b128 v[192:195], v228 offset:4096
	ds_read_b128 v[196:199], v228 offset:5120
	ds_read_b128 v[200:203], v228 offset:6144
	ds_read_b128 v[204:207], v228 offset:7168
	global_load_lds_dwordx4 v[140:141], off
	v_lshl_add_u64 v[140:141], s[56:57], 0, v[152:153]
	s_mov_b32 m0, s93
	s_nop 0
	global_load_lds_dwordx4 v[140:141], off
	s_waitcnt lgkmcnt(8)
	s_barrier
	s_waitcnt lgkmcnt(0)
	s_waitcnt lgkmcnt(0)
	v_mfma_scale_f32_16x16x128_f8f6f4 v[16:19], v[8:15], v[176:183], v[16:19], v225, v225 op_sel_hi:[0,0,0]
	v_mfma_scale_f32_16x16x128_f8f6f4 v[20:23], v[0:7], v[176:183], v[20:23], v225, v225 op_sel_hi:[0,0,0]
	v_mfma_scale_f32_16x16x128_f8f6f4 v[24:27], v[8:15], v[184:191], v[24:27], v225, v225 op_sel_hi:[0,0,0]
	v_mfma_scale_f32_16x16x128_f8f6f4 v[28:31], v[0:7], v[184:191], v[28:31], v225, v225 op_sel_hi:[0,0,0]
	v_mfma_scale_f32_16x16x128_f8f6f4 v[32:35], v[8:15], v[192:199], v[32:35], v225, v225 op_sel_hi:[0,0,0]
	v_mfma_scale_f32_16x16x128_f8f6f4 v[36:39], v[0:7], v[192:199], v[36:39], v225, v225 op_sel_hi:[0,0,0]
	v_mfma_scale_f32_16x16x128_f8f6f4 v[40:43], v[8:15], v[200:207], v[40:43], v225, v225 op_sel_hi:[0,0,0]
	v_mfma_scale_f32_16x16x128_f8f6f4 v[44:47], v[0:7], v[200:207], v[44:47], v225, v225 op_sel_hi:[0,0,0]
	s_barrier
	s_mov_b32 m0, s96
	v_lshl_add_u64 v[140:141], v[170:171], 0, s[30:31]
	ds_read_b128 v[208:211], v232
	ds_read_b128 v[212:215], v232 offset:1024
	ds_read_b128 v[236:239], v232 offset:2048
	ds_read_b128 v[240:243], v232 offset:3072
	global_load_lds_dwordx4 v[140:141], off
	v_lshl_add_u64 v[140:141], v[172:173], 0, s[30:31]
	s_mov_b32 m0, s95
	s_nop 0
	global_load_lds_dwordx4 v[140:141], off
	s_barrier
	s_waitcnt lgkmcnt(0)
	s_waitcnt lgkmcnt(0)
	v_mfma_scale_f32_16x16x128_f8f6f4 v[48:51], v[208:215], v[176:183], v[48:51], v225, v225 op_sel_hi:[0,0,0]
	v_mfma_scale_f32_16x16x128_f8f6f4 v[52:55], v[236:243], v[176:183], v[52:55], v225, v225 op_sel_hi:[0,0,0]
	v_mfma_scale_f32_16x16x128_f8f6f4 v[56:59], v[208:215], v[184:191], v[56:59], v225, v225 op_sel_hi:[0,0,0]
	v_mfma_scale_f32_16x16x128_f8f6f4 v[60:63], v[236:243], v[184:191], v[60:63], v225, v225 op_sel_hi:[0,0,0]
	v_mfma_scale_f32_16x16x128_f8f6f4 v[64:67], v[208:215], v[192:199], v[64:67], v225, v225 op_sel_hi:[0,0,0]
	v_mfma_scale_f32_16x16x128_f8f6f4 v[68:71], v[236:243], v[192:199], v[68:71], v225, v225 op_sel_hi:[0,0,0]
	v_mfma_scale_f32_16x16x128_f8f6f4 v[72:75], v[208:215], v[200:207], v[72:75], v225, v225 op_sel_hi:[0,0,0]
	v_mfma_scale_f32_16x16x128_f8f6f4 v[76:79], v[236:243], v[200:207], v[76:79], v225, v225 op_sel_hi:[0,0,0]
	s_mov_b32 m0, s73
	v_lshl_add_u64 v[140:141], v[174:175], 0, s[30:31]
	s_barrier
	ds_read_b128 v[176:179], v228 offset:16384
	ds_read_b128 v[180:183], v228 offset:17408
	ds_read_b128 v[184:187], v228 offset:18432
	ds_read_b128 v[188:191], v228 offset:19456
	ds_read_b128 v[192:195], v228 offset:20480
	ds_read_b128 v[196:199], v228 offset:21504
	ds_read_b128 v[200:203], v228 offset:22528
	ds_read_b128 v[204:207], v228 offset:23552
	global_load_lds_dwordx4 v[140:141], off
	v_lshl_add_u64 v[140:141], v[168:169], 0, s[30:31]
	s_mov_b32 m0, s74
	s_nop 0
	global_load_lds_dwordx4 v[140:141], off
	s_barrier
	s_waitcnt lgkmcnt(0)
	s_waitcnt lgkmcnt(0)
	v_mfma_scale_f32_16x16x128_f8f6f4 v[80:83], v[8:15], v[176:183], v[80:83], v225, v225 op_sel_hi:[0,0,0]
	v_mfma_scale_f32_16x16x128_f8f6f4 v[84:87], v[0:7], v[176:183], v[84:87], v225, v225 op_sel_hi:[0,0,0]
	v_mfma_scale_f32_16x16x128_f8f6f4 v[88:91], v[8:15], v[184:191], v[88:91], v225, v225 op_sel_hi:[0,0,0]
	v_mfma_scale_f32_16x16x128_f8f6f4 v[92:95], v[0:7], v[184:191], v[92:95], v225, v225 op_sel_hi:[0,0,0]
	v_mfma_scale_f32_16x16x128_f8f6f4 v[96:99], v[8:15], v[192:199], v[96:99], v225, v225 op_sel_hi:[0,0,0]
	v_mfma_scale_f32_16x16x128_f8f6f4 v[100:103], v[0:7], v[192:199], v[100:103], v225, v225 op_sel_hi:[0,0,0]
	v_mfma_scale_f32_16x16x128_f8f6f4 v[104:107], v[8:15], v[200:207], v[104:107], v225, v225 op_sel_hi:[0,0,0]
	v_mfma_scale_f32_16x16x128_f8f6f4 v[108:111], v[0:7], v[200:207], v[108:111], v225, v225 op_sel_hi:[0,0,0]
	s_barrier
	s_add_u32 s56, s50, 0x40700
	s_addc_u32 s57, s51, 0
	s_mov_b32 m0, s97
	v_lshl_add_u64 v[0:1], s[56:57], 0, v[150:151]
	global_load_lds_dwordx4 v[0:1], off
	v_lshl_add_u64 v[0:1], s[56:57], 0, v[154:155]
	s_mov_b32 m0, s52
	s_nop 0
	global_load_lds_dwordx4 v[0:1], off
	s_waitcnt vmcnt(6)
	s_barrier
	v_mfma_scale_f32_16x16x128_f8f6f4 v[112:115], v[208:215], v[176:183], v[112:115], v225, v225 op_sel_hi:[0,0,0]
	v_mfma_scale_f32_16x16x128_f8f6f4 v[116:119], v[236:243], v[176:183], v[116:119], v225, v225 op_sel_hi:[0,0,0]
	v_mfma_scale_f32_16x16x128_f8f6f4 v[120:123], v[208:215], v[184:191], v[120:123], v225, v225 op_sel_hi:[0,0,0]
	v_mfma_scale_f32_16x16x128_f8f6f4 v[124:127], v[236:243], v[184:191], v[124:127], v225, v225 op_sel_hi:[0,0,0]
	v_mfma_scale_f32_16x16x128_f8f6f4 v[128:131], v[208:215], v[192:199], v[128:131], v225, v225 op_sel_hi:[0,0,0]
	v_mfma_scale_f32_16x16x128_f8f6f4 v[132:135], v[236:243], v[192:199], v[132:135], v225, v225 op_sel_hi:[0,0,0]
	v_mfma_scale_f32_16x16x128_f8f6f4 v[144:147], v[208:215], v[200:207], v[144:147], v225, v225 op_sel_hi:[0,0,0]
	v_mfma_scale_f32_16x16x128_f8f6f4 v[136:139], v[236:243], v[200:207], v[136:139], v225, v225 op_sel_hi:[0,0,0]
	s_barrier
	ds_read_b128 v[0:3], v235
	ds_read_b128 v[4:7], v235 offset:1024
	ds_read_b128 v[8:11], v235 offset:2048
	ds_read_b128 v[12:15], v235 offset:3072
	s_add_u32 s56, s48, 0x40700
	s_addc_u32 s57, s49, 0
	s_mov_b32 m0, s75
	v_lshl_add_u64 v[140:141], s[56:57], 0, v[148:149]
	ds_read_b128 v[176:179], v228 offset:32768
	ds_read_b128 v[180:183], v228 offset:33792
	ds_read_b128 v[184:187], v228 offset:34816
	ds_read_b128 v[188:191], v228 offset:35840
	ds_read_b128 v[192:195], v228 offset:36864
	ds_read_b128 v[196:199], v228 offset:37888
	ds_read_b128 v[200:203], v228 offset:38912
	ds_read_b128 v[204:207], v228 offset:39936
	global_load_lds_dwordx4 v[140:141], off
	v_lshl_add_u64 v[140:141], s[56:57], 0, v[152:153]
	s_mov_b32 m0, s76
	s_nop 0
	global_load_lds_dwordx4 v[140:141], off
	s_waitcnt lgkmcnt(8)
	s_barrier
	s_waitcnt lgkmcnt(0)
	s_waitcnt lgkmcnt(0)
	v_mfma_scale_f32_16x16x128_f8f6f4 v[16:19], v[0:7], v[176:183], v[16:19], v225, v225 op_sel_hi:[0,0,0]
	v_mfma_scale_f32_16x16x128_f8f6f4 v[20:23], v[8:15], v[176:183], v[20:23], v225, v225 op_sel_hi:[0,0,0]
	v_mfma_scale_f32_16x16x128_f8f6f4 v[24:27], v[0:7], v[184:191], v[24:27], v225, v225 op_sel_hi:[0,0,0]
	v_mfma_scale_f32_16x16x128_f8f6f4 v[28:31], v[8:15], v[184:191], v[28:31], v225, v225 op_sel_hi:[0,0,0]
	v_mfma_scale_f32_16x16x128_f8f6f4 v[32:35], v[0:7], v[192:199], v[32:35], v225, v225 op_sel_hi:[0,0,0]
	v_mfma_scale_f32_16x16x128_f8f6f4 v[36:39], v[8:15], v[192:199], v[36:39], v225, v225 op_sel_hi:[0,0,0]
	v_mfma_scale_f32_16x16x128_f8f6f4 v[40:43], v[0:7], v[200:207], v[40:43], v225, v225 op_sel_hi:[0,0,0]
	v_mfma_scale_f32_16x16x128_f8f6f4 v[44:47], v[8:15], v[200:207], v[44:47], v225, v225 op_sel_hi:[0,0,0]
	s_barrier
	s_mov_b32 m0, s62
	v_lshl_add_u64 v[140:141], v[170:171], 0, s[38:39]
	ds_read_b128 v[208:211], v234
	ds_read_b128 v[212:215], v234 offset:1024
	ds_read_b128 v[236:239], v234 offset:2048
	ds_read_b128 v[240:243], v234 offset:3072
	global_load_lds_dwordx4 v[140:141], off
	v_lshl_add_u64 v[140:141], v[172:173], 0, s[38:39]
	s_mov_b32 m0, s63
	s_nop 0
	global_load_lds_dwordx4 v[140:141], off
	s_barrier
	s_waitcnt lgkmcnt(0)
	s_waitcnt lgkmcnt(0)
	v_mfma_scale_f32_16x16x128_f8f6f4 v[48:51], v[208:215], v[176:183], v[48:51], v225, v225 op_sel_hi:[0,0,0]
	v_mfma_scale_f32_16x16x128_f8f6f4 v[52:55], v[236:243], v[176:183], v[52:55], v225, v225 op_sel_hi:[0,0,0]
	v_mfma_scale_f32_16x16x128_f8f6f4 v[56:59], v[208:215], v[184:191], v[56:59], v225, v225 op_sel_hi:[0,0,0]
	v_mfma_scale_f32_16x16x128_f8f6f4 v[60:63], v[236:243], v[184:191], v[60:63], v225, v225 op_sel_hi:[0,0,0]
	v_mfma_scale_f32_16x16x128_f8f6f4 v[64:67], v[208:215], v[192:199], v[64:67], v225, v225 op_sel_hi:[0,0,0]
	v_mfma_scale_f32_16x16x128_f8f6f4 v[68:71], v[236:243], v[192:199], v[68:71], v225, v225 op_sel_hi:[0,0,0]
	v_mfma_scale_f32_16x16x128_f8f6f4 v[72:75], v[208:215], v[200:207], v[72:75], v225, v225 op_sel_hi:[0,0,0]
	v_mfma_scale_f32_16x16x128_f8f6f4 v[76:79], v[236:243], v[200:207], v[76:79], v225, v225 op_sel_hi:[0,0,0]
	s_mov_b32 m0, s80
	v_lshl_add_u64 v[140:141], v[174:175], 0, s[38:39]
	s_barrier
	ds_read_b128 v[176:179], v228 offset:49152
	ds_read_b128 v[180:183], v228 offset:50176
	ds_read_b128 v[184:187], v228 offset:51200
	ds_read_b128 v[188:191], v228 offset:52224
	ds_read_b128 v[192:195], v228 offset:53248
	ds_read_b128 v[196:199], v228 offset:54272
	ds_read_b128 v[200:203], v228 offset:55296
	ds_read_b128 v[204:207], v228 offset:56320
	global_load_lds_dwordx4 v[140:141], off
	v_lshl_add_u64 v[140:141], v[168:169], 0, s[38:39]
	s_mov_b32 m0, s81
	s_nop 0
	global_load_lds_dwordx4 v[140:141], off
	s_barrier
	s_waitcnt lgkmcnt(0)
	s_waitcnt lgkmcnt(0)
	v_mfma_scale_f32_16x16x128_f8f6f4 v[80:83], v[0:7], v[176:183], v[80:83], v225, v225 op_sel_hi:[0,0,0]
	v_mfma_scale_f32_16x16x128_f8f6f4 v[84:87], v[8:15], v[176:183], v[84:87], v225, v225 op_sel_hi:[0,0,0]
	v_mfma_scale_f32_16x16x128_f8f6f4 v[88:91], v[0:7], v[184:191], v[88:91], v225, v225 op_sel_hi:[0,0,0]
	v_mfma_scale_f32_16x16x128_f8f6f4 v[92:95], v[8:15], v[184:191], v[92:95], v225, v225 op_sel_hi:[0,0,0]
	v_mfma_scale_f32_16x16x128_f8f6f4 v[96:99], v[0:7], v[192:199], v[96:99], v225, v225 op_sel_hi:[0,0,0]
	v_mfma_scale_f32_16x16x128_f8f6f4 v[100:103], v[8:15], v[192:199], v[100:103], v225, v225 op_sel_hi:[0,0,0]
	v_mfma_scale_f32_16x16x128_f8f6f4 v[104:107], v[0:7], v[200:207], v[104:107], v225, v225 op_sel_hi:[0,0,0]
	v_mfma_scale_f32_16x16x128_f8f6f4 v[108:111], v[8:15], v[200:207], v[108:111], v225, v225 op_sel_hi:[0,0,0]
	s_barrier
	s_add_u32 s50, s50, 0x40780
	s_addc_u32 s51, s51, 0
	s_mov_b32 m0, s53
	v_lshl_add_u64 v[0:1], s[50:51], 0, v[150:151]
	global_load_lds_dwordx4 v[0:1], off
	v_lshl_add_u64 v[0:1], s[50:51], 0, v[154:155]
	s_mov_b32 m0, s64
	s_nop 0
	global_load_lds_dwordx4 v[0:1], off
	s_waitcnt vmcnt(6)
	s_barrier
	v_mfma_scale_f32_16x16x128_f8f6f4 v[112:115], v[208:215], v[176:183], v[112:115], v225, v225 op_sel_hi:[0,0,0]
	v_mfma_scale_f32_16x16x128_f8f6f4 v[116:119], v[236:243], v[176:183], v[116:119], v225, v225 op_sel_hi:[0,0,0]
	v_mfma_scale_f32_16x16x128_f8f6f4 v[120:123], v[208:215], v[184:191], v[120:123], v225, v225 op_sel_hi:[0,0,0]
	v_mfma_scale_f32_16x16x128_f8f6f4 v[124:127], v[236:243], v[184:191], v[124:127], v225, v225 op_sel_hi:[0,0,0]
	v_mfma_scale_f32_16x16x128_f8f6f4 v[128:131], v[208:215], v[192:199], v[128:131], v225, v225 op_sel_hi:[0,0,0]
	v_mfma_scale_f32_16x16x128_f8f6f4 v[132:135], v[236:243], v[192:199], v[132:135], v225, v225 op_sel_hi:[0,0,0]
	v_mfma_scale_f32_16x16x128_f8f6f4 v[144:147], v[208:215], v[200:207], v[144:147], v225, v225 op_sel_hi:[0,0,0]
	v_mfma_scale_f32_16x16x128_f8f6f4 v[136:139], v[236:243], v[200:207], v[136:139], v225, v225 op_sel_hi:[0,0,0]
	s_barrier
	ds_read_b128 v[8:11], v231
	ds_read_b128 v[12:15], v231 offset:1024
	ds_read_b128 v[168:171], v231 offset:2048
	ds_read_b128 v[172:175], v231 offset:3072
	s_add_u32 s48, s48, 0x40780
	s_addc_u32 s49, s49, 0
	s_mov_b32 m0, s94
	v_lshl_add_u64 v[0:1], s[48:49], 0, v[148:149]
	ds_read_b128 v[176:179], v228
	ds_read_b128 v[180:183], v228 offset:1024
	ds_read_b128 v[184:187], v228 offset:2048
	ds_read_b128 v[188:191], v228 offset:3072
	ds_read_b128 v[192:195], v228 offset:4096
	ds_read_b128 v[196:199], v228 offset:5120
	ds_read_b128 v[200:203], v228 offset:6144
	ds_read_b128 v[204:207], v228 offset:7168
	global_load_lds_dwordx4 v[0:1], off
	v_lshl_add_u64 v[0:1], s[48:49], 0, v[152:153]
	s_mov_b32 m0, s93
	s_nop 0
	global_load_lds_dwordx4 v[0:1], off
	s_waitcnt lgkmcnt(8)
	s_barrier
	s_waitcnt lgkmcnt(0)
	s_waitcnt lgkmcnt(0)
	v_mfma_scale_f32_16x16x128_f8f6f4 v[16:19], v[8:15], v[176:183], v[16:19], v225, v225 op_sel_hi:[0,0,0]
	v_mfma_scale_f32_16x16x128_f8f6f4 v[20:23], v[168:175], v[176:183], v[20:23], v225, v225 op_sel_hi:[0,0,0]
	v_mfma_scale_f32_16x16x128_f8f6f4 v[24:27], v[8:15], v[184:191], v[24:27], v225, v225 op_sel_hi:[0,0,0]
	v_mfma_scale_f32_16x16x128_f8f6f4 v[28:31], v[168:175], v[184:191], v[28:31], v225, v225 op_sel_hi:[0,0,0]
	v_mfma_scale_f32_16x16x128_f8f6f4 v[32:35], v[8:15], v[192:199], v[32:35], v225, v225 op_sel_hi:[0,0,0]
	v_mfma_scale_f32_16x16x128_f8f6f4 v[36:39], v[168:175], v[192:199], v[36:39], v225, v225 op_sel_hi:[0,0,0]
	v_mfma_scale_f32_16x16x128_f8f6f4 v[40:43], v[8:15], v[200:207], v[40:43], v225, v225 op_sel_hi:[0,0,0]
	v_mfma_scale_f32_16x16x128_f8f6f4 v[44:47], v[168:175], v[200:207], v[44:47], v225, v225 op_sel_hi:[0,0,0]
	s_barrier
	s_mov_b32 m0, s96
	v_lshl_add_u64 v[0:1], s[60:61], 0, v[150:151]
	ds_read_b128 v[208:211], v232
	ds_read_b128 v[212:215], v232 offset:1024
	ds_read_b128 v[236:239], v232 offset:2048
	ds_read_b128 v[240:243], v232 offset:3072
	global_load_lds_dwordx4 v[0:1], off
	v_lshl_add_u64 v[2:3], s[60:61], 0, v[154:155]
	s_mov_b32 m0, s95
	s_nop 0
	global_load_lds_dwordx4 v[2:3], off
	s_barrier
	s_waitcnt lgkmcnt(0)
	s_waitcnt lgkmcnt(0)
	v_mfma_scale_f32_16x16x128_f8f6f4 v[48:51], v[208:215], v[176:183], v[48:51], v225, v225 op_sel_hi:[0,0,0]
	v_mfma_scale_f32_16x16x128_f8f6f4 v[52:55], v[236:243], v[176:183], v[52:55], v225, v225 op_sel_hi:[0,0,0]
	v_mfma_scale_f32_16x16x128_f8f6f4 v[56:59], v[208:215], v[184:191], v[56:59], v225, v225 op_sel_hi:[0,0,0]
	v_mfma_scale_f32_16x16x128_f8f6f4 v[60:63], v[236:243], v[184:191], v[60:63], v225, v225 op_sel_hi:[0,0,0]
	v_mfma_scale_f32_16x16x128_f8f6f4 v[64:67], v[208:215], v[192:199], v[64:67], v225, v225 op_sel_hi:[0,0,0]
	v_mfma_scale_f32_16x16x128_f8f6f4 v[68:71], v[236:243], v[192:199], v[68:71], v225, v225 op_sel_hi:[0,0,0]
	v_mfma_scale_f32_16x16x128_f8f6f4 v[72:75], v[208:215], v[200:207], v[72:75], v225, v225 op_sel_hi:[0,0,0]
	v_mfma_scale_f32_16x16x128_f8f6f4 v[76:79], v[236:243], v[200:207], v[76:79], v225, v225 op_sel_hi:[0,0,0]
	s_mov_b32 m0, s73
	v_lshl_add_u64 v[4:5], s[54:55], 0, v[148:149]
	s_barrier
	ds_read_b128 v[176:179], v228 offset:16384
	ds_read_b128 v[180:183], v228 offset:17408
	ds_read_b128 v[184:187], v228 offset:18432
	ds_read_b128 v[188:191], v228 offset:19456
	ds_read_b128 v[192:195], v228 offset:20480
	ds_read_b128 v[196:199], v228 offset:21504
	ds_read_b128 v[200:203], v228 offset:22528
	ds_read_b128 v[204:207], v228 offset:23552
	global_load_lds_dwordx4 v[4:5], off
	v_lshl_add_u64 v[6:7], s[54:55], 0, v[152:153]
	s_mov_b32 m0, s74
	s_nop 0
	global_load_lds_dwordx4 v[6:7], off
	s_barrier
	s_waitcnt lgkmcnt(0)
	s_waitcnt lgkmcnt(0)
	v_mfma_scale_f32_16x16x128_f8f6f4 v[80:83], v[8:15], v[176:183], v[80:83], v225, v225 op_sel_hi:[0,0,0]
	v_mfma_scale_f32_16x16x128_f8f6f4 v[84:87], v[168:175], v[176:183], v[84:87], v225, v225 op_sel_hi:[0,0,0]
	v_mfma_scale_f32_16x16x128_f8f6f4 v[88:91], v[8:15], v[184:191], v[88:91], v225, v225 op_sel_hi:[0,0,0]
	v_mfma_scale_f32_16x16x128_f8f6f4 v[92:95], v[168:175], v[184:191], v[92:95], v225, v225 op_sel_hi:[0,0,0]
	v_mfma_scale_f32_16x16x128_f8f6f4 v[96:99], v[8:15], v[192:199], v[96:99], v225, v225 op_sel_hi:[0,0,0]
	v_mfma_scale_f32_16x16x128_f8f6f4 v[100:103], v[168:175], v[192:199], v[100:103], v225, v225 op_sel_hi:[0,0,0]
	v_mfma_scale_f32_16x16x128_f8f6f4 v[104:107], v[8:15], v[200:207], v[104:107], v225, v225 op_sel_hi:[0,0,0]
	v_mfma_scale_f32_16x16x128_f8f6f4 v[108:111], v[168:175], v[200:207], v[108:111], v225, v225 op_sel_hi:[0,0,0]
	s_barrier
	s_add_u32 s48, s60, 0x40000
	s_addc_u32 s49, s61, 0
	s_mov_b32 m0, s97
	v_lshl_add_u64 v[8:9], s[48:49], 0, v[150:151]
	global_load_lds_dwordx4 v[8:9], off
	v_lshl_add_u64 v[8:9], s[48:49], 0, v[154:155]
	s_mov_b32 m0, s52
	s_nop 0
	global_load_lds_dwordx4 v[8:9], off
	s_waitcnt vmcnt(6)
	s_barrier
	v_mfma_scale_f32_16x16x128_f8f6f4 v[112:115], v[208:215], v[176:183], v[112:115], v225, v225 op_sel_hi:[0,0,0]
	v_mfma_scale_f32_16x16x128_f8f6f4 v[116:119], v[236:243], v[176:183], v[116:119], v225, v225 op_sel_hi:[0,0,0]
	v_mfma_scale_f32_16x16x128_f8f6f4 v[120:123], v[208:215], v[184:191], v[120:123], v225, v225 op_sel_hi:[0,0,0]
	v_mfma_scale_f32_16x16x128_f8f6f4 v[124:127], v[236:243], v[184:191], v[124:127], v225, v225 op_sel_hi:[0,0,0]
	v_mfma_scale_f32_16x16x128_f8f6f4 v[128:131], v[208:215], v[192:199], v[128:131], v225, v225 op_sel_hi:[0,0,0]
	v_mfma_scale_f32_16x16x128_f8f6f4 v[132:135], v[236:243], v[192:199], v[132:135], v225, v225 op_sel_hi:[0,0,0]
	v_mfma_scale_f32_16x16x128_f8f6f4 v[144:147], v[208:215], v[200:207], v[144:147], v225, v225 op_sel_hi:[0,0,0]
	v_mfma_scale_f32_16x16x128_f8f6f4 v[136:139], v[236:243], v[200:207], v[136:139], v225, v225 op_sel_hi:[0,0,0]
	s_barrier
	ds_read_b128 v[8:11], v235
	ds_read_b128 v[12:15], v235 offset:1024
	ds_read_b128 v[168:171], v235 offset:2048
	ds_read_b128 v[172:175], v235 offset:3072
	s_add_u32 s48, s54, 0x40000
	s_addc_u32 s49, s55, 0
	s_mov_b32 m0, s75
	v_lshl_add_u64 v[140:141], s[48:49], 0, v[148:149]
	ds_read_b128 v[176:179], v228 offset:32768
	ds_read_b128 v[180:183], v228 offset:33792
	ds_read_b128 v[184:187], v228 offset:34816
	ds_read_b128 v[188:191], v228 offset:35840
	ds_read_b128 v[192:195], v228 offset:36864
	ds_read_b128 v[196:199], v228 offset:37888
	ds_read_b128 v[200:203], v228 offset:38912
	ds_read_b128 v[204:207], v228 offset:39936
	global_load_lds_dwordx4 v[140:141], off
	v_lshl_add_u64 v[140:141], s[48:49], 0, v[152:153]
	s_mov_b32 m0, s76
	s_nop 0
	global_load_lds_dwordx4 v[140:141], off
	s_waitcnt lgkmcnt(8)
	s_barrier
	s_waitcnt lgkmcnt(0)
	s_waitcnt lgkmcnt(0)
	v_mfma_scale_f32_16x16x128_f8f6f4 v[16:19], v[8:15], v[176:183], v[16:19], v225, v225 op_sel_hi:[0,0,0]
	v_mfma_scale_f32_16x16x128_f8f6f4 v[20:23], v[168:175], v[176:183], v[20:23], v225, v225 op_sel_hi:[0,0,0]
	v_mfma_scale_f32_16x16x128_f8f6f4 v[24:27], v[8:15], v[184:191], v[24:27], v225, v225 op_sel_hi:[0,0,0]
	v_mfma_scale_f32_16x16x128_f8f6f4 v[28:31], v[168:175], v[184:191], v[28:31], v225, v225 op_sel_hi:[0,0,0]
	v_mfma_scale_f32_16x16x128_f8f6f4 v[32:35], v[8:15], v[192:199], v[32:35], v225, v225 op_sel_hi:[0,0,0]
	v_mfma_scale_f32_16x16x128_f8f6f4 v[36:39], v[168:175], v[192:199], v[36:39], v225, v225 op_sel_hi:[0,0,0]
	v_mfma_scale_f32_16x16x128_f8f6f4 v[40:43], v[8:15], v[200:207], v[40:43], v225, v225 op_sel_hi:[0,0,0]
	v_mfma_scale_f32_16x16x128_f8f6f4 v[44:47], v[168:175], v[200:207], v[44:47], v225, v225 op_sel_hi:[0,0,0]
	s_barrier
	s_mov_b32 m0, s62
	v_lshl_add_u64 v[0:1], v[0:1], 0, s[8:9]
	ds_read_b128 v[208:211], v234
	ds_read_b128 v[212:215], v234 offset:1024
	ds_read_b128 v[236:239], v234 offset:2048
	ds_read_b128 v[240:243], v234 offset:3072
	global_load_lds_dwordx4 v[0:1], off
	v_lshl_add_u64 v[0:1], v[2:3], 0, s[8:9]
	s_mov_b32 m0, s63
	s_nop 0
	global_load_lds_dwordx4 v[0:1], off
	s_barrier
	s_waitcnt lgkmcnt(0)
	s_waitcnt lgkmcnt(0)
	v_mfma_scale_f32_16x16x128_f8f6f4 v[48:51], v[208:215], v[176:183], v[48:51], v225, v225 op_sel_hi:[0,0,0]
	v_mfma_scale_f32_16x16x128_f8f6f4 v[52:55], v[236:243], v[176:183], v[52:55], v225, v225 op_sel_hi:[0,0,0]
	v_mfma_scale_f32_16x16x128_f8f6f4 v[56:59], v[208:215], v[184:191], v[56:59], v225, v225 op_sel_hi:[0,0,0]
	v_mfma_scale_f32_16x16x128_f8f6f4 v[60:63], v[236:243], v[184:191], v[60:63], v225, v225 op_sel_hi:[0,0,0]
	v_mfma_scale_f32_16x16x128_f8f6f4 v[64:67], v[208:215], v[192:199], v[64:67], v225, v225 op_sel_hi:[0,0,0]
	v_mfma_scale_f32_16x16x128_f8f6f4 v[68:71], v[236:243], v[192:199], v[68:71], v225, v225 op_sel_hi:[0,0,0]
	v_mfma_scale_f32_16x16x128_f8f6f4 v[72:75], v[208:215], v[200:207], v[72:75], v225, v225 op_sel_hi:[0,0,0]
	v_mfma_scale_f32_16x16x128_f8f6f4 v[76:79], v[236:243], v[200:207], v[76:79], v225, v225 op_sel_hi:[0,0,0]
	s_mov_b32 m0, s80
	v_lshl_add_u64 v[0:1], v[4:5], 0, s[8:9]
	s_barrier
	ds_read_b128 v[176:179], v228 offset:49152
	ds_read_b128 v[180:183], v228 offset:50176
	ds_read_b128 v[184:187], v228 offset:51200
	ds_read_b128 v[188:191], v228 offset:52224
	ds_read_b128 v[192:195], v228 offset:53248
	ds_read_b128 v[196:199], v228 offset:54272
	ds_read_b128 v[200:203], v228 offset:55296
	ds_read_b128 v[204:207], v228 offset:56320
	global_load_lds_dwordx4 v[0:1], off
	v_lshl_add_u64 v[0:1], v[6:7], 0, s[8:9]
	s_mov_b32 m0, s81
	s_nop 0
	global_load_lds_dwordx4 v[0:1], off
	s_barrier
	s_waitcnt lgkmcnt(0)
	s_waitcnt lgkmcnt(0)
	v_mfma_scale_f32_16x16x128_f8f6f4 v[80:83], v[8:15], v[176:183], v[80:83], v225, v225 op_sel_hi:[0,0,0]
	v_mfma_scale_f32_16x16x128_f8f6f4 v[84:87], v[168:175], v[176:183], v[84:87], v225, v225 op_sel_hi:[0,0,0]
	v_mfma_scale_f32_16x16x128_f8f6f4 v[88:91], v[8:15], v[184:191], v[88:91], v225, v225 op_sel_hi:[0,0,0]
	v_mfma_scale_f32_16x16x128_f8f6f4 v[92:95], v[168:175], v[184:191], v[92:95], v225, v225 op_sel_hi:[0,0,0]
	v_mfma_scale_f32_16x16x128_f8f6f4 v[96:99], v[8:15], v[192:199], v[96:99], v225, v225 op_sel_hi:[0,0,0]
	v_mfma_scale_f32_16x16x128_f8f6f4 v[100:103], v[168:175], v[192:199], v[100:103], v225, v225 op_sel_hi:[0,0,0]
	v_mfma_scale_f32_16x16x128_f8f6f4 v[104:107], v[8:15], v[200:207], v[104:107], v225, v225 op_sel_hi:[0,0,0]
	v_mfma_scale_f32_16x16x128_f8f6f4 v[108:111], v[168:175], v[200:207], v[108:111], v225, v225 op_sel_hi:[0,0,0]
	s_barrier
	s_add_u32 s48, s60, 0x40080
	s_addc_u32 s49, s61, 0
	s_mov_b32 m0, s53
	v_lshl_add_u64 v[0:1], s[48:49], 0, v[150:151]
	global_load_lds_dwordx4 v[0:1], off
	v_lshl_add_u64 v[0:1], s[48:49], 0, v[154:155]
	s_mov_b32 m0, s64
	s_nop 0
	global_load_lds_dwordx4 v[0:1], off
	s_waitcnt vmcnt(6)
	s_barrier
	v_mfma_scale_f32_16x16x128_f8f6f4 v[112:115], v[208:215], v[176:183], v[112:115], v225, v225 op_sel_hi:[0,0,0]
	v_mfma_scale_f32_16x16x128_f8f6f4 v[116:119], v[236:243], v[176:183], v[116:119], v225, v225 op_sel_hi:[0,0,0]
	v_mfma_scale_f32_16x16x128_f8f6f4 v[120:123], v[208:215], v[184:191], v[120:123], v225, v225 op_sel_hi:[0,0,0]
	v_mfma_scale_f32_16x16x128_f8f6f4 v[124:127], v[236:243], v[184:191], v[124:127], v225, v225 op_sel_hi:[0,0,0]
	v_mfma_scale_f32_16x16x128_f8f6f4 v[128:131], v[208:215], v[192:199], v[128:131], v225, v225 op_sel_hi:[0,0,0]
	v_mfma_scale_f32_16x16x128_f8f6f4 v[132:135], v[236:243], v[192:199], v[132:135], v225, v225 op_sel_hi:[0,0,0]
	v_mfma_scale_f32_16x16x128_f8f6f4 v[144:147], v[208:215], v[200:207], v[144:147], v225, v225 op_sel_hi:[0,0,0]
	v_mfma_scale_f32_16x16x128_f8f6f4 v[136:139], v[236:243], v[200:207], v[136:139], v225, v225 op_sel_hi:[0,0,0]
	v_mov_b32_e32 v156, v230
	s_barrier
	s_nop 7
	s_nop 7
	s_nop 7
	global_load_dwordx2 v[4:5], v156, s[2:3]
	global_load_dwordx2 v[6:7], v156, s[2:3] offset:512
	global_load_dwordx2 v[8:9], v156, s[2:3] offset:1024
	global_load_dwordx2 v[10:11], v156, s[2:3] offset:1536
	global_load_dwordx2 v[168:169], v156, s[2:3] offset:2048
	global_load_dwordx2 v[202:203], v156, s[2:3] offset:2560
	global_load_dwordx2 v[200:201], v156, s[2:3] offset:3072
	global_load_dwordx2 v[198:199], v156, s[2:3] offset:3584
	v_lshl_add_u64 v[0:1], s[2:3], 0, v[156:157]
	v_add_co_u32_e32 v0, vcc, s85, v0
	s_mov_b64 s[2:3], 0x40000
	s_nop 0
	v_addc_co_u32_e32 v1, vcc, 0, v1, vcc
	global_load_dwordx2 v[196:197], v[0:1], off
	global_load_dwordx2 v[194:195], v[0:1], off offset:512
	global_load_dwordx2 v[192:193], v[0:1], off offset:1024
	global_load_dwordx2 v[190:191], v[0:1], off offset:1536
	global_load_dwordx2 v[180:181], v[0:1], off offset:2048
	global_load_dwordx2 v[170:171], v[0:1], off offset:2560
	global_load_dwordx2 v[2:3], v[0:1], off offset:3072
	s_nop 0
	global_load_dwordx2 v[0:1], v[0:1], off offset:3584
	s_mov_b64 s[50:51], s[46:47]
	s_mov_b64 s[48:49], s[44:45]
	s_waitcnt vmcnt(0)
	v_cvt_f32_ubyte1_e32 v13, v4
	v_cvt_f32_ubyte0_e32 v12, v4
	v_cvt_f32_ubyte3_e32 v15, v4
	v_cvt_f32_ubyte2_e32 v14, v4
	v_cvt_f32_ubyte1_e32 v141, v5
	v_cvt_f32_ubyte0_e32 v140, v5
	v_cvt_f32_ubyte3_e32 v143, v5
	v_cvt_f32_ubyte2_e32 v142, v5
	v_cvt_f32_ubyte1_e32 v5, v6
	v_cvt_f32_ubyte0_e32 v4, v6
	v_cvt_f32_ubyte1_e32 v175, v7
	v_cvt_f32_ubyte0_e32 v174, v7
	v_pk_add_f32 v[4:5], v[4:5], 0.5 op_sel_hi:[1,0]
	v_cvt_f32_ubyte3_e32 v173, v6
	v_cvt_f32_ubyte2_e32 v172, v6
	v_cvt_f32_ubyte3_e32 v177, v7
	v_cvt_f32_ubyte2_e32 v176, v7
	v_cvt_f32_ubyte1_e32 v7, v8
	v_cvt_f32_ubyte0_e32 v6, v8
	v_pk_add_f32 v[174:175], v[174:175], 0.5 op_sel_hi:[1,0]
	v_pk_mul_f32 v[4:5], v[4:5], s[40:41] op_sel_hi:[1,0]
	v_pk_add_f32 v[172:173], v[172:173], 0.5 op_sel_hi:[1,0]
	v_pk_add_f32 v[6:7], v[6:7], 0.5 op_sel_hi:[1,0]
	v_pk_mul_f32 v[204:205], v[174:175], s[40:41] op_sel_hi:[1,0]
	v_pk_mul_f32 v[174:175], v[48:49], v[4:5]
	v_cvt_f32_ubyte3_e32 v5, v10
	v_cvt_f32_ubyte2_e32 v4, v10
	v_cvt_f32_ubyte3_e32 v179, v8
	v_cvt_f32_ubyte2_e32 v178, v8
	v_cvt_f32_ubyte1_e32 v183, v9
	v_cvt_f32_ubyte0_e32 v182, v9
	v_cvt_f32_ubyte3_e32 v185, v9
	v_cvt_f32_ubyte2_e32 v184, v9
	v_cvt_f32_ubyte1_e32 v9, v10
	v_pk_add_f32 v[12:13], v[12:13], 0.5 op_sel_hi:[1,0]
	v_pk_mul_f32 v[172:173], v[172:173], s[40:41] op_sel_hi:[1,0]
	v_pk_mul_f32 v[6:7], v[6:7], s[40:41] op_sel_hi:[1,0]
	v_cvt_f32_ubyte0_e32 v8, v10
	v_pk_add_f32 v[4:5], v[4:5], 0.5 op_sel_hi:[1,0]
	v_pk_add_f32 v[14:15], v[14:15], 0.5 op_sel_hi:[1,0]
	v_pk_add_f32 v[184:185], v[184:185], 0.5 op_sel_hi:[1,0]
	v_pk_mul_f32 v[12:13], v[12:13], s[40:41] op_sel_hi:[1,0]
	v_pk_mul_f32 v[172:173], v[50:51], v[172:173]
	v_pk_mul_f32 v[50:51], v[24:25], v[6:7]
	v_pk_add_f32 v[6:7], v[8:9], 0.5 op_sel_hi:[1,0]
	v_pk_mul_f32 v[4:5], v[4:5], s[40:41] op_sel_hi:[1,0]
	v_pk_add_f32 v[182:183], v[182:183], 0.5 op_sel_hi:[1,0]
	v_pk_mul_f32 v[14:15], v[14:15], s[40:41] op_sel_hi:[1,0]
	v_pk_mul_f32 v[210:211], v[184:185], s[40:41] op_sel_hi:[1,0]
	v_pk_mul_f32 v[184:185], v[16:17], v[12:13]
	v_pk_mul_f32 v[6:7], v[6:7], s[40:41] op_sel_hi:[1,0]
	v_pk_mul_f32 v[12:13], v[58:59], v[4:5]
	v_cvt_f32_ubyte1_e32 v5, v11
	v_cvt_f32_ubyte0_e32 v4, v11
	v_pk_add_f32 v[142:143], v[142:143], 0.5 op_sel_hi:[1,0]
	v_pk_mul_f32 v[208:209], v[182:183], s[40:41] op_sel_hi:[1,0]
	v_pk_mul_f32 v[182:183], v[18:19], v[14:15]
	v_pk_mul_f32 v[14:15], v[56:57], v[6:7]
	v_cvt_f32_ubyte3_e32 v7, v11
	v_cvt_f32_ubyte2_e32 v6, v11
	v_pk_add_f32 v[4:5], v[4:5], 0.5 op_sel_hi:[1,0]
	v_pk_add_f32 v[140:141], v[140:141], 0.5 op_sel_hi:[1,0]
	v_pk_mul_f32 v[142:143], v[142:143], s[40:41] op_sel_hi:[1,0]
	v_pk_add_f32 v[6:7], v[6:7], 0.5 op_sel_hi:[1,0]
	v_pk_mul_f32 v[4:5], v[4:5], s[40:41] op_sel_hi:[1,0]
	v_pk_mul_f32 v[140:141], v[140:141], s[40:41] op_sel_hi:[1,0]
	v_pk_mul_f32 v[186:187], v[22:23], v[142:143]
	v_pk_mul_f32 v[6:7], v[6:7], s[40:41] op_sel_hi:[1,0]
	v_pk_mul_f32 v[142:143], v[60:61], v[4:5]
	v_cvt_f32_ubyte1_e32 v5, v168
	v_cvt_f32_ubyte0_e32 v4, v168
	v_pk_mul_f32 v[188:189], v[20:21], v[140:141]
	v_pk_mul_f32 v[140:141], v[62:63], v[6:7]
	v_cvt_f32_ubyte3_e32 v7, v168
	v_cvt_f32_ubyte2_e32 v6, v168
	v_pk_add_f32 v[4:5], v[4:5], 0.5 op_sel_hi:[1,0]
	v_pk_add_f32 v[6:7], v[6:7], 0.5 op_sel_hi:[1,0]
	v_pk_mul_f32 v[8:9], v[4:5], s[40:41] op_sel_hi:[1,0]
	v_pk_mul_f32 v[4:5], v[6:7], s[40:41] op_sel_hi:[1,0]
	v_pk_mul_f32 v[6:7], v[32:33], v[8:9]
	v_cvt_f32_ubyte1_e32 v9, v169
	v_cvt_f32_ubyte0_e32 v8, v169
	v_cvt_f32_ubyte3_e32 v11, v169
	v_cvt_f32_ubyte2_e32 v10, v169
	v_pk_add_f32 v[8:9], v[8:9], 0.5 op_sel_hi:[1,0]
	v_pk_add_f32 v[10:11], v[10:11], 0.5 op_sel_hi:[1,0]
	v_pk_mul_f32 v[8:9], v[8:9], s[40:41] op_sel_hi:[1,0]
	v_pk_mul_f32 v[10:11], v[10:11], s[40:41] op_sel_hi:[1,0]
	v_pk_mul_f32 v[58:59], v[36:37], v[8:9]
	v_cvt_f32_ubyte1_e32 v9, v202
	v_cvt_f32_ubyte0_e32 v8, v202
	v_pk_mul_f32 v[56:57], v[38:39], v[10:11]
	v_cvt_f32_ubyte3_e32 v11, v202
	v_cvt_f32_ubyte2_e32 v10, v202
	v_pk_add_f32 v[8:9], v[8:9], 0.5 op_sel_hi:[1,0]
	v_pk_add_f32 v[10:11], v[10:11], 0.5 op_sel_hi:[1,0]
	v_pk_mul_f32 v[8:9], v[8:9], s[40:41] op_sel_hi:[1,0]
	v_pk_mul_f32 v[10:11], v[10:11], s[40:41] op_sel_hi:[1,0]
	v_pk_mul_f32 v[18:19], v[64:65], v[8:9]
	v_cvt_f32_ubyte1_e32 v9, v203
	v_cvt_f32_ubyte0_e32 v8, v203
	v_pk_mul_f32 v[16:17], v[66:67], v[10:11]
	v_cvt_f32_ubyte3_e32 v11, v203
	v_cvt_f32_ubyte2_e32 v10, v203
	v_pk_add_f32 v[8:9], v[8:9], 0.5 op_sel_hi:[1,0]
	v_pk_add_f32 v[10:11], v[10:11], 0.5 op_sel_hi:[1,0]
	v_pk_mul_f32 v[8:9], v[8:9], s[40:41] op_sel_hi:[1,0]
	v_pk_mul_f32 v[10:11], v[10:11], s[40:41] op_sel_hi:[1,0]
	v_pk_mul_f32 v[168:169], v[68:69], v[8:9]
	v_cvt_f32_ubyte1_e32 v9, v200
	v_cvt_f32_ubyte0_e32 v8, v200
	v_pk_mul_f32 v[70:71], v[70:71], v[10:11]
	v_cvt_f32_ubyte3_e32 v11, v200
	v_cvt_f32_ubyte2_e32 v10, v200
	v_pk_add_f32 v[8:9], v[8:9], 0.5 op_sel_hi:[1,0]
	v_pk_add_f32 v[10:11], v[10:11], 0.5 op_sel_hi:[1,0]
	v_pk_mul_f32 v[20:21], v[8:9], s[40:41] op_sel_hi:[1,0]
	v_pk_mul_f32 v[8:9], v[10:11], s[40:41] op_sel_hi:[1,0]
	v_pk_mul_f32 v[10:11], v[40:41], v[20:21]
	v_cvt_f32_ubyte1_e32 v21, v201
	v_cvt_f32_ubyte0_e32 v20, v201
	v_cvt_f32_ubyte3_e32 v23, v201
	v_cvt_f32_ubyte2_e32 v22, v201
	v_pk_add_f32 v[20:21], v[20:21], 0.5 op_sel_hi:[1,0]
	v_pk_add_f32 v[22:23], v[22:23], 0.5 op_sel_hi:[1,0]
	v_pk_mul_f32 v[20:21], v[20:21], s[40:41] op_sel_hi:[1,0]
	v_pk_mul_f32 v[22:23], v[22:23], s[40:41] op_sel_hi:[1,0]
	v_pk_mul_f32 v[66:67], v[44:45], v[20:21]
	v_cvt_f32_ubyte1_e32 v21, v198
	v_cvt_f32_ubyte0_e32 v20, v198
	v_pk_mul_f32 v[64:65], v[46:47], v[22:23]
	v_cvt_f32_ubyte3_e32 v23, v198
	v_cvt_f32_ubyte2_e32 v22, v198
	v_pk_add_f32 v[20:21], v[20:21], 0.5 op_sel_hi:[1,0]
	v_pk_add_f32 v[178:179], v[178:179], 0.5 op_sel_hi:[1,0]
	v_pk_add_f32 v[22:23], v[22:23], 0.5 op_sel_hi:[1,0]
	v_pk_mul_f32 v[24:25], v[20:21], s[40:41] op_sel_hi:[1,0]
	v_pk_mul_f32 v[206:207], v[178:179], s[40:41] op_sel_hi:[1,0]
	v_pk_mul_f32 v[20:21], v[22:23], s[40:41] op_sel_hi:[1,0]
	v_pk_mul_f32 v[22:23], v[72:73], v[24:25]
	v_cvt_f32_ubyte1_e32 v25, v199
	v_cvt_f32_ubyte0_e32 v24, v199
	v_pk_mul_f32 v[48:49], v[26:27], v[206:207]
	v_cvt_f32_ubyte3_e32 v27, v199
	v_cvt_f32_ubyte2_e32 v26, v199
	v_pk_add_f32 v[24:25], v[24:25], 0.5 op_sel_hi:[1,0]
	v_pk_add_f32 v[26:27], v[26:27], 0.5 op_sel_hi:[1,0]
	v_pk_mul_f32 v[24:25], v[24:25], s[40:41] op_sel_hi:[1,0]
	v_pk_add_f32 v[176:177], v[176:177], 0.5 op_sel_hi:[1,0]
	v_pk_mul_f32 v[20:21], v[74:75], v[20:21]
	v_pk_mul_f32 v[26:27], v[26:27], s[40:41] op_sel_hi:[1,0]
	v_pk_mul_f32 v[74:75], v[76:77], v[24:25]
	v_cvt_f32_ubyte1_e32 v25, v196
	v_cvt_f32_ubyte0_e32 v24, v196
	v_pk_mul_f32 v[176:177], v[176:177], s[40:41] op_sel_hi:[1,0]
	v_pk_mul_f32 v[72:73], v[78:79], v[26:27]
	v_cvt_f32_ubyte3_e32 v27, v196
	v_cvt_f32_ubyte2_e32 v26, v196
	v_pk_add_f32 v[24:25], v[24:25], 0.5 op_sel_hi:[1,0]
	v_pk_mul_f32 v[176:177], v[54:55], v[176:177]
	v_pk_mul_f32 v[54:55], v[28:29], v[208:209]
	v_pk_add_f32 v[26:27], v[26:27], 0.5 op_sel_hi:[1,0]
	v_pk_mul_f32 v[28:29], v[24:25], s[40:41] op_sel_hi:[1,0]
	v_pk_mul_f32 v[24:25], v[26:27], s[40:41] op_sel_hi:[1,0]
	v_pk_mul_f32 v[26:27], v[80:81], v[28:29]
	v_cvt_f32_ubyte1_e32 v29, v197
	v_cvt_f32_ubyte0_e32 v28, v197
	v_pk_mul_f32 v[178:179], v[52:53], v[204:205]
	v_pk_mul_f32 v[52:53], v[30:31], v[210:211]
	v_cvt_f32_ubyte3_e32 v31, v197
	v_cvt_f32_ubyte2_e32 v30, v197
	v_pk_add_f32 v[28:29], v[28:29], 0.5 op_sel_hi:[1,0]
	v_pk_add_f32 v[30:31], v[30:31], 0.5 op_sel_hi:[1,0]
	v_pk_mul_f32 v[28:29], v[28:29], s[40:41] op_sel_hi:[1,0]
	v_pk_mul_f32 v[30:31], v[30:31], s[40:41] op_sel_hi:[1,0]
	v_pk_mul_f32 v[78:79], v[84:85], v[28:29]
	v_cvt_f32_ubyte1_e32 v29, v194
	v_cvt_f32_ubyte0_e32 v28, v194
	v_pk_mul_f32 v[76:77], v[86:87], v[30:31]
	v_cvt_f32_ubyte3_e32 v31, v194
	v_cvt_f32_ubyte2_e32 v30, v194
	v_pk_add_f32 v[28:29], v[28:29], 0.5 op_sel_hi:[1,0]
	v_pk_add_f32 v[30:31], v[30:31], 0.5 op_sel_hi:[1,0]
	v_pk_mul_f32 v[32:33], v[28:29], s[40:41] op_sel_hi:[1,0]
	v_pk_mul_f32 v[28:29], v[30:31], s[40:41] op_sel_hi:[1,0]
	v_pk_mul_f32 v[30:31], v[112:113], v[32:33]
	v_cvt_f32_ubyte1_e32 v33, v195
	v_cvt_f32_ubyte0_e32 v32, v195
	v_pk_mul_f32 v[4:5], v[34:35], v[4:5]
	v_cvt_f32_ubyte3_e32 v35, v195
	v_cvt_f32_ubyte2_e32 v34, v195
	v_pk_add_f32 v[32:33], v[32:33], 0.5 op_sel_hi:[1,0]
	v_pk_add_f32 v[34:35], v[34:35], 0.5 op_sel_hi:[1,0]
	v_pk_mul_f32 v[32:33], v[32:33], s[40:41] op_sel_hi:[1,0]
	v_pk_mul_f32 v[24:25], v[82:83], v[24:25]
	v_pk_mul_f32 v[34:35], v[34:35], s[40:41] op_sel_hi:[1,0]
	v_pk_mul_f32 v[82:83], v[116:117], v[32:33]
	v_cvt_f32_ubyte1_e32 v33, v192
	v_cvt_f32_ubyte0_e32 v32, v192
	v_pk_mul_f32 v[80:81], v[118:119], v[34:35]
	v_cvt_f32_ubyte3_e32 v35, v192
	v_cvt_f32_ubyte2_e32 v34, v192
	v_pk_add_f32 v[32:33], v[32:33], 0.5 op_sel_hi:[1,0]
	v_pk_add_f32 v[34:35], v[34:35], 0.5 op_sel_hi:[1,0]
	v_pk_mul_f32 v[36:37], v[32:33], s[40:41] op_sel_hi:[1,0]
	v_pk_mul_f32 v[32:33], v[34:35], s[40:41] op_sel_hi:[1,0]
	v_pk_mul_f32 v[34:35], v[88:89], v[36:37]
	v_cvt_f32_ubyte1_e32 v37, v193
	v_cvt_f32_ubyte0_e32 v36, v193
	v_cvt_f32_ubyte3_e32 v39, v193
	v_cvt_f32_ubyte2_e32 v38, v193
	v_pk_add_f32 v[36:37], v[36:37], 0.5 op_sel_hi:[1,0]
	v_pk_add_f32 v[38:39], v[38:39], 0.5 op_sel_hi:[1,0]
	v_pk_mul_f32 v[36:37], v[36:37], s[40:41] op_sel_hi:[1,0]
	v_pk_mul_f32 v[38:39], v[38:39], s[40:41] op_sel_hi:[1,0]
	v_pk_mul_f32 v[86:87], v[92:93], v[36:37]
	v_cvt_f32_ubyte1_e32 v37, v190
	v_cvt_f32_ubyte0_e32 v36, v190
	v_pk_mul_f32 v[84:85], v[94:95], v[38:39]
	v_cvt_f32_ubyte3_e32 v39, v190
	v_cvt_f32_ubyte2_e32 v38, v190
	v_pk_add_f32 v[36:37], v[36:37], 0.5 op_sel_hi:[1,0]
	v_pk_add_f32 v[38:39], v[38:39], 0.5 op_sel_hi:[1,0]
	v_pk_mul_f32 v[40:41], v[36:37], s[40:41] op_sel_hi:[1,0]
	v_pk_mul_f32 v[36:37], v[38:39], s[40:41] op_sel_hi:[1,0]
	v_pk_mul_f32 v[38:39], v[120:121], v[40:41]
	v_cvt_f32_ubyte1_e32 v41, v191
	v_cvt_f32_ubyte0_e32 v40, v191
	v_pk_mul_f32 v[8:9], v[42:43], v[8:9]
	v_cvt_f32_ubyte3_e32 v43, v191
	v_cvt_f32_ubyte2_e32 v42, v191
	v_pk_add_f32 v[40:41], v[40:41], 0.5 op_sel_hi:[1,0]
	v_pk_add_f32 v[42:43], v[42:43], 0.5 op_sel_hi:[1,0]
	v_pk_mul_f32 v[40:41], v[40:41], s[40:41] op_sel_hi:[1,0]
	v_pk_mul_f32 v[32:33], v[90:91], v[32:33]
	v_pk_mul_f32 v[42:43], v[42:43], s[40:41] op_sel_hi:[1,0]
	v_pk_mul_f32 v[90:91], v[124:125], v[40:41]
	v_cvt_f32_ubyte1_e32 v41, v180
	v_cvt_f32_ubyte0_e32 v40, v180
	v_pk_mul_f32 v[88:89], v[126:127], v[42:43]
	v_cvt_f32_ubyte3_e32 v43, v180
	v_cvt_f32_ubyte2_e32 v42, v180
	v_pk_add_f32 v[40:41], v[40:41], 0.5 op_sel_hi:[1,0]
	v_pk_add_f32 v[42:43], v[42:43], 0.5 op_sel_hi:[1,0]
	v_pk_mul_f32 v[44:45], v[40:41], s[40:41] op_sel_hi:[1,0]
	v_pk_mul_f32 v[40:41], v[42:43], s[40:41] op_sel_hi:[1,0]
	v_pk_mul_f32 v[42:43], v[96:97], v[44:45]
	v_cvt_f32_ubyte1_e32 v45, v181
	v_cvt_f32_ubyte0_e32 v44, v181
	v_cvt_f32_ubyte3_e32 v47, v181
	v_cvt_f32_ubyte2_e32 v46, v181
	v_pk_add_f32 v[44:45], v[44:45], 0.5 op_sel_hi:[1,0]
	v_pk_add_f32 v[46:47], v[46:47], 0.5 op_sel_hi:[1,0]
	v_pk_mul_f32 v[44:45], v[44:45], s[40:41] op_sel_hi:[1,0]
	v_pk_mul_f32 v[46:47], v[46:47], s[40:41] op_sel_hi:[1,0]
	v_pk_mul_f32 v[94:95], v[100:101], v[44:45]
	v_cvt_f32_ubyte1_e32 v45, v170
	v_cvt_f32_ubyte0_e32 v44, v170
	v_pk_mul_f32 v[92:93], v[102:103], v[46:47]
	v_cvt_f32_ubyte3_e32 v47, v170
	v_cvt_f32_ubyte2_e32 v46, v170
	v_pk_add_f32 v[44:45], v[44:45], 0.5 op_sel_hi:[1,0]
	v_pk_add_f32 v[46:47], v[46:47], 0.5 op_sel_hi:[1,0]
	v_pk_mul_f32 v[60:61], v[44:45], s[40:41] op_sel_hi:[1,0]
	v_pk_mul_f32 v[44:45], v[46:47], s[40:41] op_sel_hi:[1,0]
	v_pk_mul_f32 v[46:47], v[128:129], v[60:61]
	v_cvt_f32_ubyte1_e32 v61, v171
	v_cvt_f32_ubyte0_e32 v60, v171
	v_cvt_f32_ubyte3_e32 v63, v171
	v_cvt_f32_ubyte2_e32 v62, v171
	v_pk_add_f32 v[60:61], v[60:61], 0.5 op_sel_hi:[1,0]
	v_pk_add_f32 v[62:63], v[62:63], 0.5 op_sel_hi:[1,0]
	v_pk_mul_f32 v[60:61], v[60:61], s[40:41] op_sel_hi:[1,0]
	v_pk_mul_f32 v[40:41], v[98:99], v[40:41]
	v_pk_mul_f32 v[62:63], v[62:63], s[40:41] op_sel_hi:[1,0]
	v_pk_mul_f32 v[98:99], v[132:133], v[60:61]
	v_cvt_f32_ubyte1_e32 v61, v2
	v_cvt_f32_ubyte0_e32 v60, v2
	v_pk_mul_f32 v[96:97], v[134:135], v[62:63]
	v_cvt_f32_ubyte3_e32 v63, v2
	v_cvt_f32_ubyte2_e32 v62, v2
	v_pk_add_f32 v[60:61], v[60:61], 0.5 op_sel_hi:[1,0]
	v_pk_add_f32 v[62:63], v[62:63], 0.5 op_sel_hi:[1,0]
	v_pk_mul_f32 v[68:69], v[60:61], s[40:41] op_sel_hi:[1,0]
	v_cvt_f32_ubyte3_e32 v101, v3
	v_cvt_f32_ubyte2_e32 v100, v3
	v_pk_mul_f32 v[60:61], v[62:63], s[40:41] op_sel_hi:[1,0]
	v_pk_mul_f32 v[62:63], v[104:105], v[68:69]
	v_cvt_f32_ubyte1_e32 v69, v3
	v_cvt_f32_ubyte0_e32 v68, v3
	v_pk_add_f32 v[2:3], v[100:101], 0.5 op_sel_hi:[1,0]
	v_pk_add_f32 v[68:69], v[68:69], 0.5 op_sel_hi:[1,0]
	v_pk_mul_f32 v[2:3], v[2:3], s[40:41] op_sel_hi:[1,0]
	v_pk_mul_f32 v[68:69], v[68:69], s[40:41] op_sel_hi:[1,0]
	v_pk_mul_f32 v[100:101], v[110:111], v[2:3]
	v_cvt_f32_ubyte1_e32 v3, v0
	v_cvt_f32_ubyte0_e32 v2, v0
	v_pk_mul_f32 v[102:103], v[108:109], v[68:69]
	v_cvt_f32_ubyte3_e32 v69, v0
	v_cvt_f32_ubyte2_e32 v68, v0
	v_pk_add_f32 v[2:3], v[2:3], 0.5 op_sel_hi:[1,0]
	v_lshl_add_u32 v108, s92, 8, v226
	v_pk_mul_f32 v[28:29], v[114:115], v[28:29]
	v_pk_mul_f32 v[60:61], v[106:107], v[60:61]
	v_pk_add_f32 v[68:69], v[68:69], 0.5 op_sel_hi:[1,0]
	v_pk_mul_f32 v[104:105], v[2:3], s[40:41] op_sel_hi:[1,0]
	v_cvt_f32_ubyte3_e32 v107, v1
	v_cvt_f32_ubyte2_e32 v106, v1
	v_ashrrev_i32_e32 v109, 31, v108
	v_pk_mul_f32 v[112:113], v[182:183], s[42:43] op_sel_hi:[1,0]
	v_pk_mul_f32 v[114:115], v[184:185], s[42:43] op_sel_hi:[1,0]
	v_pk_mul_f32 v[2:3], v[68:69], s[40:41] op_sel_hi:[1,0]
	v_pk_mul_f32 v[68:69], v[144:145], v[104:105]
	v_cvt_f32_ubyte1_e32 v105, v1
	v_cvt_f32_ubyte0_e32 v104, v1
	v_pk_add_f32 v[0:1], v[106:107], 0.5 op_sel_hi:[1,0]
	v_lshlrev_b64 v[106:107], 11, v[108:109]
	v_pk_mul_f32 v[118:119], v[188:189], s[42:43] op_sel_hi:[1,0]
	v_med3_f32 v109, v114, s86, v233
	v_med3_f32 v114, v115, s86, v233
	v_med3_f32 v115, v112, s86, v233
	v_mov_b32_e32 v112, v157
	v_med3_f32 v120, v113, s86, v233
	v_cvt_pk_fp8_f32 v112, v109, v114
	v_med3_f32 v109, v118, s86, v233
	v_med3_f32 v114, v119, s86, v233
	v_mov_b32_e32 v113, v157
	v_cvt_pk_fp8_f32 v113, v109, v114
	v_pk_mul_f32 v[116:117], v[186:187], s[42:43] op_sel_hi:[1,0]
	v_cvt_pk_fp8_f32 v112, v115, v120 op_sel:[0,0,1]
	v_med3_f32 v109, v116, s86, v233
	v_med3_f32 v114, v117, s86, v233
	v_cvt_pk_fp8_f32 v113, v109, v114 op_sel:[0,0,1]
	v_pk_mul_f32 v[114:115], v[172:173], s[42:43] op_sel_hi:[1,0]
	v_pk_mul_f32 v[116:117], v[174:175], s[42:43] op_sel_hi:[1,0]
	v_pk_mul_f32 v[120:121], v[178:179], s[42:43] op_sel_hi:[1,0]
	v_med3_f32 v109, v116, s86, v233
	v_med3_f32 v116, v117, s86, v233
	v_med3_f32 v117, v114, s86, v233
	v_mov_b32_e32 v114, v157
	v_pk_mul_f32 v[36:37], v[122:123], v[36:37]
	v_med3_f32 v122, v115, s86, v233
	v_cvt_pk_fp8_f32 v114, v109, v116
	v_med3_f32 v109, v120, s86, v233
	v_med3_f32 v116, v121, s86, v233
	v_mov_b32_e32 v115, v157
	v_cvt_pk_fp8_f32 v115, v109, v116
	v_pk_mul_f32 v[118:119], v[176:177], s[42:43] op_sel_hi:[1,0]
	v_lshl_or_b32 v110, s91, 8, v229
	v_med3_f32 v109, v118, s86, v233
	v_med3_f32 v116, v119, s86, v233
	v_cvt_pk_fp8_f32 v114, v117, v122 op_sel:[0,0,1]
	v_cvt_pk_fp8_f32 v115, v109, v116 op_sel:[0,0,1]
	v_ashrrev_i32_e32 v111, 31, v110
	v_lshl_add_u64 v[106:107], s[6:7], 0, v[106:107]
	v_pk_mul_f32 v[48:49], v[48:49], s[42:43] op_sel_hi:[1,0]
	v_pk_mul_f32 v[50:51], v[50:51], s[42:43] op_sel_hi:[1,0]
	v_lshl_add_u64 v[106:107], v[106:107], 0, v[110:111]
	v_pk_mul_f32 v[54:55], v[54:55], s[42:43] op_sel_hi:[1,0]
	v_med3_f32 v50, v50, s86, v233
	v_med3_f32 v51, v51, s86, v233
	v_med3_f32 v109, v48, s86, v233
	v_mov_b32_e32 v48, v157
	global_store_dwordx2 v[106:107], v[112:113], off
	global_store_dwordx2 v[106:107], v[114:115], off offset:128
	v_pk_mul_f32 v[52:53], v[52:53], s[42:43] op_sel_hi:[1,0]
	v_med3_f32 v114, v49, s86, v233
	v_cvt_pk_fp8_f32 v48, v50, v51
	v_med3_f32 v50, v54, s86, v233
	v_med3_f32 v51, v55, s86, v233
	v_mov_b32_e32 v49, v157
	v_pk_mul_f32 v[12:13], v[12:13], s[42:43] op_sel_hi:[1,0]
	v_pk_mul_f32 v[14:15], v[14:15], s[42:43] op_sel_hi:[1,0]
	v_cvt_pk_fp8_f32 v49, v50, v51
	v_med3_f32 v50, v52, s86, v233
	v_med3_f32 v51, v53, s86, v233
	v_pk_mul_f32 v[52:53], v[142:143], s[42:43] op_sel_hi:[1,0]
	v_med3_f32 v14, v14, s86, v233
	v_med3_f32 v15, v15, s86, v233
	v_med3_f32 v54, v12, s86, v233
	v_mov_b32_e32 v12, v157
	v_med3_f32 v55, v13, s86, v233
	v_cvt_pk_fp8_f32 v12, v14, v15
	v_med3_f32 v14, v52, s86, v233
	v_med3_f32 v15, v53, s86, v233
	v_mov_b32_e32 v13, v157
	v_cvt_pk_fp8_f32 v13, v14, v15
	v_or_b32_e32 v112, 16, v108
	v_cvt_pk_fp8_f32 v49, v50, v51 op_sel:[0,0,1]
	v_pk_mul_f32 v[50:51], v[140:141], s[42:43] op_sel_hi:[1,0]
	v_ashrrev_i32_e32 v113, 31, v112
	v_cvt_pk_fp8_f32 v48, v109, v114 op_sel:[0,0,1]
	v_med3_f32 v14, v50, s86, v233
	v_med3_f32 v15, v51, s86, v233
	v_lshlrev_b64 v[112:113], 11, v[112:113]
	v_cvt_pk_fp8_f32 v12, v54, v55 op_sel:[0,0,1]
	v_cvt_pk_fp8_f32 v13, v14, v15 op_sel:[0,0,1]
	v_lshl_add_u64 v[14:15], s[6:7], 0, v[112:113]
	v_lshl_add_u64 v[14:15], v[14:15], 0, v[110:111]
	v_pk_mul_f32 v[4:5], v[4:5], s[42:43] op_sel_hi:[1,0]
	v_pk_mul_f32 v[6:7], v[6:7], s[42:43] op_sel_hi:[1,0]
	global_store_dwordx2 v[14:15], v[48:49], off
	global_store_dwordx2 v[14:15], v[12:13], off offset:128
	v_pk_mul_f32 v[48:49], v[58:59], s[42:43] op_sel_hi:[1,0]
	v_med3_f32 v6, v6, s86, v233
	v_med3_f32 v7, v7, s86, v233
	v_med3_f32 v50, v4, s86, v233
	v_mov_b32_e32 v4, v157
	v_med3_f32 v51, v5, s86, v233
	v_cvt_pk_fp8_f32 v4, v6, v7
	v_med3_f32 v6, v48, s86, v233
	v_med3_f32 v7, v49, s86, v233
	v_mov_b32_e32 v5, v157
	v_cvt_pk_fp8_f32 v5, v6, v7
	v_pk_mul_f32 v[14:15], v[56:57], s[42:43] op_sel_hi:[1,0]
	v_or_b32_e32 v12, 32, v108
	v_med3_f32 v6, v14, s86, v233
	v_med3_f32 v7, v15, s86, v233
	v_cvt_pk_fp8_f32 v5, v6, v7 op_sel:[0,0,1]
	v_pk_mul_f32 v[6:7], v[16:17], s[42:43] op_sel_hi:[1,0]
	v_pk_mul_f32 v[14:15], v[18:19], s[42:43] op_sel_hi:[1,0]
	v_pk_mul_f32 v[18:19], v[168:169], s[42:43] op_sel_hi:[1,0]
	v_med3_f32 v14, v14, s86, v233
	v_med3_f32 v15, v15, s86, v233
	v_med3_f32 v48, v6, s86, v233
	v_mov_b32_e32 v6, v157
	v_med3_f32 v49, v7, s86, v233
	v_cvt_pk_fp8_f32 v6, v14, v15
	v_med3_f32 v14, v18, s86, v233
	v_med3_f32 v15, v19, s86, v233
	v_mov_b32_e32 v7, v157
	v_cvt_pk_fp8_f32 v7, v14, v15
	v_pk_mul_f32 v[16:17], v[70:71], s[42:43] op_sel_hi:[1,0]
	v_ashrrev_i32_e32 v13, 31, v12
	v_cvt_pk_fp8_f32 v4, v50, v51 op_sel:[0,0,1]
	v_med3_f32 v14, v16, s86, v233
	v_med3_f32 v15, v17, s86, v233
	v_lshlrev_b64 v[12:13], 11, v[12:13]
	v_cvt_pk_fp8_f32 v6, v48, v49 op_sel:[0,0,1]
	v_cvt_pk_fp8_f32 v7, v14, v15 op_sel:[0,0,1]
	v_lshl_add_u64 v[12:13], s[6:7], 0, v[12:13]
	v_lshl_add_u64 v[12:13], v[12:13], 0, v[110:111]
	global_store_dwordx2 v[12:13], v[4:5], off
	global_store_dwordx2 v[12:13], v[6:7], off offset:128
	v_pk_mul_f32 v[6:7], v[8:9], s[42:43] op_sel_hi:[1,0]
	v_pk_mul_f32 v[8:9], v[10:11], s[42:43] op_sel_hi:[1,0]
	v_pk_mul_f32 v[12:13], v[66:67], s[42:43] op_sel_hi:[1,0]
	v_med3_f32 v8, v8, s86, v233
	v_med3_f32 v9, v9, s86, v233
	v_med3_f32 v14, v6, s86, v233
	v_mov_b32_e32 v6, v157
	v_med3_f32 v15, v7, s86, v233
	v_cvt_pk_fp8_f32 v6, v8, v9
	v_med3_f32 v8, v12, s86, v233
	v_med3_f32 v9, v13, s86, v233
	v_mov_b32_e32 v7, v157
	v_cvt_pk_fp8_f32 v7, v8, v9
	v_pk_mul_f32 v[10:11], v[64:65], s[42:43] op_sel_hi:[1,0]
	v_cvt_pk_fp8_f32 v6, v14, v15 op_sel:[0,0,1]
	v_med3_f32 v8, v10, s86, v233
	v_med3_f32 v9, v11, s86, v233
	v_cvt_pk_fp8_f32 v7, v8, v9 op_sel:[0,0,1]
	v_pk_mul_f32 v[8:9], v[20:21], s[42:43] op_sel_hi:[1,0]
	v_pk_mul_f32 v[10:11], v[22:23], s[42:43] op_sel_hi:[1,0]
	v_pk_mul_f32 v[14:15], v[74:75], s[42:43] op_sel_hi:[1,0]
	v_med3_f32 v10, v10, s86, v233
	v_med3_f32 v11, v11, s86, v233
	v_med3_f32 v16, v8, s86, v233
	v_mov_b32_e32 v8, v157
	v_med3_f32 v17, v9, s86, v233
	v_cvt_pk_fp8_f32 v8, v10, v11
	v_med3_f32 v10, v14, s86, v233
	v_med3_f32 v11, v15, s86, v233
	v_mov_b32_e32 v9, v157
	v_cvt_pk_fp8_f32 v9, v10, v11
	v_or_b32_e32 v4, 48, v108
	v_pk_mul_f32 v[12:13], v[72:73], s[42:43] op_sel_hi:[1,0]
	v_ashrrev_i32_e32 v5, 31, v4
	v_med3_f32 v10, v12, s86, v233
	v_med3_f32 v11, v13, s86, v233
	v_lshlrev_b64 v[4:5], 11, v[4:5]
	v_cvt_pk_fp8_f32 v8, v16, v17 op_sel:[0,0,1]
	v_cvt_pk_fp8_f32 v9, v10, v11 op_sel:[0,0,1]
	v_lshl_add_u64 v[4:5], s[6:7], 0, v[4:5]
	v_lshl_add_u64 v[4:5], v[4:5], 0, v[110:111]
	global_store_dwordx2 v[4:5], v[6:7], off
	global_store_dwordx2 v[4:5], v[8:9], off offset:128
	v_pk_mul_f32 v[6:7], v[24:25], s[42:43] op_sel_hi:[1,0]
	v_pk_mul_f32 v[8:9], v[26:27], s[42:43] op_sel_hi:[1,0]
	v_pk_mul_f32 v[12:13], v[78:79], s[42:43] op_sel_hi:[1,0]
	v_med3_f32 v8, v8, s86, v233
	v_med3_f32 v9, v9, s86, v233
	v_med3_f32 v14, v6, s86, v233
	v_mov_b32_e32 v6, v157
	v_med3_f32 v15, v7, s86, v233
	v_cvt_pk_fp8_f32 v6, v8, v9
	v_med3_f32 v8, v12, s86, v233
	v_med3_f32 v9, v13, s86, v233
	v_mov_b32_e32 v7, v157
	v_cvt_pk_fp8_f32 v7, v8, v9
	v_pk_mul_f32 v[10:11], v[76:77], s[42:43] op_sel_hi:[1,0]
	v_cvt_pk_fp8_f32 v6, v14, v15 op_sel:[0,0,1]
	v_med3_f32 v8, v10, s86, v233
	v_med3_f32 v9, v11, s86, v233
	v_cvt_pk_fp8_f32 v7, v8, v9 op_sel:[0,0,1]
	v_pk_mul_f32 v[8:9], v[28:29], s[42:43] op_sel_hi:[1,0]
	v_pk_mul_f32 v[10:11], v[30:31], s[42:43] op_sel_hi:[1,0]
	v_pk_mul_f32 v[14:15], v[82:83], s[42:43] op_sel_hi:[1,0]
	v_med3_f32 v10, v10, s86, v233
	v_med3_f32 v11, v11, s86, v233
	v_med3_f32 v16, v8, s86, v233
	v_mov_b32_e32 v8, v157
	v_med3_f32 v17, v9, s86, v233
	v_cvt_pk_fp8_f32 v8, v10, v11
	v_med3_f32 v10, v14, s86, v233
	v_med3_f32 v11, v15, s86, v233
	v_mov_b32_e32 v9, v157
	v_cvt_pk_fp8_f32 v9, v10, v11
	v_pk_mul_f32 v[12:13], v[80:81], s[42:43] op_sel_hi:[1,0]
	v_lshl_add_u64 v[4:5], v[106:107], 0, s[2:3]
	v_med3_f32 v10, v12, s86, v233
	v_med3_f32 v11, v13, s86, v233
	v_cvt_pk_fp8_f32 v8, v16, v17 op_sel:[0,0,1]
	v_cvt_pk_fp8_f32 v9, v10, v11 op_sel:[0,0,1]
	s_mov_b32 s2, 0x40000
	v_add_co_u32_e32 v10, vcc, s2, v106
	v_pk_mul_f32 v[12:13], v[86:87], s[42:43] op_sel_hi:[1,0]
	s_nop 0
	v_addc_co_u32_e32 v11, vcc, 0, v107, vcc
	global_store_dwordx2 v[10:11], v[6:7], off
	global_store_dwordx2 v[4:5], v[8:9], off offset:128
	v_pk_mul_f32 v[6:7], v[32:33], s[42:43] op_sel_hi:[1,0]
	v_pk_mul_f32 v[8:9], v[34:35], s[42:43] op_sel_hi:[1,0]
	v_med3_f32 v14, v6, s86, v233
	v_med3_f32 v8, v8, s86, v233
	v_med3_f32 v9, v9, s86, v233
	v_mov_b32_e32 v6, v157
	v_med3_f32 v15, v7, s86, v233
	v_cvt_pk_fp8_f32 v6, v8, v9
	v_med3_f32 v8, v12, s86, v233
	v_med3_f32 v9, v13, s86, v233
	v_mov_b32_e32 v7, v157
	v_cvt_pk_fp8_f32 v7, v8, v9
	v_pk_mul_f32 v[10:11], v[84:85], s[42:43] op_sel_hi:[1,0]
	v_cvt_pk_fp8_f32 v6, v14, v15 op_sel:[0,0,1]
	v_med3_f32 v8, v10, s86, v233
	v_med3_f32 v9, v11, s86, v233
	v_cvt_pk_fp8_f32 v7, v8, v9 op_sel:[0,0,1]
	v_pk_mul_f32 v[8:9], v[36:37], s[42:43] op_sel_hi:[1,0]
	v_pk_mul_f32 v[10:11], v[38:39], s[42:43] op_sel_hi:[1,0]
	v_pk_mul_f32 v[14:15], v[90:91], s[42:43] op_sel_hi:[1,0]
	v_med3_f32 v10, v10, s86, v233
	v_med3_f32 v11, v11, s86, v233
	v_med3_f32 v16, v8, s86, v233
	v_mov_b32_e32 v8, v157
	v_med3_f32 v17, v9, s86, v233
	v_cvt_pk_fp8_f32 v8, v10, v11
	v_med3_f32 v10, v14, s86, v233
	v_med3_f32 v11, v15, s86, v233
	v_mov_b32_e32 v9, v157
	v_cvt_pk_fp8_f32 v9, v10, v11
	v_pk_mul_f32 v[12:13], v[88:89], s[42:43] op_sel_hi:[1,0]
	s_mov_b64 s[2:3], 0x48000
	v_med3_f32 v10, v12, s86, v233
	v_med3_f32 v11, v13, s86, v233
	v_lshl_add_u64 v[4:5], v[106:107], 0, s[2:3]
	v_cvt_pk_fp8_f32 v8, v16, v17 op_sel:[0,0,1]
	v_cvt_pk_fp8_f32 v9, v10, v11 op_sel:[0,0,1]
	s_mov_b32 s2, 0x48000
	v_add_co_u32_e32 v10, vcc, s2, v106
	v_pk_mul_f32 v[12:13], v[94:95], s[42:43] op_sel_hi:[1,0]
	s_nop 0
	v_addc_co_u32_e32 v11, vcc, 0, v107, vcc
	global_store_dwordx2 v[10:11], v[6:7], off
	global_store_dwordx2 v[4:5], v[8:9], off offset:128
	v_pk_mul_f32 v[6:7], v[40:41], s[42:43] op_sel_hi:[1,0]
	v_pk_mul_f32 v[8:9], v[42:43], s[42:43] op_sel_hi:[1,0]
	v_med3_f32 v14, v6, s86, v233
	v_med3_f32 v8, v8, s86, v233
	v_med3_f32 v9, v9, s86, v233
	v_mov_b32_e32 v6, v157
	v_med3_f32 v15, v7, s86, v233
	v_cvt_pk_fp8_f32 v6, v8, v9
	v_med3_f32 v8, v12, s86, v233
	v_med3_f32 v9, v13, s86, v233
	v_mov_b32_e32 v7, v157
	v_cvt_pk_fp8_f32 v7, v8, v9
	v_pk_mul_f32 v[10:11], v[92:93], s[42:43] op_sel_hi:[1,0]
	v_pk_mul_f32 v[44:45], v[130:131], v[44:45]
	v_med3_f32 v8, v10, s86, v233
	v_med3_f32 v9, v11, s86, v233
	v_cvt_pk_fp8_f32 v7, v8, v9 op_sel:[0,0,1]
	v_pk_mul_f32 v[8:9], v[44:45], s[42:43] op_sel_hi:[1,0]
	v_pk_mul_f32 v[10:11], v[46:47], s[42:43] op_sel_hi:[1,0]
	v_cvt_pk_fp8_f32 v6, v14, v15 op_sel:[0,0,1]
	v_pk_mul_f32 v[14:15], v[98:99], s[42:43] op_sel_hi:[1,0]
	v_med3_f32 v10, v10, s86, v233
	v_med3_f32 v11, v11, s86, v233
	v_med3_f32 v16, v8, s86, v233
	v_mov_b32_e32 v8, v157
	v_med3_f32 v17, v9, s86, v233
	v_cvt_pk_fp8_f32 v8, v10, v11
	v_med3_f32 v10, v14, s86, v233
	v_med3_f32 v11, v15, s86, v233
	v_mov_b32_e32 v9, v157
	v_cvt_pk_fp8_f32 v9, v10, v11
	v_pk_mul_f32 v[12:13], v[96:97], s[42:43] op_sel_hi:[1,0]
	s_mov_b64 s[2:3], 0x50000
	v_med3_f32 v10, v12, s86, v233
	v_med3_f32 v11, v13, s86, v233
	v_lshl_add_u64 v[4:5], v[106:107], 0, s[2:3]
	v_cvt_pk_fp8_f32 v8, v16, v17 op_sel:[0,0,1]
	v_cvt_pk_fp8_f32 v9, v10, v11 op_sel:[0,0,1]
	s_mov_b32 s2, 0x50000
	v_add_co_u32_e32 v10, vcc, s2, v106
	v_pk_mul_f32 v[12:13], v[102:103], s[42:43] op_sel_hi:[1,0]
	s_nop 0
	v_addc_co_u32_e32 v11, vcc, 0, v107, vcc
	global_store_dwordx2 v[10:11], v[6:7], off
	global_store_dwordx2 v[4:5], v[8:9], off offset:128
	v_pk_mul_f32 v[6:7], v[60:61], s[42:43] op_sel_hi:[1,0]
	v_pk_mul_f32 v[8:9], v[62:63], s[42:43] op_sel_hi:[1,0]
	v_med3_f32 v14, v6, s86, v233
	v_med3_f32 v8, v8, s86, v233
	v_med3_f32 v9, v9, s86, v233
	v_mov_b32_e32 v6, v157
	v_med3_f32 v15, v7, s86, v233
	v_cvt_pk_fp8_f32 v6, v8, v9
	v_med3_f32 v8, v12, s86, v233
	v_med3_f32 v9, v13, s86, v233
	v_mov_b32_e32 v7, v157
	v_cvt_pk_fp8_f32 v7, v8, v9
	v_pk_add_f32 v[104:105], v[104:105], 0.5 op_sel_hi:[1,0]
	v_pk_mul_f32 v[10:11], v[100:101], s[42:43] op_sel_hi:[1,0]
	v_pk_mul_f32 v[2:3], v[146:147], v[2:3]
	v_pk_mul_f32 v[104:105], v[104:105], s[40:41] op_sel_hi:[1,0]
	v_med3_f32 v8, v10, s86, v233
	v_med3_f32 v9, v11, s86, v233
	v_pk_mul_f32 v[104:105], v[136:137], v[104:105]
	v_cvt_pk_fp8_f32 v7, v8, v9 op_sel:[0,0,1]
	v_pk_mul_f32 v[2:3], v[2:3], s[42:43] op_sel_hi:[1,0]
	v_pk_mul_f32 v[8:9], v[68:69], s[42:43] op_sel_hi:[1,0]
	v_pk_mul_f32 v[10:11], v[104:105], s[42:43] op_sel_hi:[1,0]
	v_med3_f32 v8, v8, s86, v233
	v_med3_f32 v9, v9, s86, v233
	v_med3_f32 v12, v2, s86, v233
	v_mov_b32_e32 v2, v157
	v_med3_f32 v13, v3, s86, v233
	v_cvt_pk_fp8_f32 v2, v8, v9
	v_med3_f32 v8, v10, s86, v233
	v_med3_f32 v9, v11, s86, v233
	v_mov_b32_e32 v3, v157
	v_pk_mul_f32 v[0:1], v[0:1], s[40:41] op_sel_hi:[1,0]
	v_cvt_pk_fp8_f32 v3, v8, v9
	v_pk_mul_f32 v[0:1], v[138:139], v[0:1]
	s_mov_b64 s[2:3], 0x58000
	v_pk_mul_f32 v[0:1], v[0:1], s[42:43] op_sel_hi:[1,0]
	v_lshl_add_u64 v[4:5], v[106:107], 0, s[2:3]
	v_cvt_pk_fp8_f32 v6, v14, v15 op_sel:[0,0,1]
	v_med3_f32 v0, v0, s86, v233
	v_med3_f32 v1, v1, s86, v233
	s_mov_b32 s2, 0x58000
	v_cvt_pk_fp8_f32 v2, v12, v13 op_sel:[0,0,1]
	v_cvt_pk_fp8_f32 v3, v0, v1 op_sel:[0,0,1]
	v_add_co_u32_e32 v0, vcc, s2, v106
	s_mov_b32 s91, s87
	s_nop 0
	v_addc_co_u32_e32 v1, vcc, 0, v107, vcc
	s_and_b64 vcc, exec, s[0:1]
	s_mov_b32 s92, s88
	global_store_dwordx2 v[0:1], v[6:7], off
	global_store_dwordx2 v[4:5], v[2:3], off offset:128
	s_cbranch_vccz .LBB0_904
	s_waitcnt vmcnt(0)
	s_cmpk_gt_u32 s68, 0xff
	s_cbranch_scc1 .LBB0_915
	s_barrier

.LBB0_985:
	ds_read_b128 v[8:11], v176
	ds_read_b128 v[12:15], v176 offset:1024
	ds_read_b128 v[0:3], v176 offset:2048
	ds_read_b128 v[4:7], v176 offset:3072
	s_add_u32 s20, s18, 0xfffc0080
	s_addc_u32 s21, s19, -1
	s_cmp_eq_u32 s67, 12
	s_cselect_b32 s23, s61, s21
	s_cselect_b32 s22, s62, s20
	s_cselect_b32 s21, s63, s66
	s_cselect_b32 s20, s64, s65
	v_lshl_add_u64 v[158:159], s[18:19], 0, v[156:157]
	s_add_i32 m0, s44, 0xc000
	ds_read_b128 v[180:183], v177
	ds_read_b128 v[184:187], v177 offset:1024
	ds_read_b128 v[188:191], v177 offset:2048
	ds_read_b128 v[192:195], v177 offset:3072
	ds_read_b128 v[196:199], v177 offset:4096
	ds_read_b128 v[200:203], v177 offset:5120
	ds_read_b128 v[204:207], v177 offset:6144
	ds_read_b128 v[208:211], v177 offset:7168
	global_load_lds_dwordx4 v[158:159], off
	v_lshl_add_u64 v[158:159], s[18:19], 0, v[154:155]
	s_add_i32 m0, s44, 0xe000
	s_nop 0
	global_load_lds_dwordx4 v[158:159], off
	s_waitcnt lgkmcnt(8)
	s_barrier
	s_waitcnt lgkmcnt(0)
	s_waitcnt lgkmcnt(0)
	v_mfma_scale_f32_16x16x128_f8f6f4 v[140:143], v[8:15], v[180:187], v[140:143], v172, v172 op_sel_hi:[0,0,0]
	v_mfma_scale_f32_16x16x128_f8f6f4 v[136:139], v[0:7], v[180:187], v[136:139], v172, v172 op_sel_hi:[0,0,0]
	v_mfma_scale_f32_16x16x128_f8f6f4 v[128:131], v[8:15], v[188:195], v[128:131], v172, v172 op_sel_hi:[0,0,0]
	v_mfma_scale_f32_16x16x128_f8f6f4 v[120:123], v[0:7], v[188:195], v[120:123], v172, v172 op_sel_hi:[0,0,0]
	v_mfma_scale_f32_16x16x128_f8f6f4 v[112:115], v[8:15], v[196:203], v[112:115], v172, v172 op_sel_hi:[0,0,0]
	v_mfma_scale_f32_16x16x128_f8f6f4 v[104:107], v[0:7], v[196:203], v[104:107], v172, v172 op_sel_hi:[0,0,0]
	v_mfma_scale_f32_16x16x128_f8f6f4 v[96:99], v[8:15], v[204:211], v[96:99], v172, v172 op_sel_hi:[0,0,0]
	v_mfma_scale_f32_16x16x128_f8f6f4 v[88:91], v[0:7], v[204:211], v[88:91], v172, v172 op_sel_hi:[0,0,0]
	s_barrier
	s_add_i32 s68, s53, s43
	v_lshl_add_u64 v[162:163], s[20:21], 0, v[146:147]
	s_mov_b32 m0, s68
	ds_read_b128 v[212:215], v178
	ds_read_b128 v[216:219], v178 offset:1024
	ds_read_b128 v[224:227], v178 offset:2048
	ds_read_b128 v[228:231], v178 offset:3072
	global_load_lds_dwordx4 v[162:163], off
	v_lshl_add_u64 v[164:165], s[20:21], 0, v[150:151]
	s_add_i32 m0, s68, 0x2000
	s_nop 0
	global_load_lds_dwordx4 v[164:165], off
	s_barrier
	s_waitcnt lgkmcnt(0)
	s_waitcnt lgkmcnt(0)
	v_mfma_scale_f32_16x16x128_f8f6f4 v[132:135], v[212:219], v[180:187], v[132:135], v172, v172 op_sel_hi:[0,0,0]
	v_mfma_scale_f32_16x16x128_f8f6f4 v[124:127], v[224:231], v[180:187], v[124:127], v172, v172 op_sel_hi:[0,0,0]
	v_mfma_scale_f32_16x16x128_f8f6f4 v[116:119], v[212:219], v[188:195], v[116:119], v172, v172 op_sel_hi:[0,0,0]
	v_mfma_scale_f32_16x16x128_f8f6f4 v[108:111], v[224:231], v[188:195], v[108:111], v172, v172 op_sel_hi:[0,0,0]
	v_mfma_scale_f32_16x16x128_f8f6f4 v[100:103], v[212:219], v[196:203], v[100:103], v172, v172 op_sel_hi:[0,0,0]
	v_mfma_scale_f32_16x16x128_f8f6f4 v[92:95], v[224:231], v[196:203], v[92:95], v172, v172 op_sel_hi:[0,0,0]
	v_mfma_scale_f32_16x16x128_f8f6f4 v[84:87], v[212:219], v[204:211], v[84:87], v172, v172 op_sel_hi:[0,0,0]
	v_mfma_scale_f32_16x16x128_f8f6f4 v[80:83], v[224:231], v[204:211], v[80:83], v172, v172 op_sel_hi:[0,0,0]
	s_mov_b32 m0, s44
	v_lshl_add_u64 v[166:167], s[22:23], 0, v[144:145]
	s_barrier
	ds_read_b128 v[180:183], v177 offset:16384
	ds_read_b128 v[184:187], v177 offset:17408
	ds_read_b128 v[188:191], v177 offset:18432
	ds_read_b128 v[192:195], v177 offset:19456
	ds_read_b128 v[196:199], v177 offset:20480
	ds_read_b128 v[200:203], v177 offset:21504
	ds_read_b128 v[204:207], v177 offset:22528
	ds_read_b128 v[208:211], v177 offset:23552
	global_load_lds_dwordx4 v[166:167], off
	v_lshl_add_u64 v[168:169], s[22:23], 0, v[148:149]
	s_mov_b32 m0, s45
	s_nop 0
	global_load_lds_dwordx4 v[168:169], off
	s_barrier
	s_waitcnt lgkmcnt(0)
	s_waitcnt lgkmcnt(0)
	v_mfma_scale_f32_16x16x128_f8f6f4 v[76:79], v[8:15], v[180:187], v[76:79], v172, v172 op_sel_hi:[0,0,0]
	v_mfma_scale_f32_16x16x128_f8f6f4 v[72:75], v[0:7], v[180:187], v[72:75], v172, v172 op_sel_hi:[0,0,0]
	v_mfma_scale_f32_16x16x128_f8f6f4 v[64:67], v[8:15], v[188:195], v[64:67], v172, v172 op_sel_hi:[0,0,0]
	v_mfma_scale_f32_16x16x128_f8f6f4 v[56:59], v[0:7], v[188:195], v[56:59], v172, v172 op_sel_hi:[0,0,0]
	v_mfma_scale_f32_16x16x128_f8f6f4 v[48:51], v[8:15], v[196:203], v[48:51], v172, v172 op_sel_hi:[0,0,0]
	v_mfma_scale_f32_16x16x128_f8f6f4 v[40:43], v[0:7], v[196:203], v[40:43], v172, v172 op_sel_hi:[0,0,0]
	v_mfma_scale_f32_16x16x128_f8f6f4 v[32:35], v[8:15], v[204:211], v[32:35], v172, v172 op_sel_hi:[0,0,0]
	v_mfma_scale_f32_16x16x128_f8f6f4 v[24:27], v[0:7], v[204:211], v[24:27], v172, v172 op_sel_hi:[0,0,0]
	s_barrier
	s_add_u32 s68, s20, 0x40000
	s_addc_u32 s69, s21, 0
	s_add_i32 s70, s54, s43
	v_lshl_add_u64 v[0:1], s[68:69], 0, v[146:147]
	s_mov_b32 m0, s70
	s_nop 0
	global_load_lds_dwordx4 v[0:1], off
	v_lshl_add_u64 v[0:1], s[68:69], 0, v[150:151]
	s_add_i32 m0, s70, 0x2000
	s_nop 0
	global_load_lds_dwordx4 v[0:1], off
	s_waitcnt vmcnt(6)
	s_barrier
	v_mfma_scale_f32_16x16x128_f8f6f4 v[68:71], v[212:219], v[180:187], v[68:71], v172, v172 op_sel_hi:[0,0,0]
	v_mfma_scale_f32_16x16x128_f8f6f4 v[60:63], v[224:231], v[180:187], v[60:63], v172, v172 op_sel_hi:[0,0,0]
	v_mfma_scale_f32_16x16x128_f8f6f4 v[52:55], v[212:219], v[188:195], v[52:55], v172, v172 op_sel_hi:[0,0,0]
	v_mfma_scale_f32_16x16x128_f8f6f4 v[44:47], v[224:231], v[188:195], v[44:47], v172, v172 op_sel_hi:[0,0,0]
	v_mfma_scale_f32_16x16x128_f8f6f4 v[36:39], v[212:219], v[196:203], v[36:39], v172, v172 op_sel_hi:[0,0,0]
	v_mfma_scale_f32_16x16x128_f8f6f4 v[28:31], v[224:231], v[196:203], v[28:31], v172, v172 op_sel_hi:[0,0,0]
	v_mfma_scale_f32_16x16x128_f8f6f4 v[20:23], v[212:219], v[204:211], v[20:23], v172, v172 op_sel_hi:[0,0,0]
	v_mfma_scale_f32_16x16x128_f8f6f4 v[16:19], v[224:231], v[204:211], v[16:19], v172, v172 op_sel_hi:[0,0,0]
	s_add_i32 s68, 0, 0x18000
	v_add_u32_e32 v12, s68, v173
	s_barrier
	ds_read_b128 v[0:3], v12
	ds_read_b128 v[4:7], v12 offset:1024
	ds_read_b128 v[8:11], v12 offset:2048
	ds_read_b128 v[12:15], v12 offset:3072
	s_add_u32 s22, s22, 0x40000
	s_addc_u32 s23, s23, 0
	s_mov_b32 m0, s46
	v_lshl_add_u64 v[158:159], s[22:23], 0, v[144:145]
	ds_read_b128 v[180:183], v177 offset:32768
	ds_read_b128 v[184:187], v177 offset:33792
	ds_read_b128 v[188:191], v177 offset:34816
	ds_read_b128 v[192:195], v177 offset:35840
	ds_read_b128 v[196:199], v177 offset:36864
	ds_read_b128 v[200:203], v177 offset:37888
	ds_read_b128 v[204:207], v177 offset:38912
	ds_read_b128 v[208:211], v177 offset:39936
	global_load_lds_dwordx4 v[158:159], off
	v_lshl_add_u64 v[158:159], s[22:23], 0, v[148:149]
	s_mov_b32 m0, s47
	s_nop 0
	global_load_lds_dwordx4 v[158:159], off
	s_waitcnt lgkmcnt(8)
	s_barrier
	s_waitcnt lgkmcnt(0)
	s_waitcnt lgkmcnt(0)
	v_mfma_scale_f32_16x16x128_f8f6f4 v[140:143], v[0:7], v[180:187], v[140:143], v172, v172 op_sel_hi:[0,0,0]
	v_mfma_scale_f32_16x16x128_f8f6f4 v[136:139], v[8:15], v[180:187], v[136:139], v172, v172 op_sel_hi:[0,0,0]
	v_mfma_scale_f32_16x16x128_f8f6f4 v[128:131], v[0:7], v[188:195], v[128:131], v172, v172 op_sel_hi:[0,0,0]
	v_mfma_scale_f32_16x16x128_f8f6f4 v[120:123], v[8:15], v[188:195], v[120:123], v172, v172 op_sel_hi:[0,0,0]
	v_mfma_scale_f32_16x16x128_f8f6f4 v[112:115], v[0:7], v[196:203], v[112:115], v172, v172 op_sel_hi:[0,0,0]
	v_mfma_scale_f32_16x16x128_f8f6f4 v[104:107], v[8:15], v[196:203], v[104:107], v172, v172 op_sel_hi:[0,0,0]
	v_mfma_scale_f32_16x16x128_f8f6f4 v[96:99], v[0:7], v[204:211], v[96:99], v172, v172 op_sel_hi:[0,0,0]
	v_mfma_scale_f32_16x16x128_f8f6f4 v[88:91], v[8:15], v[204:211], v[88:91], v172, v172 op_sel_hi:[0,0,0]
	s_barrier
	s_add_i32 s22, 0, 0x1c000
	s_add_i32 s23, s68, s43
	v_add_u32_e32 v152, s22, v173
	v_lshl_add_u64 v[158:159], v[162:163], 0, s[6:7]
	s_mov_b32 m0, s23
	ds_read_b128 v[212:215], v152
	ds_read_b128 v[216:219], v152 offset:1024
	ds_read_b128 v[224:227], v152 offset:2048
	ds_read_b128 v[228:231], v152 offset:3072
	global_load_lds_dwordx4 v[158:159], off
	v_lshl_add_u64 v[158:159], v[164:165], 0, s[6:7]
	s_add_i32 m0, s23, 0x2000
	s_nop 0
	global_load_lds_dwordx4 v[158:159], off
	s_barrier
	s_waitcnt lgkmcnt(0)
	s_waitcnt lgkmcnt(0)
	v_mfma_scale_f32_16x16x128_f8f6f4 v[132:135], v[212:219], v[180:187], v[132:135], v172, v172 op_sel_hi:[0,0,0]
	v_mfma_scale_f32_16x16x128_f8f6f4 v[124:127], v[224:231], v[180:187], v[124:127], v172, v172 op_sel_hi:[0,0,0]
	v_mfma_scale_f32_16x16x128_f8f6f4 v[116:119], v[212:219], v[188:195], v[116:119], v172, v172 op_sel_hi:[0,0,0]
	v_mfma_scale_f32_16x16x128_f8f6f4 v[108:111], v[224:231], v[188:195], v[108:111], v172, v172 op_sel_hi:[0,0,0]
	v_mfma_scale_f32_16x16x128_f8f6f4 v[100:103], v[212:219], v[196:203], v[100:103], v172, v172 op_sel_hi:[0,0,0]
	v_mfma_scale_f32_16x16x128_f8f6f4 v[92:95], v[224:231], v[196:203], v[92:95], v172, v172 op_sel_hi:[0,0,0]
	v_mfma_scale_f32_16x16x128_f8f6f4 v[84:87], v[212:219], v[204:211], v[84:87], v172, v172 op_sel_hi:[0,0,0]
	v_mfma_scale_f32_16x16x128_f8f6f4 v[80:83], v[224:231], v[204:211], v[80:83], v172, v172 op_sel_hi:[0,0,0]
	s_mov_b32 m0, s50
	v_lshl_add_u64 v[158:159], v[166:167], 0, s[6:7]
	s_barrier
	ds_read_b128 v[180:183], v177 offset:49152
	ds_read_b128 v[184:187], v177 offset:50176
	ds_read_b128 v[188:191], v177 offset:51200
	ds_read_b128 v[192:195], v177 offset:52224
	ds_read_b128 v[196:199], v177 offset:53248
	ds_read_b128 v[200:203], v177 offset:54272
	ds_read_b128 v[204:207], v177 offset:55296
	ds_read_b128 v[208:211], v177 offset:56320
	global_load_lds_dwordx4 v[158:159], off
	v_lshl_add_u64 v[158:159], v[168:169], 0, s[6:7]
	s_mov_b32 m0, s51
	s_nop 0
	global_load_lds_dwordx4 v[158:159], off
	s_barrier
	s_waitcnt lgkmcnt(0)
	s_waitcnt lgkmcnt(0)
	v_mfma_scale_f32_16x16x128_f8f6f4 v[76:79], v[0:7], v[180:187], v[76:79], v172, v172 op_sel_hi:[0,0,0]
	v_mfma_scale_f32_16x16x128_f8f6f4 v[72:75], v[8:15], v[180:187], v[72:75], v172, v172 op_sel_hi:[0,0,0]
	v_mfma_scale_f32_16x16x128_f8f6f4 v[64:67], v[0:7], v[188:195], v[64:67], v172, v172 op_sel_hi:[0,0,0]
	v_mfma_scale_f32_16x16x128_f8f6f4 v[56:59], v[8:15], v[188:195], v[56:59], v172, v172 op_sel_hi:[0,0,0]
	v_mfma_scale_f32_16x16x128_f8f6f4 v[48:51], v[0:7], v[196:203], v[48:51], v172, v172 op_sel_hi:[0,0,0]
	v_mfma_scale_f32_16x16x128_f8f6f4 v[40:43], v[8:15], v[196:203], v[40:43], v172, v172 op_sel_hi:[0,0,0]
	v_mfma_scale_f32_16x16x128_f8f6f4 v[32:35], v[0:7], v[204:211], v[32:35], v172, v172 op_sel_hi:[0,0,0]
	v_mfma_scale_f32_16x16x128_f8f6f4 v[24:27], v[8:15], v[204:211], v[24:27], v172, v172 op_sel_hi:[0,0,0]
	s_barrier
	s_add_u32 s20, s20, 0x40080
	s_addc_u32 s21, s21, 0
	s_add_i32 s22, s22, s43
	v_lshl_add_u64 v[0:1], s[20:21], 0, v[146:147]
	s_mov_b32 m0, s22
	s_nop 0
	global_load_lds_dwordx4 v[0:1], off
	v_lshl_add_u64 v[0:1], s[20:21], 0, v[150:151]
	s_add_i32 m0, s22, 0x2000
	s_nop 0
	global_load_lds_dwordx4 v[0:1], off
	s_waitcnt vmcnt(6)
	s_barrier
	v_mfma_scale_f32_16x16x128_f8f6f4 v[68:71], v[212:219], v[180:187], v[68:71], v172, v172 op_sel_hi:[0,0,0]
	v_mfma_scale_f32_16x16x128_f8f6f4 v[60:63], v[224:231], v[180:187], v[60:63], v172, v172 op_sel_hi:[0,0,0]
	v_mfma_scale_f32_16x16x128_f8f6f4 v[52:55], v[212:219], v[188:195], v[52:55], v172, v172 op_sel_hi:[0,0,0]
	v_mfma_scale_f32_16x16x128_f8f6f4 v[44:47], v[224:231], v[188:195], v[44:47], v172, v172 op_sel_hi:[0,0,0]
	v_mfma_scale_f32_16x16x128_f8f6f4 v[36:39], v[212:219], v[196:203], v[36:39], v172, v172 op_sel_hi:[0,0,0]
	v_mfma_scale_f32_16x16x128_f8f6f4 v[28:31], v[224:231], v[196:203], v[28:31], v172, v172 op_sel_hi:[0,0,0]
	v_mfma_scale_f32_16x16x128_f8f6f4 v[20:23], v[212:219], v[204:211], v[20:23], v172, v172 op_sel_hi:[0,0,0]
	v_mfma_scale_f32_16x16x128_f8f6f4 v[16:19], v[224:231], v[204:211], v[16:19], v172, v172 op_sel_hi:[0,0,0]
	s_add_i32 s67, s67, 2
	s_add_u32 s65, s65, 0x100
	s_addc_u32 s66, s66, 0
	s_add_u32 s18, s18, 0x100
	s_addc_u32 s19, s19, 0
	s_cmp_gt_u32 s67, 13
	s_barrier
	s_cbranch_scc0 .LBB0_985
	s_lshl_b32 s18, s60, 8
	s_min_i32 s19, s60, 32
	s_ashr_i32 s22, s19, 4
	s_add_i32 s19, s18, 0xffffe000
	s_cmp_lt_i32 s60, 32
	s_cselect_b32 s20, s18, s19
	s_mul_i32 s22, s22, 6
	s_cselect_b32 s60, s28, s30
	s_cselect_b32 s61, s27, s29
	s_ashr_i32 s21, s20, 31
	s_ashr_i32 s19, s18, 31
	s_ashr_i32 s23, s22, 31
	s_lshl_b64 s[20:21], s[20:21], 13
	s_lshl_b64 s[18:19], s[18:19], 12
	s_lshl_b64 s[22:23], s[22:23], 13
	v_lshl_or_b32 v8, s59, 8, v175
	s_add_u32 s22, s4, s22
	s_addc_u32 s23, s5, s23
	v_ashrrev_i32_e32 v9, 31, v8
	v_lshl_add_u64 v[0:1], v[8:9], 2, s[22:23]
	v_lshl_add_u64 v[10:11], v[0:1], 0, s[8:9]
	v_add_co_u32_e32 v0, vcc, s49, v0
	s_add_u32 s20, s61, s20
	s_nop 7
	s_nop 7
	s_nop 7
	s_nop 0
	v_addc_co_u32_e32 v1, vcc, 0, v1, vcc
	s_addc_u32 s21, s60, s21
	v_add_u32_e32 v152, v174, v8
	global_load_dwordx4 v[0:3], v[0:1], off
	s_nop 0
	global_load_dwordx4 v[164:167], v[10:11], off offset:528
	global_load_dwordx4 v[4:7], v[10:11], off offset:16
	global_load_dwordx4 v[180:183], v[10:11], off offset:512
	v_mov_b32_e32 v169, v153
	v_lshl_add_u64 v[8:9], v[152:153], 2, s[20:21]
	v_add_u32_e32 v168, 0x80, v152
	global_load_dwordx4 v[184:187], v[8:9], off
	global_load_dwordx4 v[188:191], v[8:9], off offset:16
	v_lshl_add_u64 v[8:9], v[168:169], 2, s[20:21]
	global_load_dwordx4 v[192:195], v[8:9], off
	global_load_dwordx4 v[196:199], v[8:9], off offset:16
	v_add_u32_e32 v220, 0x8000, v152
	v_mov_b32_e32 v221, v153
	v_lshl_add_u64 v[8:9], v[220:221], 2, s[20:21]
	v_add_u32_e32 v252, 0x8080, v152
	v_mov_b32_e32 v253, v153
	global_load_dwordx4 v[200:203], v[8:9], off
	global_load_dwordx4 v[204:207], v[8:9], off offset:16
	v_lshl_add_u64 v[8:9], v[252:253], 2, s[20:21]
	global_load_dwordx4 v[208:211], v[8:9], off
	global_load_dwordx4 v[212:215], v[8:9], off offset:16
	v_mov_b32_e32 v223, v153
	v_add_u32_e32 v222, 0x10000, v152
	v_lshl_add_u64 v[8:9], v[222:223], 2, s[20:21]
	v_mov_b32_e32 v171, v153
	v_add_u32_e32 v170, 0x10080, v152
	global_load_dwordx4 v[216:219], v[8:9], off
	global_load_dwordx4 v[224:227], v[8:9], off offset:16
	v_lshl_add_u64 v[8:9], v[170:171], 2, s[20:21]
	v_mov_b32_e32 v159, v153
	v_add_u32_e32 v158, 0x18000, v152
	global_load_dwordx4 v[228:231], v[8:9], off
	global_load_dwordx4 v[232:235], v[8:9], off offset:16
	v_lshl_add_u64 v[8:9], v[158:159], 2, s[20:21]
	v_mov_b32_e32 v163, v153
	v_add_u32_e32 v162, 0x18080, v152
	global_load_dwordx4 v[236:239], v[8:9], off
	global_load_dwordx4 v[240:243], v[8:9], off offset:16
	v_lshl_add_u64 v[8:9], v[162:163], 2, s[20:21]
	global_load_dwordx4 v[244:247], v[8:9], off offset:16
	global_load_dwordx4 v[248:251], v[8:9], off
	s_add_u32 s18, s2, s18
	s_addc_u32 s19, s3, s19
	v_lshl_add_u64 v[160:161], v[152:153], 1, s[18:19]
	s_and_b64 vcc, exec, s[0:1]
	s_mov_b32 s59, s55
	s_mov_b32 s60, s56
	s_waitcnt vmcnt(0)
	v_pk_mul_f32 v[14:15], v[0:1], s[10:11] op_sel_hi:[1,0]
	v_pk_mul_f32 v[12:13], v[2:3], s[10:11] op_sel_hi:[1,0]
	v_pk_mul_f32 v[8:9], v[6:7], s[10:11] op_sel_hi:[1,0]
	v_pk_mul_f32 v[10:11], v[4:5], s[10:11] op_sel_hi:[1,0]
	v_pk_mul_f32 v[6:7], v[180:181], s[10:11] op_sel_hi:[1,0]
	v_pk_mul_f32 v[4:5], v[182:183], s[10:11] op_sel_hi:[1,0]
	v_pk_mul_f32 v[0:1], v[166:167], s[10:11] op_sel_hi:[1,0]
	v_pk_mul_f32 v[2:3], v[164:165], s[10:11] op_sel_hi:[1,0]
	v_pk_fma_f32 v[140:141], v[140:141], v[14:15], v[184:185]
	v_pk_fma_f32 v[164:165], v[138:139], v[8:9], v[190:191]
	v_pk_fma_f32 v[138:139], v[136:137], v[10:11], v[188:189]
	v_pk_fma_f32 v[132:133], v[132:133], v[6:7], v[192:193]
	v_pk_fma_f32 v[142:143], v[142:143], v[12:13], v[186:187]
	v_cvt_pk_bf16_f32 v136, v140, v141
	v_pk_fma_f32 v[134:135], v[134:135], v[4:5], v[194:195]
	v_cvt_pk_bf16_f32 v137, v142, v143
	v_cvt_pk_bf16_f32 v138, v138, v139
	v_cvt_pk_bf16_f32 v139, v164, v165
	v_pk_fma_f32 v[140:141], v[126:127], v[0:1], v[198:199]
	global_store_dwordx4 v[160:161], v[136:139], off
	v_pk_fma_f32 v[126:127], v[124:125], v[2:3], v[196:197]
	v_cvt_pk_bf16_f32 v124, v132, v133
	v_cvt_pk_bf16_f32 v125, v134, v135
	v_lshl_add_u64 v[132:133], v[168:169], 1, s[18:19]
	v_cvt_pk_bf16_f32 v126, v126, v127
	v_cvt_pk_bf16_f32 v127, v140, v141
	global_store_dwordx4 v[132:133], v[124:127], off
	v_pk_fma_f32 v[116:117], v[116:117], v[6:7], v[208:209]
	v_pk_fma_f32 v[118:119], v[118:119], v[4:5], v[210:211]
	v_pk_fma_f32 v[124:125], v[130:131], v[12:13], v[202:203]
	v_pk_fma_f32 v[126:127], v[128:129], v[14:15], v[200:201]
	v_pk_fma_f32 v[128:129], v[122:123], v[8:9], v[206:207]
	v_pk_fma_f32 v[122:123], v[120:121], v[10:11], v[204:205]
	v_cvt_pk_bf16_f32 v120, v126, v127
	v_cvt_pk_bf16_f32 v121, v124, v125
	v_lshl_add_u64 v[124:125], v[220:221], 1, s[18:19]
	v_cvt_pk_bf16_f32 v122, v122, v123
	v_cvt_pk_bf16_f32 v123, v128, v129
	global_store_dwordx4 v[124:125], v[120:123], off
	v_pk_fma_f32 v[100:101], v[100:101], v[6:7], v[228:229]
	v_pk_fma_f32 v[102:103], v[102:103], v[4:5], v[230:231]
	v_pk_fma_f32 v[120:121], v[110:111], v[0:1], v[214:215]
	v_pk_fma_f32 v[110:111], v[108:109], v[2:3], v[212:213]
	v_cvt_pk_bf16_f32 v108, v116, v117
	v_cvt_pk_bf16_f32 v109, v118, v119
	v_lshl_add_u64 v[116:117], v[252:253], 1, s[18:19]
	v_cvt_pk_bf16_f32 v110, v110, v111
	v_cvt_pk_bf16_f32 v111, v120, v121
	global_store_dwordx4 v[116:117], v[108:111], off
	v_pk_fma_f32 v[84:85], v[84:85], v[6:7], v[248:249]
	v_pk_fma_f32 v[86:87], v[86:87], v[4:5], v[250:251]
	v_pk_fma_f32 v[108:109], v[114:115], v[12:13], v[218:219]
	v_pk_fma_f32 v[110:111], v[112:113], v[14:15], v[216:217]
	v_pk_fma_f32 v[112:113], v[106:107], v[8:9], v[226:227]
	v_pk_fma_f32 v[106:107], v[104:105], v[10:11], v[224:225]
	v_cvt_pk_bf16_f32 v104, v110, v111
	v_cvt_pk_bf16_f32 v105, v108, v109
	v_lshl_add_u64 v[108:109], v[222:223], 1, s[18:19]
	v_cvt_pk_bf16_f32 v106, v106, v107
	v_cvt_pk_bf16_f32 v107, v112, v113
	global_store_dwordx4 v[108:109], v[104:107], off
	v_add_u32_e32 v160, 0x40080, v152
	v_mov_b32_e32 v161, v153
	v_pk_fma_f32 v[104:105], v[94:95], v[0:1], v[234:235]
	v_pk_fma_f32 v[94:95], v[92:93], v[2:3], v[232:233]
	v_cvt_pk_bf16_f32 v92, v100, v101
	v_cvt_pk_bf16_f32 v93, v102, v103
	v_lshl_add_u64 v[100:101], v[170:171], 1, s[18:19]
	v_cvt_pk_bf16_f32 v94, v94, v95
	v_cvt_pk_bf16_f32 v95, v104, v105
	global_store_dwordx4 v[100:101], v[92:95], off
	v_add_u32_e32 v164, 0x48080, v152
	v_mov_b32_e32 v165, v153
	v_pk_fma_f32 v[92:93], v[98:99], v[12:13], v[238:239]
	v_pk_fma_f32 v[94:95], v[96:97], v[14:15], v[236:237]
	v_pk_fma_f32 v[96:97], v[90:91], v[8:9], v[242:243]
	v_pk_fma_f32 v[90:91], v[88:89], v[10:11], v[240:241]
	v_cvt_pk_bf16_f32 v88, v94, v95
	v_cvt_pk_bf16_f32 v89, v92, v93
	v_lshl_add_u64 v[92:93], v[158:159], 1, s[18:19]
	v_cvt_pk_bf16_f32 v90, v90, v91
	v_cvt_pk_bf16_f32 v91, v96, v97
	global_store_dwordx4 v[92:93], v[88:91], off
	v_add_u32_e32 v158, 0x40000, v152
	v_lshl_add_u64 v[92:93], v[160:161], 2, s[20:21]
	v_pk_fma_f32 v[88:89], v[82:83], v[0:1], v[246:247]
	v_pk_fma_f32 v[82:83], v[80:81], v[2:3], v[244:245]
	v_cvt_pk_bf16_f32 v80, v84, v85
	v_lshl_add_u64 v[84:85], v[162:163], 1, s[18:19]
	v_cvt_pk_bf16_f32 v81, v86, v87
	v_cvt_pk_bf16_f32 v82, v82, v83
	v_cvt_pk_bf16_f32 v83, v88, v89
	global_store_dwordx4 v[84:85], v[80:83], off
	v_lshl_add_u64 v[84:85], v[158:159], 2, s[20:21]
	global_load_dwordx4 v[80:83], v[84:85], off
	s_nop 0
	global_load_dwordx4 v[84:87], v[84:85], off offset:16
	s_nop 0
	global_load_dwordx4 v[88:91], v[92:93], off
	s_nop 0
	global_load_dwordx4 v[92:95], v[92:93], off offset:16
	v_add_u32_e32 v162, 0x48000, v152
	v_lshl_add_u64 v[100:101], v[162:163], 2, s[20:21]
	global_load_dwordx4 v[96:99], v[100:101], off
	s_nop 0
	global_load_dwordx4 v[100:103], v[100:101], off offset:16
	v_lshl_add_u64 v[108:109], v[164:165], 2, s[20:21]
	global_load_dwordx4 v[104:107], v[108:109], off
	s_nop 0
	global_load_dwordx4 v[108:111], v[108:109], off offset:16
	v_add_u32_e32 v166, 0x50000, v152
	v_mov_b32_e32 v167, v153
	v_lshl_add_u64 v[116:117], v[166:167], 2, s[20:21]
	v_add_u32_e32 v168, 0x50080, v152
	global_load_dwordx4 v[112:115], v[116:117], off
	s_nop 0
	global_load_dwordx4 v[116:119], v[116:117], off offset:16
	v_lshl_add_u64 v[124:125], v[168:169], 2, s[20:21]
	v_add_u32_e32 v170, 0x58000, v152
	global_load_dwordx4 v[120:123], v[124:125], off
	s_nop 0
	global_load_dwordx4 v[124:127], v[124:125], off offset:16
	v_lshl_add_u64 v[132:133], v[170:171], 2, s[20:21]
	v_add_u32_e32 v152, 0x58080, v152
	global_load_dwordx4 v[128:131], v[132:133], off
	s_nop 0
	global_load_dwordx4 v[132:135], v[132:133], off offset:16
	v_lshl_add_u64 v[140:141], v[152:153], 2, s[20:21]
	global_load_dwordx4 v[136:139], v[140:141], off
	s_nop 0
	global_load_dwordx4 v[140:143], v[140:141], off offset:16
	s_mov_b64 s[20:21], s[12:13]
	s_waitcnt vmcnt(0)
	v_pk_fma_f32 v[76:77], v[76:77], v[14:15], v[80:81]
	v_pk_fma_f32 v[78:79], v[78:79], v[12:13], v[82:83]
	v_pk_fma_f32 v[80:81], v[74:75], v[8:9], v[86:87]
	v_pk_fma_f32 v[74:75], v[72:73], v[10:11], v[84:85]
	v_cvt_pk_bf16_f32 v72, v76, v77
	v_cvt_pk_bf16_f32 v73, v78, v79
	v_lshl_add_u64 v[76:77], v[158:159], 1, s[18:19]
	v_pk_fma_f32 v[68:69], v[68:69], v[6:7], v[88:89]
	v_cvt_pk_bf16_f32 v74, v74, v75
	v_cvt_pk_bf16_f32 v75, v80, v81
	global_store_dwordx4 v[76:77], v[72:75], off
	v_pk_fma_f32 v[70:71], v[70:71], v[4:5], v[90:91]
	v_pk_fma_f32 v[52:53], v[52:53], v[6:7], v[104:105]
	v_pk_fma_f32 v[72:73], v[62:63], v[0:1], v[94:95]
	v_pk_fma_f32 v[62:63], v[60:61], v[2:3], v[92:93]
	v_cvt_pk_bf16_f32 v60, v68, v69
	v_cvt_pk_bf16_f32 v61, v70, v71
	v_lshl_add_u64 v[68:69], v[160:161], 1, s[18:19]
	v_cvt_pk_bf16_f32 v62, v62, v63
	v_cvt_pk_bf16_f32 v63, v72, v73
	global_store_dwordx4 v[68:69], v[60:63], off
	v_pk_fma_f32 v[54:55], v[54:55], v[4:5], v[106:107]
	v_pk_fma_f32 v[36:37], v[36:37], v[6:7], v[120:121]
	v_pk_fma_f32 v[60:61], v[66:67], v[12:13], v[98:99]
	v_pk_fma_f32 v[62:63], v[64:65], v[14:15], v[96:97]
	v_pk_fma_f32 v[64:65], v[58:59], v[8:9], v[102:103]
	v_pk_fma_f32 v[58:59], v[56:57], v[10:11], v[100:101]
	v_cvt_pk_bf16_f32 v56, v62, v63
	v_cvt_pk_bf16_f32 v57, v60, v61
	v_lshl_add_u64 v[60:61], v[162:163], 1, s[18:19]
	v_cvt_pk_bf16_f32 v58, v58, v59
	v_cvt_pk_bf16_f32 v59, v64, v65
	global_store_dwordx4 v[60:61], v[56:59], off
	v_pk_fma_f32 v[38:39], v[38:39], v[4:5], v[122:123]
	v_pk_fma_f32 v[26:27], v[26:27], v[8:9], v[134:135]
	v_pk_fma_f32 v[56:57], v[46:47], v[0:1], v[110:111]
	v_pk_fma_f32 v[46:47], v[44:45], v[2:3], v[108:109]
	v_cvt_pk_bf16_f32 v44, v52, v53
	v_cvt_pk_bf16_f32 v45, v54, v55
	v_lshl_add_u64 v[52:53], v[164:165], 1, s[18:19]
	v_cvt_pk_bf16_f32 v46, v46, v47
	v_cvt_pk_bf16_f32 v47, v56, v57
	global_store_dwordx4 v[52:53], v[44:47], off
	v_pk_fma_f32 v[4:5], v[22:23], v[4:5], v[138:139]
	v_pk_fma_f32 v[6:7], v[20:21], v[6:7], v[136:137]
	v_pk_fma_f32 v[44:45], v[50:51], v[12:13], v[114:115]
	v_pk_fma_f32 v[46:47], v[48:49], v[14:15], v[112:113]
	v_pk_fma_f32 v[48:49], v[42:43], v[8:9], v[118:119]
	v_pk_fma_f32 v[42:43], v[40:41], v[10:11], v[116:117]
	v_cvt_pk_bf16_f32 v40, v46, v47
	v_cvt_pk_bf16_f32 v41, v44, v45
	v_lshl_add_u64 v[44:45], v[166:167], 1, s[18:19]
	v_cvt_pk_bf16_f32 v42, v42, v43
	v_cvt_pk_bf16_f32 v43, v48, v49
	global_store_dwordx4 v[44:45], v[40:43], off
	v_pk_fma_f32 v[12:13], v[34:35], v[12:13], v[130:131]
	v_pk_fma_f32 v[14:15], v[32:33], v[14:15], v[128:129]
	v_pk_fma_f32 v[40:41], v[30:31], v[0:1], v[126:127]
	v_pk_fma_f32 v[30:31], v[28:29], v[2:3], v[124:125]
	v_cvt_pk_bf16_f32 v28, v36, v37
	v_lshl_add_u64 v[36:37], v[168:169], 1, s[18:19]
	v_cvt_pk_bf16_f32 v29, v38, v39
	v_cvt_pk_bf16_f32 v30, v30, v31
	v_cvt_pk_bf16_f32 v31, v40, v41
	global_store_dwordx4 v[36:37], v[28:31], off
	v_pk_fma_f32 v[10:11], v[24:25], v[10:11], v[132:133]
	v_cvt_pk_bf16_f32 v8, v14, v15
	v_cvt_pk_bf16_f32 v9, v12, v13
	v_lshl_add_u64 v[12:13], v[170:171], 1, s[18:19]
	v_cvt_pk_bf16_f32 v10, v10, v11
	v_cvt_pk_bf16_f32 v11, v26, v27
	global_store_dwordx4 v[12:13], v[8:11], off
	v_pk_fma_f32 v[2:3], v[16:17], v[2:3], v[140:141]
	s_nop 0
	v_pk_fma_f32 v[8:9], v[18:19], v[0:1], v[142:143]
	v_cvt_pk_bf16_f32 v0, v6, v7
	v_cvt_pk_bf16_f32 v1, v4, v5
	v_lshl_add_u64 v[4:5], v[152:153], 1, s[18:19]
	v_cvt_pk_bf16_f32 v2, v2, v3
	v_cvt_pk_bf16_f32 v3, v8, v9
	global_store_dwordx4 v[4:5], v[0:3], off
	s_mov_b64 s[18:19], s[16:17]
	s_cbranch_vccz .LBB0_978
	s_waitcnt vmcnt(0)
	s_cmpk_gt_u32 s31, 0xff
	s_cbranch_scc1 .LBB0_989
	s_barrier

.LBB0_1209:
	s_add_u32 s30, s4, s2
	s_addc_u32 s31, s5, s3
	v_add_u32_e32 v4, s60, v193
	s_add_u32 s38, s30, 0x3280c100
	ds_read_b128 v[8:11], v4
	ds_read_b128 v[12:15], v4 offset:1024
	ds_read_b128 v[0:3], v4 offset:2048
	ds_read_b128 v[4:7], v4 offset:3072
	s_addc_u32 s39, s31, 0
	s_add_u32 s71, s11, s2
	s_addc_u32 s72, s69, s3
	s_cmpk_eq_i32 s2, 0x700
	s_cselect_b64 vcc, -1, 0
	s_and_b64 s[30:31], vcc, exec
	s_cselect_b32 s39, s9, s39
	s_cselect_b32 s38, s8, s38
	s_cselect_b32 s31, s67, s72
	s_cselect_b32 s30, s68, s71
	v_lshl_add_u64 v[16:17], v[176:177], 0, s[2:3]
	s_add_i32 m0, s29, 0xc000
	ds_read_b128 v[202:205], v195
	ds_read_b128 v[206:209], v195 offset:1024
	ds_read_b128 v[210:213], v195 offset:2048
	ds_read_b128 v[214:217], v195 offset:3072
	ds_read_b128 v[224:227], v195 offset:4096
	ds_read_b128 v[228:231], v195 offset:5120
	ds_read_b128 v[232:235], v195 offset:6144
	ds_read_b128 v[236:239], v195 offset:7168
	global_load_lds_dwordx4 v[16:17], off
	v_lshl_add_u64 v[16:17], v[174:175], 0, s[2:3]
	s_add_i32 m0, s29, 0xe000
	s_nop 0
	global_load_lds_dwordx4 v[16:17], off
	s_waitcnt lgkmcnt(8)
	s_barrier
	s_waitcnt lgkmcnt(0)
	s_waitcnt lgkmcnt(0)
	v_mfma_scale_f32_16x16x128_f8f6f4 v[156:159], v[8:15], v[202:209], v[156:159], v188, v188 op_sel_hi:[0,0,0]
	v_mfma_scale_f32_16x16x128_f8f6f4 v[152:155], v[0:7], v[202:209], v[152:155], v188, v188 op_sel_hi:[0,0,0]
	v_mfma_scale_f32_16x16x128_f8f6f4 v[140:143], v[8:15], v[210:217], v[140:143], v188, v188 op_sel_hi:[0,0,0]
	v_mfma_scale_f32_16x16x128_f8f6f4 v[136:139], v[0:7], v[210:217], v[136:139], v188, v188 op_sel_hi:[0,0,0]
	v_mfma_scale_f32_16x16x128_f8f6f4 v[124:127], v[8:15], v[224:231], v[124:127], v188, v188 op_sel_hi:[0,0,0]
	v_mfma_scale_f32_16x16x128_f8f6f4 v[120:123], v[0:7], v[224:231], v[120:123], v188, v188 op_sel_hi:[0,0,0]
	v_mfma_scale_f32_16x16x128_f8f6f4 v[108:111], v[8:15], v[232:239], v[108:111], v188, v188 op_sel_hi:[0,0,0]
	v_mfma_scale_f32_16x16x128_f8f6f4 v[104:107], v[0:7], v[232:239], v[104:107], v188, v188 op_sel_hi:[0,0,0]
	s_barrier
	s_add_i32 s71, s60, s50
	v_add_u32_e32 v20, s61, v193
	v_lshl_add_u64 v[178:179], s[30:31], 0, v[162:163]
	s_mov_b32 m0, s71
	ds_read_b128 v[24:27], v20
	ds_read_b128 v[28:31], v20 offset:1024
	ds_read_b128 v[16:19], v20 offset:2048
	ds_read_b128 v[20:23], v20 offset:3072
	global_load_lds_dwordx4 v[178:179], off
	v_lshl_add_u64 v[180:181], s[30:31], 0, v[164:165]
	s_add_i32 m0, s71, 0x2000
	s_nop 0
	global_load_lds_dwordx4 v[180:181], off
	s_barrier
	s_waitcnt lgkmcnt(0)
	s_waitcnt lgkmcnt(0)
	v_mfma_scale_f32_16x16x128_f8f6f4 v[148:151], v[24:31], v[202:209], v[148:151], v188, v188 op_sel_hi:[0,0,0]
	v_mfma_scale_f32_16x16x128_f8f6f4 v[144:147], v[16:23], v[202:209], v[144:147], v188, v188 op_sel_hi:[0,0,0]
	v_mfma_scale_f32_16x16x128_f8f6f4 v[132:135], v[24:31], v[210:217], v[132:135], v188, v188 op_sel_hi:[0,0,0]
	v_mfma_scale_f32_16x16x128_f8f6f4 v[128:131], v[16:23], v[210:217], v[128:131], v188, v188 op_sel_hi:[0,0,0]
	v_mfma_scale_f32_16x16x128_f8f6f4 v[116:119], v[24:31], v[224:231], v[116:119], v188, v188 op_sel_hi:[0,0,0]
	v_mfma_scale_f32_16x16x128_f8f6f4 v[112:115], v[16:23], v[224:231], v[112:115], v188, v188 op_sel_hi:[0,0,0]
	v_mfma_scale_f32_16x16x128_f8f6f4 v[100:103], v[24:31], v[232:239], v[100:103], v188, v188 op_sel_hi:[0,0,0]
	v_mfma_scale_f32_16x16x128_f8f6f4 v[96:99], v[16:23], v[232:239], v[96:99], v188, v188 op_sel_hi:[0,0,0]
	s_mov_b32 m0, s29
	v_cndmask_b32_e32 v160, v201, v197, vcc
	s_barrier
	ds_read_b128 v[202:205], v195 offset:16384
	ds_read_b128 v[206:209], v195 offset:17408
	ds_read_b128 v[210:213], v195 offset:18432
	ds_read_b128 v[214:217], v195 offset:19456
	ds_read_b128 v[224:227], v195 offset:20480
	ds_read_b128 v[228:231], v195 offset:21504
	ds_read_b128 v[232:235], v195 offset:22528
	ds_read_b128 v[236:239], v195 offset:23552
	v_cndmask_b32_e32 v182, v172, v198, vcc
	global_load_lds_dwordx4 v160, s[38:39]
	s_mov_b32 m0, s51
	v_mov_b32_e32 v183, v161
	global_load_lds_dwordx4 v182, s[38:39]
	s_barrier
	s_waitcnt lgkmcnt(0)
	v_lshl_add_u64 v[184:185], s[38:39], 0, v[160:161]
	v_lshl_add_u64 v[182:183], s[38:39], 0, v[182:183]
	s_waitcnt lgkmcnt(0)
	v_mfma_scale_f32_16x16x128_f8f6f4 v[92:95], v[8:15], v[202:209], v[92:95], v188, v188 op_sel_hi:[0,0,0]
	v_mfma_scale_f32_16x16x128_f8f6f4 v[88:91], v[0:7], v[202:209], v[88:91], v188, v188 op_sel_hi:[0,0,0]
	v_mfma_scale_f32_16x16x128_f8f6f4 v[76:79], v[8:15], v[210:217], v[76:79], v188, v188 op_sel_hi:[0,0,0]
	v_mfma_scale_f32_16x16x128_f8f6f4 v[72:75], v[0:7], v[210:217], v[72:75], v188, v188 op_sel_hi:[0,0,0]
	v_mfma_scale_f32_16x16x128_f8f6f4 v[60:63], v[8:15], v[224:231], v[60:63], v188, v188 op_sel_hi:[0,0,0]
	v_mfma_scale_f32_16x16x128_f8f6f4 v[56:59], v[0:7], v[224:231], v[56:59], v188, v188 op_sel_hi:[0,0,0]
	v_mfma_scale_f32_16x16x128_f8f6f4 v[36:39], v[8:15], v[232:239], v[36:39], v188, v188 op_sel_hi:[0,0,0]
	v_mfma_scale_f32_16x16x128_f8f6f4 v[32:35], v[0:7], v[232:239], v[32:35], v188, v188 op_sel_hi:[0,0,0]
	s_barrier
	s_add_u32 s72, s30, 0x40000
	s_addc_u32 s73, s31, 0
	s_add_i32 s71, s61, s50
	v_lshl_add_u64 v[0:1], s[72:73], 0, v[162:163]
	s_mov_b32 m0, s71
	s_nop 0
	global_load_lds_dwordx4 v[0:1], off
	v_lshl_add_u64 v[0:1], s[72:73], 0, v[164:165]
	s_add_i32 m0, s71, 0x2000
	s_nop 0
	global_load_lds_dwordx4 v[0:1], off
	s_waitcnt vmcnt(6)
	s_barrier
	v_mfma_scale_f32_16x16x128_f8f6f4 v[84:87], v[24:31], v[202:209], v[84:87], v188, v188 op_sel_hi:[0,0,0]
	v_mfma_scale_f32_16x16x128_f8f6f4 v[80:83], v[16:23], v[202:209], v[80:83], v188, v188 op_sel_hi:[0,0,0]
	v_mfma_scale_f32_16x16x128_f8f6f4 v[68:71], v[24:31], v[210:217], v[68:71], v188, v188 op_sel_hi:[0,0,0]
	v_mfma_scale_f32_16x16x128_f8f6f4 v[64:67], v[16:23], v[210:217], v[64:67], v188, v188 op_sel_hi:[0,0,0]
	v_mfma_scale_f32_16x16x128_f8f6f4 v[52:55], v[24:31], v[224:231], v[52:55], v188, v188 op_sel_hi:[0,0,0]
	v_mfma_scale_f32_16x16x128_f8f6f4 v[40:43], v[16:23], v[224:231], v[40:43], v188, v188 op_sel_hi:[0,0,0]
	v_mfma_scale_f32_16x16x128_f8f6f4 v[48:51], v[24:31], v[232:239], v[48:51], v188, v188 op_sel_hi:[0,0,0]
	v_mfma_scale_f32_16x16x128_f8f6f4 v[44:47], v[16:23], v[232:239], v[44:47], v188, v188 op_sel_hi:[0,0,0]
	s_add_i32 s71, 0, 0x18000
	v_add_u32_e32 v12, s71, v193
	s_barrier
	ds_read_b128 v[0:3], v12
	ds_read_b128 v[4:7], v12 offset:1024
	ds_read_b128 v[8:11], v12 offset:2048
	ds_read_b128 v[12:15], v12 offset:3072
	s_mov_b32 m0, s52
	v_cndmask_b32_e32 v160, v170, v199, vcc
	ds_read_b128 v[16:19], v195 offset:32768
	ds_read_b128 v[20:23], v195 offset:33792
	ds_read_b128 v[24:27], v195 offset:34816
	ds_read_b128 v[28:31], v195 offset:35840
	ds_read_b128 v[202:205], v195 offset:36864
	ds_read_b128 v[206:209], v195 offset:37888
	ds_read_b128 v[210:213], v195 offset:38912
	ds_read_b128 v[214:217], v195 offset:39936
	v_cndmask_b32_e32 v169, v168, v200, vcc
	global_load_lds_dwordx4 v160, s[38:39]
	s_mov_b32 m0, s53
	s_nop 0
	global_load_lds_dwordx4 v169, s[38:39]
	s_waitcnt lgkmcnt(8)
	s_barrier
	s_waitcnt lgkmcnt(0)
	s_waitcnt lgkmcnt(0)
	v_mfma_scale_f32_16x16x128_f8f6f4 v[156:159], v[0:7], v[16:23], v[156:159], v188, v188 op_sel_hi:[0,0,0]
	v_mfma_scale_f32_16x16x128_f8f6f4 v[152:155], v[8:15], v[16:23], v[152:155], v188, v188 op_sel_hi:[0,0,0]
	v_mfma_scale_f32_16x16x128_f8f6f4 v[140:143], v[0:7], v[24:31], v[140:143], v188, v188 op_sel_hi:[0,0,0]
	v_mfma_scale_f32_16x16x128_f8f6f4 v[136:139], v[8:15], v[24:31], v[136:139], v188, v188 op_sel_hi:[0,0,0]
	v_mfma_scale_f32_16x16x128_f8f6f4 v[124:127], v[0:7], v[202:209], v[124:127], v188, v188 op_sel_hi:[0,0,0]
	v_mfma_scale_f32_16x16x128_f8f6f4 v[120:123], v[8:15], v[202:209], v[120:123], v188, v188 op_sel_hi:[0,0,0]
	v_mfma_scale_f32_16x16x128_f8f6f4 v[108:111], v[0:7], v[210:217], v[108:111], v188, v188 op_sel_hi:[0,0,0]
	v_mfma_scale_f32_16x16x128_f8f6f4 v[104:107], v[8:15], v[210:217], v[104:107], v188, v188 op_sel_hi:[0,0,0]
	s_barrier
	s_add_i32 s38, 0, 0x1c000
	s_add_i32 s39, s71, s50
	v_add_u32_e32 v160, s38, v193
	v_lshl_add_u64 v[178:179], v[178:179], 0, s[16:17]
	s_mov_b32 m0, s39
	ds_read_b128 v[224:227], v160
	ds_read_b128 v[228:231], v160 offset:1024
	ds_read_b128 v[232:235], v160 offset:2048
	ds_read_b128 v[236:239], v160 offset:3072
	global_load_lds_dwordx4 v[178:179], off
	v_lshl_add_u64 v[178:179], v[180:181], 0, s[16:17]
	s_add_i32 m0, s39, 0x2000
	s_nop 0
	global_load_lds_dwordx4 v[178:179], off
	s_barrier
	s_waitcnt lgkmcnt(0)
	s_waitcnt lgkmcnt(0)
	v_mfma_scale_f32_16x16x128_f8f6f4 v[148:151], v[224:231], v[16:23], v[148:151], v188, v188 op_sel_hi:[0,0,0]
	v_mfma_scale_f32_16x16x128_f8f6f4 v[144:147], v[232:239], v[16:23], v[144:147], v188, v188 op_sel_hi:[0,0,0]
	v_mfma_scale_f32_16x16x128_f8f6f4 v[132:135], v[224:231], v[24:31], v[132:135], v188, v188 op_sel_hi:[0,0,0]
	v_mfma_scale_f32_16x16x128_f8f6f4 v[128:131], v[232:239], v[24:31], v[128:131], v188, v188 op_sel_hi:[0,0,0]
	v_mfma_scale_f32_16x16x128_f8f6f4 v[116:119], v[224:231], v[202:209], v[116:119], v188, v188 op_sel_hi:[0,0,0]
	v_mfma_scale_f32_16x16x128_f8f6f4 v[112:115], v[232:239], v[202:209], v[112:115], v188, v188 op_sel_hi:[0,0,0]
	v_mfma_scale_f32_16x16x128_f8f6f4 v[100:103], v[224:231], v[210:217], v[100:103], v188, v188 op_sel_hi:[0,0,0]
	v_mfma_scale_f32_16x16x128_f8f6f4 v[96:99], v[232:239], v[210:217], v[96:99], v188, v188 op_sel_hi:[0,0,0]
	s_mov_b32 m0, s57
	v_lshl_add_u64 v[178:179], v[184:185], 0, s[16:17]
	s_barrier
	ds_read_b128 v[16:19], v195 offset:49152
	ds_read_b128 v[20:23], v195 offset:50176
	ds_read_b128 v[24:27], v195 offset:51200
	ds_read_b128 v[28:31], v195 offset:52224
	ds_read_b128 v[202:205], v195 offset:53248
	ds_read_b128 v[206:209], v195 offset:54272
	ds_read_b128 v[210:213], v195 offset:55296
	ds_read_b128 v[214:217], v195 offset:56320
	global_load_lds_dwordx4 v[178:179], off
	v_lshl_add_u64 v[178:179], v[182:183], 0, s[16:17]
	s_mov_b32 m0, s58
	s_nop 0
	global_load_lds_dwordx4 v[178:179], off
	s_barrier
	s_waitcnt lgkmcnt(0)
	s_waitcnt lgkmcnt(0)
	v_mfma_scale_f32_16x16x128_f8f6f4 v[92:95], v[0:7], v[16:23], v[92:95], v188, v188 op_sel_hi:[0,0,0]
	v_mfma_scale_f32_16x16x128_f8f6f4 v[88:91], v[8:15], v[16:23], v[88:91], v188, v188 op_sel_hi:[0,0,0]
	v_mfma_scale_f32_16x16x128_f8f6f4 v[76:79], v[0:7], v[24:31], v[76:79], v188, v188 op_sel_hi:[0,0,0]
	v_mfma_scale_f32_16x16x128_f8f6f4 v[72:75], v[8:15], v[24:31], v[72:75], v188, v188 op_sel_hi:[0,0,0]
	v_mfma_scale_f32_16x16x128_f8f6f4 v[60:63], v[0:7], v[202:209], v[60:63], v188, v188 op_sel_hi:[0,0,0]
	v_mfma_scale_f32_16x16x128_f8f6f4 v[56:59], v[8:15], v[202:209], v[56:59], v188, v188 op_sel_hi:[0,0,0]
	v_mfma_scale_f32_16x16x128_f8f6f4 v[36:39], v[0:7], v[210:217], v[36:39], v188, v188 op_sel_hi:[0,0,0]
	v_mfma_scale_f32_16x16x128_f8f6f4 v[32:35], v[8:15], v[210:217], v[32:35], v188, v188 op_sel_hi:[0,0,0]
	s_barrier
	s_add_u32 s30, s30, 0x40080
	s_addc_u32 s31, s31, 0
	s_add_i32 s38, s38, s50
	v_lshl_add_u64 v[0:1], s[30:31], 0, v[162:163]
	s_mov_b32 m0, s38
	s_nop 0
	global_load_lds_dwordx4 v[0:1], off
	v_lshl_add_u64 v[0:1], s[30:31], 0, v[164:165]
	s_add_i32 m0, s38, 0x2000
	s_nop 0
	global_load_lds_dwordx4 v[0:1], off
	s_waitcnt vmcnt(6)
	s_barrier
	v_mfma_scale_f32_16x16x128_f8f6f4 v[84:87], v[224:231], v[16:23], v[84:87], v188, v188 op_sel_hi:[0,0,0]
	v_mfma_scale_f32_16x16x128_f8f6f4 v[80:83], v[232:239], v[16:23], v[80:83], v188, v188 op_sel_hi:[0,0,0]
	v_mfma_scale_f32_16x16x128_f8f6f4 v[68:71], v[224:231], v[24:31], v[68:71], v188, v188 op_sel_hi:[0,0,0]
	v_mfma_scale_f32_16x16x128_f8f6f4 v[64:67], v[232:239], v[24:31], v[64:67], v188, v188 op_sel_hi:[0,0,0]
	v_mfma_scale_f32_16x16x128_f8f6f4 v[52:55], v[224:231], v[202:209], v[52:55], v188, v188 op_sel_hi:[0,0,0]
	v_mfma_scale_f32_16x16x128_f8f6f4 v[40:43], v[232:239], v[202:209], v[40:43], v188, v188 op_sel_hi:[0,0,0]
	v_mfma_scale_f32_16x16x128_f8f6f4 v[48:51], v[224:231], v[210:217], v[48:51], v188, v188 op_sel_hi:[0,0,0]
	v_mfma_scale_f32_16x16x128_f8f6f4 v[44:47], v[232:239], v[210:217], v[44:47], v188, v188 op_sel_hi:[0,0,0]
	s_add_i32 s70, s70, 2
	s_add_u32 s2, s2, 0x100
	s_addc_u32 s3, s3, 0
	s_cmp_gt_u32 s70, 13
	s_barrier
	s_cbranch_scc1 .LBB0_1203

.LBB0_1347:
	ds_read_b128 v[12:15], v156
	ds_read_b128 v[16:19], v156 offset:1024
	ds_read_b128 v[28:31], v156 offset:2048
	ds_read_b128 v[32:35], v156 offset:3072
	s_add_u32 s22, s43, s21
	s_addc_u32 s23, s44, 0
	s_and_b64 s[24:25], s[2:3], exec
	s_cselect_b32 s29, s23, s31
	s_cselect_b32 s28, s22, s30
	s_add_u32 s24, s45, s67
	s_addc_u32 s25, s46, 0
	s_and_b64 s[2:3], s[2:3], exec
	s_cselect_b32 s3, s25, s39
	s_cselect_b32 s2, s24, s38
	s_add_u32 s70, s30, 0x10080
	s_addc_u32 s71, s31, 0
	s_mov_b32 m0, s57
	v_lshl_add_u64 v[44:45], s[70:71], 0, v[134:135]
	ds_read_b128 v[4:7], v157
	ds_read_b128 v[8:11], v157 offset:1024
	ds_read_b128 v[20:23], v157 offset:2048
	ds_read_b128 v[24:27], v157 offset:3072
	ds_read_b128 v[36:39], v157 offset:4096
	ds_read_b128 v[40:43], v157 offset:5120
	ds_read_b128 v[52:55], v157 offset:6144
	ds_read_b128 v[56:59], v157 offset:7168
	global_load_lds_dwordx4 v[44:45], off
	v_lshl_add_u64 v[44:45], s[70:71], 0, v[138:139]
	s_mov_b32 m0, s58
	s_nop 0
	global_load_lds_dwordx4 v[44:45], off
	s_waitcnt lgkmcnt(8)
	s_barrier
	s_waitcnt lgkmcnt(0)
	v_mov_b64_e32 v[110:111], v[2:3]
	v_mov_b64_e32 v[114:115], v[2:3]
	v_mov_b64_e32 v[106:107], v[2:3]
	v_mov_b64_e32 v[102:103], v[2:3]
	v_mov_b64_e32 v[82:83], v[2:3]
	v_mov_b64_e32 v[78:79], v[2:3]
	v_mov_b64_e32 v[50:51], v[2:3]
	v_mov_b64_e32 v[46:47], v[2:3]
	v_mov_b64_e32 v[108:109], v[0:1]
	v_mov_b64_e32 v[112:113], v[0:1]
	v_mov_b64_e32 v[104:105], v[0:1]
	v_mov_b64_e32 v[100:101], v[0:1]
	v_mov_b64_e32 v[80:81], v[0:1]
	v_mov_b64_e32 v[76:77], v[0:1]
	v_mov_b64_e32 v[48:49], v[0:1]
	v_mov_b64_e32 v[44:45], v[0:1]
	s_waitcnt lgkmcnt(0)
	v_mfma_scale_f32_16x16x128_f8f6f4 v[108:111], v[12:19], v[4:11], v[108:111], v153, v153 op_sel_hi:[0,0,0]
	v_mfma_scale_f32_16x16x128_f8f6f4 v[112:115], v[28:35], v[4:11], v[112:115], v153, v153 op_sel_hi:[0,0,0]
	v_mfma_scale_f32_16x16x128_f8f6f4 v[104:107], v[12:19], v[20:27], v[104:107], v153, v153 op_sel_hi:[0,0,0]
	v_mfma_scale_f32_16x16x128_f8f6f4 v[100:103], v[28:35], v[20:27], v[100:103], v153, v153 op_sel_hi:[0,0,0]
	v_mfma_scale_f32_16x16x128_f8f6f4 v[80:83], v[12:19], v[36:43], v[80:83], v153, v153 op_sel_hi:[0,0,0]
	v_mfma_scale_f32_16x16x128_f8f6f4 v[76:79], v[28:35], v[36:43], v[76:79], v153, v153 op_sel_hi:[0,0,0]
	v_mfma_scale_f32_16x16x128_f8f6f4 v[48:51], v[12:19], v[52:59], v[48:51], v153, v153 op_sel_hi:[0,0,0]
	v_mfma_scale_f32_16x16x128_f8f6f4 v[44:47], v[28:35], v[52:59], v[44:47], v153, v153 op_sel_hi:[0,0,0]
	s_barrier
	v_lshl_add_u64 v[144:145], s[38:39], 0, v[132:133]
	s_add_i32 s71, s56, s47
	v_lshl_add_u64 v[60:61], v[144:145], 0, s[6:7]
	s_mov_b32 m0, s71
	v_lshl_add_u64 v[146:147], s[38:39], 0, v[136:137]
	s_add_i32 s69, s71, 0x2000
	ds_read_b128 v[160:163], v158
	ds_read_b128 v[164:167], v158 offset:1024
	ds_read_b128 v[168:171], v158 offset:2048
	ds_read_b128 v[172:175], v158 offset:3072
	global_load_lds_dwordx4 v[60:61], off
	v_lshl_add_u64 v[60:61], v[146:147], 0, s[6:7]
	s_mov_b32 m0, s69
	s_nop 0
	global_load_lds_dwordx4 v[60:61], off
	s_barrier
	s_waitcnt lgkmcnt(0)
	v_mov_b64_e32 v[126:127], v[2:3]
	v_mov_b64_e32 v[130:131], v[2:3]
	v_mov_b64_e32 v[122:123], v[2:3]
	v_mov_b64_e32 v[118:119], v[2:3]
	v_mov_b64_e32 v[98:99], v[2:3]
	v_mov_b64_e32 v[94:95], v[2:3]
	v_mov_b64_e32 v[66:67], v[2:3]
	v_mov_b64_e32 v[62:63], v[2:3]
	v_mov_b64_e32 v[124:125], v[0:1]
	v_mov_b64_e32 v[128:129], v[0:1]
	v_mov_b64_e32 v[120:121], v[0:1]
	v_mov_b64_e32 v[116:117], v[0:1]
	v_mov_b64_e32 v[96:97], v[0:1]
	v_mov_b64_e32 v[92:93], v[0:1]
	v_mov_b64_e32 v[64:65], v[0:1]
	v_mov_b64_e32 v[60:61], v[0:1]
	s_waitcnt lgkmcnt(0)
	v_mfma_scale_f32_16x16x128_f8f6f4 v[124:127], v[160:167], v[4:11], v[124:127], v153, v153 op_sel_hi:[0,0,0]
	v_mfma_scale_f32_16x16x128_f8f6f4 v[128:131], v[168:175], v[4:11], v[128:131], v153, v153 op_sel_hi:[0,0,0]
	v_mfma_scale_f32_16x16x128_f8f6f4 v[120:123], v[160:167], v[20:27], v[120:123], v153, v153 op_sel_hi:[0,0,0]
	v_mfma_scale_f32_16x16x128_f8f6f4 v[116:119], v[168:175], v[20:27], v[116:119], v153, v153 op_sel_hi:[0,0,0]
	v_mfma_scale_f32_16x16x128_f8f6f4 v[96:99], v[160:167], v[36:43], v[96:99], v153, v153 op_sel_hi:[0,0,0]
	v_mfma_scale_f32_16x16x128_f8f6f4 v[92:95], v[168:175], v[36:43], v[92:95], v153, v153 op_sel_hi:[0,0,0]
	v_mfma_scale_f32_16x16x128_f8f6f4 v[64:67], v[160:167], v[52:59], v[64:67], v153, v153 op_sel_hi:[0,0,0]
	v_mfma_scale_f32_16x16x128_f8f6f4 v[60:63], v[168:175], v[52:59], v[60:63], v153, v153 op_sel_hi:[0,0,0]
	v_lshl_add_u64 v[148:149], s[30:31], 0, v[134:135]
	s_mov_b32 m0, s27
	v_lshl_add_u64 v[4:5], v[148:149], 0, s[6:7]
	v_lshl_add_u64 v[150:151], s[30:31], 0, v[138:139]
	s_barrier
	ds_read_b128 v[52:55], v157 offset:16384
	ds_read_b128 v[56:59], v157 offset:17408
	ds_read_b128 v[176:179], v157 offset:18432
	ds_read_b128 v[180:183], v157 offset:19456
	ds_read_b128 v[184:187], v157 offset:20480
	ds_read_b128 v[188:191], v157 offset:21504
	ds_read_b128 v[192:195], v157 offset:22528
	ds_read_b128 v[196:199], v157 offset:23552
	global_load_lds_dwordx4 v[4:5], off
	v_lshl_add_u64 v[4:5], v[150:151], 0, s[6:7]
	s_mov_b32 m0, s48
	s_nop 0
	global_load_lds_dwordx4 v[4:5], off
	s_barrier
	s_waitcnt lgkmcnt(0)
	v_mov_b64_e32 v[74:75], v[2:3]
	v_mov_b64_e32 v[70:71], v[2:3]
	v_mov_b64_e32 v[42:43], v[2:3]
	v_mov_b64_e32 v[38:39], v[2:3]
	v_mov_b64_e32 v[26:27], v[2:3]
	v_mov_b64_e32 v[22:23], v[2:3]
	v_mov_b64_e32 v[10:11], v[2:3]
	v_mov_b64_e32 v[6:7], v[2:3]
	v_mov_b64_e32 v[72:73], v[0:1]
	v_mov_b64_e32 v[68:69], v[0:1]
	v_mov_b64_e32 v[40:41], v[0:1]
	v_mov_b64_e32 v[36:37], v[0:1]
	v_mov_b64_e32 v[24:25], v[0:1]
	v_mov_b64_e32 v[20:21], v[0:1]
	v_mov_b64_e32 v[8:9], v[0:1]
	v_mov_b64_e32 v[4:5], v[0:1]
	s_waitcnt lgkmcnt(0)
	v_mfma_scale_f32_16x16x128_f8f6f4 v[72:75], v[12:19], v[52:59], v[72:75], v153, v153 op_sel_hi:[0,0,0]
	v_mfma_scale_f32_16x16x128_f8f6f4 v[68:71], v[28:35], v[52:59], v[68:71], v153, v153 op_sel_hi:[0,0,0]
	v_mfma_scale_f32_16x16x128_f8f6f4 v[40:43], v[12:19], v[176:183], v[40:43], v153, v153 op_sel_hi:[0,0,0]
	v_mfma_scale_f32_16x16x128_f8f6f4 v[36:39], v[28:35], v[176:183], v[36:39], v153, v153 op_sel_hi:[0,0,0]
	v_mfma_scale_f32_16x16x128_f8f6f4 v[24:27], v[12:19], v[184:191], v[24:27], v153, v153 op_sel_hi:[0,0,0]
	v_mfma_scale_f32_16x16x128_f8f6f4 v[20:23], v[28:35], v[184:191], v[20:23], v153, v153 op_sel_hi:[0,0,0]
	v_mfma_scale_f32_16x16x128_f8f6f4 v[8:11], v[12:19], v[192:199], v[8:11], v153, v153 op_sel_hi:[0,0,0]
	v_mfma_scale_f32_16x16x128_f8f6f4 v[4:7], v[28:35], v[192:199], v[4:7], v153, v153 op_sel_hi:[0,0,0]
	s_barrier
	s_add_u32 s74, s38, 0x10100
	s_addc_u32 s75, s39, 0
	s_add_i32 s72, s59, s47
	v_lshl_add_u64 v[12:13], s[74:75], 0, v[132:133]
	s_mov_b32 m0, s72
	s_add_i32 s70, s72, 0x2000
	global_load_lds_dwordx4 v[12:13], off
	v_lshl_add_u64 v[12:13], s[74:75], 0, v[136:137]
	s_mov_b32 m0, s70
	s_nop 0
	global_load_lds_dwordx4 v[12:13], off
	s_waitcnt vmcnt(6)
	s_barrier
	v_mov_b64_e32 v[90:91], v[2:3]
	v_mov_b64_e32 v[86:87], v[2:3]
	v_mov_b64_e32 v[88:89], v[0:1]
	v_mov_b64_e32 v[84:85], v[0:1]
	v_mfma_scale_f32_16x16x128_f8f6f4 v[88:91], v[160:167], v[52:59], v[88:91], v153, v153 op_sel_hi:[0,0,0]
	v_mfma_scale_f32_16x16x128_f8f6f4 v[84:87], v[168:175], v[52:59], v[84:87], v153, v153 op_sel_hi:[0,0,0]
	v_mov_b64_e32 v[58:59], v[2:3]
	v_mov_b64_e32 v[54:55], v[2:3]
	v_mov_b64_e32 v[34:35], v[2:3]
	v_mov_b64_e32 v[30:31], v[2:3]
	v_mov_b64_e32 v[18:19], v[2:3]
	v_mov_b64_e32 v[14:15], v[2:3]
	v_mov_b64_e32 v[56:57], v[0:1]
	v_mov_b64_e32 v[52:53], v[0:1]
	v_mov_b64_e32 v[32:33], v[0:1]
	v_mov_b64_e32 v[28:29], v[0:1]
	v_mov_b64_e32 v[16:17], v[0:1]
	v_mov_b64_e32 v[12:13], v[0:1]
	v_mfma_scale_f32_16x16x128_f8f6f4 v[56:59], v[160:167], v[176:183], v[56:59], v153, v153 op_sel_hi:[0,0,0]
	v_mfma_scale_f32_16x16x128_f8f6f4 v[52:55], v[168:175], v[176:183], v[52:55], v153, v153 op_sel_hi:[0,0,0]
	v_mfma_scale_f32_16x16x128_f8f6f4 v[32:35], v[160:167], v[184:191], v[32:35], v153, v153 op_sel_hi:[0,0,0]
	v_mfma_scale_f32_16x16x128_f8f6f4 v[28:31], v[168:175], v[184:191], v[28:31], v153, v153 op_sel_hi:[0,0,0]
	v_mfma_scale_f32_16x16x128_f8f6f4 v[16:19], v[160:167], v[192:199], v[16:19], v153, v153 op_sel_hi:[0,0,0]
	v_mfma_scale_f32_16x16x128_f8f6f4 v[12:15], v[168:175], v[192:199], v[12:15], v153, v153 op_sel_hi:[0,0,0]
	s_add_i32 s73, 0, 0x18000
	v_add_u32_e32 v159, s73, v155
	s_barrier
	ds_read_b128 v[162:165], v159
	ds_read_b128 v[166:169], v159 offset:1024
	ds_read_b128 v[170:173], v159 offset:2048
	ds_read_b128 v[174:177], v159 offset:3072
	s_add_u32 s74, s30, 0x10100
	s_addc_u32 s75, s31, 0
	s_mov_b32 m0, s49
	v_lshl_add_u64 v[160:161], s[74:75], 0, v[134:135]
	ds_read_b128 v[178:181], v157 offset:32768
	ds_read_b128 v[182:185], v157 offset:33792
	ds_read_b128 v[186:189], v157 offset:34816
	ds_read_b128 v[190:193], v157 offset:35840
	ds_read_b128 v[194:197], v157 offset:36864
	ds_read_b128 v[198:201], v157 offset:37888
	ds_read_b128 v[202:205], v157 offset:38912
	ds_read_b128 v[206:209], v157 offset:39936
	global_load_lds_dwordx4 v[160:161], off
	v_lshl_add_u64 v[160:161], s[74:75], 0, v[138:139]
	s_mov_b32 m0, s50
	s_nop 0
	global_load_lds_dwordx4 v[160:161], off
	s_waitcnt lgkmcnt(8)
	s_barrier
	s_waitcnt lgkmcnt(0)
	s_waitcnt lgkmcnt(0)
	v_mfma_scale_f32_16x16x128_f8f6f4 v[108:111], v[162:169], v[178:185], v[108:111], v153, v153 op_sel_hi:[0,0,0]
	v_mfma_scale_f32_16x16x128_f8f6f4 v[112:115], v[170:177], v[178:185], v[112:115], v153, v153 op_sel_hi:[0,0,0]
	v_mfma_scale_f32_16x16x128_f8f6f4 v[104:107], v[162:169], v[186:193], v[104:107], v153, v153 op_sel_hi:[0,0,0]
	v_mfma_scale_f32_16x16x128_f8f6f4 v[100:103], v[170:177], v[186:193], v[100:103], v153, v153 op_sel_hi:[0,0,0]
	v_mfma_scale_f32_16x16x128_f8f6f4 v[80:83], v[162:169], v[194:201], v[80:83], v153, v153 op_sel_hi:[0,0,0]
	v_mfma_scale_f32_16x16x128_f8f6f4 v[76:79], v[170:177], v[194:201], v[76:79], v153, v153 op_sel_hi:[0,0,0]
	v_mfma_scale_f32_16x16x128_f8f6f4 v[48:51], v[162:169], v[202:209], v[48:51], v153, v153 op_sel_hi:[0,0,0]
	v_mfma_scale_f32_16x16x128_f8f6f4 v[44:47], v[170:177], v[202:209], v[44:47], v153, v153 op_sel_hi:[0,0,0]
	s_barrier
	s_add_i32 s75, 0, 0x1c000
	s_add_i32 s74, s73, s47
	v_add_u32_e32 v160, s75, v155
	v_lshl_add_u64 v[144:145], v[144:145], 0, s[16:17]
	s_mov_b32 m0, s74
	s_add_i32 s73, s74, 0x2000
	ds_read_b128 v[210:213], v160
	ds_read_b128 v[214:217], v160 offset:1024
	ds_read_b128 v[224:227], v160 offset:2048
	ds_read_b128 v[228:231], v160 offset:3072
	global_load_lds_dwordx4 v[144:145], off
	v_lshl_add_u64 v[144:145], v[146:147], 0, s[16:17]
	s_mov_b32 m0, s73
	s_nop 0
	global_load_lds_dwordx4 v[144:145], off
	s_barrier
	s_waitcnt lgkmcnt(0)
	s_waitcnt lgkmcnt(0)
	v_mfma_scale_f32_16x16x128_f8f6f4 v[124:127], v[210:217], v[178:185], v[124:127], v153, v153 op_sel_hi:[0,0,0]
	v_mfma_scale_f32_16x16x128_f8f6f4 v[128:131], v[224:231], v[178:185], v[128:131], v153, v153 op_sel_hi:[0,0,0]
	v_mfma_scale_f32_16x16x128_f8f6f4 v[120:123], v[210:217], v[186:193], v[120:123], v153, v153 op_sel_hi:[0,0,0]
	v_mfma_scale_f32_16x16x128_f8f6f4 v[116:119], v[224:231], v[186:193], v[116:119], v153, v153 op_sel_hi:[0,0,0]
	v_mfma_scale_f32_16x16x128_f8f6f4 v[96:99], v[210:217], v[194:201], v[96:99], v153, v153 op_sel_hi:[0,0,0]
	v_mfma_scale_f32_16x16x128_f8f6f4 v[92:95], v[224:231], v[194:201], v[92:95], v153, v153 op_sel_hi:[0,0,0]
	v_mfma_scale_f32_16x16x128_f8f6f4 v[64:67], v[210:217], v[202:209], v[64:67], v153, v153 op_sel_hi:[0,0,0]
	v_mfma_scale_f32_16x16x128_f8f6f4 v[60:63], v[224:231], v[202:209], v[60:63], v153, v153 op_sel_hi:[0,0,0]
	s_mov_b32 m0, s52
	v_lshl_add_u64 v[144:145], v[148:149], 0, s[16:17]
	s_barrier
	ds_read_b128 v[178:181], v157 offset:49152
	ds_read_b128 v[182:185], v157 offset:50176
	ds_read_b128 v[186:189], v157 offset:51200
	ds_read_b128 v[190:193], v157 offset:52224
	ds_read_b128 v[194:197], v157 offset:53248
	ds_read_b128 v[198:201], v157 offset:54272
	ds_read_b128 v[202:205], v157 offset:55296
	ds_read_b128 v[206:209], v157 offset:56320
	global_load_lds_dwordx4 v[144:145], off
	v_lshl_add_u64 v[144:145], v[150:151], 0, s[16:17]
	s_mov_b32 m0, s53
	s_nop 0
	global_load_lds_dwordx4 v[144:145], off
	s_barrier
	s_waitcnt lgkmcnt(0)
	s_waitcnt lgkmcnt(0)
	v_mfma_scale_f32_16x16x128_f8f6f4 v[72:75], v[162:169], v[178:185], v[72:75], v153, v153 op_sel_hi:[0,0,0]
	v_mfma_scale_f32_16x16x128_f8f6f4 v[68:71], v[170:177], v[178:185], v[68:71], v153, v153 op_sel_hi:[0,0,0]
	v_mfma_scale_f32_16x16x128_f8f6f4 v[40:43], v[162:169], v[186:193], v[40:43], v153, v153 op_sel_hi:[0,0,0]
	v_mfma_scale_f32_16x16x128_f8f6f4 v[36:39], v[170:177], v[186:193], v[36:39], v153, v153 op_sel_hi:[0,0,0]
	v_mfma_scale_f32_16x16x128_f8f6f4 v[24:27], v[162:169], v[194:201], v[24:27], v153, v153 op_sel_hi:[0,0,0]
	v_mfma_scale_f32_16x16x128_f8f6f4 v[20:23], v[170:177], v[194:201], v[20:23], v153, v153 op_sel_hi:[0,0,0]
	v_mfma_scale_f32_16x16x128_f8f6f4 v[8:11], v[162:169], v[202:209], v[8:11], v153, v153 op_sel_hi:[0,0,0]
	v_mfma_scale_f32_16x16x128_f8f6f4 v[4:7], v[170:177], v[202:209], v[4:7], v153, v153 op_sel_hi:[0,0,0]
	s_barrier
	s_add_u32 s76, s38, 0x10180
	s_addc_u32 s77, s39, 0
	s_add_i32 s39, s75, s47
	v_lshl_add_u64 v[144:145], s[76:77], 0, v[132:133]
	s_mov_b32 m0, s39
	s_add_i32 s38, s39, 0x2000
	global_load_lds_dwordx4 v[144:145], off
	v_lshl_add_u64 v[144:145], s[76:77], 0, v[136:137]
	s_mov_b32 m0, s38
	s_nop 0
	global_load_lds_dwordx4 v[144:145], off
	s_waitcnt vmcnt(6)
	s_barrier
	v_mfma_scale_f32_16x16x128_f8f6f4 v[88:91], v[210:217], v[178:185], v[88:91], v153, v153 op_sel_hi:[0,0,0]
	v_mfma_scale_f32_16x16x128_f8f6f4 v[84:87], v[224:231], v[178:185], v[84:87], v153, v153 op_sel_hi:[0,0,0]
	v_mfma_scale_f32_16x16x128_f8f6f4 v[56:59], v[210:217], v[186:193], v[56:59], v153, v153 op_sel_hi:[0,0,0]
	v_mfma_scale_f32_16x16x128_f8f6f4 v[52:55], v[224:231], v[186:193], v[52:55], v153, v153 op_sel_hi:[0,0,0]
	v_mfma_scale_f32_16x16x128_f8f6f4 v[32:35], v[210:217], v[194:201], v[32:35], v153, v153 op_sel_hi:[0,0,0]
	v_mfma_scale_f32_16x16x128_f8f6f4 v[28:31], v[224:231], v[194:201], v[28:31], v153, v153 op_sel_hi:[0,0,0]
	v_mfma_scale_f32_16x16x128_f8f6f4 v[16:19], v[210:217], v[202:209], v[16:19], v153, v153 op_sel_hi:[0,0,0]
	v_mfma_scale_f32_16x16x128_f8f6f4 v[12:15], v[224:231], v[202:209], v[12:15], v153, v153 op_sel_hi:[0,0,0]
	s_barrier
	ds_read_b128 v[162:165], v156
	ds_read_b128 v[166:169], v156 offset:1024
	ds_read_b128 v[170:173], v156 offset:2048
	ds_read_b128 v[174:177], v156 offset:3072
	s_add_u32 s30, s30, 0x10180
	s_addc_u32 s31, s31, 0
	s_mov_b32 m0, s57
	v_lshl_add_u64 v[144:145], s[30:31], 0, v[134:135]
	ds_read_b128 v[178:181], v157
	ds_read_b128 v[182:185], v157 offset:1024
	ds_read_b128 v[186:189], v157 offset:2048
	ds_read_b128 v[190:193], v157 offset:3072
	ds_read_b128 v[194:197], v157 offset:4096
	ds_read_b128 v[198:201], v157 offset:5120
	ds_read_b128 v[202:205], v157 offset:6144
	ds_read_b128 v[206:209], v157 offset:7168
	global_load_lds_dwordx4 v[144:145], off
	v_lshl_add_u64 v[144:145], s[30:31], 0, v[138:139]
	s_mov_b32 m0, s58
	s_nop 0
	global_load_lds_dwordx4 v[144:145], off
	s_waitcnt lgkmcnt(8)
	s_barrier
	s_waitcnt lgkmcnt(0)
	s_waitcnt lgkmcnt(0)
	v_mfma_scale_f32_16x16x128_f8f6f4 v[108:111], v[162:169], v[178:185], v[108:111], v153, v153 op_sel_hi:[0,0,0]
	v_mfma_scale_f32_16x16x128_f8f6f4 v[112:115], v[170:177], v[178:185], v[112:115], v153, v153 op_sel_hi:[0,0,0]
	v_mfma_scale_f32_16x16x128_f8f6f4 v[104:107], v[162:169], v[186:193], v[104:107], v153, v153 op_sel_hi:[0,0,0]
	v_mfma_scale_f32_16x16x128_f8f6f4 v[100:103], v[170:177], v[186:193], v[100:103], v153, v153 op_sel_hi:[0,0,0]
	v_mfma_scale_f32_16x16x128_f8f6f4 v[80:83], v[162:169], v[194:201], v[80:83], v153, v153 op_sel_hi:[0,0,0]
	v_mfma_scale_f32_16x16x128_f8f6f4 v[76:79], v[170:177], v[194:201], v[76:79], v153, v153 op_sel_hi:[0,0,0]
	v_mfma_scale_f32_16x16x128_f8f6f4 v[48:51], v[162:169], v[202:209], v[48:51], v153, v153 op_sel_hi:[0,0,0]
	v_mfma_scale_f32_16x16x128_f8f6f4 v[44:47], v[170:177], v[202:209], v[44:47], v153, v153 op_sel_hi:[0,0,0]
	s_barrier
	s_mov_b32 m0, s71
	v_lshl_add_u64 v[144:145], s[2:3], 0, v[132:133]
	ds_read_b128 v[210:213], v158
	ds_read_b128 v[214:217], v158 offset:1024
	ds_read_b128 v[224:227], v158 offset:2048
	ds_read_b128 v[228:231], v158 offset:3072
	global_load_lds_dwordx4 v[144:145], off
	v_lshl_add_u64 v[146:147], s[2:3], 0, v[136:137]
	s_mov_b32 m0, s69
	s_nop 0
	global_load_lds_dwordx4 v[146:147], off
	s_barrier
	s_waitcnt lgkmcnt(0)
	s_waitcnt lgkmcnt(0)
	v_mfma_scale_f32_16x16x128_f8f6f4 v[124:127], v[210:217], v[178:185], v[124:127], v153, v153 op_sel_hi:[0,0,0]
	v_mfma_scale_f32_16x16x128_f8f6f4 v[128:131], v[224:231], v[178:185], v[128:131], v153, v153 op_sel_hi:[0,0,0]
	v_mfma_scale_f32_16x16x128_f8f6f4 v[120:123], v[210:217], v[186:193], v[120:123], v153, v153 op_sel_hi:[0,0,0]
	v_mfma_scale_f32_16x16x128_f8f6f4 v[116:119], v[224:231], v[186:193], v[116:119], v153, v153 op_sel_hi:[0,0,0]
	v_mfma_scale_f32_16x16x128_f8f6f4 v[96:99], v[210:217], v[194:201], v[96:99], v153, v153 op_sel_hi:[0,0,0]
	v_mfma_scale_f32_16x16x128_f8f6f4 v[92:95], v[224:231], v[194:201], v[92:95], v153, v153 op_sel_hi:[0,0,0]
	v_mfma_scale_f32_16x16x128_f8f6f4 v[64:67], v[210:217], v[202:209], v[64:67], v153, v153 op_sel_hi:[0,0,0]
	v_mfma_scale_f32_16x16x128_f8f6f4 v[60:63], v[224:231], v[202:209], v[60:63], v153, v153 op_sel_hi:[0,0,0]
	s_mov_b32 m0, s27
	v_lshl_add_u64 v[148:149], s[28:29], 0, v[134:135]
	s_barrier
	ds_read_b128 v[178:181], v157 offset:16384
	ds_read_b128 v[182:185], v157 offset:17408
	ds_read_b128 v[186:189], v157 offset:18432
	ds_read_b128 v[190:193], v157 offset:19456
	ds_read_b128 v[194:197], v157 offset:20480
	ds_read_b128 v[198:201], v157 offset:21504
	ds_read_b128 v[202:205], v157 offset:22528
	ds_read_b128 v[206:209], v157 offset:23552
	global_load_lds_dwordx4 v[148:149], off
	v_lshl_add_u64 v[150:151], s[28:29], 0, v[138:139]
	s_mov_b32 m0, s48
	s_nop 0
	global_load_lds_dwordx4 v[150:151], off
	s_barrier
	s_waitcnt lgkmcnt(0)
	s_waitcnt lgkmcnt(0)
	v_mfma_scale_f32_16x16x128_f8f6f4 v[72:75], v[162:169], v[178:185], v[72:75], v153, v153 op_sel_hi:[0,0,0]
	v_mfma_scale_f32_16x16x128_f8f6f4 v[68:71], v[170:177], v[178:185], v[68:71], v153, v153 op_sel_hi:[0,0,0]
	v_mfma_scale_f32_16x16x128_f8f6f4 v[40:43], v[162:169], v[186:193], v[40:43], v153, v153 op_sel_hi:[0,0,0]
	v_mfma_scale_f32_16x16x128_f8f6f4 v[36:39], v[170:177], v[186:193], v[36:39], v153, v153 op_sel_hi:[0,0,0]
	v_mfma_scale_f32_16x16x128_f8f6f4 v[24:27], v[162:169], v[194:201], v[24:27], v153, v153 op_sel_hi:[0,0,0]
	v_mfma_scale_f32_16x16x128_f8f6f4 v[20:23], v[170:177], v[194:201], v[20:23], v153, v153 op_sel_hi:[0,0,0]
	v_mfma_scale_f32_16x16x128_f8f6f4 v[8:11], v[162:169], v[202:209], v[8:11], v153, v153 op_sel_hi:[0,0,0]
	v_mfma_scale_f32_16x16x128_f8f6f4 v[4:7], v[170:177], v[202:209], v[4:7], v153, v153 op_sel_hi:[0,0,0]
	s_barrier
	s_add_u32 s30, s2, 0x10000
	s_addc_u32 s31, s3, 0
	s_mov_b32 m0, s72
	v_lshl_add_u64 v[162:163], s[30:31], 0, v[132:133]
	global_load_lds_dwordx4 v[162:163], off
	v_lshl_add_u64 v[162:163], s[30:31], 0, v[136:137]
	s_mov_b32 m0, s70
	s_nop 0
	global_load_lds_dwordx4 v[162:163], off
	s_waitcnt vmcnt(6)
	s_barrier
	v_mfma_scale_f32_16x16x128_f8f6f4 v[88:91], v[210:217], v[178:185], v[88:91], v153, v153 op_sel_hi:[0,0,0]
	v_mfma_scale_f32_16x16x128_f8f6f4 v[84:87], v[224:231], v[178:185], v[84:87], v153, v153 op_sel_hi:[0,0,0]
	v_mfma_scale_f32_16x16x128_f8f6f4 v[56:59], v[210:217], v[186:193], v[56:59], v153, v153 op_sel_hi:[0,0,0]
	v_mfma_scale_f32_16x16x128_f8f6f4 v[52:55], v[224:231], v[186:193], v[52:55], v153, v153 op_sel_hi:[0,0,0]
	v_mfma_scale_f32_16x16x128_f8f6f4 v[32:35], v[210:217], v[194:201], v[32:35], v153, v153 op_sel_hi:[0,0,0]
	v_mfma_scale_f32_16x16x128_f8f6f4 v[28:31], v[224:231], v[194:201], v[28:31], v153, v153 op_sel_hi:[0,0,0]
	v_mfma_scale_f32_16x16x128_f8f6f4 v[16:19], v[210:217], v[202:209], v[16:19], v153, v153 op_sel_hi:[0,0,0]
	v_mfma_scale_f32_16x16x128_f8f6f4 v[12:15], v[224:231], v[202:209], v[12:15], v153, v153 op_sel_hi:[0,0,0]
	s_barrier
	ds_read_b128 v[162:165], v159
	ds_read_b128 v[166:169], v159 offset:1024
	ds_read_b128 v[170:173], v159 offset:2048
	ds_read_b128 v[174:177], v159 offset:3072
	s_add_u32 s28, s28, 0x10000
	s_addc_u32 s29, s29, 0
	s_mov_b32 m0, s49
	v_lshl_add_u64 v[210:211], s[28:29], 0, v[134:135]
	ds_read_b128 v[178:181], v157 offset:32768
	ds_read_b128 v[182:185], v157 offset:33792
	ds_read_b128 v[186:189], v157 offset:34816
	ds_read_b128 v[190:193], v157 offset:35840
	ds_read_b128 v[194:197], v157 offset:36864
	ds_read_b128 v[198:201], v157 offset:37888
	ds_read_b128 v[202:205], v157 offset:38912
	ds_read_b128 v[206:209], v157 offset:39936
	global_load_lds_dwordx4 v[210:211], off
	v_lshl_add_u64 v[210:211], s[28:29], 0, v[138:139]
	s_mov_b32 m0, s50
	s_nop 0
	global_load_lds_dwordx4 v[210:211], off
	s_waitcnt lgkmcnt(8)
	s_barrier
	s_waitcnt lgkmcnt(0)
	s_waitcnt lgkmcnt(0)
	v_mfma_scale_f32_16x16x128_f8f6f4 v[108:111], v[162:169], v[178:185], v[108:111], v153, v153 op_sel_hi:[0,0,0]
	v_mfma_scale_f32_16x16x128_f8f6f4 v[112:115], v[170:177], v[178:185], v[112:115], v153, v153 op_sel_hi:[0,0,0]
	v_mfma_scale_f32_16x16x128_f8f6f4 v[104:107], v[162:169], v[186:193], v[104:107], v153, v153 op_sel_hi:[0,0,0]
	v_mfma_scale_f32_16x16x128_f8f6f4 v[100:103], v[170:177], v[186:193], v[100:103], v153, v153 op_sel_hi:[0,0,0]
	v_mfma_scale_f32_16x16x128_f8f6f4 v[80:83], v[162:169], v[194:201], v[80:83], v153, v153 op_sel_hi:[0,0,0]
	v_mfma_scale_f32_16x16x128_f8f6f4 v[76:79], v[170:177], v[194:201], v[76:79], v153, v153 op_sel_hi:[0,0,0]
	v_mfma_scale_f32_16x16x128_f8f6f4 v[48:51], v[162:169], v[202:209], v[48:51], v153, v153 op_sel_hi:[0,0,0]
	v_mfma_scale_f32_16x16x128_f8f6f4 v[44:47], v[170:177], v[202:209], v[44:47], v153, v153 op_sel_hi:[0,0,0]
	s_barrier
	s_mov_b32 m0, s74
	v_lshl_add_u64 v[144:145], v[144:145], 0, s[12:13]
	ds_read_b128 v[210:213], v160
	ds_read_b128 v[214:217], v160 offset:1024
	ds_read_b128 v[224:227], v160 offset:2048
	ds_read_b128 v[228:231], v160 offset:3072
	global_load_lds_dwordx4 v[144:145], off
	v_lshl_add_u64 v[144:145], v[146:147], 0, s[12:13]
	s_mov_b32 m0, s73
	s_nop 0
	global_load_lds_dwordx4 v[144:145], off
	s_barrier
	s_waitcnt lgkmcnt(0)
	s_waitcnt lgkmcnt(0)
	v_mfma_scale_f32_16x16x128_f8f6f4 v[124:127], v[210:217], v[178:185], v[124:127], v153, v153 op_sel_hi:[0,0,0]
	v_mfma_scale_f32_16x16x128_f8f6f4 v[128:131], v[224:231], v[178:185], v[128:131], v153, v153 op_sel_hi:[0,0,0]
	v_mfma_scale_f32_16x16x128_f8f6f4 v[120:123], v[210:217], v[186:193], v[120:123], v153, v153 op_sel_hi:[0,0,0]
	v_mfma_scale_f32_16x16x128_f8f6f4 v[116:119], v[224:231], v[186:193], v[116:119], v153, v153 op_sel_hi:[0,0,0]
	v_mfma_scale_f32_16x16x128_f8f6f4 v[96:99], v[210:217], v[194:201], v[96:99], v153, v153 op_sel_hi:[0,0,0]
	v_mfma_scale_f32_16x16x128_f8f6f4 v[92:95], v[224:231], v[194:201], v[92:95], v153, v153 op_sel_hi:[0,0,0]
	v_mfma_scale_f32_16x16x128_f8f6f4 v[64:67], v[210:217], v[202:209], v[64:67], v153, v153 op_sel_hi:[0,0,0]
	v_mfma_scale_f32_16x16x128_f8f6f4 v[60:63], v[224:231], v[202:209], v[60:63], v153, v153 op_sel_hi:[0,0,0]
	s_mov_b32 m0, s52
	v_lshl_add_u64 v[144:145], v[148:149], 0, s[12:13]
	s_barrier
	ds_read_b128 v[178:181], v157 offset:49152
	ds_read_b128 v[182:185], v157 offset:50176
	ds_read_b128 v[186:189], v157 offset:51200
	ds_read_b128 v[190:193], v157 offset:52224
	ds_read_b128 v[194:197], v157 offset:53248
	ds_read_b128 v[198:201], v157 offset:54272
	ds_read_b128 v[202:205], v157 offset:55296
	ds_read_b128 v[206:209], v157 offset:56320
	global_load_lds_dwordx4 v[144:145], off
	v_lshl_add_u64 v[144:145], v[150:151], 0, s[12:13]
	s_mov_b32 m0, s53
	s_nop 0
	global_load_lds_dwordx4 v[144:145], off
	s_barrier
	s_waitcnt lgkmcnt(0)
	s_waitcnt lgkmcnt(0)
	v_mfma_scale_f32_16x16x128_f8f6f4 v[72:75], v[162:169], v[178:185], v[72:75], v153, v153 op_sel_hi:[0,0,0]
	v_mfma_scale_f32_16x16x128_f8f6f4 v[68:71], v[170:177], v[178:185], v[68:71], v153, v153 op_sel_hi:[0,0,0]
	v_mfma_scale_f32_16x16x128_f8f6f4 v[40:43], v[162:169], v[186:193], v[40:43], v153, v153 op_sel_hi:[0,0,0]
	v_mfma_scale_f32_16x16x128_f8f6f4 v[36:39], v[170:177], v[186:193], v[36:39], v153, v153 op_sel_hi:[0,0,0]
	v_mfma_scale_f32_16x16x128_f8f6f4 v[24:27], v[162:169], v[194:201], v[24:27], v153, v153 op_sel_hi:[0,0,0]
	v_mfma_scale_f32_16x16x128_f8f6f4 v[20:23], v[170:177], v[194:201], v[20:23], v153, v153 op_sel_hi:[0,0,0]
	v_mfma_scale_f32_16x16x128_f8f6f4 v[8:11], v[162:169], v[202:209], v[8:11], v153, v153 op_sel_hi:[0,0,0]
	v_mfma_scale_f32_16x16x128_f8f6f4 v[4:7], v[170:177], v[202:209], v[4:7], v153, v153 op_sel_hi:[0,0,0]
	s_barrier
	s_add_u32 s2, s2, 0x10080
	s_addc_u32 s3, s3, 0
	s_mov_b32 m0, s39
	v_lshl_add_u64 v[144:145], s[2:3], 0, v[132:133]
	global_load_lds_dwordx4 v[144:145], off
	v_lshl_add_u64 v[144:145], s[2:3], 0, v[136:137]
	s_mov_b32 m0, s38
	s_nop 0
	global_load_lds_dwordx4 v[144:145], off
	s_waitcnt vmcnt(6)
	s_barrier
	v_mfma_scale_f32_16x16x128_f8f6f4 v[88:91], v[210:217], v[178:185], v[88:91], v153, v153 op_sel_hi:[0,0,0]
	v_mfma_scale_f32_16x16x128_f8f6f4 v[84:87], v[224:231], v[178:185], v[84:87], v153, v153 op_sel_hi:[0,0,0]
	v_mfma_scale_f32_16x16x128_f8f6f4 v[56:59], v[210:217], v[186:193], v[56:59], v153, v153 op_sel_hi:[0,0,0]
	v_mfma_scale_f32_16x16x128_f8f6f4 v[52:55], v[224:231], v[186:193], v[52:55], v153, v153 op_sel_hi:[0,0,0]
	v_mfma_scale_f32_16x16x128_f8f6f4 v[32:35], v[210:217], v[194:201], v[32:35], v153, v153 op_sel_hi:[0,0,0]
	v_mfma_scale_f32_16x16x128_f8f6f4 v[28:31], v[224:231], v[194:201], v[28:31], v153, v153 op_sel_hi:[0,0,0]
	v_mfma_scale_f32_16x16x128_f8f6f4 v[16:19], v[210:217], v[202:209], v[16:19], v153, v153 op_sel_hi:[0,0,0]
	v_mfma_scale_f32_16x16x128_f8f6f4 v[12:15], v[224:231], v[202:209], v[12:15], v153, v153 op_sel_hi:[0,0,0]
	v_lshl_add_u32 v144, s26, 8, v154
	v_ashrrev_i32_e32 v145, 31, v144
	v_lshlrev_b64 v[144:145], 12, v[144:145]
	s_lshl_b32 s2, s68, 8
	v_lshl_add_u64 v[144:145], s[10:11], 0, v[144:145]
	s_ashr_i32 s3, s2, 31
	v_lshl_add_u64 v[144:145], s[2:3], 1, v[144:145]
	v_lshl_add_u64 v[144:145], v[144:145], 0, s[4:5]
	v_pk_mul_f32 v[108:109], v[108:109], s[18:19] op_sel_hi:[1,0]
	s_barrier
	s_nop 7
	s_nop 7
	s_nop 7
	v_lshl_add_u64 v[144:145], v[144:145], 0, v[142:143]
	v_pk_mul_f32 v[110:111], v[110:111], s[18:19] op_sel_hi:[1,0]
	v_cvt_pk_bf16_f32 v108, v108, v109
	v_pk_mul_f32 v[114:115], v[114:115], s[18:19] op_sel_hi:[1,0]
	v_cvt_pk_bf16_f32 v109, v110, v111
	v_pk_mul_f32 v[112:113], v[112:113], s[18:19] op_sel_hi:[1,0]
	v_pk_mul_f32 v[104:105], v[104:105], s[18:19] op_sel_hi:[1,0]
	v_cvt_pk_bf16_f32 v110, v112, v113
	v_cvt_pk_bf16_f32 v111, v114, v115
	global_store_dwordx4 v[144:145], v[108:111], off
	v_pk_mul_f32 v[112:113], v[130:131], s[18:19] op_sel_hi:[1,0]
	v_pk_mul_f32 v[114:115], v[128:129], s[18:19] op_sel_hi:[1,0]
	v_pk_mul_f32 v[108:109], v[124:125], s[18:19] op_sel_hi:[1,0]
	v_pk_mul_f32 v[110:111], v[126:127], s[18:19] op_sel_hi:[1,0]
	v_cvt_pk_bf16_f32 v108, v108, v109
	v_pk_mul_f32 v[106:107], v[106:107], s[18:19] op_sel_hi:[1,0]
	v_cvt_pk_bf16_f32 v109, v110, v111
	v_cvt_pk_bf16_f32 v110, v114, v115
	v_cvt_pk_bf16_f32 v111, v112, v113
	global_store_dwordx4 v[144:145], v[108:111], off offset:256
	v_pk_mul_f32 v[80:81], v[80:81], s[18:19] op_sel_hi:[1,0]
	v_pk_mul_f32 v[82:83], v[82:83], s[18:19] op_sel_hi:[1,0]
	v_pk_mul_f32 v[108:109], v[102:103], s[18:19] op_sel_hi:[1,0]
	v_pk_mul_f32 v[102:103], v[100:101], s[18:19] op_sel_hi:[1,0]
	v_cvt_pk_bf16_f32 v100, v104, v105
	v_add_co_u32_e32 v104, vcc, s51, v144
	v_cvt_pk_bf16_f32 v101, v106, v107
	v_cvt_pk_bf16_f32 v102, v102, v103
	v_cvt_pk_bf16_f32 v103, v108, v109
	v_pk_mul_f32 v[106:107], v[118:119], s[18:19] op_sel_hi:[1,0]
	s_nop 0
	v_addc_co_u32_e32 v105, vcc, 0, v145, vcc
	global_store_dwordx4 v[104:105], v[100:103], off
	v_pk_mul_f32 v[108:109], v[116:117], s[18:19] op_sel_hi:[1,0]
	v_pk_mul_f32 v[48:49], v[48:49], s[18:19] op_sel_hi:[1,0]
	v_pk_mul_f32 v[100:101], v[120:121], s[18:19] op_sel_hi:[1,0]
	v_pk_mul_f32 v[102:103], v[122:123], s[18:19] op_sel_hi:[1,0]
	v_cvt_pk_bf16_f32 v100, v100, v101
	v_pk_mul_f32 v[92:93], v[92:93], s[18:19] op_sel_hi:[1,0]
	v_cvt_pk_bf16_f32 v101, v102, v103
	v_cvt_pk_bf16_f32 v102, v108, v109
	v_cvt_pk_bf16_f32 v103, v106, v107
	global_store_dwordx4 v[104:105], v[100:103], off offset:256
	v_pk_mul_f32 v[50:51], v[50:51], s[18:19] op_sel_hi:[1,0]
	v_pk_mul_f32 v[60:61], v[60:61], s[18:19] op_sel_hi:[1,0]
	v_pk_mul_f32 v[100:101], v[78:79], s[18:19] op_sel_hi:[1,0]
	v_pk_mul_f32 v[78:79], v[76:77], s[18:19] op_sel_hi:[1,0]
	v_cvt_pk_bf16_f32 v76, v80, v81
	v_add_co_u32_e32 v80, vcc, s60, v144
	v_cvt_pk_bf16_f32 v77, v82, v83
	v_cvt_pk_bf16_f32 v78, v78, v79
	v_cvt_pk_bf16_f32 v79, v100, v101
	v_pk_mul_f32 v[82:83], v[94:95], s[18:19] op_sel_hi:[1,0]
	s_nop 0
	v_addc_co_u32_e32 v81, vcc, 0, v145, vcc
	global_store_dwordx4 v[80:81], v[76:79], off
	v_pk_mul_f32 v[40:41], v[40:41], s[18:19] op_sel_hi:[1,0]
	v_pk_mul_f32 v[42:43], v[42:43], s[18:19] op_sel_hi:[1,0]
	v_pk_mul_f32 v[76:77], v[96:97], s[18:19] op_sel_hi:[1,0]
	v_pk_mul_f32 v[78:79], v[98:99], s[18:19] op_sel_hi:[1,0]
	v_cvt_pk_bf16_f32 v76, v76, v77
	v_pk_mul_f32 v[24:25], v[24:25], s[18:19] op_sel_hi:[1,0]
	v_cvt_pk_bf16_f32 v77, v78, v79
	v_cvt_pk_bf16_f32 v78, v92, v93
	v_cvt_pk_bf16_f32 v79, v82, v83
	global_store_dwordx4 v[80:81], v[76:79], off offset:256
	v_pk_mul_f32 v[26:27], v[26:27], s[18:19] op_sel_hi:[1,0]
	v_pk_mul_f32 v[8:9], v[8:9], s[18:19] op_sel_hi:[1,0]
	v_pk_mul_f32 v[76:77], v[46:47], s[18:19] op_sel_hi:[1,0]
	v_pk_mul_f32 v[46:47], v[44:45], s[18:19] op_sel_hi:[1,0]
	v_cvt_pk_bf16_f32 v44, v48, v49
	v_add_co_u32_e32 v48, vcc, s61, v144
	v_cvt_pk_bf16_f32 v45, v50, v51
	v_cvt_pk_bf16_f32 v46, v46, v47
	v_cvt_pk_bf16_f32 v47, v76, v77
	v_pk_mul_f32 v[50:51], v[62:63], s[18:19] op_sel_hi:[1,0]
	s_nop 0
	v_addc_co_u32_e32 v49, vcc, 0, v145, vcc
	global_store_dwordx4 v[48:49], v[44:47], off
	v_pk_mul_f32 v[28:29], v[28:29], s[18:19] op_sel_hi:[1,0]
	v_pk_mul_f32 v[10:11], v[10:11], s[18:19] op_sel_hi:[1,0]
	v_pk_mul_f32 v[46:47], v[66:67], s[18:19] op_sel_hi:[1,0]
	v_pk_mul_f32 v[44:45], v[64:65], s[18:19] op_sel_hi:[1,0]
	s_add_i32 s55, s55, s19
	v_cvt_pk_bf16_f32 v44, v44, v45
	v_cvt_pk_bf16_f32 v45, v46, v47
	v_cvt_pk_bf16_f32 v46, v60, v61
	v_cvt_pk_bf16_f32 v47, v50, v51
	global_store_dwordx4 v[48:49], v[44:47], off offset:256
	v_pk_mul_f32 v[48:49], v[70:71], s[18:19] op_sel_hi:[1,0]
	v_pk_mul_f32 v[50:51], v[68:69], s[18:19] op_sel_hi:[1,0]
	v_pk_mul_f32 v[46:47], v[74:75], s[18:19] op_sel_hi:[1,0]
	v_pk_mul_f32 v[44:45], v[72:73], s[18:19] op_sel_hi:[1,0]
	v_pk_mul_f32 v[60:61], v[84:85], s[18:19] op_sel_hi:[1,0]
	v_cvt_pk_bf16_f32 v44, v44, v45
	v_cvt_pk_bf16_f32 v45, v46, v47
	v_cvt_pk_bf16_f32 v46, v50, v51
	v_cvt_pk_bf16_f32 v47, v48, v49
	v_add_co_u32_e32 v48, vcc, s62, v144
	v_pk_mul_f32 v[50:51], v[86:87], s[18:19] op_sel_hi:[1,0]
	s_nop 0
	v_addc_co_u32_e32 v49, vcc, 0, v145, vcc
	global_store_dwordx4 v[48:49], v[44:47], off
	s_mov_b32 s68, s66
	s_mov_b32 s26, s20
	v_pk_mul_f32 v[44:45], v[88:89], s[18:19] op_sel_hi:[1,0]
	v_pk_mul_f32 v[46:47], v[90:91], s[18:19] op_sel_hi:[1,0]
	v_cvt_pk_bf16_f32 v44, v44, v45
	s_mov_b64 s[38:39], s[24:25]
	v_cvt_pk_bf16_f32 v45, v46, v47
	v_cvt_pk_bf16_f32 v46, v60, v61
	v_cvt_pk_bf16_f32 v47, v50, v51
	global_store_dwordx4 v[48:49], v[44:47], off offset:256
	s_mov_b64 s[30:31], s[22:23]
	v_pk_mul_f32 v[12:13], v[12:13], s[18:19] op_sel_hi:[1,0]
	v_pk_mul_f32 v[44:45], v[38:39], s[18:19] op_sel_hi:[1,0]
	v_pk_mul_f32 v[38:39], v[36:37], s[18:19] op_sel_hi:[1,0]
	v_cvt_pk_bf16_f32 v36, v40, v41
	v_add_co_u32_e32 v40, vcc, s63, v144
	v_cvt_pk_bf16_f32 v37, v42, v43
	v_cvt_pk_bf16_f32 v38, v38, v39
	v_cvt_pk_bf16_f32 v39, v44, v45
	v_pk_mul_f32 v[42:43], v[54:55], s[18:19] op_sel_hi:[1,0]
	s_nop 0
	v_addc_co_u32_e32 v41, vcc, 0, v145, vcc
	global_store_dwordx4 v[40:41], v[36:39], off
	v_pk_mul_f32 v[44:45], v[52:53], s[18:19] op_sel_hi:[1,0]
	s_nop 0
	v_pk_mul_f32 v[36:37], v[56:57], s[18:19] op_sel_hi:[1,0]
	v_pk_mul_f32 v[38:39], v[58:59], s[18:19] op_sel_hi:[1,0]
	v_cvt_pk_bf16_f32 v36, v36, v37
	s_nop 0
	v_cvt_pk_bf16_f32 v37, v38, v39
	v_cvt_pk_bf16_f32 v38, v44, v45
	v_cvt_pk_bf16_f32 v39, v42, v43
	global_store_dwordx4 v[40:41], v[36:39], off offset:256
	s_nop 1
	v_pk_mul_f32 v[36:37], v[22:23], s[18:19] op_sel_hi:[1,0]
	v_pk_mul_f32 v[22:23], v[20:21], s[18:19] op_sel_hi:[1,0]
	v_cvt_pk_bf16_f32 v20, v24, v25
	v_add_co_u32_e32 v24, vcc, s64, v144
	v_cvt_pk_bf16_f32 v21, v26, v27
	v_cvt_pk_bf16_f32 v22, v22, v23
	v_cvt_pk_bf16_f32 v23, v36, v37
	v_pk_mul_f32 v[26:27], v[30:31], s[18:19] op_sel_hi:[1,0]
	s_nop 0
	v_addc_co_u32_e32 v25, vcc, 0, v145, vcc
	global_store_dwordx4 v[24:25], v[20:23], off
	s_nop 1
	v_pk_mul_f32 v[20:21], v[32:33], s[18:19] op_sel_hi:[1,0]
	v_pk_mul_f32 v[22:23], v[34:35], s[18:19] op_sel_hi:[1,0]
	v_cvt_pk_bf16_f32 v20, v20, v21
	s_nop 0
	v_cvt_pk_bf16_f32 v21, v22, v23
	v_cvt_pk_bf16_f32 v22, v28, v29
	v_cvt_pk_bf16_f32 v23, v26, v27
	global_store_dwordx4 v[24:25], v[20:23], off offset:256
	s_nop 1
	v_pk_mul_f32 v[20:21], v[6:7], s[18:19] op_sel_hi:[1,0]
	v_pk_mul_f32 v[6:7], v[4:5], s[18:19] op_sel_hi:[1,0]
	v_cvt_pk_bf16_f32 v4, v8, v9
	v_add_co_u32_e32 v8, vcc, s65, v144
	v_cvt_pk_bf16_f32 v5, v10, v11
	v_cvt_pk_bf16_f32 v6, v6, v7
	v_cvt_pk_bf16_f32 v7, v20, v21
	v_pk_mul_f32 v[10:11], v[14:15], s[18:19] op_sel_hi:[1,0]
	s_nop 0
	v_addc_co_u32_e32 v9, vcc, 0, v145, vcc
	global_store_dwordx4 v[8:9], v[4:7], off
	s_andn2_b64 vcc, exec, s[0:1]
	s_nop 0
	v_pk_mul_f32 v[6:7], v[18:19], s[18:19] op_sel_hi:[1,0]
	v_pk_mul_f32 v[4:5], v[16:17], s[18:19] op_sel_hi:[1,0]
	s_nop 0
	v_cvt_pk_bf16_f32 v4, v4, v5
	v_cvt_pk_bf16_f32 v5, v6, v7
	v_cvt_pk_bf16_f32 v6, v12, v13
	v_cvt_pk_bf16_f32 v7, v10, v11
	global_store_dwordx4 v[8:9], v[4:7], off offset:256
	s_cbranch_vccz .LBB0_1350

.LBB0_1680:
	ds_read_b128 v[12:15], v176
	ds_read_b128 v[16:19], v176 offset:1024
	ds_read_b128 v[28:31], v176 offset:2048
	ds_read_b128 v[32:35], v176 offset:3072
	s_add_u32 s18, s29, s57
	v_cmp_lt_i64_e32 vcc, s[6:7], v[144:145]
	s_addc_u32 s19, s30, 0
	s_and_b64 s[2:3], vcc, exec
	s_cselect_b32 s25, s19, s23
	s_cselect_b32 s24, s18, s22
	s_add_u32 s20, s31, s58
	s_addc_u32 s21, s38, 0
	s_and_b64 s[2:3], vcc, exec
	s_cselect_b32 s3, s21, s27
	s_cselect_b32 s2, s20, s26
	s_add_u32 s62, s22, 0x20080
	s_addc_u32 s63, s23, 0
	s_add_i32 s67, s40, 0xc000
	v_lshl_add_u64 v[44:45], s[62:63], 0, v[136:137]
	s_mov_b32 m0, s67
	s_add_i32 s61, s40, 0xe000
	ds_read_b128 v[4:7], v177
	ds_read_b128 v[8:11], v177 offset:1024
	ds_read_b128 v[20:23], v177 offset:2048
	ds_read_b128 v[24:27], v177 offset:3072
	ds_read_b128 v[36:39], v177 offset:4096
	ds_read_b128 v[40:43], v177 offset:5120
	ds_read_b128 v[52:55], v177 offset:6144
	ds_read_b128 v[56:59], v177 offset:7168
	global_load_lds_dwordx4 v[44:45], off
	v_lshl_add_u64 v[44:45], s[62:63], 0, v[140:141]
	s_mov_b32 m0, s61
	s_nop 0
	global_load_lds_dwordx4 v[44:45], off
	s_waitcnt lgkmcnt(8)
	s_barrier
	s_waitcnt lgkmcnt(0)
	v_mov_b64_e32 v[110:111], v[2:3]
	v_mov_b64_e32 v[114:115], v[2:3]
	v_mov_b64_e32 v[106:107], v[2:3]
	v_mov_b64_e32 v[102:103], v[2:3]
	v_mov_b64_e32 v[82:83], v[2:3]
	v_mov_b64_e32 v[78:79], v[2:3]
	v_mov_b64_e32 v[50:51], v[2:3]
	v_mov_b64_e32 v[46:47], v[2:3]
	v_mov_b64_e32 v[108:109], v[0:1]
	v_mov_b64_e32 v[112:113], v[0:1]
	v_mov_b64_e32 v[104:105], v[0:1]
	v_mov_b64_e32 v[100:101], v[0:1]
	v_mov_b64_e32 v[80:81], v[0:1]
	v_mov_b64_e32 v[76:77], v[0:1]
	v_mov_b64_e32 v[48:49], v[0:1]
	v_mov_b64_e32 v[44:45], v[0:1]
	s_waitcnt lgkmcnt(0)
	v_mfma_scale_f32_16x16x128_f8f6f4 v[108:111], v[12:19], v[4:11], v[108:111], v171, v171 op_sel_hi:[0,0,0]
	v_mfma_scale_f32_16x16x128_f8f6f4 v[112:115], v[28:35], v[4:11], v[112:115], v171, v171 op_sel_hi:[0,0,0]
	v_mfma_scale_f32_16x16x128_f8f6f4 v[104:107], v[12:19], v[20:27], v[104:107], v171, v171 op_sel_hi:[0,0,0]
	v_mfma_scale_f32_16x16x128_f8f6f4 v[100:103], v[28:35], v[20:27], v[100:103], v171, v171 op_sel_hi:[0,0,0]
	v_mfma_scale_f32_16x16x128_f8f6f4 v[80:83], v[12:19], v[36:43], v[80:83], v171, v171 op_sel_hi:[0,0,0]
	v_mfma_scale_f32_16x16x128_f8f6f4 v[76:79], v[28:35], v[36:43], v[76:79], v171, v171 op_sel_hi:[0,0,0]
	v_mfma_scale_f32_16x16x128_f8f6f4 v[48:51], v[12:19], v[52:59], v[48:51], v171, v171 op_sel_hi:[0,0,0]
	v_mfma_scale_f32_16x16x128_f8f6f4 v[44:47], v[28:35], v[52:59], v[44:47], v171, v171 op_sel_hi:[0,0,0]
	s_barrier
	v_lshl_add_u64 v[132:133], s[26:27], 0, v[138:139]
	s_add_i32 s64, s50, s39
	v_lshl_add_u64 v[60:61], v[132:133], 0, s[10:11]
	s_mov_b32 m0, s64
	v_lshl_add_u64 v[134:135], s[26:27], 0, v[142:143]
	s_add_i32 s62, s64, 0x2000
	ds_read_b128 v[154:157], v178
	ds_read_b128 v[158:161], v178 offset:1024
	ds_read_b128 v[180:183], v178 offset:2048
	ds_read_b128 v[184:187], v178 offset:3072
	global_load_lds_dwordx4 v[60:61], off
	v_lshl_add_u64 v[60:61], v[134:135], 0, s[10:11]
	s_mov_b32 m0, s62
	s_nop 0
	global_load_lds_dwordx4 v[60:61], off
	s_barrier
	s_waitcnt lgkmcnt(0)
	v_mov_b64_e32 v[126:127], v[2:3]
	v_mov_b64_e32 v[130:131], v[2:3]
	v_mov_b64_e32 v[122:123], v[2:3]
	v_mov_b64_e32 v[118:119], v[2:3]
	v_mov_b64_e32 v[98:99], v[2:3]
	v_mov_b64_e32 v[94:95], v[2:3]
	v_mov_b64_e32 v[66:67], v[2:3]
	v_mov_b64_e32 v[62:63], v[2:3]
	v_mov_b64_e32 v[124:125], v[0:1]
	v_mov_b64_e32 v[128:129], v[0:1]
	v_mov_b64_e32 v[120:121], v[0:1]
	v_mov_b64_e32 v[116:117], v[0:1]
	v_mov_b64_e32 v[96:97], v[0:1]
	v_mov_b64_e32 v[92:93], v[0:1]
	v_mov_b64_e32 v[64:65], v[0:1]
	v_mov_b64_e32 v[60:61], v[0:1]
	s_waitcnt lgkmcnt(0)
	v_mfma_scale_f32_16x16x128_f8f6f4 v[124:127], v[154:161], v[4:11], v[124:127], v171, v171 op_sel_hi:[0,0,0]
	v_mfma_scale_f32_16x16x128_f8f6f4 v[128:131], v[180:187], v[4:11], v[128:131], v171, v171 op_sel_hi:[0,0,0]
	v_mfma_scale_f32_16x16x128_f8f6f4 v[120:123], v[154:161], v[20:27], v[120:123], v171, v171 op_sel_hi:[0,0,0]
	v_mfma_scale_f32_16x16x128_f8f6f4 v[116:119], v[180:187], v[20:27], v[116:119], v171, v171 op_sel_hi:[0,0,0]
	v_mfma_scale_f32_16x16x128_f8f6f4 v[96:99], v[154:161], v[36:43], v[96:99], v171, v171 op_sel_hi:[0,0,0]
	v_mfma_scale_f32_16x16x128_f8f6f4 v[92:95], v[180:187], v[36:43], v[92:95], v171, v171 op_sel_hi:[0,0,0]
	v_mfma_scale_f32_16x16x128_f8f6f4 v[64:67], v[154:161], v[52:59], v[64:67], v171, v171 op_sel_hi:[0,0,0]
	v_mfma_scale_f32_16x16x128_f8f6f4 v[60:63], v[180:187], v[52:59], v[60:63], v171, v171 op_sel_hi:[0,0,0]
	v_lshl_add_u64 v[150:151], s[22:23], 0, v[136:137]
	s_mov_b32 m0, s40
	v_lshl_add_u64 v[4:5], v[150:151], 0, s[10:11]
	v_lshl_add_u64 v[152:153], s[22:23], 0, v[140:141]
	s_barrier
	ds_read_b128 v[52:55], v177 offset:16384
	ds_read_b128 v[56:59], v177 offset:17408
	ds_read_b128 v[188:191], v177 offset:18432
	ds_read_b128 v[192:195], v177 offset:19456
	ds_read_b128 v[196:199], v177 offset:20480
	ds_read_b128 v[200:203], v177 offset:21504
	ds_read_b128 v[204:207], v177 offset:22528
	ds_read_b128 v[208:211], v177 offset:23552
	global_load_lds_dwordx4 v[4:5], off
	v_lshl_add_u64 v[4:5], v[152:153], 0, s[10:11]
	s_mov_b32 m0, s41
	s_nop 0
	global_load_lds_dwordx4 v[4:5], off
	s_barrier
	s_waitcnt lgkmcnt(0)
	v_mov_b64_e32 v[74:75], v[2:3]
	v_mov_b64_e32 v[70:71], v[2:3]
	v_mov_b64_e32 v[42:43], v[2:3]
	v_mov_b64_e32 v[38:39], v[2:3]
	v_mov_b64_e32 v[26:27], v[2:3]
	v_mov_b64_e32 v[22:23], v[2:3]
	v_mov_b64_e32 v[10:11], v[2:3]
	v_mov_b64_e32 v[6:7], v[2:3]
	v_mov_b64_e32 v[72:73], v[0:1]
	v_mov_b64_e32 v[68:69], v[0:1]
	v_mov_b64_e32 v[40:41], v[0:1]
	v_mov_b64_e32 v[36:37], v[0:1]
	v_mov_b64_e32 v[24:25], v[0:1]
	v_mov_b64_e32 v[20:21], v[0:1]
	v_mov_b64_e32 v[8:9], v[0:1]
	v_mov_b64_e32 v[4:5], v[0:1]
	s_waitcnt lgkmcnt(0)
	v_mfma_scale_f32_16x16x128_f8f6f4 v[72:75], v[12:19], v[52:59], v[72:75], v171, v171 op_sel_hi:[0,0,0]
	v_mfma_scale_f32_16x16x128_f8f6f4 v[68:71], v[28:35], v[52:59], v[68:71], v171, v171 op_sel_hi:[0,0,0]
	v_mfma_scale_f32_16x16x128_f8f6f4 v[40:43], v[12:19], v[188:195], v[40:43], v171, v171 op_sel_hi:[0,0,0]
	v_mfma_scale_f32_16x16x128_f8f6f4 v[36:39], v[28:35], v[188:195], v[36:39], v171, v171 op_sel_hi:[0,0,0]
	v_mfma_scale_f32_16x16x128_f8f6f4 v[24:27], v[12:19], v[196:203], v[24:27], v171, v171 op_sel_hi:[0,0,0]
	v_mfma_scale_f32_16x16x128_f8f6f4 v[20:23], v[28:35], v[196:203], v[20:23], v171, v171 op_sel_hi:[0,0,0]
	v_mfma_scale_f32_16x16x128_f8f6f4 v[8:11], v[12:19], v[204:211], v[8:11], v171, v171 op_sel_hi:[0,0,0]
	v_mfma_scale_f32_16x16x128_f8f6f4 v[4:7], v[28:35], v[204:211], v[4:7], v171, v171 op_sel_hi:[0,0,0]
	s_barrier
	s_add_u32 s68, s26, 0x10100
	s_addc_u32 s69, s27, 0
	s_add_i32 s65, s51, s39
	v_lshl_add_u64 v[12:13], s[68:69], 0, v[138:139]
	s_mov_b32 m0, s65
	s_add_i32 s63, s65, 0x2000
	global_load_lds_dwordx4 v[12:13], off
	v_lshl_add_u64 v[12:13], s[68:69], 0, v[142:143]
	s_mov_b32 m0, s63
	s_nop 0
	global_load_lds_dwordx4 v[12:13], off
	s_waitcnt vmcnt(6)
	s_barrier
	v_mov_b64_e32 v[90:91], v[2:3]
	v_mov_b64_e32 v[86:87], v[2:3]
	v_mov_b64_e32 v[88:89], v[0:1]
	v_mov_b64_e32 v[84:85], v[0:1]
	v_mfma_scale_f32_16x16x128_f8f6f4 v[88:91], v[154:161], v[52:59], v[88:91], v171, v171 op_sel_hi:[0,0,0]
	v_mfma_scale_f32_16x16x128_f8f6f4 v[84:87], v[180:187], v[52:59], v[84:87], v171, v171 op_sel_hi:[0,0,0]
	v_mov_b64_e32 v[58:59], v[2:3]
	v_mov_b64_e32 v[54:55], v[2:3]
	v_mov_b64_e32 v[34:35], v[2:3]
	v_mov_b64_e32 v[30:31], v[2:3]
	v_mov_b64_e32 v[18:19], v[2:3]
	v_mov_b64_e32 v[14:15], v[2:3]
	v_mov_b64_e32 v[56:57], v[0:1]
	v_mov_b64_e32 v[52:53], v[0:1]
	v_mov_b64_e32 v[32:33], v[0:1]
	v_mov_b64_e32 v[28:29], v[0:1]
	v_mov_b64_e32 v[16:17], v[0:1]
	v_mov_b64_e32 v[12:13], v[0:1]
	v_mfma_scale_f32_16x16x128_f8f6f4 v[56:59], v[154:161], v[188:195], v[56:59], v171, v171 op_sel_hi:[0,0,0]
	v_mfma_scale_f32_16x16x128_f8f6f4 v[52:55], v[180:187], v[188:195], v[52:55], v171, v171 op_sel_hi:[0,0,0]
	v_mfma_scale_f32_16x16x128_f8f6f4 v[32:35], v[154:161], v[196:203], v[32:35], v171, v171 op_sel_hi:[0,0,0]
	v_mfma_scale_f32_16x16x128_f8f6f4 v[28:31], v[180:187], v[196:203], v[28:31], v171, v171 op_sel_hi:[0,0,0]
	v_mfma_scale_f32_16x16x128_f8f6f4 v[16:19], v[154:161], v[204:211], v[16:19], v171, v171 op_sel_hi:[0,0,0]
	v_mfma_scale_f32_16x16x128_f8f6f4 v[12:15], v[180:187], v[204:211], v[12:15], v171, v171 op_sel_hi:[0,0,0]
	s_add_i32 s66, 0, 0x18000
	v_add_u32_e32 v154, s66, v174
	s_barrier
	ds_read_b128 v[156:159], v154
	ds_read_b128 v[160:163], v154 offset:1024
	ds_read_b128 v[180:183], v154 offset:2048
	ds_read_b128 v[184:187], v154 offset:3072
	s_add_u32 s68, s22, 0x20100
	s_addc_u32 s69, s23, 0
	s_mov_b32 m0, s42
	v_lshl_add_u64 v[164:165], s[68:69], 0, v[136:137]
	ds_read_b128 v[188:191], v177 offset:32768
	ds_read_b128 v[192:195], v177 offset:33792
	ds_read_b128 v[196:199], v177 offset:34816
	ds_read_b128 v[200:203], v177 offset:35840
	ds_read_b128 v[204:207], v177 offset:36864
	ds_read_b128 v[208:211], v177 offset:37888
	ds_read_b128 v[212:215], v177 offset:38912
	ds_read_b128 v[216:219], v177 offset:39936
	global_load_lds_dwordx4 v[164:165], off
	v_lshl_add_u64 v[164:165], s[68:69], 0, v[140:141]
	s_mov_b32 m0, s43
	s_nop 0
	global_load_lds_dwordx4 v[164:165], off
	s_waitcnt lgkmcnt(8)
	s_barrier
	s_waitcnt lgkmcnt(0)
	s_waitcnt lgkmcnt(0)
	v_mfma_scale_f32_16x16x128_f8f6f4 v[108:111], v[156:163], v[188:195], v[108:111], v171, v171 op_sel_hi:[0,0,0]
	v_mfma_scale_f32_16x16x128_f8f6f4 v[112:115], v[180:187], v[188:195], v[112:115], v171, v171 op_sel_hi:[0,0,0]
	v_mfma_scale_f32_16x16x128_f8f6f4 v[104:107], v[156:163], v[196:203], v[104:107], v171, v171 op_sel_hi:[0,0,0]
	v_mfma_scale_f32_16x16x128_f8f6f4 v[100:103], v[180:187], v[196:203], v[100:103], v171, v171 op_sel_hi:[0,0,0]
	v_mfma_scale_f32_16x16x128_f8f6f4 v[80:83], v[156:163], v[204:211], v[80:83], v171, v171 op_sel_hi:[0,0,0]
	v_mfma_scale_f32_16x16x128_f8f6f4 v[76:79], v[180:187], v[204:211], v[76:79], v171, v171 op_sel_hi:[0,0,0]
	v_mfma_scale_f32_16x16x128_f8f6f4 v[48:51], v[156:163], v[212:219], v[48:51], v171, v171 op_sel_hi:[0,0,0]
	v_mfma_scale_f32_16x16x128_f8f6f4 v[44:47], v[180:187], v[212:219], v[44:47], v171, v171 op_sel_hi:[0,0,0]
	s_barrier
	s_add_i32 s69, 0, 0x1c000
	s_add_i32 s68, s66, s39
	v_add_u32_e32 v155, s69, v174
	v_lshl_add_u64 v[132:133], v[132:133], 0, s[12:13]
	s_mov_b32 m0, s68
	s_add_i32 s66, s68, 0x2000
	ds_read_b128 v[224:227], v155
	ds_read_b128 v[228:231], v155 offset:1024
	ds_read_b128 v[232:235], v155 offset:2048
	ds_read_b128 v[236:239], v155 offset:3072
	global_load_lds_dwordx4 v[132:133], off
	v_lshl_add_u64 v[132:133], v[134:135], 0, s[12:13]
	s_mov_b32 m0, s66
	s_nop 0
	global_load_lds_dwordx4 v[132:133], off
	s_barrier
	s_waitcnt lgkmcnt(0)
	s_waitcnt lgkmcnt(0)
	v_mfma_scale_f32_16x16x128_f8f6f4 v[124:127], v[224:231], v[188:195], v[124:127], v171, v171 op_sel_hi:[0,0,0]
	v_mfma_scale_f32_16x16x128_f8f6f4 v[128:131], v[232:239], v[188:195], v[128:131], v171, v171 op_sel_hi:[0,0,0]
	v_mfma_scale_f32_16x16x128_f8f6f4 v[120:123], v[224:231], v[196:203], v[120:123], v171, v171 op_sel_hi:[0,0,0]
	v_mfma_scale_f32_16x16x128_f8f6f4 v[116:119], v[232:239], v[196:203], v[116:119], v171, v171 op_sel_hi:[0,0,0]
	v_mfma_scale_f32_16x16x128_f8f6f4 v[96:99], v[224:231], v[204:211], v[96:99], v171, v171 op_sel_hi:[0,0,0]
	v_mfma_scale_f32_16x16x128_f8f6f4 v[92:95], v[232:239], v[204:211], v[92:95], v171, v171 op_sel_hi:[0,0,0]
	v_mfma_scale_f32_16x16x128_f8f6f4 v[64:67], v[224:231], v[212:219], v[64:67], v171, v171 op_sel_hi:[0,0,0]
	v_mfma_scale_f32_16x16x128_f8f6f4 v[60:63], v[232:239], v[212:219], v[60:63], v171, v171 op_sel_hi:[0,0,0]
	s_mov_b32 m0, s46
	v_lshl_add_u64 v[132:133], v[150:151], 0, s[12:13]
	s_barrier
	ds_read_b128 v[188:191], v177 offset:49152
	ds_read_b128 v[192:195], v177 offset:50176
	ds_read_b128 v[196:199], v177 offset:51200
	ds_read_b128 v[200:203], v177 offset:52224
	ds_read_b128 v[204:207], v177 offset:53248
	ds_read_b128 v[208:211], v177 offset:54272
	ds_read_b128 v[212:215], v177 offset:55296
	ds_read_b128 v[216:219], v177 offset:56320
	global_load_lds_dwordx4 v[132:133], off
	v_lshl_add_u64 v[132:133], v[152:153], 0, s[12:13]
	s_mov_b32 m0, s47
	s_nop 0
	global_load_lds_dwordx4 v[132:133], off
	s_barrier
	s_waitcnt lgkmcnt(0)
	s_waitcnt lgkmcnt(0)
	v_mfma_scale_f32_16x16x128_f8f6f4 v[72:75], v[156:163], v[188:195], v[72:75], v171, v171 op_sel_hi:[0,0,0]
	v_mfma_scale_f32_16x16x128_f8f6f4 v[68:71], v[180:187], v[188:195], v[68:71], v171, v171 op_sel_hi:[0,0,0]
	v_mfma_scale_f32_16x16x128_f8f6f4 v[40:43], v[156:163], v[196:203], v[40:43], v171, v171 op_sel_hi:[0,0,0]
	v_mfma_scale_f32_16x16x128_f8f6f4 v[36:39], v[180:187], v[196:203], v[36:39], v171, v171 op_sel_hi:[0,0,0]
	v_mfma_scale_f32_16x16x128_f8f6f4 v[24:27], v[156:163], v[204:211], v[24:27], v171, v171 op_sel_hi:[0,0,0]
	v_mfma_scale_f32_16x16x128_f8f6f4 v[20:23], v[180:187], v[204:211], v[20:23], v171, v171 op_sel_hi:[0,0,0]
	v_mfma_scale_f32_16x16x128_f8f6f4 v[8:11], v[156:163], v[212:219], v[8:11], v171, v171 op_sel_hi:[0,0,0]
	v_mfma_scale_f32_16x16x128_f8f6f4 v[4:7], v[180:187], v[212:219], v[4:7], v171, v171 op_sel_hi:[0,0,0]
	s_barrier
	s_add_u32 s70, s26, 0x10180
	s_addc_u32 s71, s27, 0
	s_add_i32 s27, s69, s39
	v_lshl_add_u64 v[132:133], s[70:71], 0, v[138:139]
	s_mov_b32 m0, s27
	s_add_i32 s26, s27, 0x2000
	global_load_lds_dwordx4 v[132:133], off
	v_lshl_add_u64 v[132:133], s[70:71], 0, v[142:143]
	s_mov_b32 m0, s26
	s_nop 0
	global_load_lds_dwordx4 v[132:133], off
	s_waitcnt vmcnt(6)
	s_barrier
	v_mfma_scale_f32_16x16x128_f8f6f4 v[88:91], v[224:231], v[188:195], v[88:91], v171, v171 op_sel_hi:[0,0,0]
	v_mfma_scale_f32_16x16x128_f8f6f4 v[84:87], v[232:239], v[188:195], v[84:87], v171, v171 op_sel_hi:[0,0,0]
	v_mfma_scale_f32_16x16x128_f8f6f4 v[56:59], v[224:231], v[196:203], v[56:59], v171, v171 op_sel_hi:[0,0,0]
	v_mfma_scale_f32_16x16x128_f8f6f4 v[52:55], v[232:239], v[196:203], v[52:55], v171, v171 op_sel_hi:[0,0,0]
	v_mfma_scale_f32_16x16x128_f8f6f4 v[32:35], v[224:231], v[204:211], v[32:35], v171, v171 op_sel_hi:[0,0,0]
	v_mfma_scale_f32_16x16x128_f8f6f4 v[28:31], v[232:239], v[204:211], v[28:31], v171, v171 op_sel_hi:[0,0,0]
	v_mfma_scale_f32_16x16x128_f8f6f4 v[16:19], v[224:231], v[212:219], v[16:19], v171, v171 op_sel_hi:[0,0,0]
	v_mfma_scale_f32_16x16x128_f8f6f4 v[12:15], v[232:239], v[212:219], v[12:15], v171, v171 op_sel_hi:[0,0,0]
	s_barrier
	ds_read_b128 v[156:159], v176
	ds_read_b128 v[160:163], v176 offset:1024
	ds_read_b128 v[180:183], v176 offset:2048
	ds_read_b128 v[184:187], v176 offset:3072
	s_add_u32 s22, s22, 0x20180
	s_addc_u32 s23, s23, 0
	s_mov_b32 m0, s67
	v_lshl_add_u64 v[132:133], s[22:23], 0, v[136:137]
	ds_read_b128 v[188:191], v177
	ds_read_b128 v[192:195], v177 offset:1024
	ds_read_b128 v[196:199], v177 offset:2048
	ds_read_b128 v[200:203], v177 offset:3072
	ds_read_b128 v[204:207], v177 offset:4096
	ds_read_b128 v[208:211], v177 offset:5120
	ds_read_b128 v[212:215], v177 offset:6144
	ds_read_b128 v[216:219], v177 offset:7168
	global_load_lds_dwordx4 v[132:133], off
	v_lshl_add_u64 v[132:133], s[22:23], 0, v[140:141]
	s_mov_b32 m0, s61
	s_nop 0
	global_load_lds_dwordx4 v[132:133], off
	s_waitcnt lgkmcnt(8)
	s_barrier
	s_waitcnt lgkmcnt(0)
	s_waitcnt lgkmcnt(0)
	v_mfma_scale_f32_16x16x128_f8f6f4 v[108:111], v[156:163], v[188:195], v[108:111], v171, v171 op_sel_hi:[0,0,0]
	v_mfma_scale_f32_16x16x128_f8f6f4 v[112:115], v[180:187], v[188:195], v[112:115], v171, v171 op_sel_hi:[0,0,0]
	v_mfma_scale_f32_16x16x128_f8f6f4 v[104:107], v[156:163], v[196:203], v[104:107], v171, v171 op_sel_hi:[0,0,0]
	v_mfma_scale_f32_16x16x128_f8f6f4 v[100:103], v[180:187], v[196:203], v[100:103], v171, v171 op_sel_hi:[0,0,0]
	v_mfma_scale_f32_16x16x128_f8f6f4 v[80:83], v[156:163], v[204:211], v[80:83], v171, v171 op_sel_hi:[0,0,0]
	v_mfma_scale_f32_16x16x128_f8f6f4 v[76:79], v[180:187], v[204:211], v[76:79], v171, v171 op_sel_hi:[0,0,0]
	v_mfma_scale_f32_16x16x128_f8f6f4 v[48:51], v[156:163], v[212:219], v[48:51], v171, v171 op_sel_hi:[0,0,0]
	v_mfma_scale_f32_16x16x128_f8f6f4 v[44:47], v[180:187], v[212:219], v[44:47], v171, v171 op_sel_hi:[0,0,0]
	s_barrier
	s_mov_b32 m0, s64
	v_lshl_add_u64 v[132:133], s[2:3], 0, v[138:139]
	ds_read_b128 v[224:227], v178
	ds_read_b128 v[228:231], v178 offset:1024
	ds_read_b128 v[232:235], v178 offset:2048
	ds_read_b128 v[236:239], v178 offset:3072
	global_load_lds_dwordx4 v[132:133], off
	v_lshl_add_u64 v[134:135], s[2:3], 0, v[142:143]
	s_mov_b32 m0, s62
	s_nop 0
	global_load_lds_dwordx4 v[134:135], off
	s_barrier
	s_waitcnt lgkmcnt(0)
	s_waitcnt lgkmcnt(0)
	v_mfma_scale_f32_16x16x128_f8f6f4 v[124:127], v[224:231], v[188:195], v[124:127], v171, v171 op_sel_hi:[0,0,0]
	v_mfma_scale_f32_16x16x128_f8f6f4 v[128:131], v[232:239], v[188:195], v[128:131], v171, v171 op_sel_hi:[0,0,0]
	v_mfma_scale_f32_16x16x128_f8f6f4 v[120:123], v[224:231], v[196:203], v[120:123], v171, v171 op_sel_hi:[0,0,0]
	v_mfma_scale_f32_16x16x128_f8f6f4 v[116:119], v[232:239], v[196:203], v[116:119], v171, v171 op_sel_hi:[0,0,0]
	v_mfma_scale_f32_16x16x128_f8f6f4 v[96:99], v[224:231], v[204:211], v[96:99], v171, v171 op_sel_hi:[0,0,0]
	v_mfma_scale_f32_16x16x128_f8f6f4 v[92:95], v[232:239], v[204:211], v[92:95], v171, v171 op_sel_hi:[0,0,0]
	v_mfma_scale_f32_16x16x128_f8f6f4 v[64:67], v[224:231], v[212:219], v[64:67], v171, v171 op_sel_hi:[0,0,0]
	v_mfma_scale_f32_16x16x128_f8f6f4 v[60:63], v[232:239], v[212:219], v[60:63], v171, v171 op_sel_hi:[0,0,0]
	s_mov_b32 m0, s40
	v_lshl_add_u64 v[150:151], s[24:25], 0, v[136:137]
	s_barrier
	ds_read_b128 v[188:191], v177 offset:16384
	ds_read_b128 v[192:195], v177 offset:17408
	ds_read_b128 v[196:199], v177 offset:18432
	ds_read_b128 v[200:203], v177 offset:19456
	ds_read_b128 v[204:207], v177 offset:20480
	ds_read_b128 v[208:211], v177 offset:21504
	ds_read_b128 v[212:215], v177 offset:22528
	ds_read_b128 v[216:219], v177 offset:23552
	global_load_lds_dwordx4 v[150:151], off
	v_lshl_add_u64 v[152:153], s[24:25], 0, v[140:141]
	s_mov_b32 m0, s41
	s_nop 0
	global_load_lds_dwordx4 v[152:153], off
	s_barrier
	s_waitcnt lgkmcnt(0)
	s_waitcnt lgkmcnt(0)
	v_mfma_scale_f32_16x16x128_f8f6f4 v[72:75], v[156:163], v[188:195], v[72:75], v171, v171 op_sel_hi:[0,0,0]
	v_mfma_scale_f32_16x16x128_f8f6f4 v[68:71], v[180:187], v[188:195], v[68:71], v171, v171 op_sel_hi:[0,0,0]
	v_mfma_scale_f32_16x16x128_f8f6f4 v[40:43], v[156:163], v[196:203], v[40:43], v171, v171 op_sel_hi:[0,0,0]
	v_mfma_scale_f32_16x16x128_f8f6f4 v[36:39], v[180:187], v[196:203], v[36:39], v171, v171 op_sel_hi:[0,0,0]
	v_mfma_scale_f32_16x16x128_f8f6f4 v[24:27], v[156:163], v[204:211], v[24:27], v171, v171 op_sel_hi:[0,0,0]
	v_mfma_scale_f32_16x16x128_f8f6f4 v[20:23], v[180:187], v[204:211], v[20:23], v171, v171 op_sel_hi:[0,0,0]
	v_mfma_scale_f32_16x16x128_f8f6f4 v[8:11], v[156:163], v[212:219], v[8:11], v171, v171 op_sel_hi:[0,0,0]
	v_mfma_scale_f32_16x16x128_f8f6f4 v[4:7], v[180:187], v[212:219], v[4:7], v171, v171 op_sel_hi:[0,0,0]
	s_barrier
	s_add_u32 s22, s2, 0x10000
	s_addc_u32 s23, s3, 0
	s_mov_b32 m0, s65
	v_lshl_add_u64 v[156:157], s[22:23], 0, v[138:139]
	global_load_lds_dwordx4 v[156:157], off
	v_lshl_add_u64 v[156:157], s[22:23], 0, v[142:143]
	s_mov_b32 m0, s63
	s_nop 0
	global_load_lds_dwordx4 v[156:157], off
	s_waitcnt vmcnt(6)
	s_barrier
	v_mfma_scale_f32_16x16x128_f8f6f4 v[88:91], v[224:231], v[188:195], v[88:91], v171, v171 op_sel_hi:[0,0,0]
	v_mfma_scale_f32_16x16x128_f8f6f4 v[84:87], v[232:239], v[188:195], v[84:87], v171, v171 op_sel_hi:[0,0,0]
	v_mfma_scale_f32_16x16x128_f8f6f4 v[56:59], v[224:231], v[196:203], v[56:59], v171, v171 op_sel_hi:[0,0,0]
	v_mfma_scale_f32_16x16x128_f8f6f4 v[52:55], v[232:239], v[196:203], v[52:55], v171, v171 op_sel_hi:[0,0,0]
	v_mfma_scale_f32_16x16x128_f8f6f4 v[32:35], v[224:231], v[204:211], v[32:35], v171, v171 op_sel_hi:[0,0,0]
	v_mfma_scale_f32_16x16x128_f8f6f4 v[28:31], v[232:239], v[204:211], v[28:31], v171, v171 op_sel_hi:[0,0,0]
	v_mfma_scale_f32_16x16x128_f8f6f4 v[16:19], v[224:231], v[212:219], v[16:19], v171, v171 op_sel_hi:[0,0,0]
	v_mfma_scale_f32_16x16x128_f8f6f4 v[12:15], v[232:239], v[212:219], v[12:15], v171, v171 op_sel_hi:[0,0,0]
	s_barrier
	ds_read_b128 v[156:159], v154
	ds_read_b128 v[160:163], v154 offset:1024
	ds_read_b128 v[180:183], v154 offset:2048
	ds_read_b128 v[184:187], v154 offset:3072
	s_add_u32 s22, s24, 0x20000
	s_addc_u32 s23, s25, 0
	s_mov_b32 m0, s42
	v_lshl_add_u64 v[164:165], s[22:23], 0, v[136:137]
	ds_read_b128 v[188:191], v177 offset:32768
	ds_read_b128 v[192:195], v177 offset:33792
	ds_read_b128 v[196:199], v177 offset:34816
	ds_read_b128 v[200:203], v177 offset:35840
	ds_read_b128 v[204:207], v177 offset:36864
	ds_read_b128 v[208:211], v177 offset:37888
	ds_read_b128 v[212:215], v177 offset:38912
	ds_read_b128 v[216:219], v177 offset:39936
	global_load_lds_dwordx4 v[164:165], off
	v_lshl_add_u64 v[164:165], s[22:23], 0, v[140:141]
	s_mov_b32 m0, s43
	s_nop 0
	global_load_lds_dwordx4 v[164:165], off
	s_waitcnt lgkmcnt(8)
	s_barrier
	s_waitcnt lgkmcnt(0)
	s_waitcnt lgkmcnt(0)
	v_mfma_scale_f32_16x16x128_f8f6f4 v[108:111], v[156:163], v[188:195], v[108:111], v171, v171 op_sel_hi:[0,0,0]
	v_mfma_scale_f32_16x16x128_f8f6f4 v[112:115], v[180:187], v[188:195], v[112:115], v171, v171 op_sel_hi:[0,0,0]
	v_mfma_scale_f32_16x16x128_f8f6f4 v[104:107], v[156:163], v[196:203], v[104:107], v171, v171 op_sel_hi:[0,0,0]
	v_mfma_scale_f32_16x16x128_f8f6f4 v[100:103], v[180:187], v[196:203], v[100:103], v171, v171 op_sel_hi:[0,0,0]
	v_mfma_scale_f32_16x16x128_f8f6f4 v[80:83], v[156:163], v[204:211], v[80:83], v171, v171 op_sel_hi:[0,0,0]
	v_mfma_scale_f32_16x16x128_f8f6f4 v[76:79], v[180:187], v[204:211], v[76:79], v171, v171 op_sel_hi:[0,0,0]
	v_mfma_scale_f32_16x16x128_f8f6f4 v[48:51], v[156:163], v[212:219], v[48:51], v171, v171 op_sel_hi:[0,0,0]
	v_mfma_scale_f32_16x16x128_f8f6f4 v[44:47], v[180:187], v[212:219], v[44:47], v171, v171 op_sel_hi:[0,0,0]
	s_barrier
	s_mov_b32 m0, s68
	v_lshl_add_u64 v[132:133], v[132:133], 0, s[8:9]
	ds_read_b128 v[224:227], v155
	ds_read_b128 v[228:231], v155 offset:1024
	ds_read_b128 v[232:235], v155 offset:2048
	ds_read_b128 v[236:239], v155 offset:3072
	global_load_lds_dwordx4 v[132:133], off
	v_lshl_add_u64 v[132:133], v[134:135], 0, s[8:9]
	s_mov_b32 m0, s66
	s_nop 0
	global_load_lds_dwordx4 v[132:133], off
	s_barrier
	s_waitcnt lgkmcnt(0)
	s_waitcnt lgkmcnt(0)
	v_mfma_scale_f32_16x16x128_f8f6f4 v[124:127], v[224:231], v[188:195], v[124:127], v171, v171 op_sel_hi:[0,0,0]
	v_mfma_scale_f32_16x16x128_f8f6f4 v[128:131], v[232:239], v[188:195], v[128:131], v171, v171 op_sel_hi:[0,0,0]
	v_mfma_scale_f32_16x16x128_f8f6f4 v[120:123], v[224:231], v[196:203], v[120:123], v171, v171 op_sel_hi:[0,0,0]
	v_mfma_scale_f32_16x16x128_f8f6f4 v[116:119], v[232:239], v[196:203], v[116:119], v171, v171 op_sel_hi:[0,0,0]
	v_mfma_scale_f32_16x16x128_f8f6f4 v[96:99], v[224:231], v[204:211], v[96:99], v171, v171 op_sel_hi:[0,0,0]
	v_mfma_scale_f32_16x16x128_f8f6f4 v[92:95], v[232:239], v[204:211], v[92:95], v171, v171 op_sel_hi:[0,0,0]
	v_mfma_scale_f32_16x16x128_f8f6f4 v[64:67], v[224:231], v[212:219], v[64:67], v171, v171 op_sel_hi:[0,0,0]
	v_mfma_scale_f32_16x16x128_f8f6f4 v[60:63], v[232:239], v[212:219], v[60:63], v171, v171 op_sel_hi:[0,0,0]
	s_mov_b32 m0, s46
	v_lshl_add_u64 v[132:133], v[150:151], 0, s[8:9]
	s_barrier
	ds_read_b128 v[188:191], v177 offset:49152
	ds_read_b128 v[192:195], v177 offset:50176
	ds_read_b128 v[196:199], v177 offset:51200
	ds_read_b128 v[200:203], v177 offset:52224
	ds_read_b128 v[204:207], v177 offset:53248
	ds_read_b128 v[208:211], v177 offset:54272
	ds_read_b128 v[212:215], v177 offset:55296
	ds_read_b128 v[216:219], v177 offset:56320
	global_load_lds_dwordx4 v[132:133], off
	v_lshl_add_u64 v[132:133], v[152:153], 0, s[8:9]
	s_mov_b32 m0, s47
	s_nop 0
	global_load_lds_dwordx4 v[132:133], off
	s_barrier
	s_waitcnt lgkmcnt(0)
	s_waitcnt lgkmcnt(0)
	v_mfma_scale_f32_16x16x128_f8f6f4 v[72:75], v[156:163], v[188:195], v[72:75], v171, v171 op_sel_hi:[0,0,0]
	v_mfma_scale_f32_16x16x128_f8f6f4 v[68:71], v[180:187], v[188:195], v[68:71], v171, v171 op_sel_hi:[0,0,0]
	v_mfma_scale_f32_16x16x128_f8f6f4 v[40:43], v[156:163], v[196:203], v[40:43], v171, v171 op_sel_hi:[0,0,0]
	v_mfma_scale_f32_16x16x128_f8f6f4 v[36:39], v[180:187], v[196:203], v[36:39], v171, v171 op_sel_hi:[0,0,0]
	v_mfma_scale_f32_16x16x128_f8f6f4 v[24:27], v[156:163], v[204:211], v[24:27], v171, v171 op_sel_hi:[0,0,0]
	v_mfma_scale_f32_16x16x128_f8f6f4 v[20:23], v[180:187], v[204:211], v[20:23], v171, v171 op_sel_hi:[0,0,0]
	v_mfma_scale_f32_16x16x128_f8f6f4 v[8:11], v[156:163], v[212:219], v[8:11], v171, v171 op_sel_hi:[0,0,0]
	v_mfma_scale_f32_16x16x128_f8f6f4 v[4:7], v[180:187], v[212:219], v[4:7], v171, v171 op_sel_hi:[0,0,0]
	s_barrier
	s_add_u32 s2, s2, 0x10080
	s_addc_u32 s3, s3, 0
	s_mov_b32 m0, s27
	v_lshl_add_u64 v[132:133], s[2:3], 0, v[138:139]
	global_load_lds_dwordx4 v[132:133], off
	v_lshl_add_u64 v[132:133], s[2:3], 0, v[142:143]
	s_mov_b32 m0, s26
	s_nop 0
	global_load_lds_dwordx4 v[132:133], off
	s_waitcnt vmcnt(6)
	s_barrier
	v_mfma_scale_f32_16x16x128_f8f6f4 v[88:91], v[224:231], v[188:195], v[88:91], v171, v171 op_sel_hi:[0,0,0]
	v_mfma_scale_f32_16x16x128_f8f6f4 v[84:87], v[232:239], v[188:195], v[84:87], v171, v171 op_sel_hi:[0,0,0]
	v_mfma_scale_f32_16x16x128_f8f6f4 v[56:59], v[224:231], v[196:203], v[56:59], v171, v171 op_sel_hi:[0,0,0]
	v_mfma_scale_f32_16x16x128_f8f6f4 v[52:55], v[232:239], v[196:203], v[52:55], v171, v171 op_sel_hi:[0,0,0]
	v_mfma_scale_f32_16x16x128_f8f6f4 v[32:35], v[224:231], v[204:211], v[32:35], v171, v171 op_sel_hi:[0,0,0]
	v_mfma_scale_f32_16x16x128_f8f6f4 v[28:31], v[232:239], v[204:211], v[28:31], v171, v171 op_sel_hi:[0,0,0]
	v_mfma_scale_f32_16x16x128_f8f6f4 v[16:19], v[224:231], v[212:219], v[16:19], v171, v171 op_sel_hi:[0,0,0]
	v_mfma_scale_f32_16x16x128_f8f6f4 v[12:15], v[232:239], v[212:219], v[12:15], v171, v171 op_sel_hi:[0,0,0]
	v_lshl_add_u32 v164, s60, 8, v173
	s_cmp_lt_i32 s59, 6
	s_cselect_b32 s2, 0, 32
	v_or_b32_e32 v162, 16, v164
	s_cselect_b32 s24, s52, 0x47b1c000
	s_cselect_b32 s22, s53, 0x800
	s_cselect_b32 s23, 0, -6
	s_add_u32 s2, s44, s2
	v_ashrrev_i32_e32 v165, 31, v164
	v_ashrrev_i32_e32 v163, 31, v162
	s_addc_u32 s3, s45, 0
	v_lshlrev_b64 v[132:133], 6, v[164:165]
	v_lshlrev_b64 v[150:151], 6, v[162:163]
	s_barrier
	s_nop 7
	s_nop 7
	s_nop 7
	v_lshl_add_u64 v[132:133], s[2:3], 0, v[132:133]
	v_lshl_add_u64 v[150:151], s[2:3], 0, v[150:151]
	global_load_dwordx4 v[180:183], v[132:133], off
	s_nop 0
	global_load_dwordx4 v[132:135], v[132:133], off offset:16
	s_nop 0
	global_load_dwordx4 v[184:187], v[150:151], off
	global_load_dwordx4 v[188:191], v[150:151], off offset:16
	v_or_b32_e32 v160, 32, v164
	v_ashrrev_i32_e32 v161, 31, v160
	v_lshlrev_b64 v[150:151], 6, v[160:161]
	v_or_b32_e32 v158, 48, v164
	v_lshl_add_u64 v[150:151], s[2:3], 0, v[150:151]
	v_ashrrev_i32_e32 v159, 31, v158
	global_load_dwordx4 v[192:195], v[150:151], off
	global_load_dwordx4 v[196:199], v[150:151], off offset:16
	v_lshlrev_b64 v[150:151], 6, v[158:159]
	v_lshl_add_u64 v[150:151], s[2:3], 0, v[150:151]
	global_load_dwordx4 v[200:203], v[150:151], off
	global_load_dwordx4 v[204:207], v[150:151], off offset:16
	v_add_u32_e32 v156, 0x80, v164
	v_add_u32_e32 v150, 0xb0, v164
	v_add_u32_e32 v154, 0x90, v164
	v_add_u32_e32 v152, 0xa0, v164
	v_ashrrev_i32_e32 v157, 31, v156
	v_ashrrev_i32_e32 v151, 31, v150
	v_ashrrev_i32_e32 v155, 31, v154
	v_ashrrev_i32_e32 v153, 31, v152
	v_lshlrev_b64 v[208:209], 6, v[156:157]
	v_lshlrev_b64 v[214:215], 6, v[150:151]
	v_lshlrev_b64 v[210:211], 6, v[154:155]
	v_lshlrev_b64 v[212:213], 6, v[152:153]
	v_lshl_add_u64 v[216:217], s[2:3], 0, v[208:209]
	v_lshl_add_u64 v[240:241], s[2:3], 0, v[214:215]
	v_lshl_add_u64 v[220:221], s[2:3], 0, v[210:211]
	v_lshl_add_u64 v[222:223], s[2:3], 0, v[212:213]
	global_load_dwordx4 v[208:211], v[216:217], off
	global_load_dwordx4 v[212:215], v[216:217], off offset:16
	s_nop 0
	global_load_dwordx4 v[216:219], v[220:221], off
	global_load_dwordx4 v[224:227], v[220:221], off offset:16
	global_load_dwordx4 v[228:231], v[222:223], off
	global_load_dwordx4 v[232:235], v[222:223], off offset:16
	global_load_dwordx4 v[236:239], v[240:241], off
	s_nop 0
	global_load_dwordx4 v[240:243], v[240:241], off offset:16
	s_mov_b32 s60, s56
	s_mov_b64 s[26:27], s[20:21]
	s_waitcnt vmcnt(0)
	v_mov_b32_e32 v220, v180
	v_mov_b32_e32 v221, v132
	v_mov_b32_e32 v132, v181
	v_mov_b32_e32 v180, v182
	v_mov_b32_e32 v181, v134
	v_mov_b32_e32 v134, v183
	v_mov_b32_e32 v182, v184
	v_mov_b32_e32 v183, v188
	v_mov_b32_e32 v188, v185
	v_mov_b32_e32 v184, v186
	v_mov_b32_e32 v185, v190
	v_mov_b32_e32 v190, v187
	v_pk_add_f32 v[132:133], v[220:221], v[132:133]
	v_pk_add_f32 v[134:135], v[180:181], v[134:135]
	v_pk_add_f32 v[180:181], v[182:183], v[188:189]
	v_pk_add_f32 v[182:183], v[184:185], v[190:191]
	v_pk_add_f32 v[132:133], v[132:133], v[134:135]
	v_pk_add_f32 v[134:135], v[180:181], v[182:183]
	v_mov_b32_e32 v181, v132
	v_mov_b32_e32 v180, v134
	v_mov_b32_e32 v132, v135
	v_pk_add_f32 v[132:133], v[180:181], v[132:133]
	v_mov_b32_e32 v186, v192
	v_pk_fma_f32 v[132:133], v[132:133], s[16:17], v[148:149] op_sel_hi:[1,0,0]
	v_mov_b32_e32 v187, v196
	v_mul_f32_e32 v134, 0x4b800000, v133
	v_mul_f32_e32 v135, 0x4b800000, v132
	v_cmp_gt_f32_e32 vcc, s54, v133
	v_cmp_gt_f32_e64 s[2:3], s54, v132
	v_mov_b32_e32 v196, v193
	v_cndmask_b32_e32 v133, v133, v134, vcc
	v_cndmask_b32_e64 v132, v132, v135, s[2:3]
	v_rsq_f32_e32 v134, v133
	v_rsq_f32_e32 v135, v132
	v_mov_b32_e32 v192, v194
	v_mov_b32_e32 v193, v198
	v_mul_f32_e32 v151, 0x45800000, v134
	v_mul_f32_e32 v153, 0x45800000, v135
	v_cndmask_b32_e32 v134, v134, v151, vcc
	v_cndmask_b32_e64 v135, v135, v153, s[2:3]
	v_mov_b32_e32 v198, v195
	v_pk_add_f32 v[132:133], v[186:187], v[196:197]
	v_mul_f32_e32 v180, 0x3c800000, v134
	v_mul_f32_e32 v182, 0x3c800000, v135
	v_pk_add_f32 v[134:135], v[192:193], v[198:199]
	v_mov_b32_e32 v184, v202
	v_pk_add_f32 v[132:133], v[132:133], v[134:135]
	v_mov_b32_e32 v134, v200
	v_mov_b32_e32 v135, v204
	v_mov_b32_e32 v204, v201
	v_mov_b32_e32 v185, v206
	v_mov_b32_e32 v206, v203
	v_pk_add_f32 v[134:135], v[134:135], v[204:205]
	v_pk_add_f32 v[184:185], v[184:185], v[206:207]
	v_mov_b32_e32 v186, v218
	v_pk_add_f32 v[134:135], v[134:135], v[184:185]
	v_mov_b32_e32 v185, v132
	v_mov_b32_e32 v184, v134
	v_mov_b32_e32 v132, v135
	v_pk_add_f32 v[132:133], v[184:185], v[132:133]
	v_mov_b32_e32 v135, v214
	v_pk_fma_f32 v[132:133], v[132:133], s[16:17], v[148:149] op_sel_hi:[1,0,0]
	v_mov_b32_e32 v214, v211
	v_mul_f32_e32 v134, 0x4b800000, v133
	v_cmp_gt_f32_e32 vcc, s54, v133
	v_cmp_gt_f32_e64 s[2:3], s54, v132
	v_mov_b32_e32 v187, v226
	v_cndmask_b32_e32 v133, v133, v134, vcc
	v_rsq_f32_e32 v133, v133
	v_mul_f32_e32 v134, 0x4b800000, v132
	v_cndmask_b32_e64 v132, v132, v134, s[2:3]
	v_rsq_f32_e32 v132, v132
	v_mul_f32_e32 v134, 0x45800000, v133
	v_cndmask_b32_e32 v133, v133, v134, vcc
	v_mul_f32_e32 v184, 0x3c800000, v133
	v_mul_f32_e32 v133, 0x45800000, v132
	v_cndmask_b32_e64 v132, v132, v133, s[2:3]
	v_mul_f32_e32 v172, 0x3c800000, v132
	v_mov_b32_e32 v132, v208
	v_mov_b32_e32 v133, v212
	v_mov_b32_e32 v212, v209
	v_mov_b32_e32 v134, v210
	v_pk_add_f32 v[132:133], v[132:133], v[212:213]
	v_pk_add_f32 v[134:135], v[134:135], v[214:215]
	v_mov_b32_e32 v226, v219
	v_pk_add_f32 v[132:133], v[132:133], v[134:135]
	v_mov_b32_e32 v134, v216
	v_mov_b32_e32 v135, v224
	v_mov_b32_e32 v224, v217
	v_pk_add_f32 v[134:135], v[134:135], v[224:225]
	v_pk_add_f32 v[186:187], v[186:187], v[226:227]
	v_pk_mul_f32 v[108:109], v[108:109], v[180:181] op_sel_hi:[1,0]
	v_pk_add_f32 v[134:135], v[134:135], v[186:187]
	v_mov_b32_e32 v187, v132
	v_mov_b32_e32 v186, v134
	v_mov_b32_e32 v132, v135
	v_pk_add_f32 v[132:133], v[186:187], v[132:133]
	v_mov_b32_e32 v135, v234
	v_pk_fma_f32 v[132:133], v[132:133], s[16:17], v[148:149] op_sel_hi:[1,0,0]
	v_mov_b32_e32 v234, v231
	v_mul_f32_e32 v134, 0x4b800000, v133
	v_cmp_gt_f32_e32 vcc, s54, v133
	v_cmp_gt_f32_e64 s[2:3], s54, v132
	v_mov_b32_e32 v186, v238
	v_cndmask_b32_e32 v133, v133, v134, vcc
	v_rsq_f32_e32 v133, v133
	v_mul_f32_e32 v134, 0x4b800000, v132
	v_cndmask_b32_e64 v132, v132, v134, s[2:3]
	v_rsq_f32_e32 v132, v132
	v_mul_f32_e32 v134, 0x45800000, v133
	v_cndmask_b32_e32 v133, v133, v134, vcc
	v_mul_f32_e32 v170, 0x3c800000, v133
	v_mul_f32_e32 v133, 0x45800000, v132
	v_cndmask_b32_e64 v132, v132, v133, s[2:3]
	v_mul_f32_e32 v168, 0x3c800000, v132
	v_mov_b32_e32 v132, v228
	v_mov_b32_e32 v133, v232
	v_mov_b32_e32 v232, v229
	v_mov_b32_e32 v134, v230
	v_pk_add_f32 v[132:133], v[132:133], v[232:233]
	v_pk_add_f32 v[134:135], v[134:135], v[234:235]
	v_mov_b32_e32 v187, v242
	v_pk_add_f32 v[132:133], v[132:133], v[134:135]
	v_mov_b32_e32 v134, v236
	v_mov_b32_e32 v135, v240
	v_mov_b32_e32 v240, v237
	v_mov_b32_e32 v242, v239
	v_pk_add_f32 v[134:135], v[134:135], v[240:241]
	v_pk_add_f32 v[186:187], v[186:187], v[242:243]
	v_pk_mul_f32 v[110:111], v[110:111], v[180:181] op_sel_hi:[1,0]
	v_pk_add_f32 v[134:135], v[134:135], v[186:187]
	v_mov_b32_e32 v187, v132
	v_mov_b32_e32 v186, v134
	v_mov_b32_e32 v132, v135
	v_pk_add_f32 v[132:133], v[186:187], v[132:133]
	v_cvt_pk_bf16_f32 v108, v108, v109
	v_cvt_pk_bf16_f32 v109, v110, v111
	v_pk_mul_f32 v[114:115], v[114:115], v[180:181] op_sel_hi:[1,0]
	v_pk_fma_f32 v[132:133], v[132:133], s[16:17], v[148:149] op_sel_hi:[1,0,0]
	v_pk_mul_f32 v[112:113], v[112:113], v[180:181] op_sel_hi:[1,0]
	v_mul_f32_e32 v134, 0x4b800000, v133
	v_cmp_gt_f32_e32 vcc, s54, v133
	v_cmp_gt_f32_e64 s[2:3], s54, v132
	v_cvt_pk_bf16_f32 v110, v112, v113
	v_cvt_pk_bf16_f32 v111, v114, v115
	v_pk_mul_f32 v[112:113], v[130:131], v[180:181] op_sel_hi:[1,0]
	v_cndmask_b32_e32 v133, v133, v134, vcc
	v_rsq_f32_e32 v133, v133
	v_mul_f32_e32 v134, 0x4b800000, v132
	v_cndmask_b32_e64 v132, v132, v134, s[2:3]
	v_rsq_f32_e32 v132, v132
	v_mul_f32_e32 v134, 0x45800000, v133
	v_cndmask_b32_e32 v133, v133, v134, vcc
	v_mul_f32_e32 v166, 0x3c800000, v133
	v_mul_f32_e32 v133, 0x45800000, v132
	v_cndmask_b32_e64 v132, v132, v133, s[2:3]
	s_add_u32 s2, s4, s24
	s_addc_u32 s3, s5, 0
	s_add_i32 s23, s23, s59
	v_lshl_or_b32 v134, s23, 8, v175
	v_ashrrev_i32_e32 v135, 31, v134
	v_lshl_add_u64 v[134:135], v[134:135], 1, s[2:3]
	v_mad_i64_i32 v[164:165], s[2:3], s22, v164, 0
	v_lshl_add_u64 v[164:165], v[164:165], 1, v[134:135]
	global_store_dwordx4 v[164:165], v[108:111], off
	v_pk_mul_f32 v[114:115], v[128:129], v[180:181] op_sel_hi:[1,0]
	v_pk_mul_f32 v[106:107], v[106:107], v[182:183] op_sel_hi:[1,0]
	v_pk_mul_f32 v[108:109], v[124:125], v[180:181] op_sel_hi:[1,0]
	v_pk_mul_f32 v[110:111], v[126:127], v[180:181] op_sel_hi:[1,0]
	v_cvt_pk_bf16_f32 v108, v108, v109
	v_pk_mul_f32 v[104:105], v[104:105], v[182:183] op_sel_hi:[1,0]
	v_cvt_pk_bf16_f32 v109, v110, v111
	v_cvt_pk_bf16_f32 v110, v114, v115
	v_cvt_pk_bf16_f32 v111, v112, v113
	global_store_dwordx4 v[164:165], v[108:111], off offset:256
	v_pk_mul_f32 v[82:83], v[82:83], v[184:185] op_sel_hi:[1,0]
	v_pk_mul_f32 v[80:81], v[80:81], v[184:185] op_sel_hi:[1,0]
	v_mad_i64_i32 v[108:109], s[2:3], s22, v162, 0
	v_lshl_add_u64 v[108:109], v[108:109], 1, v[134:135]
	v_pk_mul_f32 v[110:111], v[102:103], v[182:183] op_sel_hi:[1,0]
	v_pk_mul_f32 v[102:103], v[100:101], v[182:183] op_sel_hi:[1,0]
	v_cvt_pk_bf16_f32 v100, v104, v105
	v_cvt_pk_bf16_f32 v101, v106, v107
	v_pk_mul_f32 v[104:105], v[118:119], v[182:183] op_sel_hi:[1,0]
	v_cvt_pk_bf16_f32 v102, v102, v103
	v_cvt_pk_bf16_f32 v103, v110, v111
	global_store_dwordx4 v[108:109], v[100:103], off
	v_pk_mul_f32 v[106:107], v[116:117], v[182:183] op_sel_hi:[1,0]
	v_pk_mul_f32 v[50:51], v[50:51], v[172:173] op_sel_hi:[1,0]
	v_pk_mul_f32 v[100:101], v[120:121], v[182:183] op_sel_hi:[1,0]
	v_pk_mul_f32 v[102:103], v[122:123], v[182:183] op_sel_hi:[1,0]
	v_cvt_pk_bf16_f32 v100, v100, v101
	v_pk_mul_f32 v[48:49], v[48:49], v[172:173] op_sel_hi:[1,0]
	v_cvt_pk_bf16_f32 v101, v102, v103
	v_cvt_pk_bf16_f32 v102, v106, v107
	v_cvt_pk_bf16_f32 v103, v104, v105
	global_store_dwordx4 v[108:109], v[100:103], off offset:256
	v_pk_mul_f32 v[42:43], v[42:43], v[168:169] op_sel_hi:[1,0]
	v_pk_mul_f32 v[40:41], v[40:41], v[168:169] op_sel_hi:[1,0]
	v_mad_i64_i32 v[100:101], s[2:3], s22, v160, 0
	v_lshl_add_u64 v[100:101], v[100:101], 1, v[134:135]
	v_pk_mul_f32 v[102:103], v[78:79], v[184:185] op_sel_hi:[1,0]
	v_pk_mul_f32 v[78:79], v[76:77], v[184:185] op_sel_hi:[1,0]
	v_cvt_pk_bf16_f32 v76, v80, v81
	v_cvt_pk_bf16_f32 v77, v82, v83
	v_pk_mul_f32 v[80:81], v[94:95], v[184:185] op_sel_hi:[1,0]
	v_cvt_pk_bf16_f32 v78, v78, v79
	v_cvt_pk_bf16_f32 v79, v102, v103
	global_store_dwordx4 v[100:101], v[76:79], off
	v_pk_mul_f32 v[82:83], v[92:93], v[184:185] op_sel_hi:[1,0]
	v_pk_mul_f32 v[26:27], v[26:27], v[166:167] op_sel_hi:[1,0]
	v_pk_mul_f32 v[76:77], v[96:97], v[184:185] op_sel_hi:[1,0]
	v_pk_mul_f32 v[78:79], v[98:99], v[184:185] op_sel_hi:[1,0]
	v_cvt_pk_bf16_f32 v76, v76, v77
	v_pk_mul_f32 v[24:25], v[24:25], v[166:167] op_sel_hi:[1,0]
	v_cvt_pk_bf16_f32 v77, v78, v79
	v_cvt_pk_bf16_f32 v78, v82, v83
	v_cvt_pk_bf16_f32 v79, v80, v81
	global_store_dwordx4 v[100:101], v[76:79], off offset:256
	v_mul_f32_e32 v132, 0x3c800000, v132
	v_pk_mul_f32 v[10:11], v[10:11], v[132:133] op_sel_hi:[1,0]
	v_mad_i64_i32 v[76:77], s[2:3], s22, v158, 0
	v_lshl_add_u64 v[76:77], v[76:77], 1, v[134:135]
	v_pk_mul_f32 v[78:79], v[46:47], v[172:173] op_sel_hi:[1,0]
	v_pk_mul_f32 v[46:47], v[44:45], v[172:173] op_sel_hi:[1,0]
	v_cvt_pk_bf16_f32 v44, v48, v49
	v_cvt_pk_bf16_f32 v45, v50, v51
	v_pk_mul_f32 v[48:49], v[62:63], v[172:173] op_sel_hi:[1,0]
	v_cvt_pk_bf16_f32 v46, v46, v47
	v_cvt_pk_bf16_f32 v47, v78, v79
	global_store_dwordx4 v[76:77], v[44:47], off
	v_pk_mul_f32 v[50:51], v[60:61], v[172:173] op_sel_hi:[1,0]
	v_pk_mul_f32 v[60:61], v[68:69], v[170:171] op_sel_hi:[1,0]
	v_pk_mul_f32 v[44:45], v[64:65], v[172:173] op_sel_hi:[1,0]
	v_pk_mul_f32 v[46:47], v[66:67], v[172:173] op_sel_hi:[1,0]
	v_cvt_pk_bf16_f32 v44, v44, v45
	v_pk_mul_f32 v[8:9], v[8:9], v[132:133] op_sel_hi:[1,0]
	v_cvt_pk_bf16_f32 v45, v46, v47
	v_cvt_pk_bf16_f32 v46, v50, v51
	v_cvt_pk_bf16_f32 v47, v48, v49
	global_store_dwordx4 v[76:77], v[44:47], off offset:256
	v_pk_mul_f32 v[50:51], v[70:71], v[170:171] op_sel_hi:[1,0]
	s_add_i32 s49, s49, s17
	v_mad_i64_i32 v[44:45], s[2:3], s22, v156, 0
	v_lshl_add_u64 v[48:49], v[44:45], 1, v[134:135]
	v_pk_mul_f32 v[46:47], v[74:75], v[170:171] op_sel_hi:[1,0]
	v_pk_mul_f32 v[44:45], v[72:73], v[170:171] op_sel_hi:[1,0]
	s_andn2_b64 vcc, exec, s[0:1]
	v_cvt_pk_bf16_f32 v44, v44, v45
	v_cvt_pk_bf16_f32 v45, v46, v47
	v_cvt_pk_bf16_f32 v46, v60, v61
	v_cvt_pk_bf16_f32 v47, v50, v51
	global_store_dwordx4 v[48:49], v[44:47], off
	v_pk_mul_f32 v[50:51], v[86:87], v[170:171] op_sel_hi:[1,0]
	v_pk_mul_f32 v[60:61], v[84:85], v[170:171] op_sel_hi:[1,0]
	v_pk_mul_f32 v[46:47], v[90:91], v[170:171] op_sel_hi:[1,0]
	v_pk_mul_f32 v[44:45], v[88:89], v[170:171] op_sel_hi:[1,0]
	s_mov_b32 s59, s55
	v_cvt_pk_bf16_f32 v44, v44, v45
	v_cvt_pk_bf16_f32 v45, v46, v47
	v_cvt_pk_bf16_f32 v46, v60, v61
	v_cvt_pk_bf16_f32 v47, v50, v51
	global_store_dwordx4 v[48:49], v[44:47], off offset:256
	s_nop 1
	v_mad_i64_i32 v[44:45], s[2:3], s22, v154, 0
	v_pk_mul_f32 v[46:47], v[38:39], v[168:169] op_sel_hi:[1,0]
	v_pk_mul_f32 v[38:39], v[36:37], v[168:169] op_sel_hi:[1,0]
	v_lshl_add_u64 v[44:45], v[44:45], 1, v[134:135]
	v_cvt_pk_bf16_f32 v36, v40, v41
	v_cvt_pk_bf16_f32 v37, v42, v43
	v_cvt_pk_bf16_f32 v38, v38, v39
	v_cvt_pk_bf16_f32 v39, v46, v47
	global_store_dwordx4 v[44:45], v[36:39], off
	v_pk_mul_f32 v[40:41], v[54:55], v[168:169] op_sel_hi:[1,0]
	v_pk_mul_f32 v[42:43], v[52:53], v[168:169] op_sel_hi:[1,0]
	v_pk_mul_f32 v[38:39], v[58:59], v[168:169] op_sel_hi:[1,0]
	v_pk_mul_f32 v[36:37], v[56:57], v[168:169] op_sel_hi:[1,0]
	s_nop 0
	v_cvt_pk_bf16_f32 v36, v36, v37
	v_cvt_pk_bf16_f32 v37, v38, v39
	v_cvt_pk_bf16_f32 v38, v42, v43
	v_cvt_pk_bf16_f32 v39, v40, v41
	global_store_dwordx4 v[44:45], v[36:39], off offset:256
	s_nop 1
	v_mad_i64_i32 v[36:37], s[2:3], s22, v152, 0
	v_pk_mul_f32 v[38:39], v[22:23], v[166:167] op_sel_hi:[1,0]
	v_pk_mul_f32 v[22:23], v[20:21], v[166:167] op_sel_hi:[1,0]
	v_lshl_add_u64 v[36:37], v[36:37], 1, v[134:135]
	v_cvt_pk_bf16_f32 v20, v24, v25
	v_cvt_pk_bf16_f32 v21, v26, v27
	v_cvt_pk_bf16_f32 v22, v22, v23
	v_cvt_pk_bf16_f32 v23, v38, v39
	global_store_dwordx4 v[36:37], v[20:23], off
	v_pk_mul_f32 v[24:25], v[30:31], v[166:167] op_sel_hi:[1,0]
	v_pk_mul_f32 v[26:27], v[28:29], v[166:167] op_sel_hi:[1,0]
	v_pk_mul_f32 v[22:23], v[34:35], v[166:167] op_sel_hi:[1,0]
	v_pk_mul_f32 v[20:21], v[32:33], v[166:167] op_sel_hi:[1,0]
	s_nop 0
	v_cvt_pk_bf16_f32 v20, v20, v21
	v_cvt_pk_bf16_f32 v21, v22, v23
	v_cvt_pk_bf16_f32 v22, v26, v27
	v_cvt_pk_bf16_f32 v23, v24, v25
	global_store_dwordx4 v[36:37], v[20:23], off offset:256
	s_nop 1
	v_mad_i64_i32 v[20:21], s[2:3], s22, v150, 0
	v_pk_mul_f32 v[22:23], v[6:7], v[132:133] op_sel_hi:[1,0]
	v_pk_mul_f32 v[6:7], v[4:5], v[132:133] op_sel_hi:[1,0]
	v_lshl_add_u64 v[20:21], v[20:21], 1, v[134:135]
	v_cvt_pk_bf16_f32 v4, v8, v9
	v_cvt_pk_bf16_f32 v5, v10, v11
	v_cvt_pk_bf16_f32 v6, v6, v7
	v_cvt_pk_bf16_f32 v7, v22, v23
	global_store_dwordx4 v[20:21], v[4:7], off
	s_mov_b64 s[22:23], s[18:19]
	v_pk_mul_f32 v[8:9], v[14:15], v[132:133] op_sel_hi:[1,0]
	v_pk_mul_f32 v[6:7], v[18:19], v[132:133] op_sel_hi:[1,0]
	v_pk_mul_f32 v[4:5], v[16:17], v[132:133] op_sel_hi:[1,0]
	v_pk_mul_f32 v[10:11], v[12:13], v[132:133] op_sel_hi:[1,0]
	v_cvt_pk_bf16_f32 v4, v4, v5
	v_cvt_pk_bf16_f32 v5, v6, v7
	s_nop 0
	v_cvt_pk_bf16_f32 v6, v10, v11
	v_cvt_pk_bf16_f32 v7, v8, v9
	global_store_dwordx4 v[20:21], v[4:7], off offset:256
	s_cbranch_vccz .LBB0_1686

.LBB0_2191:
	ds_read_b128 v[8:11], v230
	ds_read_b128 v[12:15], v230 offset:1024
	ds_read_b128 v[0:3], v230 offset:2048
	ds_read_b128 v[4:7], v230 offset:3072
	v_lshl_add_u64 v[172:173], v[170:171], 0, s[2:3]
	s_add_i32 s92, s70, 0xc000
	v_lshl_add_u64 v[174:175], v[172:173], 0, s[8:9]
	s_mov_b32 m0, s92
	ds_read_b128 v[180:183], v227
	ds_read_b128 v[184:187], v227 offset:1024
	ds_read_b128 v[188:191], v227 offset:2048
	ds_read_b128 v[192:195], v227 offset:3072
	ds_read_b128 v[196:199], v227 offset:4096
	ds_read_b128 v[200:203], v227 offset:5120
	ds_read_b128 v[204:207], v227 offset:6144
	ds_read_b128 v[208:211], v227 offset:7168
	global_load_lds_dwordx4 v[174:175], off
	v_lshl_add_u64 v[174:175], v[168:169], 0, s[2:3]
	s_add_i32 s91, s70, 0xe000
	v_lshl_add_u64 v[176:177], v[174:175], 0, s[8:9]
	s_mov_b32 m0, s91
	s_nop 0
	global_load_lds_dwordx4 v[176:177], off
	s_waitcnt lgkmcnt(8)
	s_barrier
	s_waitcnt lgkmcnt(0)
	s_waitcnt lgkmcnt(0)
	v_mfma_scale_f32_16x16x128_f8f6f4 v[16:19], v[8:15], v[180:187], v[16:19], v224, v224 op_sel_hi:[0,0,0]
	v_mfma_scale_f32_16x16x128_f8f6f4 v[20:23], v[0:7], v[180:187], v[20:23], v224, v224 op_sel_hi:[0,0,0]
	v_mfma_scale_f32_16x16x128_f8f6f4 v[24:27], v[8:15], v[188:195], v[24:27], v224, v224 op_sel_hi:[0,0,0]
	v_mfma_scale_f32_16x16x128_f8f6f4 v[28:31], v[0:7], v[188:195], v[28:31], v224, v224 op_sel_hi:[0,0,0]
	v_mfma_scale_f32_16x16x128_f8f6f4 v[32:35], v[8:15], v[196:203], v[32:35], v224, v224 op_sel_hi:[0,0,0]
	v_mfma_scale_f32_16x16x128_f8f6f4 v[36:39], v[0:7], v[196:203], v[36:39], v224, v224 op_sel_hi:[0,0,0]
	v_mfma_scale_f32_16x16x128_f8f6f4 v[40:43], v[8:15], v[204:211], v[40:43], v224, v224 op_sel_hi:[0,0,0]
	v_mfma_scale_f32_16x16x128_f8f6f4 v[44:47], v[0:7], v[204:211], v[44:47], v224, v224 op_sel_hi:[0,0,0]
	s_barrier
	v_lshl_add_u64 v[176:177], v[146:147], 0, s[2:3]
	s_add_i32 s94, s80, s69
	v_lshl_add_u64 v[178:179], v[176:177], 0, s[10:11]
	s_mov_b32 m0, s94
	ds_read_b128 v[212:215], v231
	ds_read_b128 v[216:219], v231 offset:1024
	ds_read_b128 v[234:237], v231 offset:2048
	ds_read_b128 v[238:241], v231 offset:3072
	global_load_lds_dwordx4 v[178:179], off
	v_lshl_add_u64 v[178:179], v[144:145], 0, s[2:3]
	s_add_i32 s93, s94, 0x2000
	v_lshl_add_u64 v[220:221], v[178:179], 0, s[10:11]
	s_mov_b32 m0, s93
	s_nop 0
	global_load_lds_dwordx4 v[220:221], off
	s_barrier
	s_waitcnt lgkmcnt(0)
	s_waitcnt lgkmcnt(0)
	v_mfma_scale_f32_16x16x128_f8f6f4 v[48:51], v[212:219], v[180:187], v[48:51], v224, v224 op_sel_hi:[0,0,0]
	v_mfma_scale_f32_16x16x128_f8f6f4 v[52:55], v[234:241], v[180:187], v[52:55], v224, v224 op_sel_hi:[0,0,0]
	v_mfma_scale_f32_16x16x128_f8f6f4 v[56:59], v[212:219], v[188:195], v[56:59], v224, v224 op_sel_hi:[0,0,0]
	v_mfma_scale_f32_16x16x128_f8f6f4 v[60:63], v[234:241], v[188:195], v[60:63], v224, v224 op_sel_hi:[0,0,0]
	v_mfma_scale_f32_16x16x128_f8f6f4 v[64:67], v[212:219], v[196:203], v[64:67], v224, v224 op_sel_hi:[0,0,0]
	v_mfma_scale_f32_16x16x128_f8f6f4 v[68:71], v[234:241], v[196:203], v[68:71], v224, v224 op_sel_hi:[0,0,0]
	v_mfma_scale_f32_16x16x128_f8f6f4 v[72:75], v[212:219], v[204:211], v[72:75], v224, v224 op_sel_hi:[0,0,0]
	v_mfma_scale_f32_16x16x128_f8f6f4 v[76:79], v[234:241], v[204:211], v[76:79], v224, v224 op_sel_hi:[0,0,0]
	s_mov_b32 m0, s70
	v_lshl_add_u64 v[220:221], v[172:173], 0, s[10:11]
	s_barrier
	ds_read_b128 v[180:183], v227 offset:16384
	ds_read_b128 v[184:187], v227 offset:17408
	ds_read_b128 v[188:191], v227 offset:18432
	ds_read_b128 v[192:195], v227 offset:19456
	ds_read_b128 v[196:199], v227 offset:20480
	ds_read_b128 v[200:203], v227 offset:21504
	ds_read_b128 v[204:207], v227 offset:22528
	ds_read_b128 v[208:211], v227 offset:23552
	global_load_lds_dwordx4 v[220:221], off
	v_lshl_add_u64 v[220:221], v[174:175], 0, s[10:11]
	s_mov_b32 m0, s71
	s_nop 0
	global_load_lds_dwordx4 v[220:221], off
	s_barrier
	s_waitcnt lgkmcnt(0)
	s_waitcnt lgkmcnt(0)
	v_mfma_scale_f32_16x16x128_f8f6f4 v[80:83], v[8:15], v[180:187], v[80:83], v224, v224 op_sel_hi:[0,0,0]
	v_mfma_scale_f32_16x16x128_f8f6f4 v[84:87], v[0:7], v[180:187], v[84:87], v224, v224 op_sel_hi:[0,0,0]
	v_mfma_scale_f32_16x16x128_f8f6f4 v[88:91], v[8:15], v[188:195], v[88:91], v224, v224 op_sel_hi:[0,0,0]
	v_mfma_scale_f32_16x16x128_f8f6f4 v[92:95], v[0:7], v[188:195], v[92:95], v224, v224 op_sel_hi:[0,0,0]
	v_mfma_scale_f32_16x16x128_f8f6f4 v[96:99], v[8:15], v[196:203], v[96:99], v224, v224 op_sel_hi:[0,0,0]
	v_mfma_scale_f32_16x16x128_f8f6f4 v[100:103], v[0:7], v[196:203], v[100:103], v224, v224 op_sel_hi:[0,0,0]
	v_mfma_scale_f32_16x16x128_f8f6f4 v[104:107], v[8:15], v[204:211], v[104:107], v224, v224 op_sel_hi:[0,0,0]
	v_mfma_scale_f32_16x16x128_f8f6f4 v[108:111], v[0:7], v[204:211], v[108:111], v224, v224 op_sel_hi:[0,0,0]
	s_barrier
	s_add_i32 s52, s81, s69
	v_lshl_add_u64 v[0:1], v[176:177], 0, s[12:13]
	s_mov_b32 m0, s52
	s_add_i32 s95, s52, 0x2000
	global_load_lds_dwordx4 v[0:1], off
	v_lshl_add_u64 v[0:1], v[178:179], 0, s[12:13]
	s_mov_b32 m0, s95
	s_nop 0
	global_load_lds_dwordx4 v[0:1], off
	s_waitcnt vmcnt(6)
	s_barrier
	v_mfma_scale_f32_16x16x128_f8f6f4 v[112:115], v[212:219], v[180:187], v[112:115], v224, v224 op_sel_hi:[0,0,0]
	v_mfma_scale_f32_16x16x128_f8f6f4 v[116:119], v[234:241], v[180:187], v[116:119], v224, v224 op_sel_hi:[0,0,0]
	v_mfma_scale_f32_16x16x128_f8f6f4 v[120:123], v[212:219], v[188:195], v[120:123], v224, v224 op_sel_hi:[0,0,0]
	v_mfma_scale_f32_16x16x128_f8f6f4 v[124:127], v[234:241], v[188:195], v[124:127], v224, v224 op_sel_hi:[0,0,0]
	v_mfma_scale_f32_16x16x128_f8f6f4 v[128:131], v[212:219], v[196:203], v[128:131], v224, v224 op_sel_hi:[0,0,0]
	v_mfma_scale_f32_16x16x128_f8f6f4 v[132:135], v[234:241], v[196:203], v[132:135], v224, v224 op_sel_hi:[0,0,0]
	v_mfma_scale_f32_16x16x128_f8f6f4 v[136:139], v[212:219], v[204:211], v[136:139], v224, v224 op_sel_hi:[0,0,0]
	v_mfma_scale_f32_16x16x128_f8f6f4 v[140:143], v[234:241], v[204:211], v[140:143], v224, v224 op_sel_hi:[0,0,0]
	s_add_i32 s63, 0, 0x18000
	v_add_u32_e32 v234, s63, v226
	s_barrier
	ds_read_b128 v[0:3], v234
	ds_read_b128 v[4:7], v234 offset:1024
	ds_read_b128 v[8:11], v234 offset:2048
	ds_read_b128 v[12:15], v234 offset:3072
	s_mov_b32 m0, s72
	v_lshl_add_u64 v[212:213], v[172:173], 0, s[12:13]
	ds_read_b128 v[180:183], v227 offset:32768
	ds_read_b128 v[184:187], v227 offset:33792
	ds_read_b128 v[188:191], v227 offset:34816
	ds_read_b128 v[192:195], v227 offset:35840
	ds_read_b128 v[196:199], v227 offset:36864
	ds_read_b128 v[200:203], v227 offset:37888
	ds_read_b128 v[204:207], v227 offset:38912
	ds_read_b128 v[208:211], v227 offset:39936
	global_load_lds_dwordx4 v[212:213], off
	v_lshl_add_u64 v[212:213], v[174:175], 0, s[12:13]
	s_mov_b32 m0, s73
	s_nop 0
	global_load_lds_dwordx4 v[212:213], off
	s_waitcnt lgkmcnt(8)
	s_barrier
	s_waitcnt lgkmcnt(0)
	s_waitcnt lgkmcnt(0)
	v_mfma_scale_f32_16x16x128_f8f6f4 v[16:19], v[0:7], v[180:187], v[16:19], v224, v224 op_sel_hi:[0,0,0]
	v_mfma_scale_f32_16x16x128_f8f6f4 v[20:23], v[8:15], v[180:187], v[20:23], v224, v224 op_sel_hi:[0,0,0]
	v_mfma_scale_f32_16x16x128_f8f6f4 v[24:27], v[0:7], v[188:195], v[24:27], v224, v224 op_sel_hi:[0,0,0]
	v_mfma_scale_f32_16x16x128_f8f6f4 v[28:31], v[8:15], v[188:195], v[28:31], v224, v224 op_sel_hi:[0,0,0]
	v_mfma_scale_f32_16x16x128_f8f6f4 v[32:35], v[0:7], v[196:203], v[32:35], v224, v224 op_sel_hi:[0,0,0]
	v_mfma_scale_f32_16x16x128_f8f6f4 v[36:39], v[8:15], v[196:203], v[36:39], v224, v224 op_sel_hi:[0,0,0]
	v_mfma_scale_f32_16x16x128_f8f6f4 v[40:43], v[0:7], v[204:211], v[40:43], v224, v224 op_sel_hi:[0,0,0]
	v_mfma_scale_f32_16x16x128_f8f6f4 v[44:47], v[8:15], v[204:211], v[44:47], v224, v224 op_sel_hi:[0,0,0]
	s_barrier
	s_add_i32 s64, 0, 0x1c000
	s_add_i32 s63, s63, s69
	v_add_u32_e32 v233, s64, v226
	v_lshl_add_u64 v[220:221], v[176:177], 0, s[16:17]
	s_mov_b32 m0, s63
	s_add_i32 s62, s63, 0x2000
	ds_read_b128 v[212:215], v233
	ds_read_b128 v[216:219], v233 offset:1024
	ds_read_b128 v[236:239], v233 offset:2048
	ds_read_b128 v[240:243], v233 offset:3072
	global_load_lds_dwordx4 v[220:221], off
	v_lshl_add_u64 v[220:221], v[178:179], 0, s[16:17]
	s_mov_b32 m0, s62
	s_nop 0
	global_load_lds_dwordx4 v[220:221], off
	s_barrier
	s_waitcnt lgkmcnt(0)
	s_waitcnt lgkmcnt(0)
	v_mfma_scale_f32_16x16x128_f8f6f4 v[48:51], v[212:219], v[180:187], v[48:51], v224, v224 op_sel_hi:[0,0,0]
	v_mfma_scale_f32_16x16x128_f8f6f4 v[52:55], v[236:243], v[180:187], v[52:55], v224, v224 op_sel_hi:[0,0,0]
	v_mfma_scale_f32_16x16x128_f8f6f4 v[56:59], v[212:219], v[188:195], v[56:59], v224, v224 op_sel_hi:[0,0,0]
	v_mfma_scale_f32_16x16x128_f8f6f4 v[60:63], v[236:243], v[188:195], v[60:63], v224, v224 op_sel_hi:[0,0,0]
	v_mfma_scale_f32_16x16x128_f8f6f4 v[64:67], v[212:219], v[196:203], v[64:67], v224, v224 op_sel_hi:[0,0,0]
	v_mfma_scale_f32_16x16x128_f8f6f4 v[68:71], v[236:243], v[196:203], v[68:71], v224, v224 op_sel_hi:[0,0,0]
	v_mfma_scale_f32_16x16x128_f8f6f4 v[72:75], v[212:219], v[204:211], v[72:75], v224, v224 op_sel_hi:[0,0,0]
	v_mfma_scale_f32_16x16x128_f8f6f4 v[76:79], v[236:243], v[204:211], v[76:79], v224, v224 op_sel_hi:[0,0,0]
	s_mov_b32 m0, s77
	v_lshl_add_u64 v[172:173], v[172:173], 0, s[16:17]
	s_barrier
	ds_read_b128 v[180:183], v227 offset:49152
	ds_read_b128 v[184:187], v227 offset:50176
	ds_read_b128 v[188:191], v227 offset:51200
	ds_read_b128 v[192:195], v227 offset:52224
	ds_read_b128 v[196:199], v227 offset:53248
	ds_read_b128 v[200:203], v227 offset:54272
	ds_read_b128 v[204:207], v227 offset:55296
	ds_read_b128 v[208:211], v227 offset:56320
	global_load_lds_dwordx4 v[172:173], off
	v_lshl_add_u64 v[172:173], v[174:175], 0, s[16:17]
	s_mov_b32 m0, s78
	s_nop 0
	global_load_lds_dwordx4 v[172:173], off
	s_barrier
	s_waitcnt lgkmcnt(0)
	s_waitcnt lgkmcnt(0)
	v_mfma_scale_f32_16x16x128_f8f6f4 v[80:83], v[0:7], v[180:187], v[80:83], v224, v224 op_sel_hi:[0,0,0]
	v_mfma_scale_f32_16x16x128_f8f6f4 v[84:87], v[8:15], v[180:187], v[84:87], v224, v224 op_sel_hi:[0,0,0]
	v_mfma_scale_f32_16x16x128_f8f6f4 v[88:91], v[0:7], v[188:195], v[88:91], v224, v224 op_sel_hi:[0,0,0]
	v_mfma_scale_f32_16x16x128_f8f6f4 v[92:95], v[8:15], v[188:195], v[92:95], v224, v224 op_sel_hi:[0,0,0]
	v_mfma_scale_f32_16x16x128_f8f6f4 v[96:99], v[0:7], v[196:203], v[96:99], v224, v224 op_sel_hi:[0,0,0]
	v_mfma_scale_f32_16x16x128_f8f6f4 v[100:103], v[8:15], v[196:203], v[100:103], v224, v224 op_sel_hi:[0,0,0]
	v_mfma_scale_f32_16x16x128_f8f6f4 v[104:107], v[0:7], v[204:211], v[104:107], v224, v224 op_sel_hi:[0,0,0]
	v_mfma_scale_f32_16x16x128_f8f6f4 v[108:111], v[8:15], v[204:211], v[108:111], v224, v224 op_sel_hi:[0,0,0]
	s_barrier
	s_add_i32 s64, s64, s69
	v_lshl_add_u64 v[0:1], v[176:177], 0, s[18:19]
	s_mov_b32 m0, s64
	s_add_i32 s53, s64, 0x2000
	global_load_lds_dwordx4 v[0:1], off
	v_lshl_add_u64 v[0:1], v[178:179], 0, s[18:19]
	s_mov_b32 m0, s53
	s_nop 0
	global_load_lds_dwordx4 v[0:1], off
	s_waitcnt vmcnt(6)
	s_barrier
	v_mfma_scale_f32_16x16x128_f8f6f4 v[112:115], v[212:219], v[180:187], v[112:115], v224, v224 op_sel_hi:[0,0,0]
	v_mfma_scale_f32_16x16x128_f8f6f4 v[116:119], v[236:243], v[180:187], v[116:119], v224, v224 op_sel_hi:[0,0,0]
	v_mfma_scale_f32_16x16x128_f8f6f4 v[120:123], v[212:219], v[188:195], v[120:123], v224, v224 op_sel_hi:[0,0,0]
	v_mfma_scale_f32_16x16x128_f8f6f4 v[124:127], v[236:243], v[188:195], v[124:127], v224, v224 op_sel_hi:[0,0,0]
	v_mfma_scale_f32_16x16x128_f8f6f4 v[128:131], v[212:219], v[196:203], v[128:131], v224, v224 op_sel_hi:[0,0,0]
	v_mfma_scale_f32_16x16x128_f8f6f4 v[132:135], v[236:243], v[196:203], v[132:135], v224, v224 op_sel_hi:[0,0,0]
	v_mfma_scale_f32_16x16x128_f8f6f4 v[136:139], v[212:219], v[204:211], v[136:139], v224, v224 op_sel_hi:[0,0,0]
	v_mfma_scale_f32_16x16x128_f8f6f4 v[140:143], v[236:243], v[204:211], v[140:143], v224, v224 op_sel_hi:[0,0,0]
	s_add_i32 s42, s42, 2
	s_add_u32 s2, s2, 0x100
	s_addc_u32 s3, s3, 0
	s_cmp_gt_u32 s42, 5
	s_barrier
	s_cbranch_scc0 .LBB0_2191
	s_add_u32 s42, s65, s87
	s_addc_u32 s43, s66, 0
	s_add_u32 s44, s67, s88
	s_addc_u32 s45, s68, 0
	s_and_b64 s[2:3], vcc, exec
	s_mul_i32 s2, s90, 24
	s_cselect_b32 s51, s43, s47
	s_cselect_b32 s50, s42, s46
	s_add_i32 s56, s2, s89
	s_ashr_i32 s57, s56, 31
	s_lshl_b64 s[2:3], s[56:57], 16
	s_add_u32 s2, s75, s2
	s_addc_u32 s3, s76, s3
	s_add_i32 s54, s56, 8
	s_ashr_i32 s55, s54, 31
	v_mov_b32_e32 v156, v229
	s_lshl_b64 s[54:55], s[54:55], 16
	s_nop 7
	s_nop 7
	s_nop 7
	s_add_u32 s54, s75, s54
	s_addc_u32 s55, s76, s55
	global_load_dwordx2 v[210:211], v156, s[2:3]
	global_load_dwordx2 v[216:217], v156, s[54:55]
	global_load_dwordx2 v[206:207], v156, s[2:3] offset:512
	global_load_dwordx2 v[208:209], v156, s[54:55] offset:512
	global_load_dwordx2 v[202:203], v156, s[2:3] offset:1024
	global_load_dwordx2 v[204:205], v156, s[54:55] offset:1024
	global_load_dwordx2 v[198:199], v156, s[2:3] offset:1536
	global_load_dwordx2 v[200:201], v156, s[54:55] offset:1536
	global_load_dwordx2 v[194:195], v156, s[2:3] offset:2048
	global_load_dwordx2 v[196:197], v156, s[54:55] offset:2048
	global_load_dwordx2 v[190:191], v156, s[2:3] offset:2560
	global_load_dwordx2 v[192:193], v156, s[54:55] offset:2560
	global_load_dwordx2 v[186:187], v156, s[2:3] offset:3072
	global_load_dwordx2 v[188:189], v156, s[54:55] offset:3072
	global_load_dwordx2 v[182:183], v156, s[2:3] offset:3584
	global_load_dwordx2 v[184:185], v156, s[54:55] offset:3584
	v_lshl_add_u64 v[0:1], s[2:3], 0, v[156:157]
	v_lshl_add_u64 v[2:3], s[54:55], 0, v[156:157]
	v_add_co_u32_e64 v0, s[2:3], s82, v0
	s_waitcnt vmcnt(0)
	v_cvt_f32_ubyte3_e32 v237, v210
	v_cvt_f32_ubyte0_e32 v156, v216
	v_add_f32_e32 v156, 0.5, v156
	v_rcp_f32_e32 v218, v156
	v_cvt_f32_ubyte0_e32 v156, v217
	v_add_f32_e32 v156, 0.5, v156
	v_rcp_f32_e32 v212, v156
	v_cvt_f32_ubyte1_e32 v156, v216
	v_add_f32_e32 v156, 0.5, v156
	v_rcp_f32_e32 v219, v156
	v_cvt_f32_ubyte1_e32 v156, v217
	v_add_f32_e32 v156, 0.5, v156
	v_rcp_f32_e32 v213, v156
	v_cvt_f32_ubyte2_e32 v156, v216
	v_add_f32_e32 v156, 0.5, v156
	v_rcp_f32_e32 v220, v156
	v_cvt_f32_ubyte2_e32 v156, v217
	v_add_f32_e32 v156, 0.5, v156
	v_rcp_f32_e32 v214, v156
	v_cvt_f32_ubyte3_e32 v156, v216
	v_add_f32_e32 v156, 0.5, v156
	v_rcp_f32_e32 v221, v156
	v_cvt_f32_ubyte3_e32 v156, v217
	v_add_f32_e32 v156, 0.5, v156
	v_cvt_f32_ubyte1_e32 v217, v210
	v_cvt_f32_ubyte0_e32 v216, v210
	v_cvt_f32_ubyte2_e32 v236, v210
	v_rcp_f32_e32 v215, v156
	v_pk_add_f32 v[236:237], v[236:237], 0.5 op_sel_hi:[1,0]
	v_pk_add_f32 v[216:217], v[216:217], 0.5 op_sel_hi:[1,0]
	v_cvt_f32_ubyte0_e32 v156, v208
	v_pk_mul_f32 v[216:217], v[216:217], v[218:219]
	v_pk_mul_f32 v[218:219], v[236:237], v[220:221]
	v_pk_mul_f32 v[16:17], v[16:17], v[216:217]
	v_pk_mul_f32 v[18:19], v[18:19], v[218:219]
	v_cvt_f32_ubyte3_e32 v219, v211
	v_cvt_f32_ubyte2_e32 v218, v211
	v_cvt_f32_ubyte1_e32 v217, v211
	v_cvt_f32_ubyte0_e32 v216, v211
	v_pk_add_f32 v[210:211], v[218:219], 0.5 op_sel_hi:[1,0]
	v_add_f32_e32 v156, 0.5, v156
	v_pk_mul_f32 v[210:211], v[210:211], v[214:215]
	v_pk_add_f32 v[216:217], v[216:217], 0.5 op_sel_hi:[1,0]
	v_pk_mul_f32 v[22:23], v[22:23], v[210:211]
	v_rcp_f32_e32 v210, v156
	v_cvt_f32_ubyte0_e32 v156, v209
	v_pk_mul_f32 v[212:213], v[216:217], v[212:213]
	v_add_f32_e32 v156, 0.5, v156
	v_pk_mul_f32 v[20:21], v[20:21], v[212:213]
	v_rcp_f32_e32 v212, v156
	v_cvt_f32_ubyte1_e32 v156, v208
	v_add_f32_e32 v156, 0.5, v156
	v_rcp_f32_e32 v211, v156
	v_cvt_f32_ubyte1_e32 v156, v209
	v_add_f32_e32 v156, 0.5, v156
	v_rcp_f32_e32 v213, v156
	v_cvt_f32_ubyte2_e32 v156, v208
	v_add_f32_e32 v156, 0.5, v156
	v_rcp_f32_e32 v214, v156
	v_cvt_f32_ubyte2_e32 v156, v209
	v_add_f32_e32 v156, 0.5, v156
	v_rcp_f32_e32 v216, v156
	v_cvt_f32_ubyte3_e32 v156, v208
	v_add_f32_e32 v156, 0.5, v156
	v_rcp_f32_e32 v215, v156
	v_cvt_f32_ubyte3_e32 v156, v209
	v_add_f32_e32 v156, 0.5, v156
	v_cvt_f32_ubyte1_e32 v209, v206
	v_cvt_f32_ubyte0_e32 v208, v206
	v_cvt_f32_ubyte3_e32 v219, v206
	v_cvt_f32_ubyte2_e32 v218, v206
	v_rcp_f32_e32 v217, v156
	v_pk_add_f32 v[218:219], v[218:219], 0.5 op_sel_hi:[1,0]
	v_pk_add_f32 v[208:209], v[208:209], 0.5 op_sel_hi:[1,0]
	v_cvt_f32_ubyte0_e32 v156, v204
	v_pk_mul_f32 v[208:209], v[208:209], v[210:211]
	v_pk_mul_f32 v[210:211], v[218:219], v[214:215]
	v_pk_mul_f32 v[48:49], v[48:49], v[208:209]
	v_pk_mul_f32 v[50:51], v[50:51], v[210:211]
	v_cvt_f32_ubyte3_e32 v211, v207
	v_cvt_f32_ubyte2_e32 v210, v207
	v_cvt_f32_ubyte1_e32 v209, v207
	v_cvt_f32_ubyte0_e32 v208, v207
	v_pk_add_f32 v[206:207], v[210:211], 0.5 op_sel_hi:[1,0]
	v_add_f32_e32 v156, 0.5, v156
	v_pk_mul_f32 v[206:207], v[206:207], v[216:217]
	v_pk_add_f32 v[208:209], v[208:209], 0.5 op_sel_hi:[1,0]
	v_pk_mul_f32 v[54:55], v[54:55], v[206:207]
	v_rcp_f32_e32 v206, v156
	v_cvt_f32_ubyte0_e32 v156, v205
	v_pk_mul_f32 v[208:209], v[208:209], v[212:213]
	v_add_f32_e32 v156, 0.5, v156
	v_pk_mul_f32 v[52:53], v[52:53], v[208:209]
	v_rcp_f32_e32 v208, v156
	v_cvt_f32_ubyte1_e32 v156, v204
	v_add_f32_e32 v156, 0.5, v156
	v_rcp_f32_e32 v207, v156
	v_cvt_f32_ubyte1_e32 v156, v205
	v_add_f32_e32 v156, 0.5, v156
	v_rcp_f32_e32 v209, v156
	v_cvt_f32_ubyte2_e32 v156, v204
	v_add_f32_e32 v156, 0.5, v156
	v_rcp_f32_e32 v210, v156
	v_cvt_f32_ubyte2_e32 v156, v205
	v_add_f32_e32 v156, 0.5, v156
	v_rcp_f32_e32 v212, v156
	v_cvt_f32_ubyte3_e32 v156, v204
	v_add_f32_e32 v156, 0.5, v156
	v_rcp_f32_e32 v211, v156
	v_cvt_f32_ubyte3_e32 v156, v205
	v_add_f32_e32 v156, 0.5, v156
	v_cvt_f32_ubyte1_e32 v205, v202
	v_cvt_f32_ubyte0_e32 v204, v202
	v_cvt_f32_ubyte3_e32 v215, v202
	v_cvt_f32_ubyte2_e32 v214, v202
	v_rcp_f32_e32 v213, v156
	v_pk_add_f32 v[214:215], v[214:215], 0.5 op_sel_hi:[1,0]
	v_pk_add_f32 v[204:205], v[204:205], 0.5 op_sel_hi:[1,0]
	v_cvt_f32_ubyte0_e32 v156, v200
	v_pk_mul_f32 v[204:205], v[204:205], v[206:207]
	v_pk_mul_f32 v[206:207], v[214:215], v[210:211]
	v_pk_mul_f32 v[24:25], v[24:25], v[204:205]
	v_pk_mul_f32 v[26:27], v[26:27], v[206:207]
	v_cvt_f32_ubyte3_e32 v207, v203
	v_cvt_f32_ubyte2_e32 v206, v203
	v_cvt_f32_ubyte1_e32 v205, v203
	v_cvt_f32_ubyte0_e32 v204, v203
	v_pk_add_f32 v[202:203], v[206:207], 0.5 op_sel_hi:[1,0]
	v_add_f32_e32 v156, 0.5, v156
	v_pk_mul_f32 v[202:203], v[202:203], v[212:213]
	v_pk_add_f32 v[204:205], v[204:205], 0.5 op_sel_hi:[1,0]
	v_pk_mul_f32 v[30:31], v[30:31], v[202:203]
	v_rcp_f32_e32 v202, v156
	v_cvt_f32_ubyte0_e32 v156, v201
	v_pk_mul_f32 v[204:205], v[204:205], v[208:209]
	v_add_f32_e32 v156, 0.5, v156
	v_pk_mul_f32 v[28:29], v[28:29], v[204:205]
	v_rcp_f32_e32 v204, v156
	v_cvt_f32_ubyte1_e32 v156, v200
	v_add_f32_e32 v156, 0.5, v156
	v_rcp_f32_e32 v203, v156
	v_cvt_f32_ubyte1_e32 v156, v201
	v_add_f32_e32 v156, 0.5, v156
	v_rcp_f32_e32 v205, v156
	v_cvt_f32_ubyte2_e32 v156, v200
	v_add_f32_e32 v156, 0.5, v156
	v_rcp_f32_e32 v206, v156
	v_cvt_f32_ubyte2_e32 v156, v201
	v_add_f32_e32 v156, 0.5, v156
	v_rcp_f32_e32 v208, v156
	v_cvt_f32_ubyte3_e32 v156, v200
	v_add_f32_e32 v156, 0.5, v156
	v_rcp_f32_e32 v207, v156
	v_cvt_f32_ubyte3_e32 v156, v201
	v_add_f32_e32 v156, 0.5, v156
	v_cvt_f32_ubyte1_e32 v201, v198
	v_cvt_f32_ubyte0_e32 v200, v198
	v_cvt_f32_ubyte3_e32 v211, v198
	v_cvt_f32_ubyte2_e32 v210, v198
	v_rcp_f32_e32 v209, v156
	v_pk_add_f32 v[210:211], v[210:211], 0.5 op_sel_hi:[1,0]
	v_pk_add_f32 v[200:201], v[200:201], 0.5 op_sel_hi:[1,0]
	v_cvt_f32_ubyte0_e32 v156, v196
	v_pk_mul_f32 v[200:201], v[200:201], v[202:203]
	v_pk_mul_f32 v[202:203], v[210:211], v[206:207]
	v_pk_mul_f32 v[56:57], v[56:57], v[200:201]
	v_pk_mul_f32 v[58:59], v[58:59], v[202:203]
	v_cvt_f32_ubyte3_e32 v203, v199
	v_cvt_f32_ubyte2_e32 v202, v199
	v_cvt_f32_ubyte1_e32 v201, v199
	v_cvt_f32_ubyte0_e32 v200, v199
	v_pk_add_f32 v[198:199], v[202:203], 0.5 op_sel_hi:[1,0]
	v_add_f32_e32 v156, 0.5, v156
	v_pk_mul_f32 v[198:199], v[198:199], v[208:209]
	v_pk_add_f32 v[200:201], v[200:201], 0.5 op_sel_hi:[1,0]
	v_pk_mul_f32 v[62:63], v[62:63], v[198:199]
	v_rcp_f32_e32 v198, v156
	v_cvt_f32_ubyte0_e32 v156, v197
	v_pk_mul_f32 v[200:201], v[200:201], v[204:205]
	v_add_f32_e32 v156, 0.5, v156
	v_pk_mul_f32 v[60:61], v[60:61], v[200:201]
	v_rcp_f32_e32 v200, v156
	v_cvt_f32_ubyte1_e32 v156, v196
	v_add_f32_e32 v156, 0.5, v156
	v_rcp_f32_e32 v199, v156
	v_cvt_f32_ubyte1_e32 v156, v197
	v_add_f32_e32 v156, 0.5, v156
	v_rcp_f32_e32 v201, v156
	v_cvt_f32_ubyte2_e32 v156, v196
	v_add_f32_e32 v156, 0.5, v156
	v_rcp_f32_e32 v202, v156
	v_cvt_f32_ubyte2_e32 v156, v197
	v_addc_co_u32_e64 v1, s[2:3], 0, v1, s[2:3]
	v_add_f32_e32 v156, 0.5, v156
	v_add_co_u32_e64 v6, s[2:3], s82, v2
	v_rcp_f32_e32 v204, v156
	v_cvt_f32_ubyte3_e32 v156, v196
	v_addc_co_u32_e64 v7, s[2:3], 0, v3, s[2:3]
	v_add_f32_e32 v156, 0.5, v156
	global_load_dwordx2 v[178:179], v[0:1], off
	global_load_dwordx2 v[180:181], v[6:7], off
	global_load_dwordx2 v[174:175], v[0:1], off offset:512
	global_load_dwordx2 v[176:177], v[6:7], off offset:512
	global_load_dwordx2 v[170:171], v[0:1], off offset:1024
	global_load_dwordx2 v[172:173], v[6:7], off offset:1024
	global_load_dwordx2 v[144:145], v[0:1], off offset:1536
	global_load_dwordx2 v[146:147], v[6:7], off offset:1536
	global_load_dwordx2 v[12:13], v[0:1], off offset:2048
	global_load_dwordx2 v[14:15], v[6:7], off offset:2048
	global_load_dwordx2 v[8:9], v[0:1], off offset:2560
	global_load_dwordx2 v[10:11], v[6:7], off offset:2560
	global_load_dwordx2 v[2:3], v[0:1], off offset:3072
	global_load_dwordx2 v[4:5], v[6:7], off offset:3072
	s_nop 0
	global_load_dwordx2 v[0:1], v[0:1], off offset:3584
	s_nop 0
	global_load_dwordx2 v[6:7], v[6:7], off offset:3584
	v_rcp_f32_e32 v203, v156
	v_cvt_f32_ubyte3_e32 v156, v197
	v_add_f32_e32 v156, 0.5, v156
	v_cvt_f32_ubyte1_e32 v197, v194
	v_cvt_f32_ubyte0_e32 v196, v194
	v_cvt_f32_ubyte3_e32 v207, v194
	v_cvt_f32_ubyte2_e32 v206, v194
	v_rcp_f32_e32 v205, v156
	v_pk_add_f32 v[206:207], v[206:207], 0.5 op_sel_hi:[1,0]
	v_pk_add_f32 v[196:197], v[196:197], 0.5 op_sel_hi:[1,0]
	v_cvt_f32_ubyte0_e32 v156, v192
	v_pk_mul_f32 v[196:197], v[196:197], v[198:199]
	v_pk_mul_f32 v[198:199], v[206:207], v[202:203]
	v_pk_mul_f32 v[32:33], v[32:33], v[196:197]
	v_pk_mul_f32 v[34:35], v[34:35], v[198:199]
	v_cvt_f32_ubyte3_e32 v199, v195
	v_cvt_f32_ubyte2_e32 v198, v195
	v_cvt_f32_ubyte1_e32 v197, v195
	v_cvt_f32_ubyte0_e32 v196, v195
	v_pk_add_f32 v[194:195], v[198:199], 0.5 op_sel_hi:[1,0]
	v_add_f32_e32 v156, 0.5, v156
	v_pk_mul_f32 v[194:195], v[194:195], v[204:205]
	v_pk_add_f32 v[196:197], v[196:197], 0.5 op_sel_hi:[1,0]
	v_pk_mul_f32 v[38:39], v[38:39], v[194:195]
	v_rcp_f32_e32 v194, v156
	v_cvt_f32_ubyte0_e32 v156, v193
	v_pk_mul_f32 v[196:197], v[196:197], v[200:201]
	v_add_f32_e32 v156, 0.5, v156
	v_pk_mul_f32 v[36:37], v[36:37], v[196:197]
	v_rcp_f32_e32 v196, v156
	v_cvt_f32_ubyte1_e32 v156, v192
	v_add_f32_e32 v156, 0.5, v156
	v_rcp_f32_e32 v195, v156
	v_cvt_f32_ubyte1_e32 v156, v193
	v_add_f32_e32 v156, 0.5, v156
	v_rcp_f32_e32 v197, v156
	v_cvt_f32_ubyte2_e32 v156, v192
	v_add_f32_e32 v156, 0.5, v156
	v_rcp_f32_e32 v198, v156
	v_cvt_f32_ubyte2_e32 v156, v193
	v_add_f32_e32 v156, 0.5, v156
	v_rcp_f32_e32 v200, v156
	v_cvt_f32_ubyte3_e32 v156, v192
	v_add_f32_e32 v156, 0.5, v156
	v_rcp_f32_e32 v199, v156
	v_cvt_f32_ubyte3_e32 v156, v193
	v_add_f32_e32 v156, 0.5, v156
	v_cvt_f32_ubyte1_e32 v193, v190
	v_cvt_f32_ubyte0_e32 v192, v190
	v_cvt_f32_ubyte3_e32 v203, v190
	v_cvt_f32_ubyte2_e32 v202, v190
	v_rcp_f32_e32 v201, v156
	v_pk_add_f32 v[202:203], v[202:203], 0.5 op_sel_hi:[1,0]
	v_pk_add_f32 v[192:193], v[192:193], 0.5 op_sel_hi:[1,0]
	v_cvt_f32_ubyte0_e32 v156, v188
	v_pk_mul_f32 v[192:193], v[192:193], v[194:195]
	v_pk_mul_f32 v[194:195], v[202:203], v[198:199]
	v_pk_mul_f32 v[64:65], v[64:65], v[192:193]
	v_pk_mul_f32 v[66:67], v[66:67], v[194:195]
	v_cvt_f32_ubyte3_e32 v195, v191
	v_cvt_f32_ubyte2_e32 v194, v191
	v_cvt_f32_ubyte1_e32 v193, v191
	v_cvt_f32_ubyte0_e32 v192, v191
	v_pk_add_f32 v[190:191], v[194:195], 0.5 op_sel_hi:[1,0]
	v_add_f32_e32 v156, 0.5, v156
	v_pk_mul_f32 v[190:191], v[190:191], v[200:201]
	v_pk_add_f32 v[192:193], v[192:193], 0.5 op_sel_hi:[1,0]
	v_pk_mul_f32 v[70:71], v[70:71], v[190:191]
	v_rcp_f32_e32 v190, v156
	v_cvt_f32_ubyte0_e32 v156, v189
	v_pk_mul_f32 v[192:193], v[192:193], v[196:197]
	v_add_f32_e32 v156, 0.5, v156
	v_pk_mul_f32 v[68:69], v[68:69], v[192:193]
	v_rcp_f32_e32 v192, v156
	v_cvt_f32_ubyte1_e32 v156, v188
	v_add_f32_e32 v156, 0.5, v156
	v_rcp_f32_e32 v191, v156
	v_cvt_f32_ubyte1_e32 v156, v189
	v_add_f32_e32 v156, 0.5, v156
	v_rcp_f32_e32 v193, v156
	v_cvt_f32_ubyte2_e32 v156, v188
	v_add_f32_e32 v156, 0.5, v156
	v_rcp_f32_e32 v194, v156
	v_cvt_f32_ubyte2_e32 v156, v189
	v_add_f32_e32 v156, 0.5, v156
	v_rcp_f32_e32 v196, v156
	v_cvt_f32_ubyte3_e32 v156, v188
	v_add_f32_e32 v156, 0.5, v156
	v_rcp_f32_e32 v195, v156
	v_cvt_f32_ubyte3_e32 v156, v189
	v_add_f32_e32 v156, 0.5, v156
	v_cvt_f32_ubyte1_e32 v189, v186
	v_cvt_f32_ubyte0_e32 v188, v186
	v_cvt_f32_ubyte3_e32 v199, v186
	v_cvt_f32_ubyte2_e32 v198, v186
	v_rcp_f32_e32 v197, v156
	v_pk_add_f32 v[198:199], v[198:199], 0.5 op_sel_hi:[1,0]
	v_pk_add_f32 v[188:189], v[188:189], 0.5 op_sel_hi:[1,0]
	v_cvt_f32_ubyte0_e32 v156, v184
	v_pk_mul_f32 v[188:189], v[188:189], v[190:191]
	v_pk_mul_f32 v[190:191], v[198:199], v[194:195]
	v_pk_mul_f32 v[40:41], v[40:41], v[188:189]
	v_pk_mul_f32 v[42:43], v[42:43], v[190:191]
	v_cvt_f32_ubyte3_e32 v191, v187
	v_cvt_f32_ubyte2_e32 v190, v187
	v_cvt_f32_ubyte1_e32 v189, v187
	v_cvt_f32_ubyte0_e32 v188, v187
	v_pk_add_f32 v[186:187], v[190:191], 0.5 op_sel_hi:[1,0]
	v_add_f32_e32 v156, 0.5, v156
	v_pk_mul_f32 v[186:187], v[186:187], v[196:197]
	v_pk_add_f32 v[188:189], v[188:189], 0.5 op_sel_hi:[1,0]
	v_pk_mul_f32 v[46:47], v[46:47], v[186:187]
	v_rcp_f32_e32 v186, v156
	v_cvt_f32_ubyte0_e32 v156, v185
	v_pk_mul_f32 v[188:189], v[188:189], v[192:193]
	v_add_f32_e32 v156, 0.5, v156
	v_pk_mul_f32 v[44:45], v[44:45], v[188:189]
	v_rcp_f32_e32 v188, v156
	v_cvt_f32_ubyte1_e32 v156, v184
	v_add_f32_e32 v156, 0.5, v156
	v_rcp_f32_e32 v187, v156
	v_cvt_f32_ubyte1_e32 v156, v185
	v_add_f32_e32 v156, 0.5, v156
	v_rcp_f32_e32 v189, v156
	v_cvt_f32_ubyte2_e32 v156, v184
	v_add_f32_e32 v156, 0.5, v156
	v_rcp_f32_e32 v190, v156
	v_cvt_f32_ubyte2_e32 v156, v185
	v_add_f32_e32 v156, 0.5, v156
	v_rcp_f32_e32 v192, v156
	v_cvt_f32_ubyte3_e32 v156, v184
	v_add_f32_e32 v156, 0.5, v156
	v_rcp_f32_e32 v191, v156
	v_cvt_f32_ubyte3_e32 v156, v185
	v_add_f32_e32 v156, 0.5, v156
	v_cvt_f32_ubyte1_e32 v185, v182
	v_cvt_f32_ubyte0_e32 v184, v182
	v_cvt_f32_ubyte3_e32 v195, v182
	v_cvt_f32_ubyte2_e32 v194, v182
	v_rcp_f32_e32 v193, v156
	v_pk_add_f32 v[194:195], v[194:195], 0.5 op_sel_hi:[1,0]
	v_pk_add_f32 v[184:185], v[184:185], 0.5 op_sel_hi:[1,0]
	s_waitcnt vmcnt(0)
	v_cvt_f32_ubyte0_e32 v156, v180
	v_pk_mul_f32 v[184:185], v[184:185], v[186:187]
	v_pk_mul_f32 v[186:187], v[194:195], v[190:191]
	v_pk_mul_f32 v[72:73], v[72:73], v[184:185]
	v_pk_mul_f32 v[74:75], v[74:75], v[186:187]
	v_cvt_f32_ubyte3_e32 v187, v183
	v_cvt_f32_ubyte2_e32 v186, v183
	v_cvt_f32_ubyte1_e32 v185, v183
	v_cvt_f32_ubyte0_e32 v184, v183
	v_pk_add_f32 v[182:183], v[186:187], 0.5 op_sel_hi:[1,0]
	v_add_f32_e32 v156, 0.5, v156
	v_pk_mul_f32 v[182:183], v[182:183], v[192:193]
	v_pk_add_f32 v[184:185], v[184:185], 0.5 op_sel_hi:[1,0]
	v_pk_mul_f32 v[78:79], v[78:79], v[182:183]
	v_rcp_f32_e32 v182, v156
	v_cvt_f32_ubyte0_e32 v156, v181
	v_pk_mul_f32 v[184:185], v[184:185], v[188:189]
	v_add_f32_e32 v156, 0.5, v156
	v_pk_mul_f32 v[76:77], v[76:77], v[184:185]
	v_rcp_f32_e32 v184, v156
	v_cvt_f32_ubyte1_e32 v156, v180
	v_add_f32_e32 v156, 0.5, v156
	v_rcp_f32_e32 v183, v156
	v_cvt_f32_ubyte1_e32 v156, v181
	v_add_f32_e32 v156, 0.5, v156
	v_rcp_f32_e32 v185, v156
	v_cvt_f32_ubyte2_e32 v156, v180
	v_add_f32_e32 v156, 0.5, v156
	v_rcp_f32_e32 v186, v156
	v_cvt_f32_ubyte2_e32 v156, v181
	v_add_f32_e32 v156, 0.5, v156
	v_rcp_f32_e32 v188, v156
	v_cvt_f32_ubyte3_e32 v156, v180
	v_add_f32_e32 v156, 0.5, v156
	v_rcp_f32_e32 v187, v156
	v_cvt_f32_ubyte3_e32 v156, v181
	v_add_f32_e32 v156, 0.5, v156
	v_cvt_f32_ubyte1_e32 v181, v178
	v_cvt_f32_ubyte0_e32 v180, v178
	v_cvt_f32_ubyte3_e32 v191, v178
	v_cvt_f32_ubyte2_e32 v190, v178
	v_rcp_f32_e32 v189, v156
	v_pk_add_f32 v[190:191], v[190:191], 0.5 op_sel_hi:[1,0]
	v_pk_add_f32 v[180:181], v[180:181], 0.5 op_sel_hi:[1,0]
	v_cvt_f32_ubyte0_e32 v156, v176
	v_pk_mul_f32 v[180:181], v[180:181], v[182:183]
	v_pk_mul_f32 v[182:183], v[190:191], v[186:187]
	v_pk_mul_f32 v[80:81], v[80:81], v[180:181]
	v_pk_mul_f32 v[82:83], v[82:83], v[182:183]
	v_cvt_f32_ubyte3_e32 v183, v179
	v_cvt_f32_ubyte2_e32 v182, v179
	v_cvt_f32_ubyte1_e32 v181, v179
	v_cvt_f32_ubyte0_e32 v180, v179
	v_pk_add_f32 v[178:179], v[182:183], 0.5 op_sel_hi:[1,0]
	v_add_f32_e32 v156, 0.5, v156
	v_pk_mul_f32 v[178:179], v[178:179], v[188:189]
	v_pk_add_f32 v[180:181], v[180:181], 0.5 op_sel_hi:[1,0]
	v_pk_mul_f32 v[86:87], v[86:87], v[178:179]
	v_rcp_f32_e32 v178, v156
	v_cvt_f32_ubyte0_e32 v156, v177
	v_pk_mul_f32 v[180:181], v[180:181], v[184:185]
	v_add_f32_e32 v156, 0.5, v156
	v_pk_mul_f32 v[84:85], v[84:85], v[180:181]
	v_rcp_f32_e32 v180, v156
	v_cvt_f32_ubyte1_e32 v156, v176
	v_add_f32_e32 v156, 0.5, v156
	v_rcp_f32_e32 v179, v156
	v_cvt_f32_ubyte1_e32 v156, v177
	v_add_f32_e32 v156, 0.5, v156
	v_rcp_f32_e32 v181, v156
	v_cvt_f32_ubyte2_e32 v156, v176
	v_add_f32_e32 v156, 0.5, v156
	v_rcp_f32_e32 v182, v156
	v_cvt_f32_ubyte2_e32 v156, v177
	v_add_f32_e32 v156, 0.5, v156
	v_rcp_f32_e32 v184, v156
	v_cvt_f32_ubyte3_e32 v156, v176
	v_add_f32_e32 v156, 0.5, v156
	v_rcp_f32_e32 v183, v156
	v_cvt_f32_ubyte3_e32 v156, v177
	v_add_f32_e32 v156, 0.5, v156
	v_cvt_f32_ubyte1_e32 v177, v174
	v_cvt_f32_ubyte0_e32 v176, v174
	v_cvt_f32_ubyte3_e32 v187, v174
	v_cvt_f32_ubyte2_e32 v186, v174
	v_rcp_f32_e32 v185, v156
	v_pk_add_f32 v[186:187], v[186:187], 0.5 op_sel_hi:[1,0]
	v_pk_add_f32 v[176:177], v[176:177], 0.5 op_sel_hi:[1,0]
	v_cvt_f32_ubyte0_e32 v156, v172
	v_pk_mul_f32 v[176:177], v[176:177], v[178:179]
	v_pk_mul_f32 v[178:179], v[186:187], v[182:183]
	v_pk_mul_f32 v[112:113], v[112:113], v[176:177]
	v_pk_mul_f32 v[114:115], v[114:115], v[178:179]
	v_cvt_f32_ubyte3_e32 v179, v175
	v_cvt_f32_ubyte2_e32 v178, v175
	v_cvt_f32_ubyte1_e32 v177, v175
	v_cvt_f32_ubyte0_e32 v176, v175
	v_pk_add_f32 v[174:175], v[178:179], 0.5 op_sel_hi:[1,0]
	v_add_f32_e32 v156, 0.5, v156
	v_pk_mul_f32 v[174:175], v[174:175], v[184:185]
	v_pk_add_f32 v[176:177], v[176:177], 0.5 op_sel_hi:[1,0]
	v_pk_mul_f32 v[118:119], v[118:119], v[174:175]
	v_rcp_f32_e32 v174, v156
	v_cvt_f32_ubyte0_e32 v156, v173
	v_pk_mul_f32 v[176:177], v[176:177], v[180:181]
	v_add_f32_e32 v156, 0.5, v156
	v_pk_mul_f32 v[116:117], v[116:117], v[176:177]
	v_rcp_f32_e32 v176, v156
	v_cvt_f32_ubyte1_e32 v156, v172
	v_add_f32_e32 v156, 0.5, v156
	v_rcp_f32_e32 v175, v156
	v_cvt_f32_ubyte1_e32 v156, v173
	v_add_f32_e32 v156, 0.5, v156
	v_rcp_f32_e32 v177, v156
	v_cvt_f32_ubyte2_e32 v156, v172
	v_add_f32_e32 v156, 0.5, v156
	v_rcp_f32_e32 v178, v156
	v_cvt_f32_ubyte2_e32 v156, v173
	v_add_f32_e32 v156, 0.5, v156
	v_rcp_f32_e32 v180, v156
	v_cvt_f32_ubyte3_e32 v156, v172
	v_add_f32_e32 v156, 0.5, v156
	v_rcp_f32_e32 v179, v156
	v_cvt_f32_ubyte3_e32 v156, v173
	v_add_f32_e32 v156, 0.5, v156
	v_cvt_f32_ubyte1_e32 v173, v170
	v_cvt_f32_ubyte0_e32 v172, v170
	v_cvt_f32_ubyte3_e32 v183, v170
	v_cvt_f32_ubyte2_e32 v182, v170
	v_rcp_f32_e32 v181, v156
	v_pk_add_f32 v[182:183], v[182:183], 0.5 op_sel_hi:[1,0]
	v_pk_add_f32 v[172:173], v[172:173], 0.5 op_sel_hi:[1,0]
	v_cvt_f32_ubyte0_e32 v156, v146
	v_pk_mul_f32 v[172:173], v[172:173], v[174:175]
	v_pk_mul_f32 v[174:175], v[182:183], v[178:179]
	v_pk_mul_f32 v[88:89], v[88:89], v[172:173]
	v_pk_mul_f32 v[90:91], v[90:91], v[174:175]
	v_cvt_f32_ubyte3_e32 v175, v171
	v_cvt_f32_ubyte2_e32 v174, v171
	v_cvt_f32_ubyte1_e32 v173, v171
	v_cvt_f32_ubyte0_e32 v172, v171
	v_pk_add_f32 v[170:171], v[174:175], 0.5 op_sel_hi:[1,0]
	v_add_f32_e32 v156, 0.5, v156
	v_pk_mul_f32 v[170:171], v[170:171], v[180:181]
	v_pk_add_f32 v[172:173], v[172:173], 0.5 op_sel_hi:[1,0]
	v_pk_mul_f32 v[94:95], v[94:95], v[170:171]
	v_rcp_f32_e32 v170, v156
	v_cvt_f32_ubyte0_e32 v156, v147
	v_pk_mul_f32 v[172:173], v[172:173], v[176:177]
	v_add_f32_e32 v156, 0.5, v156
	v_pk_mul_f32 v[92:93], v[92:93], v[172:173]
	v_rcp_f32_e32 v172, v156
	v_cvt_f32_ubyte1_e32 v156, v146
	v_add_f32_e32 v156, 0.5, v156
	v_rcp_f32_e32 v171, v156
	v_cvt_f32_ubyte1_e32 v156, v147
	v_add_f32_e32 v156, 0.5, v156
	v_rcp_f32_e32 v173, v156
	v_cvt_f32_ubyte2_e32 v156, v146
	v_cvt_f32_ubyte3_e32 v146, v146
	v_add_f32_e32 v156, 0.5, v156
	v_add_f32_e32 v146, 0.5, v146
	v_rcp_f32_e32 v174, v156
	v_rcp_f32_e32 v175, v146
	v_cvt_f32_ubyte3_e32 v146, v147
	v_cvt_f32_ubyte2_e32 v156, v147
	v_add_f32_e32 v146, 0.5, v146
	v_add_f32_e32 v156, 0.5, v156
	v_rcp_f32_e32 v177, v146
	v_cvt_f32_ubyte1_e32 v147, v144
	v_cvt_f32_ubyte0_e32 v146, v144
	v_cvt_f32_ubyte3_e32 v179, v144
	v_cvt_f32_ubyte2_e32 v178, v144
	v_rcp_f32_e32 v176, v156
	v_pk_add_f32 v[178:179], v[178:179], 0.5 op_sel_hi:[1,0]
	v_pk_add_f32 v[146:147], v[146:147], 0.5 op_sel_hi:[1,0]
	v_cvt_f32_ubyte2_e32 v156, v14
	v_pk_mul_f32 v[146:147], v[146:147], v[170:171]
	v_pk_mul_f32 v[170:171], v[178:179], v[174:175]
	v_pk_mul_f32 v[120:121], v[120:121], v[146:147]
	v_pk_mul_f32 v[122:123], v[122:123], v[170:171]
	v_cvt_f32_ubyte3_e32 v171, v145
	v_cvt_f32_ubyte2_e32 v170, v145
	v_cvt_f32_ubyte1_e32 v147, v145
	v_cvt_f32_ubyte0_e32 v146, v145
	v_pk_add_f32 v[144:145], v[170:171], 0.5 op_sel_hi:[1,0]
	v_pk_add_f32 v[146:147], v[146:147], 0.5 op_sel_hi:[1,0]
	v_pk_mul_f32 v[144:145], v[144:145], v[176:177]
	v_pk_mul_f32 v[146:147], v[146:147], v[172:173]
	v_pk_mul_f32 v[126:127], v[126:127], v[144:145]
	v_cvt_f32_ubyte0_e32 v145, v15
	v_add_f32_e32 v145, 0.5, v145
	v_pk_mul_f32 v[124:125], v[124:125], v[146:147]
	v_cvt_f32_ubyte0_e32 v144, v14
	v_rcp_f32_e32 v146, v145
	v_cvt_f32_ubyte1_e32 v145, v14
	v_cvt_f32_ubyte3_e32 v14, v14
	v_add_f32_e32 v144, 0.5, v144
	v_add_f32_e32 v145, 0.5, v145
	v_add_f32_e32 v156, 0.5, v156
	v_add_f32_e32 v14, 0.5, v14
	v_rcp_f32_e32 v144, v144
	v_rcp_f32_e32 v145, v145
	v_rcp_f32_e32 v170, v156
	v_rcp_f32_e32 v171, v14
	v_cvt_f32_ubyte3_e32 v14, v15
	v_cvt_f32_ubyte2_e32 v156, v15
	v_add_f32_e32 v14, 0.5, v14
	v_cvt_f32_ubyte1_e32 v147, v15
	v_add_f32_e32 v156, 0.5, v156
	v_rcp_f32_e32 v173, v14
	v_cvt_f32_ubyte1_e32 v15, v12
	v_cvt_f32_ubyte0_e32 v14, v12
	v_cvt_f32_ubyte3_e32 v175, v12
	v_cvt_f32_ubyte2_e32 v174, v12
	v_rcp_f32_e32 v172, v156
	v_pk_add_f32 v[174:175], v[174:175], 0.5 op_sel_hi:[1,0]
	v_pk_add_f32 v[14:15], v[14:15], 0.5 op_sel_hi:[1,0]
	v_add_f32_e32 v147, 0.5, v147
	v_pk_mul_f32 v[14:15], v[14:15], v[144:145]
	v_pk_mul_f32 v[144:145], v[174:175], v[170:171]
	v_rcp_f32_e32 v147, v147
	v_pk_mul_f32 v[98:99], v[98:99], v[144:145]
	v_cvt_f32_ubyte3_e32 v145, v13
	v_cvt_f32_ubyte2_e32 v144, v13
	v_pk_mul_f32 v[96:97], v[96:97], v[14:15]
	v_cvt_f32_ubyte1_e32 v15, v13
	v_cvt_f32_ubyte0_e32 v14, v13
	v_pk_add_f32 v[12:13], v[144:145], 0.5 op_sel_hi:[1,0]
	v_pk_add_f32 v[14:15], v[14:15], 0.5 op_sel_hi:[1,0]
	v_pk_mul_f32 v[12:13], v[12:13], v[172:173]
	v_pk_mul_f32 v[14:15], v[14:15], v[146:147]
	v_pk_mul_f32 v[102:103], v[102:103], v[12:13]
	v_cvt_f32_ubyte0_e32 v13, v11
	v_add_f32_e32 v13, 0.5, v13
	v_pk_mul_f32 v[100:101], v[100:101], v[14:15]
	v_cvt_f32_ubyte0_e32 v12, v10
	v_rcp_f32_e32 v14, v13
	v_cvt_f32_ubyte1_e32 v13, v10
	v_cvt_f32_ubyte2_e32 v144, v10
	v_cvt_f32_ubyte2_e32 v145, v11
	v_cvt_f32_ubyte3_e32 v10, v10
	v_add_f32_e32 v12, 0.5, v12
	v_add_f32_e32 v13, 0.5, v13
	v_add_f32_e32 v144, 0.5, v144
	v_add_f32_e32 v145, 0.5, v145
	v_add_f32_e32 v10, 0.5, v10
	v_rcp_f32_e32 v12, v12
	v_rcp_f32_e32 v13, v13
	v_rcp_f32_e32 v144, v144
	v_rcp_f32_e32 v146, v145
	v_rcp_f32_e32 v145, v10
	v_cvt_f32_ubyte3_e32 v10, v11
	v_add_f32_e32 v10, 0.5, v10
	v_cvt_f32_ubyte1_e32 v15, v11
	v_rcp_f32_e32 v147, v10
	v_cvt_f32_ubyte1_e32 v11, v8
	v_cvt_f32_ubyte0_e32 v10, v8
	v_cvt_f32_ubyte3_e32 v171, v8
	v_cvt_f32_ubyte2_e32 v170, v8
	v_pk_add_f32 v[170:171], v[170:171], 0.5 op_sel_hi:[1,0]
	v_pk_add_f32 v[10:11], v[10:11], 0.5 op_sel_hi:[1,0]
	v_add_f32_e32 v15, 0.5, v15
	v_pk_mul_f32 v[10:11], v[10:11], v[12:13]
	v_pk_mul_f32 v[12:13], v[170:171], v[144:145]
	v_rcp_f32_e32 v15, v15
	v_pk_mul_f32 v[130:131], v[130:131], v[12:13]
	v_cvt_f32_ubyte3_e32 v13, v9
	v_cvt_f32_ubyte2_e32 v12, v9
	v_pk_mul_f32 v[128:129], v[128:129], v[10:11]
	v_cvt_f32_ubyte1_e32 v11, v9
	v_cvt_f32_ubyte0_e32 v10, v9
	v_pk_add_f32 v[8:9], v[12:13], 0.5 op_sel_hi:[1,0]
	v_pk_add_f32 v[10:11], v[10:11], 0.5 op_sel_hi:[1,0]
	v_pk_mul_f32 v[8:9], v[8:9], v[146:147]
	v_pk_mul_f32 v[10:11], v[10:11], v[14:15]
	v_pk_mul_f32 v[134:135], v[134:135], v[8:9]
	v_cvt_f32_ubyte0_e32 v9, v5
	v_add_f32_e32 v9, 0.5, v9
	v_pk_mul_f32 v[132:133], v[132:133], v[10:11]
	v_cvt_f32_ubyte0_e32 v8, v4
	v_rcp_f32_e32 v10, v9
	v_cvt_f32_ubyte1_e32 v9, v4
	v_cvt_f32_ubyte2_e32 v12, v4
	v_cvt_f32_ubyte2_e32 v13, v5
	v_cvt_f32_ubyte3_e32 v4, v4
	v_add_f32_e32 v8, 0.5, v8
	v_add_f32_e32 v9, 0.5, v9
	v_add_f32_e32 v12, 0.5, v12
	v_add_f32_e32 v13, 0.5, v13
	v_add_f32_e32 v4, 0.5, v4
	v_rcp_f32_e32 v8, v8
	v_rcp_f32_e32 v9, v9
	v_rcp_f32_e32 v12, v12
	v_rcp_f32_e32 v14, v13
	v_rcp_f32_e32 v13, v4
	v_cvt_f32_ubyte3_e32 v4, v5
	v_add_f32_e32 v4, 0.5, v4
	v_cvt_f32_ubyte1_e32 v11, v5
	v_rcp_f32_e32 v15, v4
	v_cvt_f32_ubyte1_e32 v5, v2
	v_cvt_f32_ubyte0_e32 v4, v2
	v_cvt_f32_ubyte3_e32 v145, v2
	v_cvt_f32_ubyte2_e32 v144, v2
	v_pk_add_f32 v[144:145], v[144:145], 0.5 op_sel_hi:[1,0]
	v_pk_add_f32 v[4:5], v[4:5], 0.5 op_sel_hi:[1,0]
	v_add_f32_e32 v11, 0.5, v11
	v_pk_mul_f32 v[4:5], v[4:5], v[8:9]
	v_pk_mul_f32 v[8:9], v[144:145], v[12:13]
	v_rcp_f32_e32 v11, v11
	v_pk_mul_f32 v[106:107], v[106:107], v[8:9]
	v_cvt_f32_ubyte3_e32 v9, v3
	v_cvt_f32_ubyte2_e32 v8, v3
	v_pk_mul_f32 v[104:105], v[104:105], v[4:5]
	v_cvt_f32_ubyte1_e32 v5, v3
	v_cvt_f32_ubyte0_e32 v4, v3
	v_pk_add_f32 v[2:3], v[8:9], 0.5 op_sel_hi:[1,0]
	v_pk_add_f32 v[4:5], v[4:5], 0.5 op_sel_hi:[1,0]
	v_pk_mul_f32 v[2:3], v[2:3], v[14:15]
	v_pk_mul_f32 v[4:5], v[4:5], v[10:11]
	v_pk_mul_f32 v[110:111], v[110:111], v[2:3]
	v_cvt_f32_ubyte0_e32 v3, v7
	v_add_f32_e32 v3, 0.5, v3
	v_pk_mul_f32 v[108:109], v[108:109], v[4:5]
	v_cvt_f32_ubyte0_e32 v2, v6
	v_rcp_f32_e32 v4, v3
	v_cvt_f32_ubyte1_e32 v3, v6
	v_cvt_f32_ubyte2_e32 v8, v6
	v_cvt_f32_ubyte2_e32 v9, v7
	v_cvt_f32_ubyte3_e32 v6, v6
	v_add_f32_e32 v2, 0.5, v2
	v_add_f32_e32 v3, 0.5, v3
	v_add_f32_e32 v8, 0.5, v8
	v_add_f32_e32 v9, 0.5, v9
	v_add_f32_e32 v6, 0.5, v6
	v_rcp_f32_e32 v2, v2
	v_rcp_f32_e32 v3, v3
	v_rcp_f32_e32 v8, v8
	v_rcp_f32_e32 v10, v9
	v_rcp_f32_e32 v9, v6
	v_cvt_f32_ubyte3_e32 v6, v7
	v_cvt_f32_ubyte1_e32 v5, v7
	v_add_f32_e32 v6, 0.5, v6
	v_add_f32_e32 v5, 0.5, v5
	v_rcp_f32_e32 v11, v6
	v_cvt_f32_ubyte1_e32 v7, v0
	v_cvt_f32_ubyte0_e32 v6, v0
	v_cvt_f32_ubyte3_e32 v13, v0
	v_cvt_f32_ubyte2_e32 v12, v0
	v_rcp_f32_e32 v5, v5
	v_pk_add_f32 v[12:13], v[12:13], 0.5 op_sel_hi:[1,0]
	v_pk_add_f32 v[6:7], v[6:7], 0.5 op_sel_hi:[1,0]
	s_nop 0
	v_pk_mul_f32 v[2:3], v[6:7], v[2:3]
	v_pk_mul_f32 v[6:7], v[12:13], v[8:9]
	v_pk_mul_f32 v[136:137], v[136:137], v[2:3]
	v_pk_mul_f32 v[138:139], v[138:139], v[6:7]
	v_cvt_f32_ubyte1_e32 v3, v1
	v_cvt_f32_ubyte0_e32 v2, v1
	v_cvt_f32_ubyte3_e32 v7, v1
	v_cvt_f32_ubyte2_e32 v6, v1
	v_pk_add_f32 v[0:1], v[6:7], 0.5 op_sel_hi:[1,0]
	v_pk_add_f32 v[2:3], v[2:3], 0.5 op_sel_hi:[1,0]
	v_pk_mul_f32 v[0:1], v[0:1], v[10:11]
	v_pk_mul_f32 v[2:3], v[2:3], v[4:5]
	v_pk_mul_f32 v[142:143], v[142:143], v[0:1]
	v_pk_mul_f32 v[140:141], v[140:141], v[2:3]
	ds_read_b128 v[8:11], v230
	ds_read_b128 v[12:15], v230 offset:1024
	ds_read_b128 v[0:3], v230 offset:2048
	ds_read_b128 v[4:7], v230 offset:3072
	s_add_u32 s2, s46, 0x40480
	s_addc_u32 s3, s47, 0
	s_mov_b32 m0, s92
	v_lshl_add_u64 v[144:145], s[2:3], 0, v[148:149]
	ds_read_b128 v[174:177], v227
	ds_read_b128 v[178:181], v227 offset:1024
	ds_read_b128 v[182:185], v227 offset:2048
	ds_read_b128 v[186:189], v227 offset:3072
	ds_read_b128 v[190:193], v227 offset:4096
	ds_read_b128 v[194:197], v227 offset:5120
	ds_read_b128 v[198:201], v227 offset:6144
	ds_read_b128 v[202:205], v227 offset:7168
	global_load_lds_dwordx4 v[144:145], off
	v_lshl_add_u64 v[144:145], s[2:3], 0, v[152:153]
	s_mov_b32 m0, s91
	s_nop 0
	global_load_lds_dwordx4 v[144:145], off
	s_waitcnt lgkmcnt(8)
	s_barrier
	s_waitcnt lgkmcnt(0)
	s_waitcnt lgkmcnt(0)
	v_mfma_scale_f32_16x16x128_f8f6f4 v[16:19], v[8:15], v[174:181], v[16:19], v224, v224 op_sel_hi:[0,0,0]
	v_mfma_scale_f32_16x16x128_f8f6f4 v[20:23], v[0:7], v[174:181], v[20:23], v224, v224 op_sel_hi:[0,0,0]
	v_mfma_scale_f32_16x16x128_f8f6f4 v[24:27], v[8:15], v[182:189], v[24:27], v224, v224 op_sel_hi:[0,0,0]
	v_mfma_scale_f32_16x16x128_f8f6f4 v[28:31], v[0:7], v[182:189], v[28:31], v224, v224 op_sel_hi:[0,0,0]
	v_mfma_scale_f32_16x16x128_f8f6f4 v[32:35], v[8:15], v[190:197], v[32:35], v224, v224 op_sel_hi:[0,0,0]
	v_mfma_scale_f32_16x16x128_f8f6f4 v[36:39], v[0:7], v[190:197], v[36:39], v224, v224 op_sel_hi:[0,0,0]
	v_mfma_scale_f32_16x16x128_f8f6f4 v[40:43], v[8:15], v[198:205], v[40:43], v224, v224 op_sel_hi:[0,0,0]
	v_mfma_scale_f32_16x16x128_f8f6f4 v[44:47], v[0:7], v[198:205], v[44:47], v224, v224 op_sel_hi:[0,0,0]
	s_barrier
	v_lshl_add_u64 v[170:171], s[48:49], 0, v[150:151]
	s_mov_b32 m0, s94
	v_lshl_add_u64 v[144:145], v[170:171], 0, s[20:21]
	v_lshl_add_u64 v[172:173], s[48:49], 0, v[154:155]
	ds_read_b128 v[206:209], v231
	ds_read_b128 v[210:213], v231 offset:1024
	ds_read_b128 v[214:217], v231 offset:2048
	ds_read_b128 v[218:221], v231 offset:3072
	global_load_lds_dwordx4 v[144:145], off
	v_lshl_add_u64 v[144:145], v[172:173], 0, s[20:21]
	s_mov_b32 m0, s93
	s_nop 0
	global_load_lds_dwordx4 v[144:145], off
	s_barrier
	s_waitcnt lgkmcnt(0)
	s_waitcnt lgkmcnt(0)
	v_mfma_scale_f32_16x16x128_f8f6f4 v[48:51], v[206:213], v[174:181], v[48:51], v224, v224 op_sel_hi:[0,0,0]
	v_mfma_scale_f32_16x16x128_f8f6f4 v[52:55], v[214:221], v[174:181], v[52:55], v224, v224 op_sel_hi:[0,0,0]
	v_mfma_scale_f32_16x16x128_f8f6f4 v[56:59], v[206:213], v[182:189], v[56:59], v224, v224 op_sel_hi:[0,0,0]
	v_mfma_scale_f32_16x16x128_f8f6f4 v[60:63], v[214:221], v[182:189], v[60:63], v224, v224 op_sel_hi:[0,0,0]
	v_mfma_scale_f32_16x16x128_f8f6f4 v[64:67], v[206:213], v[190:197], v[64:67], v224, v224 op_sel_hi:[0,0,0]
	v_mfma_scale_f32_16x16x128_f8f6f4 v[68:71], v[214:221], v[190:197], v[68:71], v224, v224 op_sel_hi:[0,0,0]
	v_mfma_scale_f32_16x16x128_f8f6f4 v[72:75], v[206:213], v[198:205], v[72:75], v224, v224 op_sel_hi:[0,0,0]
	v_mfma_scale_f32_16x16x128_f8f6f4 v[76:79], v[214:221], v[198:205], v[76:79], v224, v224 op_sel_hi:[0,0,0]
	v_lshl_add_u64 v[174:175], s[46:47], 0, v[148:149]
	s_mov_b32 m0, s70
	v_lshl_add_u64 v[144:145], v[174:175], 0, s[20:21]
	s_barrier
	ds_read_b128 v[176:179], v227 offset:16384
	ds_read_b128 v[180:183], v227 offset:17408
	ds_read_b128 v[184:187], v227 offset:18432
	ds_read_b128 v[188:191], v227 offset:19456
	ds_read_b128 v[192:195], v227 offset:20480
	ds_read_b128 v[196:199], v227 offset:21504
	ds_read_b128 v[236:239], v227 offset:22528
	ds_read_b128 v[240:243], v227 offset:23552
	global_load_lds_dwordx4 v[144:145], off
	v_lshl_add_u64 v[144:145], v[168:169], 0, s[20:21]
	s_mov_b32 m0, s71
	s_nop 0
	global_load_lds_dwordx4 v[144:145], off
	s_barrier
	s_waitcnt lgkmcnt(0)
	s_waitcnt lgkmcnt(0)
	v_mfma_scale_f32_16x16x128_f8f6f4 v[80:83], v[8:15], v[176:183], v[80:83], v224, v224 op_sel_hi:[0,0,0]
	v_mfma_scale_f32_16x16x128_f8f6f4 v[84:87], v[0:7], v[176:183], v[84:87], v224, v224 op_sel_hi:[0,0,0]
	v_mfma_scale_f32_16x16x128_f8f6f4 v[88:91], v[8:15], v[184:191], v[88:91], v224, v224 op_sel_hi:[0,0,0]
	v_mfma_scale_f32_16x16x128_f8f6f4 v[92:95], v[0:7], v[184:191], v[92:95], v224, v224 op_sel_hi:[0,0,0]
	v_mfma_scale_f32_16x16x128_f8f6f4 v[96:99], v[8:15], v[192:199], v[96:99], v224, v224 op_sel_hi:[0,0,0]
	v_mfma_scale_f32_16x16x128_f8f6f4 v[100:103], v[0:7], v[192:199], v[100:103], v224, v224 op_sel_hi:[0,0,0]
	v_mfma_scale_f32_16x16x128_f8f6f4 v[104:107], v[8:15], v[236:243], v[104:107], v224, v224 op_sel_hi:[0,0,0]
	v_mfma_scale_f32_16x16x128_f8f6f4 v[108:111], v[0:7], v[236:243], v[108:111], v224, v224 op_sel_hi:[0,0,0]
	s_barrier
	s_add_u32 s2, s48, 0x40500
	s_addc_u32 s3, s49, 0
	s_mov_b32 m0, s52
	v_lshl_add_u64 v[0:1], s[2:3], 0, v[150:151]
	global_load_lds_dwordx4 v[0:1], off
	v_lshl_add_u64 v[0:1], s[2:3], 0, v[154:155]
	s_mov_b32 m0, s95
	s_nop 0
	global_load_lds_dwordx4 v[0:1], off
	s_waitcnt vmcnt(6)
	s_barrier
	v_mfma_scale_f32_16x16x128_f8f6f4 v[112:115], v[206:213], v[176:183], v[112:115], v224, v224 op_sel_hi:[0,0,0]
	v_mfma_scale_f32_16x16x128_f8f6f4 v[116:119], v[214:221], v[176:183], v[116:119], v224, v224 op_sel_hi:[0,0,0]
	v_mfma_scale_f32_16x16x128_f8f6f4 v[120:123], v[206:213], v[184:191], v[120:123], v224, v224 op_sel_hi:[0,0,0]
	v_mfma_scale_f32_16x16x128_f8f6f4 v[124:127], v[214:221], v[184:191], v[124:127], v224, v224 op_sel_hi:[0,0,0]
	v_mfma_scale_f32_16x16x128_f8f6f4 v[128:131], v[206:213], v[192:199], v[128:131], v224, v224 op_sel_hi:[0,0,0]
	v_mfma_scale_f32_16x16x128_f8f6f4 v[132:135], v[214:221], v[192:199], v[132:135], v224, v224 op_sel_hi:[0,0,0]
	v_mfma_scale_f32_16x16x128_f8f6f4 v[136:139], v[206:213], v[236:243], v[136:139], v224, v224 op_sel_hi:[0,0,0]
	v_mfma_scale_f32_16x16x128_f8f6f4 v[140:143], v[214:221], v[236:243], v[140:143], v224, v224 op_sel_hi:[0,0,0]
	s_barrier
	ds_read_b128 v[0:3], v234
	ds_read_b128 v[4:7], v234 offset:1024
	ds_read_b128 v[8:11], v234 offset:2048
	ds_read_b128 v[12:15], v234 offset:3072
	s_add_u32 s2, s46, 0x40500
	s_addc_u32 s3, s47, 0
	s_mov_b32 m0, s72
	v_lshl_add_u64 v[144:145], s[2:3], 0, v[148:149]
	ds_read_b128 v[176:179], v227 offset:32768
	ds_read_b128 v[180:183], v227 offset:33792
	ds_read_b128 v[184:187], v227 offset:34816
	ds_read_b128 v[188:191], v227 offset:35840
	ds_read_b128 v[192:195], v227 offset:36864
	ds_read_b128 v[196:199], v227 offset:37888
	ds_read_b128 v[200:203], v227 offset:38912
	ds_read_b128 v[204:207], v227 offset:39936
	global_load_lds_dwordx4 v[144:145], off
	v_lshl_add_u64 v[144:145], s[2:3], 0, v[152:153]
	s_mov_b32 m0, s73
	s_nop 0
	global_load_lds_dwordx4 v[144:145], off
	s_waitcnt lgkmcnt(8)
	s_barrier
	s_waitcnt lgkmcnt(0)
	s_waitcnt lgkmcnt(0)
	v_mfma_scale_f32_16x16x128_f8f6f4 v[16:19], v[0:7], v[176:183], v[16:19], v224, v224 op_sel_hi:[0,0,0]
	v_mfma_scale_f32_16x16x128_f8f6f4 v[20:23], v[8:15], v[176:183], v[20:23], v224, v224 op_sel_hi:[0,0,0]
	v_mfma_scale_f32_16x16x128_f8f6f4 v[24:27], v[0:7], v[184:191], v[24:27], v224, v224 op_sel_hi:[0,0,0]
	v_mfma_scale_f32_16x16x128_f8f6f4 v[28:31], v[8:15], v[184:191], v[28:31], v224, v224 op_sel_hi:[0,0,0]
	v_mfma_scale_f32_16x16x128_f8f6f4 v[32:35], v[0:7], v[192:199], v[32:35], v224, v224 op_sel_hi:[0,0,0]
	v_mfma_scale_f32_16x16x128_f8f6f4 v[36:39], v[8:15], v[192:199], v[36:39], v224, v224 op_sel_hi:[0,0,0]
	v_mfma_scale_f32_16x16x128_f8f6f4 v[40:43], v[0:7], v[200:207], v[40:43], v224, v224 op_sel_hi:[0,0,0]
	v_mfma_scale_f32_16x16x128_f8f6f4 v[44:47], v[8:15], v[200:207], v[44:47], v224, v224 op_sel_hi:[0,0,0]
	s_barrier
	s_mov_b32 m0, s63
	v_lshl_add_u64 v[144:145], v[170:171], 0, s[22:23]
	ds_read_b128 v[208:211], v233
	ds_read_b128 v[212:215], v233 offset:1024
	ds_read_b128 v[236:239], v233 offset:2048
	ds_read_b128 v[240:243], v233 offset:3072
	global_load_lds_dwordx4 v[144:145], off
	v_lshl_add_u64 v[144:145], v[172:173], 0, s[22:23]
	s_mov_b32 m0, s62
	s_nop 0
	global_load_lds_dwordx4 v[144:145], off
	s_barrier
	s_waitcnt lgkmcnt(0)
	s_waitcnt lgkmcnt(0)
	v_mfma_scale_f32_16x16x128_f8f6f4 v[48:51], v[208:215], v[176:183], v[48:51], v224, v224 op_sel_hi:[0,0,0]
	v_mfma_scale_f32_16x16x128_f8f6f4 v[52:55], v[236:243], v[176:183], v[52:55], v224, v224 op_sel_hi:[0,0,0]
	v_mfma_scale_f32_16x16x128_f8f6f4 v[56:59], v[208:215], v[184:191], v[56:59], v224, v224 op_sel_hi:[0,0,0]
	v_mfma_scale_f32_16x16x128_f8f6f4 v[60:63], v[236:243], v[184:191], v[60:63], v224, v224 op_sel_hi:[0,0,0]
	v_mfma_scale_f32_16x16x128_f8f6f4 v[64:67], v[208:215], v[192:199], v[64:67], v224, v224 op_sel_hi:[0,0,0]
	v_mfma_scale_f32_16x16x128_f8f6f4 v[68:71], v[236:243], v[192:199], v[68:71], v224, v224 op_sel_hi:[0,0,0]
	v_mfma_scale_f32_16x16x128_f8f6f4 v[72:75], v[208:215], v[200:207], v[72:75], v224, v224 op_sel_hi:[0,0,0]
	v_mfma_scale_f32_16x16x128_f8f6f4 v[76:79], v[236:243], v[200:207], v[76:79], v224, v224 op_sel_hi:[0,0,0]
	s_mov_b32 m0, s77
	v_lshl_add_u64 v[144:145], v[174:175], 0, s[22:23]
	s_barrier
	ds_read_b128 v[176:179], v227 offset:49152
	ds_read_b128 v[180:183], v227 offset:50176
	ds_read_b128 v[184:187], v227 offset:51200
	ds_read_b128 v[188:191], v227 offset:52224
	ds_read_b128 v[192:195], v227 offset:53248
	ds_read_b128 v[196:199], v227 offset:54272
	ds_read_b128 v[200:203], v227 offset:55296
	ds_read_b128 v[204:207], v227 offset:56320
	global_load_lds_dwordx4 v[144:145], off
	v_lshl_add_u64 v[144:145], v[168:169], 0, s[22:23]
	s_mov_b32 m0, s78
	s_nop 0
	global_load_lds_dwordx4 v[144:145], off
	s_barrier
	s_waitcnt lgkmcnt(0)
	s_waitcnt lgkmcnt(0)
	v_mfma_scale_f32_16x16x128_f8f6f4 v[80:83], v[0:7], v[176:183], v[80:83], v224, v224 op_sel_hi:[0,0,0]
	v_mfma_scale_f32_16x16x128_f8f6f4 v[84:87], v[8:15], v[176:183], v[84:87], v224, v224 op_sel_hi:[0,0,0]
	v_mfma_scale_f32_16x16x128_f8f6f4 v[88:91], v[0:7], v[184:191], v[88:91], v224, v224 op_sel_hi:[0,0,0]
	v_mfma_scale_f32_16x16x128_f8f6f4 v[92:95], v[8:15], v[184:191], v[92:95], v224, v224 op_sel_hi:[0,0,0]
	v_mfma_scale_f32_16x16x128_f8f6f4 v[96:99], v[0:7], v[192:199], v[96:99], v224, v224 op_sel_hi:[0,0,0]
	v_mfma_scale_f32_16x16x128_f8f6f4 v[100:103], v[8:15], v[192:199], v[100:103], v224, v224 op_sel_hi:[0,0,0]
	v_mfma_scale_f32_16x16x128_f8f6f4 v[104:107], v[0:7], v[200:207], v[104:107], v224, v224 op_sel_hi:[0,0,0]
	v_mfma_scale_f32_16x16x128_f8f6f4 v[108:111], v[8:15], v[200:207], v[108:111], v224, v224 op_sel_hi:[0,0,0]
	s_barrier
	s_add_u32 s2, s48, 0x40580
	s_addc_u32 s3, s49, 0
	s_mov_b32 m0, s64
	v_lshl_add_u64 v[0:1], s[2:3], 0, v[150:151]
	global_load_lds_dwordx4 v[0:1], off
	v_lshl_add_u64 v[0:1], s[2:3], 0, v[154:155]
	s_mov_b32 m0, s53
	s_nop 0
	global_load_lds_dwordx4 v[0:1], off
	s_waitcnt vmcnt(6)
	s_barrier
	v_mfma_scale_f32_16x16x128_f8f6f4 v[112:115], v[208:215], v[176:183], v[112:115], v224, v224 op_sel_hi:[0,0,0]
	v_mfma_scale_f32_16x16x128_f8f6f4 v[116:119], v[236:243], v[176:183], v[116:119], v224, v224 op_sel_hi:[0,0,0]
	v_mfma_scale_f32_16x16x128_f8f6f4 v[120:123], v[208:215], v[184:191], v[120:123], v224, v224 op_sel_hi:[0,0,0]
	v_mfma_scale_f32_16x16x128_f8f6f4 v[124:127], v[236:243], v[184:191], v[124:127], v224, v224 op_sel_hi:[0,0,0]
	v_mfma_scale_f32_16x16x128_f8f6f4 v[128:131], v[208:215], v[192:199], v[128:131], v224, v224 op_sel_hi:[0,0,0]
	v_mfma_scale_f32_16x16x128_f8f6f4 v[132:135], v[236:243], v[192:199], v[132:135], v224, v224 op_sel_hi:[0,0,0]
	v_mfma_scale_f32_16x16x128_f8f6f4 v[136:139], v[208:215], v[200:207], v[136:139], v224, v224 op_sel_hi:[0,0,0]
	v_mfma_scale_f32_16x16x128_f8f6f4 v[140:143], v[236:243], v[200:207], v[140:143], v224, v224 op_sel_hi:[0,0,0]
	s_barrier
	ds_read_b128 v[0:3], v230
	ds_read_b128 v[4:7], v230 offset:1024
	ds_read_b128 v[8:11], v230 offset:2048
	ds_read_b128 v[12:15], v230 offset:3072
	s_add_u32 s2, s46, 0x40580
	s_addc_u32 s3, s47, 0
	s_mov_b32 m0, s92
	v_lshl_add_u64 v[144:145], s[2:3], 0, v[148:149]
	ds_read_b128 v[176:179], v227
	ds_read_b128 v[180:183], v227 offset:1024
	ds_read_b128 v[184:187], v227 offset:2048
	ds_read_b128 v[188:191], v227 offset:3072
	ds_read_b128 v[192:195], v227 offset:4096
	ds_read_b128 v[196:199], v227 offset:5120
	ds_read_b128 v[200:203], v227 offset:6144
	ds_read_b128 v[204:207], v227 offset:7168
	global_load_lds_dwordx4 v[144:145], off
	v_lshl_add_u64 v[144:145], s[2:3], 0, v[152:153]
	s_mov_b32 m0, s91
	s_nop 0
	global_load_lds_dwordx4 v[144:145], off
	s_waitcnt lgkmcnt(8)
	s_barrier
	s_waitcnt lgkmcnt(0)
	s_waitcnt lgkmcnt(0)
	v_mfma_scale_f32_16x16x128_f8f6f4 v[16:19], v[0:7], v[176:183], v[16:19], v224, v224 op_sel_hi:[0,0,0]
	v_mfma_scale_f32_16x16x128_f8f6f4 v[20:23], v[8:15], v[176:183], v[20:23], v224, v224 op_sel_hi:[0,0,0]
	v_mfma_scale_f32_16x16x128_f8f6f4 v[24:27], v[0:7], v[184:191], v[24:27], v224, v224 op_sel_hi:[0,0,0]
	v_mfma_scale_f32_16x16x128_f8f6f4 v[28:31], v[8:15], v[184:191], v[28:31], v224, v224 op_sel_hi:[0,0,0]
	v_mfma_scale_f32_16x16x128_f8f6f4 v[32:35], v[0:7], v[192:199], v[32:35], v224, v224 op_sel_hi:[0,0,0]
	v_mfma_scale_f32_16x16x128_f8f6f4 v[36:39], v[8:15], v[192:199], v[36:39], v224, v224 op_sel_hi:[0,0,0]
	v_mfma_scale_f32_16x16x128_f8f6f4 v[40:43], v[0:7], v[200:207], v[40:43], v224, v224 op_sel_hi:[0,0,0]
	v_mfma_scale_f32_16x16x128_f8f6f4 v[44:47], v[8:15], v[200:207], v[44:47], v224, v224 op_sel_hi:[0,0,0]
	s_barrier
	s_mov_b32 m0, s94
	v_lshl_add_u64 v[144:145], v[170:171], 0, s[24:25]
	ds_read_b128 v[208:211], v231
	ds_read_b128 v[212:215], v231 offset:1024
	ds_read_b128 v[236:239], v231 offset:2048
	ds_read_b128 v[240:243], v231 offset:3072
	global_load_lds_dwordx4 v[144:145], off
	v_lshl_add_u64 v[144:145], v[172:173], 0, s[24:25]
	s_mov_b32 m0, s93
	s_nop 0
	global_load_lds_dwordx4 v[144:145], off
	s_barrier
	s_waitcnt lgkmcnt(0)
	s_waitcnt lgkmcnt(0)
	v_mfma_scale_f32_16x16x128_f8f6f4 v[48:51], v[208:215], v[176:183], v[48:51], v224, v224 op_sel_hi:[0,0,0]
	v_mfma_scale_f32_16x16x128_f8f6f4 v[52:55], v[236:243], v[176:183], v[52:55], v224, v224 op_sel_hi:[0,0,0]
	v_mfma_scale_f32_16x16x128_f8f6f4 v[56:59], v[208:215], v[184:191], v[56:59], v224, v224 op_sel_hi:[0,0,0]
	v_mfma_scale_f32_16x16x128_f8f6f4 v[60:63], v[236:243], v[184:191], v[60:63], v224, v224 op_sel_hi:[0,0,0]
	v_mfma_scale_f32_16x16x128_f8f6f4 v[64:67], v[208:215], v[192:199], v[64:67], v224, v224 op_sel_hi:[0,0,0]
	v_mfma_scale_f32_16x16x128_f8f6f4 v[68:71], v[236:243], v[192:199], v[68:71], v224, v224 op_sel_hi:[0,0,0]
	v_mfma_scale_f32_16x16x128_f8f6f4 v[72:75], v[208:215], v[200:207], v[72:75], v224, v224 op_sel_hi:[0,0,0]
	v_mfma_scale_f32_16x16x128_f8f6f4 v[76:79], v[236:243], v[200:207], v[76:79], v224, v224 op_sel_hi:[0,0,0]
	s_mov_b32 m0, s70
	v_lshl_add_u64 v[144:145], v[174:175], 0, s[24:25]
	s_barrier
	ds_read_b128 v[176:179], v227 offset:16384
	ds_read_b128 v[180:183], v227 offset:17408
	ds_read_b128 v[184:187], v227 offset:18432
	ds_read_b128 v[188:191], v227 offset:19456
	ds_read_b128 v[192:195], v227 offset:20480
	ds_read_b128 v[196:199], v227 offset:21504
	ds_read_b128 v[200:203], v227 offset:22528
	ds_read_b128 v[204:207], v227 offset:23552
	global_load_lds_dwordx4 v[144:145], off
	v_lshl_add_u64 v[144:145], v[168:169], 0, s[24:25]
	s_mov_b32 m0, s71
	s_nop 0
	global_load_lds_dwordx4 v[144:145], off
	s_barrier
	s_waitcnt lgkmcnt(0)
	s_waitcnt lgkmcnt(0)
	v_mfma_scale_f32_16x16x128_f8f6f4 v[80:83], v[0:7], v[176:183], v[80:83], v224, v224 op_sel_hi:[0,0,0]
	v_mfma_scale_f32_16x16x128_f8f6f4 v[84:87], v[8:15], v[176:183], v[84:87], v224, v224 op_sel_hi:[0,0,0]
	v_mfma_scale_f32_16x16x128_f8f6f4 v[88:91], v[0:7], v[184:191], v[88:91], v224, v224 op_sel_hi:[0,0,0]
	v_mfma_scale_f32_16x16x128_f8f6f4 v[92:95], v[8:15], v[184:191], v[92:95], v224, v224 op_sel_hi:[0,0,0]
	v_mfma_scale_f32_16x16x128_f8f6f4 v[96:99], v[0:7], v[192:199], v[96:99], v224, v224 op_sel_hi:[0,0,0]
	v_mfma_scale_f32_16x16x128_f8f6f4 v[100:103], v[8:15], v[192:199], v[100:103], v224, v224 op_sel_hi:[0,0,0]
	v_mfma_scale_f32_16x16x128_f8f6f4 v[104:107], v[0:7], v[200:207], v[104:107], v224, v224 op_sel_hi:[0,0,0]
	v_mfma_scale_f32_16x16x128_f8f6f4 v[108:111], v[8:15], v[200:207], v[108:111], v224, v224 op_sel_hi:[0,0,0]
	s_barrier
	s_add_u32 s2, s48, 0x40600
	s_addc_u32 s3, s49, 0
	s_mov_b32 m0, s52
	v_lshl_add_u64 v[0:1], s[2:3], 0, v[150:151]
	global_load_lds_dwordx4 v[0:1], off
	v_lshl_add_u64 v[0:1], s[2:3], 0, v[154:155]
	s_mov_b32 m0, s95
	s_nop 0
	global_load_lds_dwordx4 v[0:1], off
	s_waitcnt vmcnt(6)
	s_barrier
	v_mfma_scale_f32_16x16x128_f8f6f4 v[112:115], v[208:215], v[176:183], v[112:115], v224, v224 op_sel_hi:[0,0,0]
	v_mfma_scale_f32_16x16x128_f8f6f4 v[116:119], v[236:243], v[176:183], v[116:119], v224, v224 op_sel_hi:[0,0,0]
	v_mfma_scale_f32_16x16x128_f8f6f4 v[120:123], v[208:215], v[184:191], v[120:123], v224, v224 op_sel_hi:[0,0,0]
	v_mfma_scale_f32_16x16x128_f8f6f4 v[124:127], v[236:243], v[184:191], v[124:127], v224, v224 op_sel_hi:[0,0,0]
	v_mfma_scale_f32_16x16x128_f8f6f4 v[128:131], v[208:215], v[192:199], v[128:131], v224, v224 op_sel_hi:[0,0,0]
	v_mfma_scale_f32_16x16x128_f8f6f4 v[132:135], v[236:243], v[192:199], v[132:135], v224, v224 op_sel_hi:[0,0,0]
	v_mfma_scale_f32_16x16x128_f8f6f4 v[136:139], v[208:215], v[200:207], v[136:139], v224, v224 op_sel_hi:[0,0,0]
	v_mfma_scale_f32_16x16x128_f8f6f4 v[140:143], v[236:243], v[200:207], v[140:143], v224, v224 op_sel_hi:[0,0,0]
	s_barrier
	ds_read_b128 v[0:3], v234
	ds_read_b128 v[4:7], v234 offset:1024
	ds_read_b128 v[8:11], v234 offset:2048
	ds_read_b128 v[12:15], v234 offset:3072
	s_add_u32 s2, s46, 0x40600
	s_addc_u32 s3, s47, 0
	s_mov_b32 m0, s72
	v_lshl_add_u64 v[144:145], s[2:3], 0, v[148:149]
	ds_read_b128 v[176:179], v227 offset:32768
	ds_read_b128 v[180:183], v227 offset:33792
	ds_read_b128 v[184:187], v227 offset:34816
	ds_read_b128 v[188:191], v227 offset:35840
	ds_read_b128 v[192:195], v227 offset:36864
	ds_read_b128 v[196:199], v227 offset:37888
	ds_read_b128 v[200:203], v227 offset:38912
	ds_read_b128 v[204:207], v227 offset:39936
	global_load_lds_dwordx4 v[144:145], off
	v_lshl_add_u64 v[144:145], s[2:3], 0, v[152:153]
	s_mov_b32 m0, s73
	s_nop 0
	global_load_lds_dwordx4 v[144:145], off
	s_waitcnt lgkmcnt(8)
	s_barrier
	s_waitcnt lgkmcnt(0)
	s_waitcnt lgkmcnt(0)
	v_mfma_scale_f32_16x16x128_f8f6f4 v[16:19], v[0:7], v[176:183], v[16:19], v224, v224 op_sel_hi:[0,0,0]
	v_mfma_scale_f32_16x16x128_f8f6f4 v[20:23], v[8:15], v[176:183], v[20:23], v224, v224 op_sel_hi:[0,0,0]
	v_mfma_scale_f32_16x16x128_f8f6f4 v[24:27], v[0:7], v[184:191], v[24:27], v224, v224 op_sel_hi:[0,0,0]
	v_mfma_scale_f32_16x16x128_f8f6f4 v[28:31], v[8:15], v[184:191], v[28:31], v224, v224 op_sel_hi:[0,0,0]
	v_mfma_scale_f32_16x16x128_f8f6f4 v[32:35], v[0:7], v[192:199], v[32:35], v224, v224 op_sel_hi:[0,0,0]
	v_mfma_scale_f32_16x16x128_f8f6f4 v[36:39], v[8:15], v[192:199], v[36:39], v224, v224 op_sel_hi:[0,0,0]
	v_mfma_scale_f32_16x16x128_f8f6f4 v[40:43], v[0:7], v[200:207], v[40:43], v224, v224 op_sel_hi:[0,0,0]
	v_mfma_scale_f32_16x16x128_f8f6f4 v[44:47], v[8:15], v[200:207], v[44:47], v224, v224 op_sel_hi:[0,0,0]
	s_barrier
	s_mov_b32 m0, s63
	v_lshl_add_u64 v[144:145], v[170:171], 0, s[26:27]
	ds_read_b128 v[208:211], v233
	ds_read_b128 v[212:215], v233 offset:1024
	ds_read_b128 v[236:239], v233 offset:2048
	ds_read_b128 v[240:243], v233 offset:3072
	global_load_lds_dwordx4 v[144:145], off
	v_lshl_add_u64 v[144:145], v[172:173], 0, s[26:27]
	s_mov_b32 m0, s62
	s_nop 0
	global_load_lds_dwordx4 v[144:145], off
	s_barrier
	s_waitcnt lgkmcnt(0)
	s_waitcnt lgkmcnt(0)
	v_mfma_scale_f32_16x16x128_f8f6f4 v[48:51], v[208:215], v[176:183], v[48:51], v224, v224 op_sel_hi:[0,0,0]
	v_mfma_scale_f32_16x16x128_f8f6f4 v[52:55], v[236:243], v[176:183], v[52:55], v224, v224 op_sel_hi:[0,0,0]
	v_mfma_scale_f32_16x16x128_f8f6f4 v[56:59], v[208:215], v[184:191], v[56:59], v224, v224 op_sel_hi:[0,0,0]
	v_mfma_scale_f32_16x16x128_f8f6f4 v[60:63], v[236:243], v[184:191], v[60:63], v224, v224 op_sel_hi:[0,0,0]
	v_mfma_scale_f32_16x16x128_f8f6f4 v[64:67], v[208:215], v[192:199], v[64:67], v224, v224 op_sel_hi:[0,0,0]
	v_mfma_scale_f32_16x16x128_f8f6f4 v[68:71], v[236:243], v[192:199], v[68:71], v224, v224 op_sel_hi:[0,0,0]
	v_mfma_scale_f32_16x16x128_f8f6f4 v[72:75], v[208:215], v[200:207], v[72:75], v224, v224 op_sel_hi:[0,0,0]
	v_mfma_scale_f32_16x16x128_f8f6f4 v[76:79], v[236:243], v[200:207], v[76:79], v224, v224 op_sel_hi:[0,0,0]
	s_mov_b32 m0, s77
	v_lshl_add_u64 v[144:145], v[174:175], 0, s[26:27]
	s_barrier
	ds_read_b128 v[176:179], v227 offset:49152
	ds_read_b128 v[180:183], v227 offset:50176
	ds_read_b128 v[184:187], v227 offset:51200
	ds_read_b128 v[188:191], v227 offset:52224
	ds_read_b128 v[192:195], v227 offset:53248
	ds_read_b128 v[196:199], v227 offset:54272
	ds_read_b128 v[200:203], v227 offset:55296
	ds_read_b128 v[204:207], v227 offset:56320
	global_load_lds_dwordx4 v[144:145], off
	v_lshl_add_u64 v[144:145], v[168:169], 0, s[26:27]
	s_mov_b32 m0, s78
	s_nop 0
	global_load_lds_dwordx4 v[144:145], off
	s_barrier
	s_waitcnt lgkmcnt(0)
	s_waitcnt lgkmcnt(0)
	v_mfma_scale_f32_16x16x128_f8f6f4 v[80:83], v[0:7], v[176:183], v[80:83], v224, v224 op_sel_hi:[0,0,0]
	v_mfma_scale_f32_16x16x128_f8f6f4 v[84:87], v[8:15], v[176:183], v[84:87], v224, v224 op_sel_hi:[0,0,0]
	v_mfma_scale_f32_16x16x128_f8f6f4 v[88:91], v[0:7], v[184:191], v[88:91], v224, v224 op_sel_hi:[0,0,0]
	v_mfma_scale_f32_16x16x128_f8f6f4 v[92:95], v[8:15], v[184:191], v[92:95], v224, v224 op_sel_hi:[0,0,0]
	v_mfma_scale_f32_16x16x128_f8f6f4 v[96:99], v[0:7], v[192:199], v[96:99], v224, v224 op_sel_hi:[0,0,0]
	v_mfma_scale_f32_16x16x128_f8f6f4 v[100:103], v[8:15], v[192:199], v[100:103], v224, v224 op_sel_hi:[0,0,0]
	v_mfma_scale_f32_16x16x128_f8f6f4 v[104:107], v[0:7], v[200:207], v[104:107], v224, v224 op_sel_hi:[0,0,0]
	v_mfma_scale_f32_16x16x128_f8f6f4 v[108:111], v[8:15], v[200:207], v[108:111], v224, v224 op_sel_hi:[0,0,0]
	s_barrier
	s_add_u32 s2, s48, 0x40680
	s_addc_u32 s3, s49, 0
	s_mov_b32 m0, s64
	v_lshl_add_u64 v[0:1], s[2:3], 0, v[150:151]
	global_load_lds_dwordx4 v[0:1], off
	v_lshl_add_u64 v[0:1], s[2:3], 0, v[154:155]
	s_mov_b32 m0, s53
	s_nop 0
	global_load_lds_dwordx4 v[0:1], off
	s_waitcnt vmcnt(6)
	s_barrier
	v_mfma_scale_f32_16x16x128_f8f6f4 v[112:115], v[208:215], v[176:183], v[112:115], v224, v224 op_sel_hi:[0,0,0]
	v_mfma_scale_f32_16x16x128_f8f6f4 v[116:119], v[236:243], v[176:183], v[116:119], v224, v224 op_sel_hi:[0,0,0]
	v_mfma_scale_f32_16x16x128_f8f6f4 v[120:123], v[208:215], v[184:191], v[120:123], v224, v224 op_sel_hi:[0,0,0]
	v_mfma_scale_f32_16x16x128_f8f6f4 v[124:127], v[236:243], v[184:191], v[124:127], v224, v224 op_sel_hi:[0,0,0]
	v_mfma_scale_f32_16x16x128_f8f6f4 v[128:131], v[208:215], v[192:199], v[128:131], v224, v224 op_sel_hi:[0,0,0]
	v_mfma_scale_f32_16x16x128_f8f6f4 v[132:135], v[236:243], v[192:199], v[132:135], v224, v224 op_sel_hi:[0,0,0]
	v_mfma_scale_f32_16x16x128_f8f6f4 v[136:139], v[208:215], v[200:207], v[136:139], v224, v224 op_sel_hi:[0,0,0]
	v_mfma_scale_f32_16x16x128_f8f6f4 v[140:143], v[236:243], v[200:207], v[140:143], v224, v224 op_sel_hi:[0,0,0]
	s_and_b64 s[2:3], vcc, exec
	s_cselect_b32 s59, s45, s49
	s_cselect_b32 s58, s44, s48
	s_add_i32 s2, s56, 16
	s_ashr_i32 s3, s2, 31
	v_mov_b32_e32 v156, v229
	s_lshl_b64 s[2:3], s[2:3], 16
	s_barrier
	s_nop 7
	s_nop 7
	s_nop 7
	s_add_u32 s2, s75, s2
	s_addc_u32 s3, s76, s3
	global_load_dwordx2 v[216:217], v156, s[54:55]
	global_load_dwordx2 v[236:237], v156, s[2:3]
	global_load_dwordx2 v[212:213], v156, s[54:55] offset:512
	global_load_dwordx2 v[214:215], v156, s[2:3] offset:512
	global_load_dwordx2 v[208:209], v156, s[54:55] offset:1024
	global_load_dwordx2 v[210:211], v156, s[2:3] offset:1024
	global_load_dwordx2 v[204:205], v156, s[54:55] offset:1536
	global_load_dwordx2 v[206:207], v156, s[2:3] offset:1536
	global_load_dwordx2 v[200:201], v156, s[54:55] offset:2048
	global_load_dwordx2 v[202:203], v156, s[2:3] offset:2048
	global_load_dwordx2 v[196:197], v156, s[54:55] offset:2560
	global_load_dwordx2 v[198:199], v156, s[2:3] offset:2560
	global_load_dwordx2 v[192:193], v156, s[54:55] offset:3072
	global_load_dwordx2 v[194:195], v156, s[2:3] offset:3072
	global_load_dwordx2 v[188:189], v156, s[54:55] offset:3584
	global_load_dwordx2 v[190:191], v156, s[2:3] offset:3584
	v_lshl_add_u64 v[0:1], s[54:55], 0, v[156:157]
	v_lshl_add_u64 v[2:3], s[2:3], 0, v[156:157]
	v_add_co_u32_e32 v0, vcc, s82, v0
	s_waitcnt vmcnt(0)
	v_cvt_f32_ubyte3_e32 v243, v216
	v_cvt_f32_ubyte0_e32 v156, v236
	v_add_f32_e32 v156, 0.5, v156
	v_rcp_f32_e32 v238, v156
	v_cvt_f32_ubyte0_e32 v156, v237
	v_add_f32_e32 v156, 0.5, v156
	v_rcp_f32_e32 v218, v156
	v_cvt_f32_ubyte1_e32 v156, v236
	v_add_f32_e32 v156, 0.5, v156
	v_rcp_f32_e32 v239, v156
	v_cvt_f32_ubyte1_e32 v156, v237
	v_add_f32_e32 v156, 0.5, v156
	v_rcp_f32_e32 v219, v156
	v_cvt_f32_ubyte2_e32 v156, v236
	v_add_f32_e32 v156, 0.5, v156
	v_rcp_f32_e32 v240, v156
	v_cvt_f32_ubyte2_e32 v156, v237
	v_add_f32_e32 v156, 0.5, v156
	v_rcp_f32_e32 v220, v156
	v_cvt_f32_ubyte3_e32 v156, v236
	v_add_f32_e32 v156, 0.5, v156
	v_rcp_f32_e32 v241, v156
	v_cvt_f32_ubyte3_e32 v156, v237
	v_add_f32_e32 v156, 0.5, v156
	v_cvt_f32_ubyte1_e32 v237, v216
	v_cvt_f32_ubyte0_e32 v236, v216
	v_cvt_f32_ubyte2_e32 v242, v216
	v_rcp_f32_e32 v221, v156
	v_pk_add_f32 v[242:243], v[242:243], 0.5 op_sel_hi:[1,0]
	v_pk_add_f32 v[236:237], v[236:237], 0.5 op_sel_hi:[1,0]
	v_cvt_f32_ubyte0_e32 v156, v214
	v_pk_mul_f32 v[236:237], v[236:237], v[238:239]
	v_pk_mul_f32 v[238:239], v[242:243], v[240:241]
	v_pk_mul_f32 v[16:17], v[16:17], v[236:237]
	v_pk_mul_f32 v[18:19], v[18:19], v[238:239]
	v_cvt_f32_ubyte3_e32 v239, v217
	v_cvt_f32_ubyte2_e32 v238, v217
	v_cvt_f32_ubyte1_e32 v237, v217
	v_cvt_f32_ubyte0_e32 v236, v217
	v_pk_add_f32 v[216:217], v[238:239], 0.5 op_sel_hi:[1,0]
	v_add_f32_e32 v156, 0.5, v156
	v_pk_mul_f32 v[216:217], v[216:217], v[220:221]
	v_pk_add_f32 v[236:237], v[236:237], 0.5 op_sel_hi:[1,0]
	v_pk_mul_f32 v[22:23], v[22:23], v[216:217]
	v_rcp_f32_e32 v216, v156
	v_cvt_f32_ubyte0_e32 v156, v215
	v_pk_mul_f32 v[218:219], v[236:237], v[218:219]
	v_add_f32_e32 v156, 0.5, v156
	v_pk_mul_f32 v[20:21], v[20:21], v[218:219]
	v_rcp_f32_e32 v218, v156
	v_cvt_f32_ubyte1_e32 v156, v214
	v_add_f32_e32 v156, 0.5, v156
	v_rcp_f32_e32 v217, v156
	v_cvt_f32_ubyte1_e32 v156, v215
	v_add_f32_e32 v156, 0.5, v156
	v_rcp_f32_e32 v219, v156
	v_cvt_f32_ubyte2_e32 v156, v214
	v_add_f32_e32 v156, 0.5, v156
	v_rcp_f32_e32 v220, v156
	v_cvt_f32_ubyte2_e32 v156, v215
	v_add_f32_e32 v156, 0.5, v156
	v_rcp_f32_e32 v236, v156
	v_cvt_f32_ubyte3_e32 v156, v214
	v_add_f32_e32 v156, 0.5, v156
	v_rcp_f32_e32 v221, v156
	v_cvt_f32_ubyte3_e32 v156, v215
	v_add_f32_e32 v156, 0.5, v156
	v_cvt_f32_ubyte1_e32 v215, v212
	v_cvt_f32_ubyte0_e32 v214, v212
	v_cvt_f32_ubyte3_e32 v239, v212
	v_cvt_f32_ubyte2_e32 v238, v212
	v_rcp_f32_e32 v237, v156
	v_pk_add_f32 v[238:239], v[238:239], 0.5 op_sel_hi:[1,0]
	v_pk_add_f32 v[214:215], v[214:215], 0.5 op_sel_hi:[1,0]
	v_cvt_f32_ubyte0_e32 v156, v210
	v_pk_mul_f32 v[214:215], v[214:215], v[216:217]
	v_pk_mul_f32 v[216:217], v[238:239], v[220:221]
	v_pk_mul_f32 v[48:49], v[48:49], v[214:215]
	v_pk_mul_f32 v[50:51], v[50:51], v[216:217]
	v_cvt_f32_ubyte3_e32 v217, v213
	v_cvt_f32_ubyte2_e32 v216, v213
	v_cvt_f32_ubyte1_e32 v215, v213
	v_cvt_f32_ubyte0_e32 v214, v213
	v_pk_add_f32 v[212:213], v[216:217], 0.5 op_sel_hi:[1,0]
	v_add_f32_e32 v156, 0.5, v156
	v_pk_mul_f32 v[212:213], v[212:213], v[236:237]
	v_pk_add_f32 v[214:215], v[214:215], 0.5 op_sel_hi:[1,0]
	v_pk_mul_f32 v[54:55], v[54:55], v[212:213]
	v_rcp_f32_e32 v212, v156
	v_cvt_f32_ubyte0_e32 v156, v211
	v_pk_mul_f32 v[214:215], v[214:215], v[218:219]
	v_add_f32_e32 v156, 0.5, v156
	v_pk_mul_f32 v[52:53], v[52:53], v[214:215]
	v_rcp_f32_e32 v214, v156
	v_cvt_f32_ubyte1_e32 v156, v210
	v_add_f32_e32 v156, 0.5, v156
	v_rcp_f32_e32 v213, v156
	v_cvt_f32_ubyte1_e32 v156, v211
	v_add_f32_e32 v156, 0.5, v156
	v_rcp_f32_e32 v215, v156
	v_cvt_f32_ubyte2_e32 v156, v210
	v_add_f32_e32 v156, 0.5, v156
	v_rcp_f32_e32 v216, v156
	v_cvt_f32_ubyte2_e32 v156, v211
	v_add_f32_e32 v156, 0.5, v156
	v_rcp_f32_e32 v218, v156
	v_cvt_f32_ubyte3_e32 v156, v210
	v_add_f32_e32 v156, 0.5, v156
	v_rcp_f32_e32 v217, v156
	v_cvt_f32_ubyte3_e32 v156, v211
	v_add_f32_e32 v156, 0.5, v156
	v_cvt_f32_ubyte1_e32 v211, v208
	v_cvt_f32_ubyte0_e32 v210, v208
	v_cvt_f32_ubyte3_e32 v221, v208
	v_cvt_f32_ubyte2_e32 v220, v208
	v_rcp_f32_e32 v219, v156
	v_pk_add_f32 v[220:221], v[220:221], 0.5 op_sel_hi:[1,0]
	v_pk_add_f32 v[210:211], v[210:211], 0.5 op_sel_hi:[1,0]
	v_cvt_f32_ubyte0_e32 v156, v206
	v_pk_mul_f32 v[210:211], v[210:211], v[212:213]
	v_pk_mul_f32 v[212:213], v[220:221], v[216:217]
	v_pk_mul_f32 v[24:25], v[24:25], v[210:211]
	v_pk_mul_f32 v[26:27], v[26:27], v[212:213]
	v_cvt_f32_ubyte3_e32 v213, v209
	v_cvt_f32_ubyte2_e32 v212, v209
	v_cvt_f32_ubyte1_e32 v211, v209
	v_cvt_f32_ubyte0_e32 v210, v209
	v_pk_add_f32 v[208:209], v[212:213], 0.5 op_sel_hi:[1,0]
	v_add_f32_e32 v156, 0.5, v156
	v_pk_mul_f32 v[208:209], v[208:209], v[218:219]
	v_pk_add_f32 v[210:211], v[210:211], 0.5 op_sel_hi:[1,0]
	v_pk_mul_f32 v[30:31], v[30:31], v[208:209]
	v_rcp_f32_e32 v208, v156
	v_cvt_f32_ubyte0_e32 v156, v207
	v_pk_mul_f32 v[210:211], v[210:211], v[214:215]
	v_add_f32_e32 v156, 0.5, v156
	v_pk_mul_f32 v[28:29], v[28:29], v[210:211]
	v_rcp_f32_e32 v210, v156
	v_cvt_f32_ubyte1_e32 v156, v206
	v_add_f32_e32 v156, 0.5, v156
	v_rcp_f32_e32 v209, v156
	v_cvt_f32_ubyte1_e32 v156, v207
	v_add_f32_e32 v156, 0.5, v156
	v_rcp_f32_e32 v211, v156
	v_cvt_f32_ubyte2_e32 v156, v206
	v_add_f32_e32 v156, 0.5, v156
	v_rcp_f32_e32 v212, v156
	v_cvt_f32_ubyte2_e32 v156, v207
	v_add_f32_e32 v156, 0.5, v156
	v_rcp_f32_e32 v214, v156
	v_cvt_f32_ubyte3_e32 v156, v206
	v_add_f32_e32 v156, 0.5, v156
	v_rcp_f32_e32 v213, v156
	v_cvt_f32_ubyte3_e32 v156, v207
	v_add_f32_e32 v156, 0.5, v156
	v_cvt_f32_ubyte1_e32 v207, v204
	v_cvt_f32_ubyte0_e32 v206, v204
	v_cvt_f32_ubyte3_e32 v217, v204
	v_cvt_f32_ubyte2_e32 v216, v204
	v_rcp_f32_e32 v215, v156
	v_pk_add_f32 v[216:217], v[216:217], 0.5 op_sel_hi:[1,0]
	v_pk_add_f32 v[206:207], v[206:207], 0.5 op_sel_hi:[1,0]
	v_cvt_f32_ubyte0_e32 v156, v202
	v_pk_mul_f32 v[206:207], v[206:207], v[208:209]
	v_pk_mul_f32 v[208:209], v[216:217], v[212:213]
	v_pk_mul_f32 v[56:57], v[56:57], v[206:207]
	v_pk_mul_f32 v[58:59], v[58:59], v[208:209]
	v_cvt_f32_ubyte3_e32 v209, v205
	v_cvt_f32_ubyte2_e32 v208, v205
	v_cvt_f32_ubyte1_e32 v207, v205
	v_cvt_f32_ubyte0_e32 v206, v205
	v_pk_add_f32 v[204:205], v[208:209], 0.5 op_sel_hi:[1,0]
	v_add_f32_e32 v156, 0.5, v156
	v_pk_mul_f32 v[204:205], v[204:205], v[214:215]
	v_pk_add_f32 v[206:207], v[206:207], 0.5 op_sel_hi:[1,0]
	v_pk_mul_f32 v[62:63], v[62:63], v[204:205]
	v_rcp_f32_e32 v204, v156
	v_cvt_f32_ubyte0_e32 v156, v203
	v_pk_mul_f32 v[206:207], v[206:207], v[210:211]
	v_add_f32_e32 v156, 0.5, v156
	v_pk_mul_f32 v[60:61], v[60:61], v[206:207]
	v_rcp_f32_e32 v206, v156
	v_cvt_f32_ubyte1_e32 v156, v202
	v_add_f32_e32 v156, 0.5, v156
	v_rcp_f32_e32 v205, v156
	v_cvt_f32_ubyte1_e32 v156, v203
	v_add_f32_e32 v156, 0.5, v156
	v_rcp_f32_e32 v207, v156
	v_cvt_f32_ubyte2_e32 v156, v202
	v_add_f32_e32 v156, 0.5, v156
	v_rcp_f32_e32 v208, v156
	v_cvt_f32_ubyte2_e32 v156, v203
	v_addc_co_u32_e32 v1, vcc, 0, v1, vcc
	v_add_f32_e32 v156, 0.5, v156
	v_add_co_u32_e32 v6, vcc, s82, v2
	v_rcp_f32_e32 v210, v156
	v_cvt_f32_ubyte3_e32 v156, v202
	v_addc_co_u32_e32 v7, vcc, 0, v3, vcc
	v_add_f32_e32 v156, 0.5, v156
	global_load_dwordx2 v[184:185], v[0:1], off
	global_load_dwordx2 v[186:187], v[6:7], off
	global_load_dwordx2 v[180:181], v[0:1], off offset:512
	global_load_dwordx2 v[182:183], v[6:7], off offset:512
	global_load_dwordx2 v[176:177], v[0:1], off offset:1024
	global_load_dwordx2 v[178:179], v[6:7], off offset:1024
	global_load_dwordx2 v[144:145], v[0:1], off offset:1536
	global_load_dwordx2 v[146:147], v[6:7], off offset:1536
	global_load_dwordx2 v[12:13], v[0:1], off offset:2048
	global_load_dwordx2 v[14:15], v[6:7], off offset:2048
	global_load_dwordx2 v[8:9], v[0:1], off offset:2560
	global_load_dwordx2 v[10:11], v[6:7], off offset:2560
	global_load_dwordx2 v[2:3], v[0:1], off offset:3072
	global_load_dwordx2 v[4:5], v[6:7], off offset:3072
	s_nop 0
	global_load_dwordx2 v[0:1], v[0:1], off offset:3584
	s_nop 0
	global_load_dwordx2 v[6:7], v[6:7], off offset:3584
	v_rcp_f32_e32 v209, v156
	v_cvt_f32_ubyte3_e32 v156, v203
	v_add_f32_e32 v156, 0.5, v156
	v_cvt_f32_ubyte1_e32 v203, v200
	v_cvt_f32_ubyte0_e32 v202, v200
	v_cvt_f32_ubyte3_e32 v213, v200
	v_cvt_f32_ubyte2_e32 v212, v200
	v_rcp_f32_e32 v211, v156
	v_pk_add_f32 v[212:213], v[212:213], 0.5 op_sel_hi:[1,0]
	v_pk_add_f32 v[202:203], v[202:203], 0.5 op_sel_hi:[1,0]
	v_cvt_f32_ubyte0_e32 v156, v198
	v_pk_mul_f32 v[202:203], v[202:203], v[204:205]
	v_pk_mul_f32 v[204:205], v[212:213], v[208:209]
	v_pk_mul_f32 v[32:33], v[32:33], v[202:203]
	v_pk_mul_f32 v[34:35], v[34:35], v[204:205]
	v_cvt_f32_ubyte3_e32 v205, v201
	v_cvt_f32_ubyte2_e32 v204, v201
	v_cvt_f32_ubyte1_e32 v203, v201
	v_cvt_f32_ubyte0_e32 v202, v201
	v_pk_add_f32 v[200:201], v[204:205], 0.5 op_sel_hi:[1,0]
	v_add_f32_e32 v156, 0.5, v156
	v_pk_mul_f32 v[200:201], v[200:201], v[210:211]
	v_pk_add_f32 v[202:203], v[202:203], 0.5 op_sel_hi:[1,0]
	v_pk_mul_f32 v[38:39], v[38:39], v[200:201]
	v_rcp_f32_e32 v200, v156
	v_cvt_f32_ubyte0_e32 v156, v199
	v_pk_mul_f32 v[202:203], v[202:203], v[206:207]
	v_add_f32_e32 v156, 0.5, v156
	v_pk_mul_f32 v[36:37], v[36:37], v[202:203]
	v_rcp_f32_e32 v202, v156
	v_cvt_f32_ubyte1_e32 v156, v198
	v_add_f32_e32 v156, 0.5, v156
	v_rcp_f32_e32 v201, v156
	v_cvt_f32_ubyte1_e32 v156, v199
	v_add_f32_e32 v156, 0.5, v156
	v_rcp_f32_e32 v203, v156
	v_cvt_f32_ubyte2_e32 v156, v198
	v_add_f32_e32 v156, 0.5, v156
	v_rcp_f32_e32 v204, v156
	v_cvt_f32_ubyte2_e32 v156, v199
	v_add_f32_e32 v156, 0.5, v156
	v_rcp_f32_e32 v206, v156
	v_cvt_f32_ubyte3_e32 v156, v198
	v_add_f32_e32 v156, 0.5, v156
	v_rcp_f32_e32 v205, v156
	v_cvt_f32_ubyte3_e32 v156, v199
	v_add_f32_e32 v156, 0.5, v156
	v_cvt_f32_ubyte1_e32 v199, v196
	v_cvt_f32_ubyte0_e32 v198, v196
	v_cvt_f32_ubyte3_e32 v209, v196
	v_cvt_f32_ubyte2_e32 v208, v196
	v_rcp_f32_e32 v207, v156
	v_pk_add_f32 v[208:209], v[208:209], 0.5 op_sel_hi:[1,0]
	v_pk_add_f32 v[198:199], v[198:199], 0.5 op_sel_hi:[1,0]
	v_cvt_f32_ubyte0_e32 v156, v194
	v_pk_mul_f32 v[198:199], v[198:199], v[200:201]
	v_pk_mul_f32 v[200:201], v[208:209], v[204:205]
	v_pk_mul_f32 v[64:65], v[64:65], v[198:199]
	v_pk_mul_f32 v[66:67], v[66:67], v[200:201]
	v_cvt_f32_ubyte3_e32 v201, v197
	v_cvt_f32_ubyte2_e32 v200, v197
	v_cvt_f32_ubyte1_e32 v199, v197
	v_cvt_f32_ubyte0_e32 v198, v197
	v_pk_add_f32 v[196:197], v[200:201], 0.5 op_sel_hi:[1,0]
	v_add_f32_e32 v156, 0.5, v156
	v_pk_mul_f32 v[196:197], v[196:197], v[206:207]
	v_pk_add_f32 v[198:199], v[198:199], 0.5 op_sel_hi:[1,0]
	v_pk_mul_f32 v[70:71], v[70:71], v[196:197]
	v_rcp_f32_e32 v196, v156
	v_cvt_f32_ubyte0_e32 v156, v195
	v_pk_mul_f32 v[198:199], v[198:199], v[202:203]
	v_add_f32_e32 v156, 0.5, v156
	v_pk_mul_f32 v[68:69], v[68:69], v[198:199]
	v_rcp_f32_e32 v198, v156
	v_cvt_f32_ubyte1_e32 v156, v194
	v_add_f32_e32 v156, 0.5, v156
	v_rcp_f32_e32 v197, v156
	v_cvt_f32_ubyte1_e32 v156, v195
	v_add_f32_e32 v156, 0.5, v156
	v_rcp_f32_e32 v199, v156
	v_cvt_f32_ubyte2_e32 v156, v194
	v_add_f32_e32 v156, 0.5, v156
	v_rcp_f32_e32 v200, v156
	v_cvt_f32_ubyte2_e32 v156, v195
	v_add_f32_e32 v156, 0.5, v156
	v_rcp_f32_e32 v202, v156
	v_cvt_f32_ubyte3_e32 v156, v194
	v_add_f32_e32 v156, 0.5, v156
	v_rcp_f32_e32 v201, v156
	v_cvt_f32_ubyte3_e32 v156, v195
	v_add_f32_e32 v156, 0.5, v156
	v_cvt_f32_ubyte1_e32 v195, v192
	v_cvt_f32_ubyte0_e32 v194, v192
	v_cvt_f32_ubyte3_e32 v205, v192
	v_cvt_f32_ubyte2_e32 v204, v192
	v_rcp_f32_e32 v203, v156
	v_pk_add_f32 v[204:205], v[204:205], 0.5 op_sel_hi:[1,0]
	v_pk_add_f32 v[194:195], v[194:195], 0.5 op_sel_hi:[1,0]
	v_cvt_f32_ubyte0_e32 v156, v190
	v_pk_mul_f32 v[194:195], v[194:195], v[196:197]
	v_pk_mul_f32 v[196:197], v[204:205], v[200:201]
	v_pk_mul_f32 v[40:41], v[40:41], v[194:195]
	v_pk_mul_f32 v[42:43], v[42:43], v[196:197]
	v_cvt_f32_ubyte3_e32 v197, v193
	v_cvt_f32_ubyte2_e32 v196, v193
	v_cvt_f32_ubyte1_e32 v195, v193
	v_cvt_f32_ubyte0_e32 v194, v193
	v_pk_add_f32 v[192:193], v[196:197], 0.5 op_sel_hi:[1,0]
	v_add_f32_e32 v156, 0.5, v156
	v_pk_mul_f32 v[192:193], v[192:193], v[202:203]
	v_pk_add_f32 v[194:195], v[194:195], 0.5 op_sel_hi:[1,0]
	v_pk_mul_f32 v[46:47], v[46:47], v[192:193]
	v_rcp_f32_e32 v192, v156
	v_cvt_f32_ubyte0_e32 v156, v191
	v_pk_mul_f32 v[194:195], v[194:195], v[198:199]
	v_add_f32_e32 v156, 0.5, v156
	v_pk_mul_f32 v[44:45], v[44:45], v[194:195]
	v_rcp_f32_e32 v194, v156
	v_cvt_f32_ubyte1_e32 v156, v190
	v_add_f32_e32 v156, 0.5, v156
	v_rcp_f32_e32 v193, v156
	v_cvt_f32_ubyte1_e32 v156, v191
	v_add_f32_e32 v156, 0.5, v156
	v_rcp_f32_e32 v195, v156
	v_cvt_f32_ubyte2_e32 v156, v190
	v_add_f32_e32 v156, 0.5, v156
	v_rcp_f32_e32 v196, v156
	v_cvt_f32_ubyte2_e32 v156, v191
	v_add_f32_e32 v156, 0.5, v156
	v_rcp_f32_e32 v198, v156
	v_cvt_f32_ubyte3_e32 v156, v190
	v_add_f32_e32 v156, 0.5, v156
	v_rcp_f32_e32 v197, v156
	v_cvt_f32_ubyte3_e32 v156, v191
	v_add_f32_e32 v156, 0.5, v156
	v_cvt_f32_ubyte1_e32 v191, v188
	v_cvt_f32_ubyte0_e32 v190, v188
	v_cvt_f32_ubyte3_e32 v201, v188
	v_cvt_f32_ubyte2_e32 v200, v188
	v_rcp_f32_e32 v199, v156
	v_pk_add_f32 v[200:201], v[200:201], 0.5 op_sel_hi:[1,0]
	v_pk_add_f32 v[190:191], v[190:191], 0.5 op_sel_hi:[1,0]
	s_waitcnt vmcnt(0)
	v_cvt_f32_ubyte0_e32 v156, v186
	v_pk_mul_f32 v[190:191], v[190:191], v[192:193]
	v_pk_mul_f32 v[192:193], v[200:201], v[196:197]
	v_pk_mul_f32 v[72:73], v[72:73], v[190:191]
	v_pk_mul_f32 v[74:75], v[74:75], v[192:193]
	v_cvt_f32_ubyte3_e32 v193, v189
	v_cvt_f32_ubyte2_e32 v192, v189
	v_cvt_f32_ubyte1_e32 v191, v189
	v_cvt_f32_ubyte0_e32 v190, v189
	v_pk_add_f32 v[188:189], v[192:193], 0.5 op_sel_hi:[1,0]
	v_add_f32_e32 v156, 0.5, v156
	v_pk_mul_f32 v[188:189], v[188:189], v[198:199]
	v_pk_add_f32 v[190:191], v[190:191], 0.5 op_sel_hi:[1,0]
	v_pk_mul_f32 v[78:79], v[78:79], v[188:189]
	v_rcp_f32_e32 v188, v156
	v_cvt_f32_ubyte0_e32 v156, v187
	v_pk_mul_f32 v[190:191], v[190:191], v[194:195]
	v_add_f32_e32 v156, 0.5, v156
	v_pk_mul_f32 v[76:77], v[76:77], v[190:191]
	v_rcp_f32_e32 v190, v156
	v_cvt_f32_ubyte1_e32 v156, v186
	v_add_f32_e32 v156, 0.5, v156
	v_rcp_f32_e32 v189, v156
	v_cvt_f32_ubyte1_e32 v156, v187
	v_add_f32_e32 v156, 0.5, v156
	v_rcp_f32_e32 v191, v156
	v_cvt_f32_ubyte2_e32 v156, v186
	v_add_f32_e32 v156, 0.5, v156
	v_rcp_f32_e32 v192, v156
	v_cvt_f32_ubyte2_e32 v156, v187
	v_add_f32_e32 v156, 0.5, v156
	v_rcp_f32_e32 v194, v156
	v_cvt_f32_ubyte3_e32 v156, v186
	v_add_f32_e32 v156, 0.5, v156
	v_rcp_f32_e32 v193, v156
	v_cvt_f32_ubyte3_e32 v156, v187
	v_add_f32_e32 v156, 0.5, v156
	v_cvt_f32_ubyte1_e32 v187, v184
	v_cvt_f32_ubyte0_e32 v186, v184
	v_cvt_f32_ubyte3_e32 v197, v184
	v_cvt_f32_ubyte2_e32 v196, v184
	v_rcp_f32_e32 v195, v156
	v_pk_add_f32 v[196:197], v[196:197], 0.5 op_sel_hi:[1,0]
	v_pk_add_f32 v[186:187], v[186:187], 0.5 op_sel_hi:[1,0]
	v_cvt_f32_ubyte0_e32 v156, v182
	v_pk_mul_f32 v[186:187], v[186:187], v[188:189]
	v_pk_mul_f32 v[188:189], v[196:197], v[192:193]
	v_pk_mul_f32 v[80:81], v[80:81], v[186:187]
	v_pk_mul_f32 v[82:83], v[82:83], v[188:189]
	v_cvt_f32_ubyte3_e32 v189, v185
	v_cvt_f32_ubyte2_e32 v188, v185
	v_cvt_f32_ubyte1_e32 v187, v185
	v_cvt_f32_ubyte0_e32 v186, v185
	v_pk_add_f32 v[184:185], v[188:189], 0.5 op_sel_hi:[1,0]
	v_add_f32_e32 v156, 0.5, v156
	v_pk_mul_f32 v[184:185], v[184:185], v[194:195]
	v_pk_add_f32 v[186:187], v[186:187], 0.5 op_sel_hi:[1,0]
	v_pk_mul_f32 v[86:87], v[86:87], v[184:185]
	v_rcp_f32_e32 v184, v156
	v_cvt_f32_ubyte0_e32 v156, v183
	v_pk_mul_f32 v[186:187], v[186:187], v[190:191]
	v_add_f32_e32 v156, 0.5, v156
	v_pk_mul_f32 v[84:85], v[84:85], v[186:187]
	v_rcp_f32_e32 v186, v156
	v_cvt_f32_ubyte1_e32 v156, v182
	v_add_f32_e32 v156, 0.5, v156
	v_rcp_f32_e32 v185, v156
	v_cvt_f32_ubyte1_e32 v156, v183
	v_add_f32_e32 v156, 0.5, v156
	v_rcp_f32_e32 v187, v156
	v_cvt_f32_ubyte2_e32 v156, v182
	v_add_f32_e32 v156, 0.5, v156
	v_rcp_f32_e32 v188, v156
	v_cvt_f32_ubyte2_e32 v156, v183
	v_add_f32_e32 v156, 0.5, v156
	v_rcp_f32_e32 v190, v156
	v_cvt_f32_ubyte3_e32 v156, v182
	v_add_f32_e32 v156, 0.5, v156
	v_rcp_f32_e32 v189, v156
	v_cvt_f32_ubyte3_e32 v156, v183
	v_add_f32_e32 v156, 0.5, v156
	v_cvt_f32_ubyte1_e32 v183, v180
	v_cvt_f32_ubyte0_e32 v182, v180
	v_cvt_f32_ubyte3_e32 v193, v180
	v_cvt_f32_ubyte2_e32 v192, v180
	v_rcp_f32_e32 v191, v156
	v_pk_add_f32 v[192:193], v[192:193], 0.5 op_sel_hi:[1,0]
	v_pk_add_f32 v[182:183], v[182:183], 0.5 op_sel_hi:[1,0]
	v_cvt_f32_ubyte0_e32 v156, v178
	v_pk_mul_f32 v[182:183], v[182:183], v[184:185]
	v_pk_mul_f32 v[184:185], v[192:193], v[188:189]
	v_pk_mul_f32 v[112:113], v[112:113], v[182:183]
	v_pk_mul_f32 v[114:115], v[114:115], v[184:185]
	v_cvt_f32_ubyte3_e32 v185, v181
	v_cvt_f32_ubyte2_e32 v184, v181
	v_cvt_f32_ubyte1_e32 v183, v181
	v_cvt_f32_ubyte0_e32 v182, v181
	v_pk_add_f32 v[180:181], v[184:185], 0.5 op_sel_hi:[1,0]
	v_add_f32_e32 v156, 0.5, v156
	v_pk_mul_f32 v[180:181], v[180:181], v[190:191]
	v_pk_add_f32 v[182:183], v[182:183], 0.5 op_sel_hi:[1,0]
	v_pk_mul_f32 v[118:119], v[118:119], v[180:181]
	v_rcp_f32_e32 v180, v156
	v_cvt_f32_ubyte0_e32 v156, v179
	v_pk_mul_f32 v[182:183], v[182:183], v[186:187]
	v_add_f32_e32 v156, 0.5, v156
	v_pk_mul_f32 v[116:117], v[116:117], v[182:183]
	v_rcp_f32_e32 v182, v156
	v_cvt_f32_ubyte1_e32 v156, v178
	v_add_f32_e32 v156, 0.5, v156
	v_rcp_f32_e32 v181, v156
	v_cvt_f32_ubyte1_e32 v156, v179
	v_add_f32_e32 v156, 0.5, v156
	v_rcp_f32_e32 v183, v156
	v_cvt_f32_ubyte2_e32 v156, v178
	v_add_f32_e32 v156, 0.5, v156
	v_rcp_f32_e32 v184, v156
	v_cvt_f32_ubyte2_e32 v156, v179
	v_add_f32_e32 v156, 0.5, v156
	v_rcp_f32_e32 v186, v156
	v_cvt_f32_ubyte3_e32 v156, v178
	v_add_f32_e32 v156, 0.5, v156
	v_rcp_f32_e32 v185, v156
	v_cvt_f32_ubyte3_e32 v156, v179
	v_add_f32_e32 v156, 0.5, v156
	v_cvt_f32_ubyte1_e32 v179, v176
	v_cvt_f32_ubyte0_e32 v178, v176
	v_cvt_f32_ubyte3_e32 v189, v176
	v_cvt_f32_ubyte2_e32 v188, v176
	v_rcp_f32_e32 v187, v156
	v_pk_add_f32 v[188:189], v[188:189], 0.5 op_sel_hi:[1,0]
	v_pk_add_f32 v[178:179], v[178:179], 0.5 op_sel_hi:[1,0]
	v_cvt_f32_ubyte0_e32 v156, v146
	v_pk_mul_f32 v[178:179], v[178:179], v[180:181]
	v_pk_mul_f32 v[180:181], v[188:189], v[184:185]
	v_pk_mul_f32 v[88:89], v[88:89], v[178:179]
	v_pk_mul_f32 v[90:91], v[90:91], v[180:181]
	v_cvt_f32_ubyte3_e32 v181, v177
	v_cvt_f32_ubyte2_e32 v180, v177
	v_cvt_f32_ubyte1_e32 v179, v177
	v_cvt_f32_ubyte0_e32 v178, v177
	v_pk_add_f32 v[176:177], v[180:181], 0.5 op_sel_hi:[1,0]
	v_add_f32_e32 v156, 0.5, v156
	v_pk_mul_f32 v[176:177], v[176:177], v[186:187]
	v_pk_add_f32 v[178:179], v[178:179], 0.5 op_sel_hi:[1,0]
	v_pk_mul_f32 v[94:95], v[94:95], v[176:177]
	v_rcp_f32_e32 v176, v156
	v_cvt_f32_ubyte0_e32 v156, v147
	v_pk_mul_f32 v[178:179], v[178:179], v[182:183]
	v_add_f32_e32 v156, 0.5, v156
	v_pk_mul_f32 v[92:93], v[92:93], v[178:179]
	v_rcp_f32_e32 v178, v156
	v_cvt_f32_ubyte1_e32 v156, v146
	v_add_f32_e32 v156, 0.5, v156
	v_rcp_f32_e32 v177, v156
	v_cvt_f32_ubyte1_e32 v156, v147
	v_add_f32_e32 v156, 0.5, v156
	v_rcp_f32_e32 v179, v156
	v_cvt_f32_ubyte2_e32 v156, v146
	v_cvt_f32_ubyte3_e32 v146, v146
	v_add_f32_e32 v156, 0.5, v156
	v_add_f32_e32 v146, 0.5, v146
	v_rcp_f32_e32 v180, v156
	v_rcp_f32_e32 v181, v146
	v_cvt_f32_ubyte3_e32 v146, v147
	v_cvt_f32_ubyte2_e32 v156, v147
	v_add_f32_e32 v146, 0.5, v146
	v_add_f32_e32 v156, 0.5, v156
	v_rcp_f32_e32 v183, v146
	v_cvt_f32_ubyte1_e32 v147, v144
	v_cvt_f32_ubyte0_e32 v146, v144
	v_cvt_f32_ubyte3_e32 v185, v144
	v_cvt_f32_ubyte2_e32 v184, v144
	v_rcp_f32_e32 v182, v156
	v_pk_add_f32 v[184:185], v[184:185], 0.5 op_sel_hi:[1,0]
	v_pk_add_f32 v[146:147], v[146:147], 0.5 op_sel_hi:[1,0]
	v_cvt_f32_ubyte2_e32 v156, v14
	v_pk_mul_f32 v[146:147], v[146:147], v[176:177]
	v_pk_mul_f32 v[176:177], v[184:185], v[180:181]
	v_pk_mul_f32 v[120:121], v[120:121], v[146:147]
	v_pk_mul_f32 v[122:123], v[122:123], v[176:177]
	v_cvt_f32_ubyte3_e32 v177, v145
	v_cvt_f32_ubyte2_e32 v176, v145
	v_cvt_f32_ubyte1_e32 v147, v145
	v_cvt_f32_ubyte0_e32 v146, v145
	v_pk_add_f32 v[144:145], v[176:177], 0.5 op_sel_hi:[1,0]
	v_pk_add_f32 v[146:147], v[146:147], 0.5 op_sel_hi:[1,0]
	v_pk_mul_f32 v[144:145], v[144:145], v[182:183]
	v_pk_mul_f32 v[146:147], v[146:147], v[178:179]
	v_pk_mul_f32 v[126:127], v[126:127], v[144:145]
	v_cvt_f32_ubyte0_e32 v145, v15
	v_add_f32_e32 v145, 0.5, v145
	v_pk_mul_f32 v[124:125], v[124:125], v[146:147]
	v_cvt_f32_ubyte0_e32 v144, v14
	v_rcp_f32_e32 v146, v145
	v_cvt_f32_ubyte1_e32 v145, v14
	v_cvt_f32_ubyte3_e32 v14, v14
	v_add_f32_e32 v144, 0.5, v144
	v_add_f32_e32 v145, 0.5, v145
	v_add_f32_e32 v156, 0.5, v156
	v_add_f32_e32 v14, 0.5, v14
	v_rcp_f32_e32 v144, v144
	v_rcp_f32_e32 v145, v145
	v_rcp_f32_e32 v176, v156
	v_rcp_f32_e32 v177, v14
	v_cvt_f32_ubyte3_e32 v14, v15
	v_cvt_f32_ubyte2_e32 v156, v15
	v_add_f32_e32 v14, 0.5, v14
	v_cvt_f32_ubyte1_e32 v147, v15
	v_add_f32_e32 v156, 0.5, v156
	v_rcp_f32_e32 v179, v14
	v_cvt_f32_ubyte1_e32 v15, v12
	v_cvt_f32_ubyte0_e32 v14, v12
	v_cvt_f32_ubyte3_e32 v181, v12
	v_cvt_f32_ubyte2_e32 v180, v12
	v_rcp_f32_e32 v178, v156
	v_pk_add_f32 v[180:181], v[180:181], 0.5 op_sel_hi:[1,0]
	v_pk_add_f32 v[14:15], v[14:15], 0.5 op_sel_hi:[1,0]
	v_add_f32_e32 v147, 0.5, v147
	v_pk_mul_f32 v[14:15], v[14:15], v[144:145]
	v_pk_mul_f32 v[144:145], v[180:181], v[176:177]
	v_rcp_f32_e32 v147, v147
	v_pk_mul_f32 v[98:99], v[98:99], v[144:145]
	v_cvt_f32_ubyte3_e32 v145, v13
	v_cvt_f32_ubyte2_e32 v144, v13
	v_pk_mul_f32 v[96:97], v[96:97], v[14:15]
	v_cvt_f32_ubyte1_e32 v15, v13
	v_cvt_f32_ubyte0_e32 v14, v13
	v_pk_add_f32 v[12:13], v[144:145], 0.5 op_sel_hi:[1,0]
	v_pk_add_f32 v[14:15], v[14:15], 0.5 op_sel_hi:[1,0]
	v_pk_mul_f32 v[12:13], v[12:13], v[178:179]
	v_pk_mul_f32 v[14:15], v[14:15], v[146:147]
	v_pk_mul_f32 v[102:103], v[102:103], v[12:13]
	v_cvt_f32_ubyte0_e32 v13, v11
	v_add_f32_e32 v13, 0.5, v13
	v_pk_mul_f32 v[100:101], v[100:101], v[14:15]
	v_cvt_f32_ubyte0_e32 v12, v10
	v_rcp_f32_e32 v14, v13
	v_cvt_f32_ubyte1_e32 v13, v10
	v_cvt_f32_ubyte2_e32 v144, v10
	v_cvt_f32_ubyte2_e32 v145, v11
	v_cvt_f32_ubyte3_e32 v10, v10
	v_add_f32_e32 v12, 0.5, v12
	v_add_f32_e32 v13, 0.5, v13
	v_add_f32_e32 v144, 0.5, v144
	v_add_f32_e32 v145, 0.5, v145
	v_add_f32_e32 v10, 0.5, v10
	v_rcp_f32_e32 v12, v12
	v_rcp_f32_e32 v13, v13
	v_rcp_f32_e32 v144, v144
	v_rcp_f32_e32 v146, v145
	v_rcp_f32_e32 v145, v10
	v_cvt_f32_ubyte3_e32 v10, v11
	v_add_f32_e32 v10, 0.5, v10
	v_cvt_f32_ubyte1_e32 v15, v11
	v_rcp_f32_e32 v147, v10
	v_cvt_f32_ubyte1_e32 v11, v8
	v_cvt_f32_ubyte0_e32 v10, v8
	v_cvt_f32_ubyte3_e32 v177, v8
	v_cvt_f32_ubyte2_e32 v176, v8
	v_pk_add_f32 v[176:177], v[176:177], 0.5 op_sel_hi:[1,0]
	v_pk_add_f32 v[10:11], v[10:11], 0.5 op_sel_hi:[1,0]
	v_add_f32_e32 v15, 0.5, v15
	v_pk_mul_f32 v[10:11], v[10:11], v[12:13]
	v_pk_mul_f32 v[12:13], v[176:177], v[144:145]
	v_rcp_f32_e32 v15, v15
	v_pk_mul_f32 v[130:131], v[130:131], v[12:13]
	v_cvt_f32_ubyte3_e32 v13, v9
	v_cvt_f32_ubyte2_e32 v12, v9
	v_pk_mul_f32 v[128:129], v[128:129], v[10:11]
	v_cvt_f32_ubyte1_e32 v11, v9
	v_cvt_f32_ubyte0_e32 v10, v9
	v_pk_add_f32 v[8:9], v[12:13], 0.5 op_sel_hi:[1,0]
	v_pk_add_f32 v[10:11], v[10:11], 0.5 op_sel_hi:[1,0]
	v_pk_mul_f32 v[8:9], v[8:9], v[146:147]
	v_pk_mul_f32 v[10:11], v[10:11], v[14:15]
	v_pk_mul_f32 v[134:135], v[134:135], v[8:9]
	v_cvt_f32_ubyte0_e32 v9, v5
	v_add_f32_e32 v9, 0.5, v9
	v_pk_mul_f32 v[132:133], v[132:133], v[10:11]
	v_cvt_f32_ubyte0_e32 v8, v4
	v_rcp_f32_e32 v10, v9
	v_cvt_f32_ubyte1_e32 v9, v4
	v_cvt_f32_ubyte2_e32 v12, v4
	v_cvt_f32_ubyte2_e32 v13, v5
	v_cvt_f32_ubyte3_e32 v4, v4
	v_add_f32_e32 v8, 0.5, v8
	v_add_f32_e32 v9, 0.5, v9
	v_add_f32_e32 v12, 0.5, v12
	v_add_f32_e32 v13, 0.5, v13
	v_add_f32_e32 v4, 0.5, v4
	v_rcp_f32_e32 v8, v8
	v_rcp_f32_e32 v9, v9
	v_rcp_f32_e32 v12, v12
	v_rcp_f32_e32 v14, v13
	v_rcp_f32_e32 v13, v4
	v_cvt_f32_ubyte3_e32 v4, v5
	v_add_f32_e32 v4, 0.5, v4
	v_cvt_f32_ubyte1_e32 v11, v5
	v_rcp_f32_e32 v15, v4
	v_cvt_f32_ubyte1_e32 v5, v2
	v_cvt_f32_ubyte0_e32 v4, v2
	v_cvt_f32_ubyte3_e32 v145, v2
	v_cvt_f32_ubyte2_e32 v144, v2
	v_pk_add_f32 v[144:145], v[144:145], 0.5 op_sel_hi:[1,0]
	v_pk_add_f32 v[4:5], v[4:5], 0.5 op_sel_hi:[1,0]
	v_add_f32_e32 v11, 0.5, v11
	v_pk_mul_f32 v[4:5], v[4:5], v[8:9]
	v_pk_mul_f32 v[8:9], v[144:145], v[12:13]
	v_rcp_f32_e32 v11, v11
	v_pk_mul_f32 v[106:107], v[106:107], v[8:9]
	v_cvt_f32_ubyte3_e32 v9, v3
	v_cvt_f32_ubyte2_e32 v8, v3
	v_pk_mul_f32 v[104:105], v[104:105], v[4:5]
	v_cvt_f32_ubyte1_e32 v5, v3
	v_cvt_f32_ubyte0_e32 v4, v3
	v_pk_add_f32 v[2:3], v[8:9], 0.5 op_sel_hi:[1,0]
	v_pk_add_f32 v[4:5], v[4:5], 0.5 op_sel_hi:[1,0]
	v_pk_mul_f32 v[2:3], v[2:3], v[14:15]
	v_pk_mul_f32 v[4:5], v[4:5], v[10:11]
	v_pk_mul_f32 v[110:111], v[110:111], v[2:3]
	v_cvt_f32_ubyte0_e32 v3, v7
	v_add_f32_e32 v3, 0.5, v3
	v_pk_mul_f32 v[108:109], v[108:109], v[4:5]
	v_cvt_f32_ubyte0_e32 v2, v6
	v_rcp_f32_e32 v4, v3
	v_cvt_f32_ubyte1_e32 v3, v6
	v_cvt_f32_ubyte2_e32 v8, v6
	v_cvt_f32_ubyte2_e32 v9, v7
	v_cvt_f32_ubyte3_e32 v6, v6
	v_add_f32_e32 v2, 0.5, v2
	v_add_f32_e32 v3, 0.5, v3
	v_add_f32_e32 v8, 0.5, v8
	v_add_f32_e32 v9, 0.5, v9
	v_add_f32_e32 v6, 0.5, v6
	v_rcp_f32_e32 v2, v2
	v_rcp_f32_e32 v3, v3
	v_rcp_f32_e32 v8, v8
	v_rcp_f32_e32 v10, v9
	v_rcp_f32_e32 v9, v6
	v_cvt_f32_ubyte3_e32 v6, v7
	v_cvt_f32_ubyte1_e32 v5, v7
	v_add_f32_e32 v6, 0.5, v6
	v_add_f32_e32 v5, 0.5, v5
	v_rcp_f32_e32 v11, v6
	v_cvt_f32_ubyte1_e32 v7, v0
	v_cvt_f32_ubyte0_e32 v6, v0
	v_cvt_f32_ubyte3_e32 v13, v0
	v_cvt_f32_ubyte2_e32 v12, v0
	v_rcp_f32_e32 v5, v5
	v_pk_add_f32 v[12:13], v[12:13], 0.5 op_sel_hi:[1,0]
	v_pk_add_f32 v[6:7], v[6:7], 0.5 op_sel_hi:[1,0]
	s_nop 0
	v_pk_mul_f32 v[2:3], v[6:7], v[2:3]
	v_pk_mul_f32 v[6:7], v[12:13], v[8:9]
	v_pk_mul_f32 v[144:145], v[136:137], v[2:3]
	v_pk_mul_f32 v[146:147], v[138:139], v[6:7]
	v_cvt_f32_ubyte1_e32 v3, v1
	v_cvt_f32_ubyte0_e32 v2, v1
	v_cvt_f32_ubyte3_e32 v7, v1
	v_cvt_f32_ubyte2_e32 v6, v1
	v_pk_add_f32 v[0:1], v[6:7], 0.5 op_sel_hi:[1,0]
	v_pk_add_f32 v[2:3], v[2:3], 0.5 op_sel_hi:[1,0]
	v_pk_mul_f32 v[0:1], v[0:1], v[10:11]
	v_pk_mul_f32 v[2:3], v[2:3], v[4:5]
	v_pk_mul_f32 v[138:139], v[142:143], v[0:1]
	v_pk_mul_f32 v[136:137], v[140:141], v[2:3]
	ds_read_b128 v[8:11], v230
	ds_read_b128 v[12:15], v230 offset:1024
	ds_read_b128 v[0:3], v230 offset:2048
	ds_read_b128 v[4:7], v230 offset:3072
	s_add_u32 s54, s46, 0x40680
	s_addc_u32 s55, s47, 0
	s_mov_b32 m0, s92
	v_lshl_add_u64 v[140:141], s[54:55], 0, v[148:149]
	ds_read_b128 v[176:179], v227
	ds_read_b128 v[180:183], v227 offset:1024
	ds_read_b128 v[184:187], v227 offset:2048
	ds_read_b128 v[188:191], v227 offset:3072
	ds_read_b128 v[192:195], v227 offset:4096
	ds_read_b128 v[196:199], v227 offset:5120
	ds_read_b128 v[200:203], v227 offset:6144
	ds_read_b128 v[204:207], v227 offset:7168
	global_load_lds_dwordx4 v[140:141], off
	v_lshl_add_u64 v[140:141], s[54:55], 0, v[152:153]
	s_mov_b32 m0, s91
	s_nop 0
	global_load_lds_dwordx4 v[140:141], off
	s_waitcnt lgkmcnt(8)
	s_barrier
	s_waitcnt lgkmcnt(0)
	s_waitcnt lgkmcnt(0)
	v_mfma_scale_f32_16x16x128_f8f6f4 v[16:19], v[8:15], v[176:183], v[16:19], v224, v224 op_sel_hi:[0,0,0]
	v_mfma_scale_f32_16x16x128_f8f6f4 v[20:23], v[0:7], v[176:183], v[20:23], v224, v224 op_sel_hi:[0,0,0]
	v_mfma_scale_f32_16x16x128_f8f6f4 v[24:27], v[8:15], v[184:191], v[24:27], v224, v224 op_sel_hi:[0,0,0]
	v_mfma_scale_f32_16x16x128_f8f6f4 v[28:31], v[0:7], v[184:191], v[28:31], v224, v224 op_sel_hi:[0,0,0]
	v_mfma_scale_f32_16x16x128_f8f6f4 v[32:35], v[8:15], v[192:199], v[32:35], v224, v224 op_sel_hi:[0,0,0]
	v_mfma_scale_f32_16x16x128_f8f6f4 v[36:39], v[0:7], v[192:199], v[36:39], v224, v224 op_sel_hi:[0,0,0]
	v_mfma_scale_f32_16x16x128_f8f6f4 v[40:43], v[8:15], v[200:207], v[40:43], v224, v224 op_sel_hi:[0,0,0]
	v_mfma_scale_f32_16x16x128_f8f6f4 v[44:47], v[0:7], v[200:207], v[44:47], v224, v224 op_sel_hi:[0,0,0]
	s_barrier
	s_mov_b32 m0, s94
	v_lshl_add_u64 v[140:141], v[170:171], 0, s[28:29]
	ds_read_b128 v[208:211], v231
	ds_read_b128 v[212:215], v231 offset:1024
	ds_read_b128 v[236:239], v231 offset:2048
	ds_read_b128 v[240:243], v231 offset:3072
	global_load_lds_dwordx4 v[140:141], off
	v_lshl_add_u64 v[140:141], v[172:173], 0, s[28:29]
	s_mov_b32 m0, s93
	s_nop 0
	global_load_lds_dwordx4 v[140:141], off
	s_barrier
	s_waitcnt lgkmcnt(0)
	s_waitcnt lgkmcnt(0)
	v_mfma_scale_f32_16x16x128_f8f6f4 v[48:51], v[208:215], v[176:183], v[48:51], v224, v224 op_sel_hi:[0,0,0]
	v_mfma_scale_f32_16x16x128_f8f6f4 v[52:55], v[236:243], v[176:183], v[52:55], v224, v224 op_sel_hi:[0,0,0]
	v_mfma_scale_f32_16x16x128_f8f6f4 v[56:59], v[208:215], v[184:191], v[56:59], v224, v224 op_sel_hi:[0,0,0]
	v_mfma_scale_f32_16x16x128_f8f6f4 v[60:63], v[236:243], v[184:191], v[60:63], v224, v224 op_sel_hi:[0,0,0]
	v_mfma_scale_f32_16x16x128_f8f6f4 v[64:67], v[208:215], v[192:199], v[64:67], v224, v224 op_sel_hi:[0,0,0]
	v_mfma_scale_f32_16x16x128_f8f6f4 v[68:71], v[236:243], v[192:199], v[68:71], v224, v224 op_sel_hi:[0,0,0]
	v_mfma_scale_f32_16x16x128_f8f6f4 v[72:75], v[208:215], v[200:207], v[72:75], v224, v224 op_sel_hi:[0,0,0]
	v_mfma_scale_f32_16x16x128_f8f6f4 v[76:79], v[236:243], v[200:207], v[76:79], v224, v224 op_sel_hi:[0,0,0]
	s_mov_b32 m0, s70
	v_lshl_add_u64 v[140:141], v[174:175], 0, s[28:29]
	s_barrier
	ds_read_b128 v[176:179], v227 offset:16384
	ds_read_b128 v[180:183], v227 offset:17408
	ds_read_b128 v[184:187], v227 offset:18432
	ds_read_b128 v[188:191], v227 offset:19456
	ds_read_b128 v[192:195], v227 offset:20480
	ds_read_b128 v[196:199], v227 offset:21504
	ds_read_b128 v[200:203], v227 offset:22528
	ds_read_b128 v[204:207], v227 offset:23552
	global_load_lds_dwordx4 v[140:141], off
	v_lshl_add_u64 v[140:141], v[168:169], 0, s[28:29]
	s_mov_b32 m0, s71
	s_nop 0
	global_load_lds_dwordx4 v[140:141], off
	s_barrier
	s_waitcnt lgkmcnt(0)
	s_waitcnt lgkmcnt(0)
	v_mfma_scale_f32_16x16x128_f8f6f4 v[80:83], v[8:15], v[176:183], v[80:83], v224, v224 op_sel_hi:[0,0,0]
	v_mfma_scale_f32_16x16x128_f8f6f4 v[84:87], v[0:7], v[176:183], v[84:87], v224, v224 op_sel_hi:[0,0,0]
	v_mfma_scale_f32_16x16x128_f8f6f4 v[88:91], v[8:15], v[184:191], v[88:91], v224, v224 op_sel_hi:[0,0,0]
	v_mfma_scale_f32_16x16x128_f8f6f4 v[92:95], v[0:7], v[184:191], v[92:95], v224, v224 op_sel_hi:[0,0,0]
	v_mfma_scale_f32_16x16x128_f8f6f4 v[96:99], v[8:15], v[192:199], v[96:99], v224, v224 op_sel_hi:[0,0,0]
	v_mfma_scale_f32_16x16x128_f8f6f4 v[100:103], v[0:7], v[192:199], v[100:103], v224, v224 op_sel_hi:[0,0,0]
	v_mfma_scale_f32_16x16x128_f8f6f4 v[104:107], v[8:15], v[200:207], v[104:107], v224, v224 op_sel_hi:[0,0,0]
	v_mfma_scale_f32_16x16x128_f8f6f4 v[108:111], v[0:7], v[200:207], v[108:111], v224, v224 op_sel_hi:[0,0,0]
	s_barrier
	s_add_u32 s54, s48, 0x40700
	s_addc_u32 s55, s49, 0
	s_mov_b32 m0, s52
	v_lshl_add_u64 v[0:1], s[54:55], 0, v[150:151]
	global_load_lds_dwordx4 v[0:1], off
	v_lshl_add_u64 v[0:1], s[54:55], 0, v[154:155]
	s_mov_b32 m0, s95
	s_nop 0
	global_load_lds_dwordx4 v[0:1], off
	s_waitcnt vmcnt(6)
	s_barrier
	v_mfma_scale_f32_16x16x128_f8f6f4 v[112:115], v[208:215], v[176:183], v[112:115], v224, v224 op_sel_hi:[0,0,0]
	v_mfma_scale_f32_16x16x128_f8f6f4 v[116:119], v[236:243], v[176:183], v[116:119], v224, v224 op_sel_hi:[0,0,0]
	v_mfma_scale_f32_16x16x128_f8f6f4 v[120:123], v[208:215], v[184:191], v[120:123], v224, v224 op_sel_hi:[0,0,0]
	v_mfma_scale_f32_16x16x128_f8f6f4 v[124:127], v[236:243], v[184:191], v[124:127], v224, v224 op_sel_hi:[0,0,0]
	v_mfma_scale_f32_16x16x128_f8f6f4 v[128:131], v[208:215], v[192:199], v[128:131], v224, v224 op_sel_hi:[0,0,0]
	v_mfma_scale_f32_16x16x128_f8f6f4 v[132:135], v[236:243], v[192:199], v[132:135], v224, v224 op_sel_hi:[0,0,0]
	v_mfma_scale_f32_16x16x128_f8f6f4 v[144:147], v[208:215], v[200:207], v[144:147], v224, v224 op_sel_hi:[0,0,0]
	v_mfma_scale_f32_16x16x128_f8f6f4 v[136:139], v[236:243], v[200:207], v[136:139], v224, v224 op_sel_hi:[0,0,0]
	s_barrier
	ds_read_b128 v[0:3], v234
	ds_read_b128 v[4:7], v234 offset:1024
	ds_read_b128 v[8:11], v234 offset:2048
	ds_read_b128 v[12:15], v234 offset:3072
	s_add_u32 s54, s46, 0x40700
	s_addc_u32 s55, s47, 0
	s_mov_b32 m0, s72
	v_lshl_add_u64 v[140:141], s[54:55], 0, v[148:149]
	ds_read_b128 v[176:179], v227 offset:32768
	ds_read_b128 v[180:183], v227 offset:33792
	ds_read_b128 v[184:187], v227 offset:34816
	ds_read_b128 v[188:191], v227 offset:35840
	ds_read_b128 v[192:195], v227 offset:36864
	ds_read_b128 v[196:199], v227 offset:37888
	ds_read_b128 v[200:203], v227 offset:38912
	ds_read_b128 v[204:207], v227 offset:39936
	global_load_lds_dwordx4 v[140:141], off
	v_lshl_add_u64 v[140:141], s[54:55], 0, v[152:153]
	s_mov_b32 m0, s73
	s_nop 0
	global_load_lds_dwordx4 v[140:141], off
	s_waitcnt lgkmcnt(8)
	s_barrier
	s_waitcnt lgkmcnt(0)
	s_waitcnt lgkmcnt(0)
	v_mfma_scale_f32_16x16x128_f8f6f4 v[16:19], v[0:7], v[176:183], v[16:19], v224, v224 op_sel_hi:[0,0,0]
	v_mfma_scale_f32_16x16x128_f8f6f4 v[20:23], v[8:15], v[176:183], v[20:23], v224, v224 op_sel_hi:[0,0,0]
	v_mfma_scale_f32_16x16x128_f8f6f4 v[24:27], v[0:7], v[184:191], v[24:27], v224, v224 op_sel_hi:[0,0,0]
	v_mfma_scale_f32_16x16x128_f8f6f4 v[28:31], v[8:15], v[184:191], v[28:31], v224, v224 op_sel_hi:[0,0,0]
	v_mfma_scale_f32_16x16x128_f8f6f4 v[32:35], v[0:7], v[192:199], v[32:35], v224, v224 op_sel_hi:[0,0,0]
	v_mfma_scale_f32_16x16x128_f8f6f4 v[36:39], v[8:15], v[192:199], v[36:39], v224, v224 op_sel_hi:[0,0,0]
	v_mfma_scale_f32_16x16x128_f8f6f4 v[40:43], v[0:7], v[200:207], v[40:43], v224, v224 op_sel_hi:[0,0,0]
	v_mfma_scale_f32_16x16x128_f8f6f4 v[44:47], v[8:15], v[200:207], v[44:47], v224, v224 op_sel_hi:[0,0,0]
	s_barrier
	s_mov_b32 m0, s63
	v_lshl_add_u64 v[140:141], v[170:171], 0, s[30:31]
	ds_read_b128 v[208:211], v233
	ds_read_b128 v[212:215], v233 offset:1024
	ds_read_b128 v[236:239], v233 offset:2048
	ds_read_b128 v[240:243], v233 offset:3072
	global_load_lds_dwordx4 v[140:141], off
	v_lshl_add_u64 v[140:141], v[172:173], 0, s[30:31]
	s_mov_b32 m0, s62
	s_nop 0
	global_load_lds_dwordx4 v[140:141], off
	s_barrier
	s_waitcnt lgkmcnt(0)
	s_waitcnt lgkmcnt(0)
	v_mfma_scale_f32_16x16x128_f8f6f4 v[48:51], v[208:215], v[176:183], v[48:51], v224, v224 op_sel_hi:[0,0,0]
	v_mfma_scale_f32_16x16x128_f8f6f4 v[52:55], v[236:243], v[176:183], v[52:55], v224, v224 op_sel_hi:[0,0,0]
	v_mfma_scale_f32_16x16x128_f8f6f4 v[56:59], v[208:215], v[184:191], v[56:59], v224, v224 op_sel_hi:[0,0,0]
	v_mfma_scale_f32_16x16x128_f8f6f4 v[60:63], v[236:243], v[184:191], v[60:63], v224, v224 op_sel_hi:[0,0,0]
	v_mfma_scale_f32_16x16x128_f8f6f4 v[64:67], v[208:215], v[192:199], v[64:67], v224, v224 op_sel_hi:[0,0,0]
	v_mfma_scale_f32_16x16x128_f8f6f4 v[68:71], v[236:243], v[192:199], v[68:71], v224, v224 op_sel_hi:[0,0,0]
	v_mfma_scale_f32_16x16x128_f8f6f4 v[72:75], v[208:215], v[200:207], v[72:75], v224, v224 op_sel_hi:[0,0,0]
	v_mfma_scale_f32_16x16x128_f8f6f4 v[76:79], v[236:243], v[200:207], v[76:79], v224, v224 op_sel_hi:[0,0,0]
	s_mov_b32 m0, s77
	v_lshl_add_u64 v[140:141], v[174:175], 0, s[30:31]
	s_barrier
	ds_read_b128 v[176:179], v227 offset:49152
	ds_read_b128 v[180:183], v227 offset:50176
	ds_read_b128 v[184:187], v227 offset:51200
	ds_read_b128 v[188:191], v227 offset:52224
	ds_read_b128 v[192:195], v227 offset:53248
	ds_read_b128 v[196:199], v227 offset:54272
	ds_read_b128 v[200:203], v227 offset:55296
	ds_read_b128 v[204:207], v227 offset:56320
	global_load_lds_dwordx4 v[140:141], off
	v_lshl_add_u64 v[140:141], v[168:169], 0, s[30:31]
	s_mov_b32 m0, s78
	s_nop 0
	global_load_lds_dwordx4 v[140:141], off
	s_barrier
	s_waitcnt lgkmcnt(0)
	s_waitcnt lgkmcnt(0)
	v_mfma_scale_f32_16x16x128_f8f6f4 v[80:83], v[0:7], v[176:183], v[80:83], v224, v224 op_sel_hi:[0,0,0]
	v_mfma_scale_f32_16x16x128_f8f6f4 v[84:87], v[8:15], v[176:183], v[84:87], v224, v224 op_sel_hi:[0,0,0]
	v_mfma_scale_f32_16x16x128_f8f6f4 v[88:91], v[0:7], v[184:191], v[88:91], v224, v224 op_sel_hi:[0,0,0]
	v_mfma_scale_f32_16x16x128_f8f6f4 v[92:95], v[8:15], v[184:191], v[92:95], v224, v224 op_sel_hi:[0,0,0]
	v_mfma_scale_f32_16x16x128_f8f6f4 v[96:99], v[0:7], v[192:199], v[96:99], v224, v224 op_sel_hi:[0,0,0]
	v_mfma_scale_f32_16x16x128_f8f6f4 v[100:103], v[8:15], v[192:199], v[100:103], v224, v224 op_sel_hi:[0,0,0]
	v_mfma_scale_f32_16x16x128_f8f6f4 v[104:107], v[0:7], v[200:207], v[104:107], v224, v224 op_sel_hi:[0,0,0]
	v_mfma_scale_f32_16x16x128_f8f6f4 v[108:111], v[8:15], v[200:207], v[108:111], v224, v224 op_sel_hi:[0,0,0]
	s_barrier
	s_add_u32 s48, s48, 0x40780
	s_addc_u32 s49, s49, 0
	s_mov_b32 m0, s64
	v_lshl_add_u64 v[0:1], s[48:49], 0, v[150:151]
	global_load_lds_dwordx4 v[0:1], off
	v_lshl_add_u64 v[0:1], s[48:49], 0, v[154:155]
	s_mov_b32 m0, s53
	s_nop 0
	global_load_lds_dwordx4 v[0:1], off
	s_waitcnt vmcnt(6)
	s_barrier
	v_mfma_scale_f32_16x16x128_f8f6f4 v[112:115], v[208:215], v[176:183], v[112:115], v224, v224 op_sel_hi:[0,0,0]
	v_mfma_scale_f32_16x16x128_f8f6f4 v[116:119], v[236:243], v[176:183], v[116:119], v224, v224 op_sel_hi:[0,0,0]
	v_mfma_scale_f32_16x16x128_f8f6f4 v[120:123], v[208:215], v[184:191], v[120:123], v224, v224 op_sel_hi:[0,0,0]
	v_mfma_scale_f32_16x16x128_f8f6f4 v[124:127], v[236:243], v[184:191], v[124:127], v224, v224 op_sel_hi:[0,0,0]
	v_mfma_scale_f32_16x16x128_f8f6f4 v[128:131], v[208:215], v[192:199], v[128:131], v224, v224 op_sel_hi:[0,0,0]
	v_mfma_scale_f32_16x16x128_f8f6f4 v[132:135], v[236:243], v[192:199], v[132:135], v224, v224 op_sel_hi:[0,0,0]
	v_mfma_scale_f32_16x16x128_f8f6f4 v[144:147], v[208:215], v[200:207], v[144:147], v224, v224 op_sel_hi:[0,0,0]
	v_mfma_scale_f32_16x16x128_f8f6f4 v[136:139], v[236:243], v[200:207], v[136:139], v224, v224 op_sel_hi:[0,0,0]
	s_barrier
	ds_read_b128 v[8:11], v230
	ds_read_b128 v[12:15], v230 offset:1024
	ds_read_b128 v[168:171], v230 offset:2048
	ds_read_b128 v[172:175], v230 offset:3072
	s_add_u32 s46, s46, 0x40780
	s_addc_u32 s47, s47, 0
	s_mov_b32 m0, s92
	v_lshl_add_u64 v[0:1], s[46:47], 0, v[148:149]
	ds_read_b128 v[176:179], v227
	ds_read_b128 v[180:183], v227 offset:1024
	ds_read_b128 v[184:187], v227 offset:2048
	ds_read_b128 v[188:191], v227 offset:3072
	ds_read_b128 v[192:195], v227 offset:4096
	ds_read_b128 v[196:199], v227 offset:5120
	ds_read_b128 v[200:203], v227 offset:6144
	ds_read_b128 v[204:207], v227 offset:7168
	global_load_lds_dwordx4 v[0:1], off
	v_lshl_add_u64 v[0:1], s[46:47], 0, v[152:153]
	s_mov_b32 m0, s91
	s_nop 0
	global_load_lds_dwordx4 v[0:1], off
	s_waitcnt lgkmcnt(8)
	s_barrier
	s_waitcnt lgkmcnt(0)
	s_waitcnt lgkmcnt(0)
	v_mfma_scale_f32_16x16x128_f8f6f4 v[16:19], v[8:15], v[176:183], v[16:19], v224, v224 op_sel_hi:[0,0,0]
	v_mfma_scale_f32_16x16x128_f8f6f4 v[20:23], v[168:175], v[176:183], v[20:23], v224, v224 op_sel_hi:[0,0,0]
	v_mfma_scale_f32_16x16x128_f8f6f4 v[24:27], v[8:15], v[184:191], v[24:27], v224, v224 op_sel_hi:[0,0,0]
	v_mfma_scale_f32_16x16x128_f8f6f4 v[28:31], v[168:175], v[184:191], v[28:31], v224, v224 op_sel_hi:[0,0,0]
	v_mfma_scale_f32_16x16x128_f8f6f4 v[32:35], v[8:15], v[192:199], v[32:35], v224, v224 op_sel_hi:[0,0,0]
	v_mfma_scale_f32_16x16x128_f8f6f4 v[36:39], v[168:175], v[192:199], v[36:39], v224, v224 op_sel_hi:[0,0,0]
	v_mfma_scale_f32_16x16x128_f8f6f4 v[40:43], v[8:15], v[200:207], v[40:43], v224, v224 op_sel_hi:[0,0,0]
	v_mfma_scale_f32_16x16x128_f8f6f4 v[44:47], v[168:175], v[200:207], v[44:47], v224, v224 op_sel_hi:[0,0,0]
	s_barrier
	s_mov_b32 m0, s94
	v_lshl_add_u64 v[0:1], s[58:59], 0, v[150:151]
	ds_read_b128 v[208:211], v231
	ds_read_b128 v[212:215], v231 offset:1024
	ds_read_b128 v[236:239], v231 offset:2048
	ds_read_b128 v[240:243], v231 offset:3072
	global_load_lds_dwordx4 v[0:1], off
	v_lshl_add_u64 v[2:3], s[58:59], 0, v[154:155]
	s_mov_b32 m0, s93
	s_nop 0
	global_load_lds_dwordx4 v[2:3], off
	s_barrier
	s_waitcnt lgkmcnt(0)
	s_waitcnt lgkmcnt(0)
	v_mfma_scale_f32_16x16x128_f8f6f4 v[48:51], v[208:215], v[176:183], v[48:51], v224, v224 op_sel_hi:[0,0,0]
	v_mfma_scale_f32_16x16x128_f8f6f4 v[52:55], v[236:243], v[176:183], v[52:55], v224, v224 op_sel_hi:[0,0,0]
	v_mfma_scale_f32_16x16x128_f8f6f4 v[56:59], v[208:215], v[184:191], v[56:59], v224, v224 op_sel_hi:[0,0,0]
	v_mfma_scale_f32_16x16x128_f8f6f4 v[60:63], v[236:243], v[184:191], v[60:63], v224, v224 op_sel_hi:[0,0,0]
	v_mfma_scale_f32_16x16x128_f8f6f4 v[64:67], v[208:215], v[192:199], v[64:67], v224, v224 op_sel_hi:[0,0,0]
	v_mfma_scale_f32_16x16x128_f8f6f4 v[68:71], v[236:243], v[192:199], v[68:71], v224, v224 op_sel_hi:[0,0,0]
	v_mfma_scale_f32_16x16x128_f8f6f4 v[72:75], v[208:215], v[200:207], v[72:75], v224, v224 op_sel_hi:[0,0,0]
	v_mfma_scale_f32_16x16x128_f8f6f4 v[76:79], v[236:243], v[200:207], v[76:79], v224, v224 op_sel_hi:[0,0,0]
	s_mov_b32 m0, s70
	v_lshl_add_u64 v[4:5], s[50:51], 0, v[148:149]
	s_barrier
	ds_read_b128 v[176:179], v227 offset:16384
	ds_read_b128 v[180:183], v227 offset:17408
	ds_read_b128 v[184:187], v227 offset:18432
	ds_read_b128 v[188:191], v227 offset:19456
	ds_read_b128 v[192:195], v227 offset:20480
	ds_read_b128 v[196:199], v227 offset:21504
	ds_read_b128 v[200:203], v227 offset:22528
	ds_read_b128 v[204:207], v227 offset:23552
	global_load_lds_dwordx4 v[4:5], off
	v_lshl_add_u64 v[6:7], s[50:51], 0, v[152:153]
	s_mov_b32 m0, s71
	s_nop 0
	global_load_lds_dwordx4 v[6:7], off
	s_barrier
	s_waitcnt lgkmcnt(0)
	s_waitcnt lgkmcnt(0)
	v_mfma_scale_f32_16x16x128_f8f6f4 v[80:83], v[8:15], v[176:183], v[80:83], v224, v224 op_sel_hi:[0,0,0]
	v_mfma_scale_f32_16x16x128_f8f6f4 v[84:87], v[168:175], v[176:183], v[84:87], v224, v224 op_sel_hi:[0,0,0]
	v_mfma_scale_f32_16x16x128_f8f6f4 v[88:91], v[8:15], v[184:191], v[88:91], v224, v224 op_sel_hi:[0,0,0]
	v_mfma_scale_f32_16x16x128_f8f6f4 v[92:95], v[168:175], v[184:191], v[92:95], v224, v224 op_sel_hi:[0,0,0]
	v_mfma_scale_f32_16x16x128_f8f6f4 v[96:99], v[8:15], v[192:199], v[96:99], v224, v224 op_sel_hi:[0,0,0]
	v_mfma_scale_f32_16x16x128_f8f6f4 v[100:103], v[168:175], v[192:199], v[100:103], v224, v224 op_sel_hi:[0,0,0]
	v_mfma_scale_f32_16x16x128_f8f6f4 v[104:107], v[8:15], v[200:207], v[104:107], v224, v224 op_sel_hi:[0,0,0]
	v_mfma_scale_f32_16x16x128_f8f6f4 v[108:111], v[168:175], v[200:207], v[108:111], v224, v224 op_sel_hi:[0,0,0]
	s_barrier
	s_add_u32 s46, s58, 0x40000
	s_addc_u32 s47, s59, 0
	s_mov_b32 m0, s52
	v_lshl_add_u64 v[8:9], s[46:47], 0, v[150:151]
	global_load_lds_dwordx4 v[8:9], off
	v_lshl_add_u64 v[8:9], s[46:47], 0, v[154:155]
	s_mov_b32 m0, s95
	s_nop 0
	global_load_lds_dwordx4 v[8:9], off
	s_waitcnt vmcnt(6)
	s_barrier
	v_mfma_scale_f32_16x16x128_f8f6f4 v[112:115], v[208:215], v[176:183], v[112:115], v224, v224 op_sel_hi:[0,0,0]
	v_mfma_scale_f32_16x16x128_f8f6f4 v[116:119], v[236:243], v[176:183], v[116:119], v224, v224 op_sel_hi:[0,0,0]
	v_mfma_scale_f32_16x16x128_f8f6f4 v[120:123], v[208:215], v[184:191], v[120:123], v224, v224 op_sel_hi:[0,0,0]
	v_mfma_scale_f32_16x16x128_f8f6f4 v[124:127], v[236:243], v[184:191], v[124:127], v224, v224 op_sel_hi:[0,0,0]
	v_mfma_scale_f32_16x16x128_f8f6f4 v[128:131], v[208:215], v[192:199], v[128:131], v224, v224 op_sel_hi:[0,0,0]
	v_mfma_scale_f32_16x16x128_f8f6f4 v[132:135], v[236:243], v[192:199], v[132:135], v224, v224 op_sel_hi:[0,0,0]
	v_mfma_scale_f32_16x16x128_f8f6f4 v[144:147], v[208:215], v[200:207], v[144:147], v224, v224 op_sel_hi:[0,0,0]
	v_mfma_scale_f32_16x16x128_f8f6f4 v[136:139], v[236:243], v[200:207], v[136:139], v224, v224 op_sel_hi:[0,0,0]
	s_barrier
	ds_read_b128 v[8:11], v234
	ds_read_b128 v[12:15], v234 offset:1024
	ds_read_b128 v[168:171], v234 offset:2048
	ds_read_b128 v[172:175], v234 offset:3072
	s_add_u32 s46, s50, 0x40000
	s_addc_u32 s47, s51, 0
	s_mov_b32 m0, s72
	v_lshl_add_u64 v[140:141], s[46:47], 0, v[148:149]
	ds_read_b128 v[176:179], v227 offset:32768
	ds_read_b128 v[180:183], v227 offset:33792
	ds_read_b128 v[184:187], v227 offset:34816
	ds_read_b128 v[188:191], v227 offset:35840
	ds_read_b128 v[192:195], v227 offset:36864
	ds_read_b128 v[196:199], v227 offset:37888
	ds_read_b128 v[200:203], v227 offset:38912
	ds_read_b128 v[204:207], v227 offset:39936
	global_load_lds_dwordx4 v[140:141], off
	v_lshl_add_u64 v[140:141], s[46:47], 0, v[152:153]
	s_mov_b32 m0, s73
	s_nop 0
	global_load_lds_dwordx4 v[140:141], off
	s_waitcnt lgkmcnt(8)
	s_barrier
	s_waitcnt lgkmcnt(0)
	s_waitcnt lgkmcnt(0)
	v_mfma_scale_f32_16x16x128_f8f6f4 v[16:19], v[8:15], v[176:183], v[16:19], v224, v224 op_sel_hi:[0,0,0]
	v_mfma_scale_f32_16x16x128_f8f6f4 v[20:23], v[168:175], v[176:183], v[20:23], v224, v224 op_sel_hi:[0,0,0]
	v_mfma_scale_f32_16x16x128_f8f6f4 v[24:27], v[8:15], v[184:191], v[24:27], v224, v224 op_sel_hi:[0,0,0]
	v_mfma_scale_f32_16x16x128_f8f6f4 v[28:31], v[168:175], v[184:191], v[28:31], v224, v224 op_sel_hi:[0,0,0]
	v_mfma_scale_f32_16x16x128_f8f6f4 v[32:35], v[8:15], v[192:199], v[32:35], v224, v224 op_sel_hi:[0,0,0]
	v_mfma_scale_f32_16x16x128_f8f6f4 v[36:39], v[168:175], v[192:199], v[36:39], v224, v224 op_sel_hi:[0,0,0]
	v_mfma_scale_f32_16x16x128_f8f6f4 v[40:43], v[8:15], v[200:207], v[40:43], v224, v224 op_sel_hi:[0,0,0]
	v_mfma_scale_f32_16x16x128_f8f6f4 v[44:47], v[168:175], v[200:207], v[44:47], v224, v224 op_sel_hi:[0,0,0]
	s_barrier
	s_mov_b32 m0, s63
	v_lshl_add_u64 v[0:1], v[0:1], 0, s[6:7]
	ds_read_b128 v[208:211], v233
	ds_read_b128 v[212:215], v233 offset:1024
	ds_read_b128 v[234:237], v233 offset:2048
	ds_read_b128 v[238:241], v233 offset:3072
	global_load_lds_dwordx4 v[0:1], off
	v_lshl_add_u64 v[0:1], v[2:3], 0, s[6:7]
	s_mov_b32 m0, s62
	s_nop 0
	global_load_lds_dwordx4 v[0:1], off
	s_barrier
	s_waitcnt lgkmcnt(0)
	s_waitcnt lgkmcnt(0)
	v_mfma_scale_f32_16x16x128_f8f6f4 v[48:51], v[208:215], v[176:183], v[48:51], v224, v224 op_sel_hi:[0,0,0]
	v_mfma_scale_f32_16x16x128_f8f6f4 v[52:55], v[234:241], v[176:183], v[52:55], v224, v224 op_sel_hi:[0,0,0]
	v_mfma_scale_f32_16x16x128_f8f6f4 v[56:59], v[208:215], v[184:191], v[56:59], v224, v224 op_sel_hi:[0,0,0]
	v_mfma_scale_f32_16x16x128_f8f6f4 v[60:63], v[234:241], v[184:191], v[60:63], v224, v224 op_sel_hi:[0,0,0]
	v_mfma_scale_f32_16x16x128_f8f6f4 v[64:67], v[208:215], v[192:199], v[64:67], v224, v224 op_sel_hi:[0,0,0]
	v_mfma_scale_f32_16x16x128_f8f6f4 v[68:71], v[234:241], v[192:199], v[68:71], v224, v224 op_sel_hi:[0,0,0]
	v_mfma_scale_f32_16x16x128_f8f6f4 v[72:75], v[208:215], v[200:207], v[72:75], v224, v224 op_sel_hi:[0,0,0]
	v_mfma_scale_f32_16x16x128_f8f6f4 v[76:79], v[234:241], v[200:207], v[76:79], v224, v224 op_sel_hi:[0,0,0]
	s_mov_b32 m0, s77
	v_lshl_add_u64 v[0:1], v[4:5], 0, s[6:7]
	s_barrier
	ds_read_b128 v[176:179], v227 offset:49152
	ds_read_b128 v[180:183], v227 offset:50176
	ds_read_b128 v[184:187], v227 offset:51200
	ds_read_b128 v[188:191], v227 offset:52224
	ds_read_b128 v[192:195], v227 offset:53248
	ds_read_b128 v[196:199], v227 offset:54272
	ds_read_b128 v[200:203], v227 offset:55296
	ds_read_b128 v[204:207], v227 offset:56320
	global_load_lds_dwordx4 v[0:1], off
	v_lshl_add_u64 v[0:1], v[6:7], 0, s[6:7]
	s_mov_b32 m0, s78
	s_nop 0
	global_load_lds_dwordx4 v[0:1], off
	s_barrier
	s_waitcnt lgkmcnt(0)
	s_waitcnt lgkmcnt(0)
	v_mfma_scale_f32_16x16x128_f8f6f4 v[80:83], v[8:15], v[176:183], v[80:83], v224, v224 op_sel_hi:[0,0,0]
	v_mfma_scale_f32_16x16x128_f8f6f4 v[84:87], v[168:175], v[176:183], v[84:87], v224, v224 op_sel_hi:[0,0,0]
	v_mfma_scale_f32_16x16x128_f8f6f4 v[88:91], v[8:15], v[184:191], v[88:91], v224, v224 op_sel_hi:[0,0,0]
	v_mfma_scale_f32_16x16x128_f8f6f4 v[92:95], v[168:175], v[184:191], v[92:95], v224, v224 op_sel_hi:[0,0,0]
	v_mfma_scale_f32_16x16x128_f8f6f4 v[96:99], v[8:15], v[192:199], v[96:99], v224, v224 op_sel_hi:[0,0,0]
	v_mfma_scale_f32_16x16x128_f8f6f4 v[100:103], v[168:175], v[192:199], v[100:103], v224, v224 op_sel_hi:[0,0,0]
	v_mfma_scale_f32_16x16x128_f8f6f4 v[104:107], v[8:15], v[200:207], v[104:107], v224, v224 op_sel_hi:[0,0,0]
	v_mfma_scale_f32_16x16x128_f8f6f4 v[108:111], v[168:175], v[200:207], v[108:111], v224, v224 op_sel_hi:[0,0,0]
	s_barrier
	s_add_u32 s46, s58, 0x40080
	s_addc_u32 s47, s59, 0
	s_mov_b32 m0, s64
	v_lshl_add_u64 v[0:1], s[46:47], 0, v[150:151]
	global_load_lds_dwordx4 v[0:1], off
	v_lshl_add_u64 v[0:1], s[46:47], 0, v[154:155]
	s_mov_b32 m0, s53
	s_nop 0
	global_load_lds_dwordx4 v[0:1], off
	s_waitcnt vmcnt(6)
	s_barrier
	v_mfma_scale_f32_16x16x128_f8f6f4 v[112:115], v[208:215], v[176:183], v[112:115], v224, v224 op_sel_hi:[0,0,0]
	v_mfma_scale_f32_16x16x128_f8f6f4 v[116:119], v[234:241], v[176:183], v[116:119], v224, v224 op_sel_hi:[0,0,0]
	v_mfma_scale_f32_16x16x128_f8f6f4 v[120:123], v[208:215], v[184:191], v[120:123], v224, v224 op_sel_hi:[0,0,0]
	v_mfma_scale_f32_16x16x128_f8f6f4 v[124:127], v[234:241], v[184:191], v[124:127], v224, v224 op_sel_hi:[0,0,0]
	v_mfma_scale_f32_16x16x128_f8f6f4 v[128:131], v[208:215], v[192:199], v[128:131], v224, v224 op_sel_hi:[0,0,0]
	v_mfma_scale_f32_16x16x128_f8f6f4 v[132:135], v[234:241], v[192:199], v[132:135], v224, v224 op_sel_hi:[0,0,0]
	v_mfma_scale_f32_16x16x128_f8f6f4 v[144:147], v[208:215], v[200:207], v[144:147], v224, v224 op_sel_hi:[0,0,0]
	v_mfma_scale_f32_16x16x128_f8f6f4 v[136:139], v[234:241], v[200:207], v[136:139], v224, v224 op_sel_hi:[0,0,0]
	v_mov_b32_e32 v156, v229
	s_barrier
	s_nop 7
	s_nop 7
	s_nop 7
	global_load_dwordx2 v[4:5], v156, s[2:3]
	global_load_dwordx2 v[6:7], v156, s[2:3] offset:512
	global_load_dwordx2 v[8:9], v156, s[2:3] offset:1024
	global_load_dwordx2 v[10:11], v156, s[2:3] offset:1536
	global_load_dwordx2 v[168:169], v156, s[2:3] offset:2048
	global_load_dwordx2 v[202:203], v156, s[2:3] offset:2560
	global_load_dwordx2 v[200:201], v156, s[2:3] offset:3072
	global_load_dwordx2 v[198:199], v156, s[2:3] offset:3584
	v_lshl_add_u64 v[0:1], s[2:3], 0, v[156:157]
	v_add_co_u32_e32 v0, vcc, s82, v0
	s_mov_b64 s[2:3], 0x40000
	s_nop 0
	v_addc_co_u32_e32 v1, vcc, 0, v1, vcc
	global_load_dwordx2 v[196:197], v[0:1], off
	global_load_dwordx2 v[194:195], v[0:1], off offset:512
	global_load_dwordx2 v[192:193], v[0:1], off offset:1024
	global_load_dwordx2 v[190:191], v[0:1], off offset:1536
	global_load_dwordx2 v[180:181], v[0:1], off offset:2048
	global_load_dwordx2 v[170:171], v[0:1], off offset:2560
	global_load_dwordx2 v[2:3], v[0:1], off offset:3072
	s_nop 0
	global_load_dwordx2 v[0:1], v[0:1], off offset:3584
	s_mov_b64 s[48:49], s[44:45]
	s_mov_b64 s[46:47], s[42:43]
	s_waitcnt vmcnt(0)
	v_cvt_f32_ubyte1_e32 v13, v4
	v_cvt_f32_ubyte0_e32 v12, v4
	v_cvt_f32_ubyte3_e32 v15, v4
	v_cvt_f32_ubyte2_e32 v14, v4
	v_cvt_f32_ubyte1_e32 v141, v5
	v_cvt_f32_ubyte0_e32 v140, v5
	v_cvt_f32_ubyte3_e32 v143, v5
	v_cvt_f32_ubyte2_e32 v142, v5
	v_cvt_f32_ubyte1_e32 v5, v6
	v_cvt_f32_ubyte0_e32 v4, v6
	v_cvt_f32_ubyte1_e32 v175, v7
	v_cvt_f32_ubyte0_e32 v174, v7
	v_pk_add_f32 v[4:5], v[4:5], 0.5 op_sel_hi:[1,0]
	v_cvt_f32_ubyte3_e32 v173, v6
	v_cvt_f32_ubyte2_e32 v172, v6
	v_cvt_f32_ubyte3_e32 v177, v7
	v_cvt_f32_ubyte2_e32 v176, v7
	v_cvt_f32_ubyte1_e32 v7, v8
	v_cvt_f32_ubyte0_e32 v6, v8
	v_pk_add_f32 v[174:175], v[174:175], 0.5 op_sel_hi:[1,0]
	v_pk_mul_f32 v[4:5], v[4:5], s[38:39] op_sel_hi:[1,0]
	v_pk_add_f32 v[172:173], v[172:173], 0.5 op_sel_hi:[1,0]
	v_pk_add_f32 v[6:7], v[6:7], 0.5 op_sel_hi:[1,0]
	v_pk_mul_f32 v[204:205], v[174:175], s[38:39] op_sel_hi:[1,0]
	v_pk_mul_f32 v[174:175], v[48:49], v[4:5]
	v_cvt_f32_ubyte3_e32 v5, v10
	v_cvt_f32_ubyte2_e32 v4, v10
	v_cvt_f32_ubyte3_e32 v179, v8
	v_cvt_f32_ubyte2_e32 v178, v8
	v_cvt_f32_ubyte1_e32 v183, v9
	v_cvt_f32_ubyte0_e32 v182, v9
	v_cvt_f32_ubyte3_e32 v185, v9
	v_cvt_f32_ubyte2_e32 v184, v9
	v_cvt_f32_ubyte1_e32 v9, v10
	v_pk_add_f32 v[12:13], v[12:13], 0.5 op_sel_hi:[1,0]
	v_pk_mul_f32 v[172:173], v[172:173], s[38:39] op_sel_hi:[1,0]
	v_pk_mul_f32 v[6:7], v[6:7], s[38:39] op_sel_hi:[1,0]
	v_cvt_f32_ubyte0_e32 v8, v10
	v_pk_add_f32 v[4:5], v[4:5], 0.5 op_sel_hi:[1,0]
	v_pk_add_f32 v[14:15], v[14:15], 0.5 op_sel_hi:[1,0]
	v_pk_add_f32 v[184:185], v[184:185], 0.5 op_sel_hi:[1,0]
	v_pk_mul_f32 v[12:13], v[12:13], s[38:39] op_sel_hi:[1,0]
	v_pk_mul_f32 v[172:173], v[50:51], v[172:173]
	v_pk_mul_f32 v[50:51], v[24:25], v[6:7]
	v_pk_add_f32 v[6:7], v[8:9], 0.5 op_sel_hi:[1,0]
	v_pk_mul_f32 v[4:5], v[4:5], s[38:39] op_sel_hi:[1,0]
	v_pk_add_f32 v[182:183], v[182:183], 0.5 op_sel_hi:[1,0]
	v_pk_mul_f32 v[14:15], v[14:15], s[38:39] op_sel_hi:[1,0]
	v_pk_mul_f32 v[210:211], v[184:185], s[38:39] op_sel_hi:[1,0]
	v_pk_mul_f32 v[184:185], v[16:17], v[12:13]
	v_pk_mul_f32 v[6:7], v[6:7], s[38:39] op_sel_hi:[1,0]
	v_pk_mul_f32 v[12:13], v[58:59], v[4:5]
	v_cvt_f32_ubyte1_e32 v5, v11
	v_cvt_f32_ubyte0_e32 v4, v11
	v_pk_add_f32 v[142:143], v[142:143], 0.5 op_sel_hi:[1,0]
	v_pk_mul_f32 v[208:209], v[182:183], s[38:39] op_sel_hi:[1,0]
	v_pk_mul_f32 v[182:183], v[18:19], v[14:15]
	v_pk_mul_f32 v[14:15], v[56:57], v[6:7]
	v_cvt_f32_ubyte3_e32 v7, v11
	v_cvt_f32_ubyte2_e32 v6, v11
	v_pk_add_f32 v[4:5], v[4:5], 0.5 op_sel_hi:[1,0]
	v_pk_add_f32 v[140:141], v[140:141], 0.5 op_sel_hi:[1,0]
	v_pk_mul_f32 v[142:143], v[142:143], s[38:39] op_sel_hi:[1,0]
	v_pk_add_f32 v[6:7], v[6:7], 0.5 op_sel_hi:[1,0]
	v_pk_mul_f32 v[4:5], v[4:5], s[38:39] op_sel_hi:[1,0]
	v_pk_mul_f32 v[140:141], v[140:141], s[38:39] op_sel_hi:[1,0]
	v_pk_mul_f32 v[186:187], v[22:23], v[142:143]
	v_pk_mul_f32 v[6:7], v[6:7], s[38:39] op_sel_hi:[1,0]
	v_pk_mul_f32 v[142:143], v[60:61], v[4:5]
	v_cvt_f32_ubyte1_e32 v5, v168
	v_cvt_f32_ubyte0_e32 v4, v168
	v_pk_mul_f32 v[188:189], v[20:21], v[140:141]
	v_pk_mul_f32 v[140:141], v[62:63], v[6:7]
	v_cvt_f32_ubyte3_e32 v7, v168
	v_cvt_f32_ubyte2_e32 v6, v168
	v_pk_add_f32 v[4:5], v[4:5], 0.5 op_sel_hi:[1,0]
	v_pk_add_f32 v[6:7], v[6:7], 0.5 op_sel_hi:[1,0]
	v_pk_mul_f32 v[8:9], v[4:5], s[38:39] op_sel_hi:[1,0]
	v_pk_mul_f32 v[4:5], v[6:7], s[38:39] op_sel_hi:[1,0]
	v_pk_mul_f32 v[6:7], v[32:33], v[8:9]
	v_cvt_f32_ubyte1_e32 v9, v169
	v_cvt_f32_ubyte0_e32 v8, v169
	v_cvt_f32_ubyte3_e32 v11, v169
	v_cvt_f32_ubyte2_e32 v10, v169
	v_pk_add_f32 v[8:9], v[8:9], 0.5 op_sel_hi:[1,0]
	v_pk_add_f32 v[10:11], v[10:11], 0.5 op_sel_hi:[1,0]
	v_pk_mul_f32 v[8:9], v[8:9], s[38:39] op_sel_hi:[1,0]
	v_pk_mul_f32 v[10:11], v[10:11], s[38:39] op_sel_hi:[1,0]
	v_pk_mul_f32 v[58:59], v[36:37], v[8:9]
	v_cvt_f32_ubyte1_e32 v9, v202
	v_cvt_f32_ubyte0_e32 v8, v202
	v_pk_mul_f32 v[56:57], v[38:39], v[10:11]
	v_cvt_f32_ubyte3_e32 v11, v202
	v_cvt_f32_ubyte2_e32 v10, v202
	v_pk_add_f32 v[8:9], v[8:9], 0.5 op_sel_hi:[1,0]
	v_pk_add_f32 v[10:11], v[10:11], 0.5 op_sel_hi:[1,0]
	v_pk_mul_f32 v[8:9], v[8:9], s[38:39] op_sel_hi:[1,0]
	v_pk_mul_f32 v[10:11], v[10:11], s[38:39] op_sel_hi:[1,0]
	v_pk_mul_f32 v[18:19], v[64:65], v[8:9]
	v_cvt_f32_ubyte1_e32 v9, v203
	v_cvt_f32_ubyte0_e32 v8, v203
	v_pk_mul_f32 v[16:17], v[66:67], v[10:11]
	v_cvt_f32_ubyte3_e32 v11, v203
	v_cvt_f32_ubyte2_e32 v10, v203
	v_pk_add_f32 v[8:9], v[8:9], 0.5 op_sel_hi:[1,0]
	v_pk_add_f32 v[10:11], v[10:11], 0.5 op_sel_hi:[1,0]
	v_pk_mul_f32 v[8:9], v[8:9], s[38:39] op_sel_hi:[1,0]
	v_pk_mul_f32 v[10:11], v[10:11], s[38:39] op_sel_hi:[1,0]
	v_pk_mul_f32 v[168:169], v[68:69], v[8:9]
	v_cvt_f32_ubyte1_e32 v9, v200
	v_cvt_f32_ubyte0_e32 v8, v200
	v_pk_mul_f32 v[70:71], v[70:71], v[10:11]
	v_cvt_f32_ubyte3_e32 v11, v200
	v_cvt_f32_ubyte2_e32 v10, v200
	v_pk_add_f32 v[8:9], v[8:9], 0.5 op_sel_hi:[1,0]
	v_pk_add_f32 v[10:11], v[10:11], 0.5 op_sel_hi:[1,0]
	v_pk_mul_f32 v[20:21], v[8:9], s[38:39] op_sel_hi:[1,0]
	v_pk_mul_f32 v[8:9], v[10:11], s[38:39] op_sel_hi:[1,0]
	v_pk_mul_f32 v[10:11], v[40:41], v[20:21]
	v_cvt_f32_ubyte1_e32 v21, v201
	v_cvt_f32_ubyte0_e32 v20, v201
	v_cvt_f32_ubyte3_e32 v23, v201
	v_cvt_f32_ubyte2_e32 v22, v201
	v_pk_add_f32 v[20:21], v[20:21], 0.5 op_sel_hi:[1,0]
	v_pk_add_f32 v[22:23], v[22:23], 0.5 op_sel_hi:[1,0]
	v_pk_mul_f32 v[20:21], v[20:21], s[38:39] op_sel_hi:[1,0]
	v_pk_mul_f32 v[22:23], v[22:23], s[38:39] op_sel_hi:[1,0]
	v_pk_mul_f32 v[66:67], v[44:45], v[20:21]
	v_cvt_f32_ubyte1_e32 v21, v198
	v_cvt_f32_ubyte0_e32 v20, v198
	v_pk_mul_f32 v[64:65], v[46:47], v[22:23]
	v_cvt_f32_ubyte3_e32 v23, v198
	v_cvt_f32_ubyte2_e32 v22, v198
	v_pk_add_f32 v[20:21], v[20:21], 0.5 op_sel_hi:[1,0]
	v_pk_add_f32 v[178:179], v[178:179], 0.5 op_sel_hi:[1,0]
	v_pk_add_f32 v[22:23], v[22:23], 0.5 op_sel_hi:[1,0]
	v_pk_mul_f32 v[24:25], v[20:21], s[38:39] op_sel_hi:[1,0]
	v_pk_mul_f32 v[206:207], v[178:179], s[38:39] op_sel_hi:[1,0]
	v_pk_mul_f32 v[20:21], v[22:23], s[38:39] op_sel_hi:[1,0]
	v_pk_mul_f32 v[22:23], v[72:73], v[24:25]
	v_cvt_f32_ubyte1_e32 v25, v199
	v_cvt_f32_ubyte0_e32 v24, v199
	v_pk_mul_f32 v[48:49], v[26:27], v[206:207]
	v_cvt_f32_ubyte3_e32 v27, v199
	v_cvt_f32_ubyte2_e32 v26, v199
	v_pk_add_f32 v[24:25], v[24:25], 0.5 op_sel_hi:[1,0]
	v_pk_add_f32 v[26:27], v[26:27], 0.5 op_sel_hi:[1,0]
	v_pk_mul_f32 v[24:25], v[24:25], s[38:39] op_sel_hi:[1,0]
	v_pk_add_f32 v[176:177], v[176:177], 0.5 op_sel_hi:[1,0]
	v_pk_mul_f32 v[20:21], v[74:75], v[20:21]
	v_pk_mul_f32 v[26:27], v[26:27], s[38:39] op_sel_hi:[1,0]
	v_pk_mul_f32 v[74:75], v[76:77], v[24:25]
	v_cvt_f32_ubyte1_e32 v25, v196
	v_cvt_f32_ubyte0_e32 v24, v196
	v_pk_mul_f32 v[176:177], v[176:177], s[38:39] op_sel_hi:[1,0]
	v_pk_mul_f32 v[72:73], v[78:79], v[26:27]
	v_cvt_f32_ubyte3_e32 v27, v196
	v_cvt_f32_ubyte2_e32 v26, v196
	v_pk_add_f32 v[24:25], v[24:25], 0.5 op_sel_hi:[1,0]
	v_pk_mul_f32 v[176:177], v[54:55], v[176:177]
	v_pk_mul_f32 v[54:55], v[28:29], v[208:209]
	v_pk_add_f32 v[26:27], v[26:27], 0.5 op_sel_hi:[1,0]
	v_pk_mul_f32 v[28:29], v[24:25], s[38:39] op_sel_hi:[1,0]
	v_pk_mul_f32 v[24:25], v[26:27], s[38:39] op_sel_hi:[1,0]
	v_pk_mul_f32 v[26:27], v[80:81], v[28:29]
	v_cvt_f32_ubyte1_e32 v29, v197
	v_cvt_f32_ubyte0_e32 v28, v197
	v_pk_mul_f32 v[178:179], v[52:53], v[204:205]
	v_pk_mul_f32 v[52:53], v[30:31], v[210:211]
	v_cvt_f32_ubyte3_e32 v31, v197
	v_cvt_f32_ubyte2_e32 v30, v197
	v_pk_add_f32 v[28:29], v[28:29], 0.5 op_sel_hi:[1,0]
	v_pk_add_f32 v[30:31], v[30:31], 0.5 op_sel_hi:[1,0]
	v_pk_mul_f32 v[28:29], v[28:29], s[38:39] op_sel_hi:[1,0]
	v_pk_mul_f32 v[30:31], v[30:31], s[38:39] op_sel_hi:[1,0]
	v_pk_mul_f32 v[78:79], v[84:85], v[28:29]
	v_cvt_f32_ubyte1_e32 v29, v194
	v_cvt_f32_ubyte0_e32 v28, v194
	v_pk_mul_f32 v[76:77], v[86:87], v[30:31]
	v_cvt_f32_ubyte3_e32 v31, v194
	v_cvt_f32_ubyte2_e32 v30, v194
	v_pk_add_f32 v[28:29], v[28:29], 0.5 op_sel_hi:[1,0]
	v_pk_add_f32 v[30:31], v[30:31], 0.5 op_sel_hi:[1,0]
	v_pk_mul_f32 v[32:33], v[28:29], s[38:39] op_sel_hi:[1,0]
	v_pk_mul_f32 v[28:29], v[30:31], s[38:39] op_sel_hi:[1,0]
	v_pk_mul_f32 v[30:31], v[112:113], v[32:33]
	v_cvt_f32_ubyte1_e32 v33, v195
	v_cvt_f32_ubyte0_e32 v32, v195
	v_pk_mul_f32 v[4:5], v[34:35], v[4:5]
	v_cvt_f32_ubyte3_e32 v35, v195
	v_cvt_f32_ubyte2_e32 v34, v195
	v_pk_add_f32 v[32:33], v[32:33], 0.5 op_sel_hi:[1,0]
	v_pk_add_f32 v[34:35], v[34:35], 0.5 op_sel_hi:[1,0]
	v_pk_mul_f32 v[32:33], v[32:33], s[38:39] op_sel_hi:[1,0]
	v_pk_mul_f32 v[24:25], v[82:83], v[24:25]
	v_pk_mul_f32 v[34:35], v[34:35], s[38:39] op_sel_hi:[1,0]
	v_pk_mul_f32 v[82:83], v[116:117], v[32:33]
	v_cvt_f32_ubyte1_e32 v33, v192
	v_cvt_f32_ubyte0_e32 v32, v192
	v_pk_mul_f32 v[80:81], v[118:119], v[34:35]
	v_cvt_f32_ubyte3_e32 v35, v192
	v_cvt_f32_ubyte2_e32 v34, v192
	v_pk_add_f32 v[32:33], v[32:33], 0.5 op_sel_hi:[1,0]
	v_pk_add_f32 v[34:35], v[34:35], 0.5 op_sel_hi:[1,0]
	v_pk_mul_f32 v[36:37], v[32:33], s[38:39] op_sel_hi:[1,0]
	v_pk_mul_f32 v[32:33], v[34:35], s[38:39] op_sel_hi:[1,0]
	v_pk_mul_f32 v[34:35], v[88:89], v[36:37]
	v_cvt_f32_ubyte1_e32 v37, v193
	v_cvt_f32_ubyte0_e32 v36, v193
	v_cvt_f32_ubyte3_e32 v39, v193
	v_cvt_f32_ubyte2_e32 v38, v193
	v_pk_add_f32 v[36:37], v[36:37], 0.5 op_sel_hi:[1,0]
	v_pk_add_f32 v[38:39], v[38:39], 0.5 op_sel_hi:[1,0]
	v_pk_mul_f32 v[36:37], v[36:37], s[38:39] op_sel_hi:[1,0]
	v_pk_mul_f32 v[38:39], v[38:39], s[38:39] op_sel_hi:[1,0]
	v_pk_mul_f32 v[86:87], v[92:93], v[36:37]
	v_cvt_f32_ubyte1_e32 v37, v190
	v_cvt_f32_ubyte0_e32 v36, v190
	v_pk_mul_f32 v[84:85], v[94:95], v[38:39]
	v_cvt_f32_ubyte3_e32 v39, v190
	v_cvt_f32_ubyte2_e32 v38, v190
	v_pk_add_f32 v[36:37], v[36:37], 0.5 op_sel_hi:[1,0]
	v_pk_add_f32 v[38:39], v[38:39], 0.5 op_sel_hi:[1,0]
	v_pk_mul_f32 v[40:41], v[36:37], s[38:39] op_sel_hi:[1,0]
	v_pk_mul_f32 v[36:37], v[38:39], s[38:39] op_sel_hi:[1,0]
	v_pk_mul_f32 v[38:39], v[120:121], v[40:41]
	v_cvt_f32_ubyte1_e32 v41, v191
	v_cvt_f32_ubyte0_e32 v40, v191
	v_pk_mul_f32 v[8:9], v[42:43], v[8:9]
	v_cvt_f32_ubyte3_e32 v43, v191
	v_cvt_f32_ubyte2_e32 v42, v191
	v_pk_add_f32 v[40:41], v[40:41], 0.5 op_sel_hi:[1,0]
	v_pk_add_f32 v[42:43], v[42:43], 0.5 op_sel_hi:[1,0]
	v_pk_mul_f32 v[40:41], v[40:41], s[38:39] op_sel_hi:[1,0]
	v_pk_mul_f32 v[32:33], v[90:91], v[32:33]
	v_pk_mul_f32 v[42:43], v[42:43], s[38:39] op_sel_hi:[1,0]
	v_pk_mul_f32 v[90:91], v[124:125], v[40:41]
	v_cvt_f32_ubyte1_e32 v41, v180
	v_cvt_f32_ubyte0_e32 v40, v180
	v_pk_mul_f32 v[88:89], v[126:127], v[42:43]
	v_cvt_f32_ubyte3_e32 v43, v180
	v_cvt_f32_ubyte2_e32 v42, v180
	v_pk_add_f32 v[40:41], v[40:41], 0.5 op_sel_hi:[1,0]
	v_pk_add_f32 v[42:43], v[42:43], 0.5 op_sel_hi:[1,0]
	v_pk_mul_f32 v[44:45], v[40:41], s[38:39] op_sel_hi:[1,0]
	v_pk_mul_f32 v[40:41], v[42:43], s[38:39] op_sel_hi:[1,0]
	v_pk_mul_f32 v[42:43], v[96:97], v[44:45]
	v_cvt_f32_ubyte1_e32 v45, v181
	v_cvt_f32_ubyte0_e32 v44, v181
	v_cvt_f32_ubyte3_e32 v47, v181
	v_cvt_f32_ubyte2_e32 v46, v181
	v_pk_add_f32 v[44:45], v[44:45], 0.5 op_sel_hi:[1,0]
	v_pk_add_f32 v[46:47], v[46:47], 0.5 op_sel_hi:[1,0]
	v_pk_mul_f32 v[44:45], v[44:45], s[38:39] op_sel_hi:[1,0]
	v_pk_mul_f32 v[46:47], v[46:47], s[38:39] op_sel_hi:[1,0]
	v_pk_mul_f32 v[94:95], v[100:101], v[44:45]
	v_cvt_f32_ubyte1_e32 v45, v170
	v_cvt_f32_ubyte0_e32 v44, v170
	v_pk_mul_f32 v[92:93], v[102:103], v[46:47]
	v_cvt_f32_ubyte3_e32 v47, v170
	v_cvt_f32_ubyte2_e32 v46, v170
	v_pk_add_f32 v[44:45], v[44:45], 0.5 op_sel_hi:[1,0]
	v_pk_add_f32 v[46:47], v[46:47], 0.5 op_sel_hi:[1,0]
	v_pk_mul_f32 v[60:61], v[44:45], s[38:39] op_sel_hi:[1,0]
	v_pk_mul_f32 v[44:45], v[46:47], s[38:39] op_sel_hi:[1,0]
	v_pk_mul_f32 v[46:47], v[128:129], v[60:61]
	v_cvt_f32_ubyte1_e32 v61, v171
	v_cvt_f32_ubyte0_e32 v60, v171
	v_cvt_f32_ubyte3_e32 v63, v171
	v_cvt_f32_ubyte2_e32 v62, v171
	v_pk_add_f32 v[60:61], v[60:61], 0.5 op_sel_hi:[1,0]
	v_pk_add_f32 v[62:63], v[62:63], 0.5 op_sel_hi:[1,0]
	v_pk_mul_f32 v[60:61], v[60:61], s[38:39] op_sel_hi:[1,0]
	v_pk_mul_f32 v[40:41], v[98:99], v[40:41]
	v_pk_mul_f32 v[62:63], v[62:63], s[38:39] op_sel_hi:[1,0]
	v_pk_mul_f32 v[98:99], v[132:133], v[60:61]
	v_cvt_f32_ubyte1_e32 v61, v2
	v_cvt_f32_ubyte0_e32 v60, v2
	v_pk_mul_f32 v[96:97], v[134:135], v[62:63]
	v_cvt_f32_ubyte3_e32 v63, v2
	v_cvt_f32_ubyte2_e32 v62, v2
	v_pk_add_f32 v[60:61], v[60:61], 0.5 op_sel_hi:[1,0]
	v_pk_add_f32 v[62:63], v[62:63], 0.5 op_sel_hi:[1,0]
	v_pk_mul_f32 v[68:69], v[60:61], s[38:39] op_sel_hi:[1,0]
	v_cvt_f32_ubyte3_e32 v101, v3
	v_cvt_f32_ubyte2_e32 v100, v3
	v_pk_mul_f32 v[60:61], v[62:63], s[38:39] op_sel_hi:[1,0]
	v_pk_mul_f32 v[62:63], v[104:105], v[68:69]
	v_cvt_f32_ubyte1_e32 v69, v3
	v_cvt_f32_ubyte0_e32 v68, v3
	v_pk_add_f32 v[2:3], v[100:101], 0.5 op_sel_hi:[1,0]
	v_pk_add_f32 v[68:69], v[68:69], 0.5 op_sel_hi:[1,0]
	v_pk_mul_f32 v[2:3], v[2:3], s[38:39] op_sel_hi:[1,0]
	v_pk_mul_f32 v[68:69], v[68:69], s[38:39] op_sel_hi:[1,0]
	v_pk_mul_f32 v[100:101], v[110:111], v[2:3]
	v_cvt_f32_ubyte1_e32 v3, v0
	v_cvt_f32_ubyte0_e32 v2, v0
	v_pk_mul_f32 v[102:103], v[108:109], v[68:69]
	v_cvt_f32_ubyte3_e32 v69, v0
	v_cvt_f32_ubyte2_e32 v68, v0
	v_pk_add_f32 v[2:3], v[2:3], 0.5 op_sel_hi:[1,0]
	v_lshl_add_u32 v108, s90, 8, v225
	v_pk_mul_f32 v[28:29], v[114:115], v[28:29]
	v_pk_mul_f32 v[60:61], v[106:107], v[60:61]
	v_pk_add_f32 v[68:69], v[68:69], 0.5 op_sel_hi:[1,0]
	v_pk_mul_f32 v[104:105], v[2:3], s[38:39] op_sel_hi:[1,0]
	v_cvt_f32_ubyte3_e32 v107, v1
	v_cvt_f32_ubyte2_e32 v106, v1
	v_ashrrev_i32_e32 v109, 31, v108
	v_pk_mul_f32 v[112:113], v[182:183], s[40:41] op_sel_hi:[1,0]
	v_pk_mul_f32 v[114:115], v[184:185], s[40:41] op_sel_hi:[1,0]
	v_pk_mul_f32 v[2:3], v[68:69], s[38:39] op_sel_hi:[1,0]
	v_pk_mul_f32 v[68:69], v[144:145], v[104:105]
	v_cvt_f32_ubyte1_e32 v105, v1
	v_cvt_f32_ubyte0_e32 v104, v1
	v_pk_add_f32 v[0:1], v[106:107], 0.5 op_sel_hi:[1,0]
	v_lshlrev_b64 v[106:107], 11, v[108:109]
	v_pk_mul_f32 v[118:119], v[188:189], s[40:41] op_sel_hi:[1,0]
	v_med3_f32 v109, v114, s83, v232
	v_med3_f32 v114, v115, s83, v232
	v_med3_f32 v115, v112, s83, v232
	v_mov_b32_e32 v112, v157
	v_med3_f32 v120, v113, s83, v232
	v_cvt_pk_fp8_f32 v112, v109, v114
	v_med3_f32 v109, v118, s83, v232
	v_med3_f32 v114, v119, s83, v232
	v_mov_b32_e32 v113, v157
	v_cvt_pk_fp8_f32 v113, v109, v114
	v_pk_mul_f32 v[116:117], v[186:187], s[40:41] op_sel_hi:[1,0]
	v_cvt_pk_fp8_f32 v112, v115, v120 op_sel:[0,0,1]
	v_med3_f32 v109, v116, s83, v232
	v_med3_f32 v114, v117, s83, v232
	v_cvt_pk_fp8_f32 v113, v109, v114 op_sel:[0,0,1]
	v_pk_mul_f32 v[114:115], v[172:173], s[40:41] op_sel_hi:[1,0]
	v_pk_mul_f32 v[116:117], v[174:175], s[40:41] op_sel_hi:[1,0]
	v_pk_mul_f32 v[120:121], v[178:179], s[40:41] op_sel_hi:[1,0]
	v_med3_f32 v109, v116, s83, v232
	v_med3_f32 v116, v117, s83, v232
	v_med3_f32 v117, v114, s83, v232
	v_mov_b32_e32 v114, v157
	v_pk_mul_f32 v[36:37], v[122:123], v[36:37]
	v_med3_f32 v122, v115, s83, v232
	v_cvt_pk_fp8_f32 v114, v109, v116
	v_med3_f32 v109, v120, s83, v232
	v_med3_f32 v116, v121, s83, v232
	v_mov_b32_e32 v115, v157
	v_cvt_pk_fp8_f32 v115, v109, v116
	v_pk_mul_f32 v[118:119], v[176:177], s[40:41] op_sel_hi:[1,0]
	v_lshl_or_b32 v110, s89, 8, v228
	v_med3_f32 v109, v118, s83, v232
	v_med3_f32 v116, v119, s83, v232
	v_cvt_pk_fp8_f32 v114, v117, v122 op_sel:[0,0,1]
	v_cvt_pk_fp8_f32 v115, v109, v116 op_sel:[0,0,1]
	v_ashrrev_i32_e32 v111, 31, v110
	v_lshl_add_u64 v[106:107], s[4:5], 0, v[106:107]
	v_pk_mul_f32 v[48:49], v[48:49], s[40:41] op_sel_hi:[1,0]
	v_pk_mul_f32 v[50:51], v[50:51], s[40:41] op_sel_hi:[1,0]
	v_lshl_add_u64 v[106:107], v[106:107], 0, v[110:111]
	v_pk_mul_f32 v[54:55], v[54:55], s[40:41] op_sel_hi:[1,0]
	v_med3_f32 v50, v50, s83, v232
	v_med3_f32 v51, v51, s83, v232
	v_med3_f32 v109, v48, s83, v232
	v_mov_b32_e32 v48, v157
	global_store_dwordx2 v[106:107], v[112:113], off
	global_store_dwordx2 v[106:107], v[114:115], off offset:128
	v_pk_mul_f32 v[52:53], v[52:53], s[40:41] op_sel_hi:[1,0]
	v_med3_f32 v114, v49, s83, v232
	v_cvt_pk_fp8_f32 v48, v50, v51
	v_med3_f32 v50, v54, s83, v232
	v_med3_f32 v51, v55, s83, v232
	v_mov_b32_e32 v49, v157
	v_pk_mul_f32 v[12:13], v[12:13], s[40:41] op_sel_hi:[1,0]
	v_pk_mul_f32 v[14:15], v[14:15], s[40:41] op_sel_hi:[1,0]
	v_cvt_pk_fp8_f32 v49, v50, v51
	v_med3_f32 v50, v52, s83, v232
	v_med3_f32 v51, v53, s83, v232
	v_pk_mul_f32 v[52:53], v[142:143], s[40:41] op_sel_hi:[1,0]
	v_med3_f32 v14, v14, s83, v232
	v_med3_f32 v15, v15, s83, v232
	v_med3_f32 v54, v12, s83, v232
	v_mov_b32_e32 v12, v157
	v_med3_f32 v55, v13, s83, v232
	v_cvt_pk_fp8_f32 v12, v14, v15
	v_med3_f32 v14, v52, s83, v232
	v_med3_f32 v15, v53, s83, v232
	v_mov_b32_e32 v13, v157
	v_cvt_pk_fp8_f32 v13, v14, v15
	v_or_b32_e32 v112, 16, v108
	v_cvt_pk_fp8_f32 v49, v50, v51 op_sel:[0,0,1]
	v_pk_mul_f32 v[50:51], v[140:141], s[40:41] op_sel_hi:[1,0]
	v_ashrrev_i32_e32 v113, 31, v112
	v_cvt_pk_fp8_f32 v48, v109, v114 op_sel:[0,0,1]
	v_med3_f32 v14, v50, s83, v232
	v_med3_f32 v15, v51, s83, v232
	v_lshlrev_b64 v[112:113], 11, v[112:113]
	v_cvt_pk_fp8_f32 v12, v54, v55 op_sel:[0,0,1]
	v_cvt_pk_fp8_f32 v13, v14, v15 op_sel:[0,0,1]
	v_lshl_add_u64 v[14:15], s[4:5], 0, v[112:113]
	v_lshl_add_u64 v[14:15], v[14:15], 0, v[110:111]
	v_pk_mul_f32 v[4:5], v[4:5], s[40:41] op_sel_hi:[1,0]
	v_pk_mul_f32 v[6:7], v[6:7], s[40:41] op_sel_hi:[1,0]
	global_store_dwordx2 v[14:15], v[48:49], off
	global_store_dwordx2 v[14:15], v[12:13], off offset:128
	v_pk_mul_f32 v[48:49], v[58:59], s[40:41] op_sel_hi:[1,0]
	v_med3_f32 v6, v6, s83, v232
	v_med3_f32 v7, v7, s83, v232
	v_med3_f32 v50, v4, s83, v232
	v_mov_b32_e32 v4, v157
	v_med3_f32 v51, v5, s83, v232
	v_cvt_pk_fp8_f32 v4, v6, v7
	v_med3_f32 v6, v48, s83, v232
	v_med3_f32 v7, v49, s83, v232
	v_mov_b32_e32 v5, v157
	v_cvt_pk_fp8_f32 v5, v6, v7
	v_pk_mul_f32 v[14:15], v[56:57], s[40:41] op_sel_hi:[1,0]
	v_or_b32_e32 v12, 32, v108
	v_med3_f32 v6, v14, s83, v232
	v_med3_f32 v7, v15, s83, v232
	v_cvt_pk_fp8_f32 v5, v6, v7 op_sel:[0,0,1]
	v_pk_mul_f32 v[6:7], v[16:17], s[40:41] op_sel_hi:[1,0]
	v_pk_mul_f32 v[14:15], v[18:19], s[40:41] op_sel_hi:[1,0]
	v_pk_mul_f32 v[18:19], v[168:169], s[40:41] op_sel_hi:[1,0]
	v_med3_f32 v14, v14, s83, v232
	v_med3_f32 v15, v15, s83, v232
	v_med3_f32 v48, v6, s83, v232
	v_mov_b32_e32 v6, v157
	v_med3_f32 v49, v7, s83, v232
	v_cvt_pk_fp8_f32 v6, v14, v15
	v_med3_f32 v14, v18, s83, v232
	v_med3_f32 v15, v19, s83, v232
	v_mov_b32_e32 v7, v157
	v_cvt_pk_fp8_f32 v7, v14, v15
	v_pk_mul_f32 v[16:17], v[70:71], s[40:41] op_sel_hi:[1,0]
	v_ashrrev_i32_e32 v13, 31, v12
	v_cvt_pk_fp8_f32 v4, v50, v51 op_sel:[0,0,1]
	v_med3_f32 v14, v16, s83, v232
	v_med3_f32 v15, v17, s83, v232
	v_lshlrev_b64 v[12:13], 11, v[12:13]
	v_cvt_pk_fp8_f32 v6, v48, v49 op_sel:[0,0,1]
	v_cvt_pk_fp8_f32 v7, v14, v15 op_sel:[0,0,1]
	v_lshl_add_u64 v[12:13], s[4:5], 0, v[12:13]
	v_lshl_add_u64 v[12:13], v[12:13], 0, v[110:111]
	global_store_dwordx2 v[12:13], v[4:5], off
	global_store_dwordx2 v[12:13], v[6:7], off offset:128
	v_pk_mul_f32 v[6:7], v[8:9], s[40:41] op_sel_hi:[1,0]
	v_pk_mul_f32 v[8:9], v[10:11], s[40:41] op_sel_hi:[1,0]
	v_pk_mul_f32 v[12:13], v[66:67], s[40:41] op_sel_hi:[1,0]
	v_med3_f32 v8, v8, s83, v232
	v_med3_f32 v9, v9, s83, v232
	v_med3_f32 v14, v6, s83, v232
	v_mov_b32_e32 v6, v157
	v_med3_f32 v15, v7, s83, v232
	v_cvt_pk_fp8_f32 v6, v8, v9
	v_med3_f32 v8, v12, s83, v232
	v_med3_f32 v9, v13, s83, v232
	v_mov_b32_e32 v7, v157
	v_cvt_pk_fp8_f32 v7, v8, v9
	v_pk_mul_f32 v[10:11], v[64:65], s[40:41] op_sel_hi:[1,0]
	v_cvt_pk_fp8_f32 v6, v14, v15 op_sel:[0,0,1]
	v_med3_f32 v8, v10, s83, v232
	v_med3_f32 v9, v11, s83, v232
	v_cvt_pk_fp8_f32 v7, v8, v9 op_sel:[0,0,1]
	v_pk_mul_f32 v[8:9], v[20:21], s[40:41] op_sel_hi:[1,0]
	v_pk_mul_f32 v[10:11], v[22:23], s[40:41] op_sel_hi:[1,0]
	v_pk_mul_f32 v[14:15], v[74:75], s[40:41] op_sel_hi:[1,0]
	v_med3_f32 v10, v10, s83, v232
	v_med3_f32 v11, v11, s83, v232
	v_med3_f32 v16, v8, s83, v232
	v_mov_b32_e32 v8, v157
	v_med3_f32 v17, v9, s83, v232
	v_cvt_pk_fp8_f32 v8, v10, v11
	v_med3_f32 v10, v14, s83, v232
	v_med3_f32 v11, v15, s83, v232
	v_mov_b32_e32 v9, v157
	v_cvt_pk_fp8_f32 v9, v10, v11
	v_or_b32_e32 v4, 48, v108
	v_pk_mul_f32 v[12:13], v[72:73], s[40:41] op_sel_hi:[1,0]
	v_ashrrev_i32_e32 v5, 31, v4
	v_med3_f32 v10, v12, s83, v232
	v_med3_f32 v11, v13, s83, v232
	v_lshlrev_b64 v[4:5], 11, v[4:5]
	v_cvt_pk_fp8_f32 v8, v16, v17 op_sel:[0,0,1]
	v_cvt_pk_fp8_f32 v9, v10, v11 op_sel:[0,0,1]
	v_lshl_add_u64 v[4:5], s[4:5], 0, v[4:5]
	v_lshl_add_u64 v[4:5], v[4:5], 0, v[110:111]
	global_store_dwordx2 v[4:5], v[6:7], off
	global_store_dwordx2 v[4:5], v[8:9], off offset:128
	v_pk_mul_f32 v[6:7], v[24:25], s[40:41] op_sel_hi:[1,0]
	v_pk_mul_f32 v[8:9], v[26:27], s[40:41] op_sel_hi:[1,0]
	v_pk_mul_f32 v[12:13], v[78:79], s[40:41] op_sel_hi:[1,0]
	v_med3_f32 v8, v8, s83, v232
	v_med3_f32 v9, v9, s83, v232
	v_med3_f32 v14, v6, s83, v232
	v_mov_b32_e32 v6, v157
	v_med3_f32 v15, v7, s83, v232
	v_cvt_pk_fp8_f32 v6, v8, v9
	v_med3_f32 v8, v12, s83, v232
	v_med3_f32 v9, v13, s83, v232
	v_mov_b32_e32 v7, v157
	v_cvt_pk_fp8_f32 v7, v8, v9
	v_pk_mul_f32 v[10:11], v[76:77], s[40:41] op_sel_hi:[1,0]
	v_cvt_pk_fp8_f32 v6, v14, v15 op_sel:[0,0,1]
	v_med3_f32 v8, v10, s83, v232
	v_med3_f32 v9, v11, s83, v232
	v_cvt_pk_fp8_f32 v7, v8, v9 op_sel:[0,0,1]
	v_pk_mul_f32 v[8:9], v[28:29], s[40:41] op_sel_hi:[1,0]
	v_pk_mul_f32 v[10:11], v[30:31], s[40:41] op_sel_hi:[1,0]
	v_pk_mul_f32 v[14:15], v[82:83], s[40:41] op_sel_hi:[1,0]
	v_med3_f32 v10, v10, s83, v232
	v_med3_f32 v11, v11, s83, v232
	v_med3_f32 v16, v8, s83, v232
	v_mov_b32_e32 v8, v157
	v_med3_f32 v17, v9, s83, v232
	v_cvt_pk_fp8_f32 v8, v10, v11
	v_med3_f32 v10, v14, s83, v232
	v_med3_f32 v11, v15, s83, v232
	v_mov_b32_e32 v9, v157
	v_cvt_pk_fp8_f32 v9, v10, v11
	v_pk_mul_f32 v[12:13], v[80:81], s[40:41] op_sel_hi:[1,0]
	v_lshl_add_u64 v[4:5], v[106:107], 0, s[2:3]
	v_med3_f32 v10, v12, s83, v232
	v_med3_f32 v11, v13, s83, v232
	v_cvt_pk_fp8_f32 v8, v16, v17 op_sel:[0,0,1]
	v_cvt_pk_fp8_f32 v9, v10, v11 op_sel:[0,0,1]
	s_mov_b32 s2, 0x40000
	v_add_co_u32_e32 v10, vcc, s2, v106
	v_pk_mul_f32 v[12:13], v[86:87], s[40:41] op_sel_hi:[1,0]
	s_nop 0
	v_addc_co_u32_e32 v11, vcc, 0, v107, vcc
	global_store_dwordx2 v[10:11], v[6:7], off
	global_store_dwordx2 v[4:5], v[8:9], off offset:128
	v_pk_mul_f32 v[6:7], v[32:33], s[40:41] op_sel_hi:[1,0]
	v_pk_mul_f32 v[8:9], v[34:35], s[40:41] op_sel_hi:[1,0]
	v_med3_f32 v14, v6, s83, v232
	v_med3_f32 v8, v8, s83, v232
	v_med3_f32 v9, v9, s83, v232
	v_mov_b32_e32 v6, v157
	v_med3_f32 v15, v7, s83, v232
	v_cvt_pk_fp8_f32 v6, v8, v9
	v_med3_f32 v8, v12, s83, v232
	v_med3_f32 v9, v13, s83, v232
	v_mov_b32_e32 v7, v157
	v_cvt_pk_fp8_f32 v7, v8, v9
	v_pk_mul_f32 v[10:11], v[84:85], s[40:41] op_sel_hi:[1,0]
	v_cvt_pk_fp8_f32 v6, v14, v15 op_sel:[0,0,1]
	v_med3_f32 v8, v10, s83, v232
	v_med3_f32 v9, v11, s83, v232
	v_cvt_pk_fp8_f32 v7, v8, v9 op_sel:[0,0,1]
	v_pk_mul_f32 v[8:9], v[36:37], s[40:41] op_sel_hi:[1,0]
	v_pk_mul_f32 v[10:11], v[38:39], s[40:41] op_sel_hi:[1,0]
	v_pk_mul_f32 v[14:15], v[90:91], s[40:41] op_sel_hi:[1,0]
	v_med3_f32 v10, v10, s83, v232
	v_med3_f32 v11, v11, s83, v232
	v_med3_f32 v16, v8, s83, v232
	v_mov_b32_e32 v8, v157
	v_med3_f32 v17, v9, s83, v232
	v_cvt_pk_fp8_f32 v8, v10, v11
	v_med3_f32 v10, v14, s83, v232
	v_med3_f32 v11, v15, s83, v232
	v_mov_b32_e32 v9, v157
	v_cvt_pk_fp8_f32 v9, v10, v11
	v_pk_mul_f32 v[12:13], v[88:89], s[40:41] op_sel_hi:[1,0]
	s_mov_b64 s[2:3], 0x48000
	v_med3_f32 v10, v12, s83, v232
	v_med3_f32 v11, v13, s83, v232
	v_lshl_add_u64 v[4:5], v[106:107], 0, s[2:3]
	v_cvt_pk_fp8_f32 v8, v16, v17 op_sel:[0,0,1]
	v_cvt_pk_fp8_f32 v9, v10, v11 op_sel:[0,0,1]
	s_mov_b32 s2, 0x48000
	v_add_co_u32_e32 v10, vcc, s2, v106
	v_pk_mul_f32 v[12:13], v[94:95], s[40:41] op_sel_hi:[1,0]
	s_nop 0
	v_addc_co_u32_e32 v11, vcc, 0, v107, vcc
	global_store_dwordx2 v[10:11], v[6:7], off
	global_store_dwordx2 v[4:5], v[8:9], off offset:128
	v_pk_mul_f32 v[6:7], v[40:41], s[40:41] op_sel_hi:[1,0]
	v_pk_mul_f32 v[8:9], v[42:43], s[40:41] op_sel_hi:[1,0]
	v_med3_f32 v14, v6, s83, v232
	v_med3_f32 v8, v8, s83, v232
	v_med3_f32 v9, v9, s83, v232
	v_mov_b32_e32 v6, v157
	v_med3_f32 v15, v7, s83, v232
	v_cvt_pk_fp8_f32 v6, v8, v9
	v_med3_f32 v8, v12, s83, v232
	v_med3_f32 v9, v13, s83, v232
	v_mov_b32_e32 v7, v157
	v_cvt_pk_fp8_f32 v7, v8, v9
	v_pk_mul_f32 v[10:11], v[92:93], s[40:41] op_sel_hi:[1,0]
	v_pk_mul_f32 v[44:45], v[130:131], v[44:45]
	v_med3_f32 v8, v10, s83, v232
	v_med3_f32 v9, v11, s83, v232
	v_cvt_pk_fp8_f32 v7, v8, v9 op_sel:[0,0,1]
	v_pk_mul_f32 v[8:9], v[44:45], s[40:41] op_sel_hi:[1,0]
	v_pk_mul_f32 v[10:11], v[46:47], s[40:41] op_sel_hi:[1,0]
	v_cvt_pk_fp8_f32 v6, v14, v15 op_sel:[0,0,1]
	v_pk_mul_f32 v[14:15], v[98:99], s[40:41] op_sel_hi:[1,0]
	v_med3_f32 v10, v10, s83, v232
	v_med3_f32 v11, v11, s83, v232
	v_med3_f32 v16, v8, s83, v232
	v_mov_b32_e32 v8, v157
	v_med3_f32 v17, v9, s83, v232
	v_cvt_pk_fp8_f32 v8, v10, v11
	v_med3_f32 v10, v14, s83, v232
	v_med3_f32 v11, v15, s83, v232
	v_mov_b32_e32 v9, v157
	v_cvt_pk_fp8_f32 v9, v10, v11
	v_pk_mul_f32 v[12:13], v[96:97], s[40:41] op_sel_hi:[1,0]
	s_mov_b64 s[2:3], 0x50000
	v_med3_f32 v10, v12, s83, v232
	v_med3_f32 v11, v13, s83, v232
	v_lshl_add_u64 v[4:5], v[106:107], 0, s[2:3]
	v_cvt_pk_fp8_f32 v8, v16, v17 op_sel:[0,0,1]
	v_cvt_pk_fp8_f32 v9, v10, v11 op_sel:[0,0,1]
	s_mov_b32 s2, 0x50000
	v_add_co_u32_e32 v10, vcc, s2, v106
	v_pk_mul_f32 v[12:13], v[102:103], s[40:41] op_sel_hi:[1,0]
	s_nop 0
	v_addc_co_u32_e32 v11, vcc, 0, v107, vcc
	global_store_dwordx2 v[10:11], v[6:7], off
	global_store_dwordx2 v[4:5], v[8:9], off offset:128
	v_pk_mul_f32 v[6:7], v[60:61], s[40:41] op_sel_hi:[1,0]
	v_pk_mul_f32 v[8:9], v[62:63], s[40:41] op_sel_hi:[1,0]
	v_med3_f32 v14, v6, s83, v232
	v_med3_f32 v8, v8, s83, v232
	v_med3_f32 v9, v9, s83, v232
	v_mov_b32_e32 v6, v157
	v_med3_f32 v15, v7, s83, v232
	v_cvt_pk_fp8_f32 v6, v8, v9
	v_med3_f32 v8, v12, s83, v232
	v_med3_f32 v9, v13, s83, v232
	v_mov_b32_e32 v7, v157
	v_cvt_pk_fp8_f32 v7, v8, v9
	v_pk_add_f32 v[104:105], v[104:105], 0.5 op_sel_hi:[1,0]
	v_pk_mul_f32 v[10:11], v[100:101], s[40:41] op_sel_hi:[1,0]
	v_pk_mul_f32 v[2:3], v[146:147], v[2:3]
	v_pk_mul_f32 v[104:105], v[104:105], s[38:39] op_sel_hi:[1,0]
	v_med3_f32 v8, v10, s83, v232
	v_med3_f32 v9, v11, s83, v232
	v_pk_mul_f32 v[104:105], v[136:137], v[104:105]
	v_cvt_pk_fp8_f32 v7, v8, v9 op_sel:[0,0,1]
	v_pk_mul_f32 v[2:3], v[2:3], s[40:41] op_sel_hi:[1,0]
	v_pk_mul_f32 v[8:9], v[68:69], s[40:41] op_sel_hi:[1,0]
	v_pk_mul_f32 v[10:11], v[104:105], s[40:41] op_sel_hi:[1,0]
	v_med3_f32 v8, v8, s83, v232
	v_med3_f32 v9, v9, s83, v232
	v_med3_f32 v12, v2, s83, v232
	v_mov_b32_e32 v2, v157
	v_med3_f32 v13, v3, s83, v232
	v_cvt_pk_fp8_f32 v2, v8, v9
	v_med3_f32 v8, v10, s83, v232
	v_med3_f32 v9, v11, s83, v232
	v_mov_b32_e32 v3, v157
	v_pk_mul_f32 v[0:1], v[0:1], s[38:39] op_sel_hi:[1,0]
	v_cvt_pk_fp8_f32 v3, v8, v9
	v_pk_mul_f32 v[0:1], v[138:139], v[0:1]
	v_cvt_pk_fp8_f32 v6, v14, v15 op_sel:[0,0,1]
	v_pk_mul_f32 v[0:1], v[0:1], s[40:41] op_sel_hi:[1,0]
	v_cvt_pk_fp8_f32 v2, v12, v13 op_sel:[0,0,1]
	v_med3_f32 v0, v0, s83, v232
	v_med3_f32 v1, v1, s83, v232
	v_cvt_pk_fp8_f32 v3, v0, v1 op_sel:[0,0,1]
	v_add_co_u32_e32 v0, vcc, s84, v106
	s_mov_b64 s[2:3], 0x58000
	s_nop 0
	v_addc_co_u32_e32 v1, vcc, 0, v107, vcc
	s_and_b64 vcc, exec, s[0:1]
	s_mov_b32 s89, s85
	s_mov_b32 s90, s86
	v_lshl_add_u64 v[4:5], v[106:107], 0, s[2:3]
	global_store_dwordx2 v[0:1], v[6:7], off
	global_store_dwordx2 v[4:5], v[2:3], off offset:128
	s_cbranch_vccz .LBB0_2184
	s_waitcnt vmcnt(0)
	s_cmpk_gt_u32 s60, 0xff
	s_cbranch_scc1 .LBB0_2195
	s_barrier

.LBB0_2262:
	ds_read_b128 v[8:11], v179
	ds_read_b128 v[12:15], v179 offset:1024
	ds_read_b128 v[0:3], v179 offset:2048
	ds_read_b128 v[4:7], v179 offset:3072
	s_add_u32 s18, s16, 0xfffc0080
	s_addc_u32 s19, s17, -1
	s_cmp_eq_u32 s62, 12
	s_cselect_b32 s21, s56, s19
	s_cselect_b32 s20, s57, s18
	s_cselect_b32 s19, s58, s61
	s_cselect_b32 s18, s59, s60
	v_lshl_add_u64 v[162:163], s[16:17], 0, v[156:157]
	s_add_i32 m0, s30, 0xc000
	ds_read_b128 v[166:169], v180
	ds_read_b128 v[170:173], v180 offset:1024
	ds_read_b128 v[182:185], v180 offset:2048
	ds_read_b128 v[186:189], v180 offset:3072
	ds_read_b128 v[190:193], v180 offset:4096
	ds_read_b128 v[194:197], v180 offset:5120
	ds_read_b128 v[198:201], v180 offset:6144
	ds_read_b128 v[202:205], v180 offset:7168
	global_load_lds_dwordx4 v[162:163], off
	v_lshl_add_u64 v[162:163], s[16:17], 0, v[154:155]
	s_add_i32 m0, s30, 0xe000
	s_nop 0
	global_load_lds_dwordx4 v[162:163], off
	s_waitcnt lgkmcnt(8)
	s_barrier
	s_waitcnt lgkmcnt(0)
	s_waitcnt lgkmcnt(0)
	v_mfma_scale_f32_16x16x128_f8f6f4 v[140:143], v[8:15], v[166:173], v[140:143], v175, v175 op_sel_hi:[0,0,0]
	v_mfma_scale_f32_16x16x128_f8f6f4 v[136:139], v[0:7], v[166:173], v[136:139], v175, v175 op_sel_hi:[0,0,0]
	v_mfma_scale_f32_16x16x128_f8f6f4 v[128:131], v[8:15], v[182:189], v[128:131], v175, v175 op_sel_hi:[0,0,0]
	v_mfma_scale_f32_16x16x128_f8f6f4 v[120:123], v[0:7], v[182:189], v[120:123], v175, v175 op_sel_hi:[0,0,0]
	v_mfma_scale_f32_16x16x128_f8f6f4 v[112:115], v[8:15], v[190:197], v[112:115], v175, v175 op_sel_hi:[0,0,0]
	v_mfma_scale_f32_16x16x128_f8f6f4 v[104:107], v[0:7], v[190:197], v[104:107], v175, v175 op_sel_hi:[0,0,0]
	v_mfma_scale_f32_16x16x128_f8f6f4 v[96:99], v[8:15], v[198:205], v[96:99], v175, v175 op_sel_hi:[0,0,0]
	v_mfma_scale_f32_16x16x128_f8f6f4 v[88:91], v[0:7], v[198:205], v[88:91], v175, v175 op_sel_hi:[0,0,0]
	s_barrier
	s_add_i32 s63, s46, s29
	v_lshl_add_u64 v[162:163], s[18:19], 0, v[146:147]
	s_mov_b32 m0, s63
	ds_read_b128 v[206:209], v181
	ds_read_b128 v[210:213], v181 offset:1024
	ds_read_b128 v[214:217], v181 offset:2048
	ds_read_b128 v[218:221], v181 offset:3072
	global_load_lds_dwordx4 v[162:163], off
	v_lshl_add_u64 v[164:165], s[18:19], 0, v[150:151]
	s_add_i32 m0, s63, 0x2000
	s_nop 0
	global_load_lds_dwordx4 v[164:165], off
	s_barrier
	s_waitcnt lgkmcnt(0)
	s_waitcnt lgkmcnt(0)
	v_mfma_scale_f32_16x16x128_f8f6f4 v[132:135], v[206:213], v[166:173], v[132:135], v175, v175 op_sel_hi:[0,0,0]
	v_mfma_scale_f32_16x16x128_f8f6f4 v[124:127], v[214:221], v[166:173], v[124:127], v175, v175 op_sel_hi:[0,0,0]
	v_mfma_scale_f32_16x16x128_f8f6f4 v[116:119], v[206:213], v[182:189], v[116:119], v175, v175 op_sel_hi:[0,0,0]
	v_mfma_scale_f32_16x16x128_f8f6f4 v[108:111], v[214:221], v[182:189], v[108:111], v175, v175 op_sel_hi:[0,0,0]
	v_mfma_scale_f32_16x16x128_f8f6f4 v[100:103], v[206:213], v[190:197], v[100:103], v175, v175 op_sel_hi:[0,0,0]
	v_mfma_scale_f32_16x16x128_f8f6f4 v[92:95], v[214:221], v[190:197], v[92:95], v175, v175 op_sel_hi:[0,0,0]
	v_mfma_scale_f32_16x16x128_f8f6f4 v[84:87], v[206:213], v[198:205], v[84:87], v175, v175 op_sel_hi:[0,0,0]
	v_mfma_scale_f32_16x16x128_f8f6f4 v[80:83], v[214:221], v[198:205], v[80:83], v175, v175 op_sel_hi:[0,0,0]
	s_mov_b32 m0, s30
	v_lshl_add_u64 v[166:167], s[20:21], 0, v[144:145]
	s_barrier
	ds_read_b128 v[182:185], v180 offset:16384
	ds_read_b128 v[186:189], v180 offset:17408
	ds_read_b128 v[190:193], v180 offset:18432
	ds_read_b128 v[194:197], v180 offset:19456
	ds_read_b128 v[198:201], v180 offset:20480
	ds_read_b128 v[202:205], v180 offset:21504
	ds_read_b128 v[224:227], v180 offset:22528
	ds_read_b128 v[228:231], v180 offset:23552
	global_load_lds_dwordx4 v[166:167], off
	v_lshl_add_u64 v[168:169], s[20:21], 0, v[148:149]
	s_mov_b32 m0, s31
	s_nop 0
	global_load_lds_dwordx4 v[168:169], off
	s_barrier
	s_waitcnt lgkmcnt(0)
	s_waitcnt lgkmcnt(0)
	v_mfma_scale_f32_16x16x128_f8f6f4 v[76:79], v[8:15], v[182:189], v[76:79], v175, v175 op_sel_hi:[0,0,0]
	v_mfma_scale_f32_16x16x128_f8f6f4 v[72:75], v[0:7], v[182:189], v[72:75], v175, v175 op_sel_hi:[0,0,0]
	v_mfma_scale_f32_16x16x128_f8f6f4 v[64:67], v[8:15], v[190:197], v[64:67], v175, v175 op_sel_hi:[0,0,0]
	v_mfma_scale_f32_16x16x128_f8f6f4 v[56:59], v[0:7], v[190:197], v[56:59], v175, v175 op_sel_hi:[0,0,0]
	v_mfma_scale_f32_16x16x128_f8f6f4 v[48:51], v[8:15], v[198:205], v[48:51], v175, v175 op_sel_hi:[0,0,0]
	v_mfma_scale_f32_16x16x128_f8f6f4 v[40:43], v[0:7], v[198:205], v[40:43], v175, v175 op_sel_hi:[0,0,0]
	v_mfma_scale_f32_16x16x128_f8f6f4 v[32:35], v[8:15], v[224:231], v[32:35], v175, v175 op_sel_hi:[0,0,0]
	v_mfma_scale_f32_16x16x128_f8f6f4 v[24:27], v[0:7], v[224:231], v[24:27], v175, v175 op_sel_hi:[0,0,0]
	s_barrier
	s_add_u32 s64, s18, 0x40000
	s_addc_u32 s65, s19, 0
	s_add_i32 s63, s47, s29
	v_lshl_add_u64 v[0:1], s[64:65], 0, v[146:147]
	s_mov_b32 m0, s63
	s_nop 0
	global_load_lds_dwordx4 v[0:1], off
	v_lshl_add_u64 v[0:1], s[64:65], 0, v[150:151]
	s_add_i32 m0, s63, 0x2000
	s_nop 0
	global_load_lds_dwordx4 v[0:1], off
	s_waitcnt vmcnt(6)
	s_barrier
	v_mfma_scale_f32_16x16x128_f8f6f4 v[68:71], v[206:213], v[182:189], v[68:71], v175, v175 op_sel_hi:[0,0,0]
	v_mfma_scale_f32_16x16x128_f8f6f4 v[60:63], v[214:221], v[182:189], v[60:63], v175, v175 op_sel_hi:[0,0,0]
	v_mfma_scale_f32_16x16x128_f8f6f4 v[52:55], v[206:213], v[190:197], v[52:55], v175, v175 op_sel_hi:[0,0,0]
	v_mfma_scale_f32_16x16x128_f8f6f4 v[44:47], v[214:221], v[190:197], v[44:47], v175, v175 op_sel_hi:[0,0,0]
	v_mfma_scale_f32_16x16x128_f8f6f4 v[36:39], v[206:213], v[198:205], v[36:39], v175, v175 op_sel_hi:[0,0,0]
	v_mfma_scale_f32_16x16x128_f8f6f4 v[28:31], v[214:221], v[198:205], v[28:31], v175, v175 op_sel_hi:[0,0,0]
	v_mfma_scale_f32_16x16x128_f8f6f4 v[20:23], v[206:213], v[224:231], v[20:23], v175, v175 op_sel_hi:[0,0,0]
	v_mfma_scale_f32_16x16x128_f8f6f4 v[16:19], v[214:221], v[224:231], v[16:19], v175, v175 op_sel_hi:[0,0,0]
	s_add_i32 s63, 0, 0x18000
	v_add_u32_e32 v12, s63, v176
	s_barrier
	ds_read_b128 v[0:3], v12
	ds_read_b128 v[4:7], v12 offset:1024
	ds_read_b128 v[8:11], v12 offset:2048
	ds_read_b128 v[12:15], v12 offset:3072
	s_add_u32 s20, s20, 0x40000
	s_addc_u32 s21, s21, 0
	s_mov_b32 m0, s38
	v_lshl_add_u64 v[170:171], s[20:21], 0, v[144:145]
	ds_read_b128 v[182:185], v180 offset:32768
	ds_read_b128 v[186:189], v180 offset:33792
	ds_read_b128 v[190:193], v180 offset:34816
	ds_read_b128 v[194:197], v180 offset:35840
	ds_read_b128 v[198:201], v180 offset:36864
	ds_read_b128 v[202:205], v180 offset:37888
	ds_read_b128 v[206:209], v180 offset:38912
	ds_read_b128 v[210:213], v180 offset:39936
	global_load_lds_dwordx4 v[170:171], off
	v_lshl_add_u64 v[170:171], s[20:21], 0, v[148:149]
	s_mov_b32 m0, s39
	s_nop 0
	global_load_lds_dwordx4 v[170:171], off
	s_waitcnt lgkmcnt(8)
	s_barrier
	s_waitcnt lgkmcnt(0)
	s_waitcnt lgkmcnt(0)
	v_mfma_scale_f32_16x16x128_f8f6f4 v[140:143], v[0:7], v[182:189], v[140:143], v175, v175 op_sel_hi:[0,0,0]
	v_mfma_scale_f32_16x16x128_f8f6f4 v[136:139], v[8:15], v[182:189], v[136:139], v175, v175 op_sel_hi:[0,0,0]
	v_mfma_scale_f32_16x16x128_f8f6f4 v[128:131], v[0:7], v[190:197], v[128:131], v175, v175 op_sel_hi:[0,0,0]
	v_mfma_scale_f32_16x16x128_f8f6f4 v[120:123], v[8:15], v[190:197], v[120:123], v175, v175 op_sel_hi:[0,0,0]
	v_mfma_scale_f32_16x16x128_f8f6f4 v[112:115], v[0:7], v[198:205], v[112:115], v175, v175 op_sel_hi:[0,0,0]
	v_mfma_scale_f32_16x16x128_f8f6f4 v[104:107], v[8:15], v[198:205], v[104:107], v175, v175 op_sel_hi:[0,0,0]
	v_mfma_scale_f32_16x16x128_f8f6f4 v[96:99], v[0:7], v[206:213], v[96:99], v175, v175 op_sel_hi:[0,0,0]
	v_mfma_scale_f32_16x16x128_f8f6f4 v[88:91], v[8:15], v[206:213], v[88:91], v175, v175 op_sel_hi:[0,0,0]
	s_barrier
	s_add_i32 s20, 0, 0x1c000
	s_add_i32 s21, s63, s29
	v_add_u32_e32 v152, s20, v176
	v_lshl_add_u64 v[162:163], v[162:163], 0, s[4:5]
	s_mov_b32 m0, s21
	ds_read_b128 v[214:217], v152
	ds_read_b128 v[218:221], v152 offset:1024
	ds_read_b128 v[224:227], v152 offset:2048
	ds_read_b128 v[228:231], v152 offset:3072
	global_load_lds_dwordx4 v[162:163], off
	v_lshl_add_u64 v[162:163], v[164:165], 0, s[4:5]
	s_add_i32 m0, s21, 0x2000
	s_nop 0
	global_load_lds_dwordx4 v[162:163], off
	s_barrier
	s_waitcnt lgkmcnt(0)
	s_waitcnt lgkmcnt(0)
	v_mfma_scale_f32_16x16x128_f8f6f4 v[132:135], v[214:221], v[182:189], v[132:135], v175, v175 op_sel_hi:[0,0,0]
	v_mfma_scale_f32_16x16x128_f8f6f4 v[124:127], v[224:231], v[182:189], v[124:127], v175, v175 op_sel_hi:[0,0,0]
	v_mfma_scale_f32_16x16x128_f8f6f4 v[116:119], v[214:221], v[190:197], v[116:119], v175, v175 op_sel_hi:[0,0,0]
	v_mfma_scale_f32_16x16x128_f8f6f4 v[108:111], v[224:231], v[190:197], v[108:111], v175, v175 op_sel_hi:[0,0,0]
	v_mfma_scale_f32_16x16x128_f8f6f4 v[100:103], v[214:221], v[198:205], v[100:103], v175, v175 op_sel_hi:[0,0,0]
	v_mfma_scale_f32_16x16x128_f8f6f4 v[92:95], v[224:231], v[198:205], v[92:95], v175, v175 op_sel_hi:[0,0,0]
	v_mfma_scale_f32_16x16x128_f8f6f4 v[84:87], v[214:221], v[206:213], v[84:87], v175, v175 op_sel_hi:[0,0,0]
	v_mfma_scale_f32_16x16x128_f8f6f4 v[80:83], v[224:231], v[206:213], v[80:83], v175, v175 op_sel_hi:[0,0,0]
	s_mov_b32 m0, s43
	v_lshl_add_u64 v[162:163], v[166:167], 0, s[4:5]
	s_barrier
	ds_read_b128 v[182:185], v180 offset:49152
	ds_read_b128 v[186:189], v180 offset:50176
	ds_read_b128 v[190:193], v180 offset:51200
	ds_read_b128 v[194:197], v180 offset:52224
	ds_read_b128 v[198:201], v180 offset:53248
	ds_read_b128 v[202:205], v180 offset:54272
	ds_read_b128 v[206:209], v180 offset:55296
	ds_read_b128 v[210:213], v180 offset:56320
	global_load_lds_dwordx4 v[162:163], off
	v_lshl_add_u64 v[162:163], v[168:169], 0, s[4:5]
	s_mov_b32 m0, s44
	s_nop 0
	global_load_lds_dwordx4 v[162:163], off
	s_barrier
	s_waitcnt lgkmcnt(0)
	s_waitcnt lgkmcnt(0)
	v_mfma_scale_f32_16x16x128_f8f6f4 v[76:79], v[0:7], v[182:189], v[76:79], v175, v175 op_sel_hi:[0,0,0]
	v_mfma_scale_f32_16x16x128_f8f6f4 v[72:75], v[8:15], v[182:189], v[72:75], v175, v175 op_sel_hi:[0,0,0]
	v_mfma_scale_f32_16x16x128_f8f6f4 v[64:67], v[0:7], v[190:197], v[64:67], v175, v175 op_sel_hi:[0,0,0]
	v_mfma_scale_f32_16x16x128_f8f6f4 v[56:59], v[8:15], v[190:197], v[56:59], v175, v175 op_sel_hi:[0,0,0]
	v_mfma_scale_f32_16x16x128_f8f6f4 v[48:51], v[0:7], v[198:205], v[48:51], v175, v175 op_sel_hi:[0,0,0]
	v_mfma_scale_f32_16x16x128_f8f6f4 v[40:43], v[8:15], v[198:205], v[40:43], v175, v175 op_sel_hi:[0,0,0]
	v_mfma_scale_f32_16x16x128_f8f6f4 v[32:35], v[0:7], v[206:213], v[32:35], v175, v175 op_sel_hi:[0,0,0]
	v_mfma_scale_f32_16x16x128_f8f6f4 v[24:27], v[8:15], v[206:213], v[24:27], v175, v175 op_sel_hi:[0,0,0]
	s_barrier
	s_add_u32 s18, s18, 0x40080
	s_addc_u32 s19, s19, 0
	s_add_i32 s20, s20, s29
	v_lshl_add_u64 v[0:1], s[18:19], 0, v[146:147]
	s_mov_b32 m0, s20
	s_nop 0
	global_load_lds_dwordx4 v[0:1], off
	v_lshl_add_u64 v[0:1], s[18:19], 0, v[150:151]
	s_add_i32 m0, s20, 0x2000
	s_nop 0
	global_load_lds_dwordx4 v[0:1], off
	s_waitcnt vmcnt(6)
	s_barrier
	v_mfma_scale_f32_16x16x128_f8f6f4 v[68:71], v[214:221], v[182:189], v[68:71], v175, v175 op_sel_hi:[0,0,0]
	v_mfma_scale_f32_16x16x128_f8f6f4 v[60:63], v[224:231], v[182:189], v[60:63], v175, v175 op_sel_hi:[0,0,0]
	v_mfma_scale_f32_16x16x128_f8f6f4 v[52:55], v[214:221], v[190:197], v[52:55], v175, v175 op_sel_hi:[0,0,0]
	v_mfma_scale_f32_16x16x128_f8f6f4 v[44:47], v[224:231], v[190:197], v[44:47], v175, v175 op_sel_hi:[0,0,0]
	v_mfma_scale_f32_16x16x128_f8f6f4 v[36:39], v[214:221], v[198:205], v[36:39], v175, v175 op_sel_hi:[0,0,0]
	v_mfma_scale_f32_16x16x128_f8f6f4 v[28:31], v[224:231], v[198:205], v[28:31], v175, v175 op_sel_hi:[0,0,0]
	v_mfma_scale_f32_16x16x128_f8f6f4 v[20:23], v[214:221], v[206:213], v[20:23], v175, v175 op_sel_hi:[0,0,0]
	v_mfma_scale_f32_16x16x128_f8f6f4 v[16:19], v[224:231], v[206:213], v[16:19], v175, v175 op_sel_hi:[0,0,0]
	s_add_i32 s62, s62, 2
	s_add_u32 s60, s60, 0x100
	s_addc_u32 s61, s61, 0
	s_add_u32 s16, s16, 0x100
	s_addc_u32 s17, s17, 0
	s_cmp_gt_u32 s62, 13
	s_barrier
	s_cbranch_scc0 .LBB0_2262
	s_lshl_b32 s16, s55, 8
	s_min_i32 s17, s55, 32
	s_ashr_i32 s20, s17, 4
	s_add_i32 s17, s16, 0xffffe000
	s_cmp_lt_i32 s55, 32
	s_cselect_b32 s19, s48, 0x302b8000
	s_cselect_b32 s18, s16, s17
	s_add_u32 s55, s2, s19
	s_mul_i32 s20, s20, 6
	s_addc_u32 s56, s3, 0
	s_ashr_i32 s19, s18, 31
	s_ashr_i32 s17, s16, 31
	s_ashr_i32 s21, s20, 31
	s_lshl_b64 s[18:19], s[18:19], 12
	s_lshl_b64 s[16:17], s[16:17], 12
	s_lshl_b64 s[20:21], s[20:21], 13
	v_lshl_or_b32 v8, s54, 8, v178
	s_add_u32 s20, s2, s20
	s_addc_u32 s21, s3, s21
	v_ashrrev_i32_e32 v9, 31, v8
	v_lshl_add_u64 v[0:1], v[8:9], 2, s[20:21]
	v_lshl_add_u64 v[10:11], v[0:1], 0, s[6:7]
	v_add_co_u32_e32 v0, vcc, s49, v0
	s_nop 7
	s_nop 7
	s_nop 7
	s_add_u32 s18, s55, s18
	s_nop 0
	v_addc_co_u32_e32 v1, vcc, 0, v1, vcc
	v_add_u32_e32 v152, v177, v8
	global_load_dwordx4 v[0:3], v[0:1], off
	s_nop 0
	global_load_dwordx4 v[182:185], v[10:11], off offset:528
	global_load_dwordx4 v[4:7], v[10:11], off offset:16
	global_load_dwordx4 v[186:189], v[10:11], off offset:512
	s_addc_u32 s19, s56, s19
	s_add_u32 s16, s41, s16
	v_lshlrev_b64 v[222:223], 1, v[152:153]
	v_lshl_add_u64 v[8:9], s[18:19], 0, v[222:223]
	global_load_dwordx4 v[190:193], v[8:9], off
	v_add_u32_e32 v8, 0x80, v152
	v_mov_b32_e32 v9, v153
	v_lshlrev_b64 v[224:225], 1, v[8:9]
	v_lshl_add_u64 v[8:9], s[18:19], 0, v[224:225]
	global_load_dwordx4 v[194:197], v[8:9], off
	v_add_u32_e32 v8, 0x8000, v152
	v_mov_b32_e32 v9, v153
	v_lshlrev_b64 v[226:227], 1, v[8:9]
	v_lshl_add_u64 v[8:9], s[18:19], 0, v[226:227]
	global_load_dwordx4 v[198:201], v[8:9], off
	v_add_u32_e32 v8, 0x8080, v152
	v_mov_b32_e32 v9, v153
	v_lshlrev_b64 v[170:171], 1, v[8:9]
	v_lshl_add_u64 v[8:9], s[18:19], 0, v[170:171]
	global_load_dwordx4 v[202:205], v[8:9], off
	v_add_u32_e32 v8, 0x10000, v152
	v_mov_b32_e32 v9, v153
	v_lshlrev_b64 v[168:169], 1, v[8:9]
	v_lshl_add_u64 v[8:9], s[18:19], 0, v[168:169]
	global_load_dwordx4 v[206:209], v[8:9], off
	v_add_u32_e32 v8, 0x10080, v152
	v_mov_b32_e32 v9, v153
	v_lshlrev_b64 v[166:167], 1, v[8:9]
	v_lshl_add_u64 v[8:9], s[18:19], 0, v[166:167]
	global_load_dwordx4 v[210:213], v[8:9], off
	v_mov_b32_e32 v9, v153
	v_add_u32_e32 v8, 0x18000, v152
	v_lshlrev_b64 v[164:165], 1, v[8:9]
	v_lshl_add_u64 v[8:9], s[18:19], 0, v[164:165]
	global_load_dwordx4 v[214:217], v[8:9], off
	v_mov_b32_e32 v9, v153
	v_add_u32_e32 v8, 0x18080, v152
	v_lshlrev_b64 v[162:163], 1, v[8:9]
	v_lshl_add_u64 v[8:9], s[18:19], 0, v[162:163]
	global_load_dwordx4 v[218:221], v[8:9], off
	s_addc_u32 s17, s42, s17
	s_and_b64 vcc, exec, s[0:1]
	s_mov_b32 s54, s50
	s_mov_b32 s55, s51
	s_waitcnt vmcnt(0)
	v_pk_mul_f32 v[12:13], v[0:1], s[8:9] op_sel_hi:[1,0]
	v_pk_mul_f32 v[0:1], v[182:183], s[8:9] op_sel_hi:[1,0]
	v_pk_mul_f32 v[14:15], v[2:3], s[8:9] op_sel_hi:[1,0]
	v_pk_mul_f32 v[10:11], v[6:7], s[8:9] op_sel_hi:[1,0]
	v_pk_mul_f32 v[8:9], v[4:5], s[8:9] op_sel_hi:[1,0]
	v_pk_mul_f32 v[6:7], v[188:189], s[8:9] op_sel_hi:[1,0]
	v_pk_mul_f32 v[4:5], v[186:187], s[8:9] op_sel_hi:[1,0]
	v_pk_mul_f32 v[2:3], v[184:185], s[8:9] op_sel_hi:[1,0]
	v_lshlrev_b32_e32 v182, 16, v190
	v_and_b32_e32 v183, 0xffff0000, v190
	v_lshlrev_b32_e32 v184, 16, v191
	v_and_b32_e32 v185, 0xffff0000, v191
	v_lshlrev_b32_e32 v186, 16, v192
	v_and_b32_e32 v187, 0xffff0000, v192
	v_lshlrev_b32_e32 v188, 16, v193
	v_and_b32_e32 v189, 0xffff0000, v193
	v_lshlrev_b32_e32 v190, 16, v194
	v_and_b32_e32 v191, 0xffff0000, v194
	v_pk_fma_f32 v[140:141], v[140:141], v[12:13], v[182:183]
	v_lshlrev_b32_e32 v192, 16, v195
	v_and_b32_e32 v193, 0xffff0000, v195
	v_lshlrev_b32_e32 v194, 16, v196
	v_and_b32_e32 v195, 0xffff0000, v196
	v_lshlrev_b32_e32 v196, 16, v197
	v_and_b32_e32 v197, 0xffff0000, v197
	v_pk_fma_f32 v[142:143], v[142:143], v[14:15], v[184:185]
	v_pk_fma_f32 v[182:183], v[138:139], v[10:11], v[188:189]
	v_pk_fma_f32 v[138:139], v[136:137], v[8:9], v[186:187]
	v_cvt_pk_bf16_f32 v136, v140, v141
	v_cvt_pk_bf16_f32 v137, v142, v143
	v_lshl_add_u64 v[140:141], s[16:17], 0, v[222:223]
	v_pk_fma_f32 v[132:133], v[132:133], v[4:5], v[190:191]
	v_lshlrev_b32_e32 v228, 16, v198
	v_and_b32_e32 v229, 0xffff0000, v198
	v_lshlrev_b32_e32 v198, 16, v199
	v_and_b32_e32 v199, 0xffff0000, v199
	v_cvt_pk_bf16_f32 v138, v138, v139
	v_cvt_pk_bf16_f32 v139, v182, v183
	global_store_dwordx4 v[140:141], v[136:139], off
	v_pk_fma_f32 v[134:135], v[134:135], v[6:7], v[192:193]
	v_lshlrev_b32_e32 v230, 16, v200
	v_pk_fma_f32 v[136:137], v[126:127], v[2:3], v[196:197]
	v_pk_fma_f32 v[126:127], v[124:125], v[0:1], v[194:195]
	v_cvt_pk_bf16_f32 v124, v132, v133
	v_cvt_pk_bf16_f32 v125, v134, v135
	v_lshl_add_u64 v[132:133], s[16:17], 0, v[224:225]
	v_and_b32_e32 v231, 0xffff0000, v200
	v_lshlrev_b32_e32 v200, 16, v201
	v_and_b32_e32 v201, 0xffff0000, v201
	v_lshlrev_b32_e32 v232, 16, v202
	v_and_b32_e32 v233, 0xffff0000, v202
	v_cvt_pk_bf16_f32 v126, v126, v127
	v_cvt_pk_bf16_f32 v127, v136, v137
	global_store_dwordx4 v[132:133], v[124:127], off
	v_lshlrev_b32_e32 v202, 16, v203
	v_and_b32_e32 v203, 0xffff0000, v203
	v_pk_fma_f32 v[124:125], v[130:131], v[14:15], v[198:199]
	v_lshlrev_b32_e32 v234, 16, v204
	v_and_b32_e32 v235, 0xffff0000, v204
	v_lshlrev_b32_e32 v204, 16, v205
	v_and_b32_e32 v205, 0xffff0000, v205
	v_pk_fma_f32 v[126:127], v[128:129], v[12:13], v[228:229]
	v_pk_fma_f32 v[128:129], v[122:123], v[10:11], v[200:201]
	v_pk_fma_f32 v[122:123], v[120:121], v[8:9], v[230:231]
	v_cvt_pk_bf16_f32 v120, v126, v127
	v_cvt_pk_bf16_f32 v121, v124, v125
	v_lshl_add_u64 v[124:125], s[16:17], 0, v[226:227]
	v_pk_fma_f32 v[116:117], v[116:117], v[4:5], v[232:233]
	v_lshlrev_b32_e32 v236, 16, v206
	v_and_b32_e32 v237, 0xffff0000, v206
	v_lshlrev_b32_e32 v206, 16, v207
	v_and_b32_e32 v207, 0xffff0000, v207
	v_cvt_pk_bf16_f32 v122, v122, v123
	v_cvt_pk_bf16_f32 v123, v128, v129
	global_store_dwordx4 v[124:125], v[120:123], off
	v_pk_fma_f32 v[118:119], v[118:119], v[6:7], v[202:203]
	v_lshlrev_b32_e32 v238, 16, v208
	v_pk_fma_f32 v[120:121], v[110:111], v[2:3], v[204:205]
	v_pk_fma_f32 v[110:111], v[108:109], v[0:1], v[234:235]
	v_cvt_pk_bf16_f32 v108, v116, v117
	v_cvt_pk_bf16_f32 v109, v118, v119
	v_lshl_add_u64 v[116:117], s[16:17], 0, v[170:171]
	v_and_b32_e32 v239, 0xffff0000, v208
	v_lshlrev_b32_e32 v208, 16, v209
	v_and_b32_e32 v209, 0xffff0000, v209
	v_lshlrev_b32_e32 v240, 16, v210
	v_and_b32_e32 v241, 0xffff0000, v210
	v_cvt_pk_bf16_f32 v110, v110, v111
	v_cvt_pk_bf16_f32 v111, v120, v121
	global_store_dwordx4 v[116:117], v[108:111], off
	v_lshlrev_b32_e32 v210, 16, v211
	v_and_b32_e32 v211, 0xffff0000, v211
	v_pk_fma_f32 v[108:109], v[114:115], v[14:15], v[206:207]
	v_lshlrev_b32_e32 v242, 16, v212
	v_and_b32_e32 v243, 0xffff0000, v212
	v_lshlrev_b32_e32 v212, 16, v213
	v_and_b32_e32 v213, 0xffff0000, v213
	v_pk_fma_f32 v[110:111], v[112:113], v[12:13], v[236:237]
	v_pk_fma_f32 v[112:113], v[106:107], v[10:11], v[208:209]
	v_pk_fma_f32 v[106:107], v[104:105], v[8:9], v[238:239]
	v_cvt_pk_bf16_f32 v104, v110, v111
	v_cvt_pk_bf16_f32 v105, v108, v109
	v_lshl_add_u64 v[108:109], s[16:17], 0, v[168:169]
	v_pk_fma_f32 v[100:101], v[100:101], v[4:5], v[240:241]
	v_lshlrev_b32_e32 v244, 16, v214
	v_and_b32_e32 v245, 0xffff0000, v214
	v_lshlrev_b32_e32 v214, 16, v215
	v_and_b32_e32 v215, 0xffff0000, v215
	v_cvt_pk_bf16_f32 v106, v106, v107
	v_cvt_pk_bf16_f32 v107, v112, v113
	global_store_dwordx4 v[108:109], v[104:107], off
	v_pk_fma_f32 v[102:103], v[102:103], v[6:7], v[210:211]
	v_lshlrev_b32_e32 v246, 16, v216
	v_pk_fma_f32 v[104:105], v[94:95], v[2:3], v[212:213]
	v_pk_fma_f32 v[94:95], v[92:93], v[0:1], v[242:243]
	v_cvt_pk_bf16_f32 v92, v100, v101
	v_cvt_pk_bf16_f32 v93, v102, v103
	v_lshl_add_u64 v[100:101], s[16:17], 0, v[166:167]
	v_and_b32_e32 v247, 0xffff0000, v216
	v_lshlrev_b32_e32 v216, 16, v217
	v_and_b32_e32 v217, 0xffff0000, v217
	v_lshlrev_b32_e32 v248, 16, v218
	v_and_b32_e32 v249, 0xffff0000, v218
	v_cvt_pk_bf16_f32 v94, v94, v95
	v_cvt_pk_bf16_f32 v95, v104, v105
	global_store_dwordx4 v[100:101], v[92:95], off
	v_lshlrev_b32_e32 v218, 16, v219
	v_and_b32_e32 v219, 0xffff0000, v219
	v_pk_fma_f32 v[92:93], v[98:99], v[14:15], v[214:215]
	v_lshlrev_b32_e32 v172, 16, v220
	v_and_b32_e32 v173, 0xffff0000, v220
	v_lshlrev_b32_e32 v220, 16, v221
	v_and_b32_e32 v221, 0xffff0000, v221
	v_pk_fma_f32 v[94:95], v[96:97], v[12:13], v[244:245]
	v_pk_fma_f32 v[96:97], v[90:91], v[10:11], v[216:217]
	v_pk_fma_f32 v[90:91], v[88:89], v[8:9], v[246:247]
	v_cvt_pk_bf16_f32 v88, v94, v95
	v_cvt_pk_bf16_f32 v89, v92, v93
	v_lshl_add_u64 v[92:93], s[16:17], 0, v[164:165]
	v_pk_fma_f32 v[84:85], v[84:85], v[4:5], v[248:249]
	v_cvt_pk_bf16_f32 v90, v90, v91
	v_cvt_pk_bf16_f32 v91, v96, v97
	global_store_dwordx4 v[92:93], v[88:91], off
	v_pk_fma_f32 v[86:87], v[86:87], v[6:7], v[218:219]
	s_nop 0
	v_pk_fma_f32 v[88:89], v[82:83], v[2:3], v[220:221]
	v_pk_fma_f32 v[82:83], v[80:81], v[0:1], v[172:173]
	v_cvt_pk_bf16_f32 v80, v84, v85
	v_cvt_pk_bf16_f32 v81, v86, v87
	v_lshl_add_u64 v[84:85], s[16:17], 0, v[162:163]
	v_cvt_pk_bf16_f32 v82, v82, v83
	v_cvt_pk_bf16_f32 v83, v88, v89
	global_store_dwordx4 v[84:85], v[80:83], off
	s_nop 1
	v_add_u32_e32 v80, 0x40000, v152
	v_mov_b32_e32 v81, v153
	v_lshlrev_b64 v[122:123], 1, v[80:81]
	v_lshl_add_u64 v[80:81], s[18:19], 0, v[122:123]
	global_load_dwordx4 v[90:93], v[80:81], off
	v_add_u32_e32 v80, 0x40080, v152
	v_mov_b32_e32 v81, v153
	v_lshlrev_b64 v[124:125], 1, v[80:81]
	v_lshl_add_u64 v[80:81], s[18:19], 0, v[124:125]
	global_load_dwordx4 v[94:97], v[80:81], off
	v_add_u32_e32 v80, 0x48000, v152
	v_mov_b32_e32 v81, v153
	v_lshlrev_b64 v[126:127], 1, v[80:81]
	v_lshl_add_u64 v[80:81], s[18:19], 0, v[126:127]
	global_load_dwordx4 v[98:101], v[80:81], off
	v_add_u32_e32 v80, 0x48080, v152
	v_mov_b32_e32 v81, v153
	v_lshlrev_b64 v[88:89], 1, v[80:81]
	v_lshl_add_u64 v[80:81], s[18:19], 0, v[88:89]
	global_load_dwordx4 v[102:105], v[80:81], off
	v_add_u32_e32 v80, 0x50000, v152
	v_mov_b32_e32 v81, v153
	v_lshlrev_b64 v[86:87], 1, v[80:81]
	v_lshl_add_u64 v[80:81], s[18:19], 0, v[86:87]
	global_load_dwordx4 v[106:109], v[80:81], off
	v_add_u32_e32 v80, 0x50080, v152
	v_mov_b32_e32 v81, v153
	v_lshlrev_b64 v[84:85], 1, v[80:81]
	v_lshl_add_u64 v[80:81], s[18:19], 0, v[84:85]
	global_load_dwordx4 v[110:113], v[80:81], off
	v_add_u32_e32 v80, 0x58000, v152
	v_mov_b32_e32 v81, v153
	v_lshlrev_b64 v[82:83], 1, v[80:81]
	v_lshl_add_u64 v[80:81], s[18:19], 0, v[82:83]
	v_add_u32_e32 v152, 0x58080, v152
	global_load_dwordx4 v[114:117], v[80:81], off
	v_lshlrev_b64 v[80:81], 1, v[152:153]
	v_lshl_add_u64 v[118:119], s[18:19], 0, v[80:81]
	global_load_dwordx4 v[118:121], v[118:119], off
	s_mov_b64 s[18:19], s[10:11]
	s_waitcnt vmcnt(0)
	v_lshlrev_b32_e32 v128, 16, v90
	v_and_b32_e32 v129, 0xffff0000, v90
	v_lshlrev_b32_e32 v130, 16, v91
	v_and_b32_e32 v131, 0xffff0000, v91
	v_lshlrev_b32_e32 v132, 16, v92
	v_and_b32_e32 v133, 0xffff0000, v92
	v_lshlrev_b32_e32 v92, 16, v93
	v_and_b32_e32 v93, 0xffff0000, v93
	v_lshlrev_b32_e32 v134, 16, v94
	v_and_b32_e32 v135, 0xffff0000, v94
	v_pk_fma_f32 v[76:77], v[76:77], v[12:13], v[128:129]
	v_lshlrev_b32_e32 v94, 16, v95
	v_and_b32_e32 v95, 0xffff0000, v95
	v_lshlrev_b32_e32 v136, 16, v96
	v_and_b32_e32 v137, 0xffff0000, v96
	v_lshlrev_b32_e32 v96, 16, v97
	v_and_b32_e32 v97, 0xffff0000, v97
	v_pk_fma_f32 v[78:79], v[78:79], v[14:15], v[130:131]
	v_pk_fma_f32 v[92:93], v[74:75], v[10:11], v[92:93]
	v_pk_fma_f32 v[74:75], v[72:73], v[8:9], v[132:133]
	v_cvt_pk_bf16_f32 v72, v76, v77
	v_cvt_pk_bf16_f32 v73, v78, v79
	v_lshl_add_u64 v[76:77], s[16:17], 0, v[122:123]
	v_pk_fma_f32 v[68:69], v[68:69], v[4:5], v[134:135]
	v_lshlrev_b32_e32 v138, 16, v98
	v_and_b32_e32 v139, 0xffff0000, v98
	v_lshlrev_b32_e32 v98, 16, v99
	v_and_b32_e32 v99, 0xffff0000, v99
	v_cvt_pk_bf16_f32 v74, v74, v75
	v_cvt_pk_bf16_f32 v75, v92, v93
	global_store_dwordx4 v[76:77], v[72:75], off
	v_pk_fma_f32 v[70:71], v[70:71], v[6:7], v[94:95]
	v_lshlrev_b32_e32 v140, 16, v100
	v_pk_fma_f32 v[72:73], v[62:63], v[2:3], v[96:97]
	v_pk_fma_f32 v[62:63], v[60:61], v[0:1], v[136:137]
	v_cvt_pk_bf16_f32 v60, v68, v69
	v_cvt_pk_bf16_f32 v61, v70, v71
	v_lshl_add_u64 v[68:69], s[16:17], 0, v[124:125]
	v_and_b32_e32 v141, 0xffff0000, v100
	v_lshlrev_b32_e32 v100, 16, v101
	v_and_b32_e32 v101, 0xffff0000, v101
	v_lshlrev_b32_e32 v142, 16, v102
	v_and_b32_e32 v143, 0xffff0000, v102
	v_cvt_pk_bf16_f32 v62, v62, v63
	v_cvt_pk_bf16_f32 v63, v72, v73
	global_store_dwordx4 v[68:69], v[60:63], off
	v_lshlrev_b32_e32 v102, 16, v103
	v_and_b32_e32 v103, 0xffff0000, v103
	v_pk_fma_f32 v[60:61], v[66:67], v[14:15], v[98:99]
	v_lshlrev_b32_e32 v162, 16, v104
	v_and_b32_e32 v163, 0xffff0000, v104
	v_lshlrev_b32_e32 v104, 16, v105
	v_and_b32_e32 v105, 0xffff0000, v105
	v_pk_fma_f32 v[62:63], v[64:65], v[12:13], v[138:139]
	v_pk_fma_f32 v[64:65], v[58:59], v[10:11], v[100:101]
	v_pk_fma_f32 v[58:59], v[56:57], v[8:9], v[140:141]
	v_cvt_pk_bf16_f32 v56, v62, v63
	v_cvt_pk_bf16_f32 v57, v60, v61
	v_lshl_add_u64 v[60:61], s[16:17], 0, v[126:127]
	v_pk_fma_f32 v[52:53], v[52:53], v[4:5], v[142:143]
	v_lshlrev_b32_e32 v164, 16, v106
	v_and_b32_e32 v165, 0xffff0000, v106
	v_lshlrev_b32_e32 v106, 16, v107
	v_and_b32_e32 v107, 0xffff0000, v107
	v_cvt_pk_bf16_f32 v58, v58, v59
	v_cvt_pk_bf16_f32 v59, v64, v65
	global_store_dwordx4 v[60:61], v[56:59], off
	v_pk_fma_f32 v[54:55], v[54:55], v[6:7], v[102:103]
	v_lshlrev_b32_e32 v166, 16, v108
	v_pk_fma_f32 v[56:57], v[46:47], v[2:3], v[104:105]
	v_pk_fma_f32 v[46:47], v[44:45], v[0:1], v[162:163]
	v_cvt_pk_bf16_f32 v44, v52, v53
	v_cvt_pk_bf16_f32 v45, v54, v55
	v_lshl_add_u64 v[52:53], s[16:17], 0, v[88:89]
	v_and_b32_e32 v167, 0xffff0000, v108
	v_lshlrev_b32_e32 v108, 16, v109
	v_and_b32_e32 v109, 0xffff0000, v109
	v_lshlrev_b32_e32 v168, 16, v110
	v_and_b32_e32 v169, 0xffff0000, v110
	v_cvt_pk_bf16_f32 v46, v46, v47
	v_cvt_pk_bf16_f32 v47, v56, v57
	global_store_dwordx4 v[52:53], v[44:47], off
	v_lshlrev_b32_e32 v170, 16, v112
	v_and_b32_e32 v171, 0xffff0000, v112
	v_pk_fma_f32 v[44:45], v[50:51], v[14:15], v[106:107]
	v_lshlrev_b32_e32 v112, 16, v113
	v_and_b32_e32 v113, 0xffff0000, v113
	v_lshlrev_b32_e32 v172, 16, v114
	v_and_b32_e32 v173, 0xffff0000, v114
	v_pk_fma_f32 v[46:47], v[48:49], v[12:13], v[164:165]
	v_pk_fma_f32 v[48:49], v[42:43], v[10:11], v[108:109]
	v_pk_fma_f32 v[42:43], v[40:41], v[8:9], v[166:167]
	v_cvt_pk_bf16_f32 v40, v46, v47
	v_cvt_pk_bf16_f32 v41, v44, v45
	v_lshl_add_u64 v[44:45], s[16:17], 0, v[86:87]
	v_pk_fma_f32 v[36:37], v[36:37], v[4:5], v[168:169]
	v_lshlrev_b32_e32 v110, 16, v111
	v_and_b32_e32 v111, 0xffff0000, v111
	v_lshlrev_b32_e32 v114, 16, v115
	v_and_b32_e32 v115, 0xffff0000, v115
	v_lshlrev_b32_e32 v182, 16, v116
	v_and_b32_e32 v183, 0xffff0000, v116
	v_lshlrev_b32_e32 v116, 16, v117
	v_and_b32_e32 v117, 0xffff0000, v117
	v_lshlrev_b32_e32 v184, 16, v118
	v_and_b32_e32 v185, 0xffff0000, v118
	v_cvt_pk_bf16_f32 v42, v42, v43
	v_cvt_pk_bf16_f32 v43, v48, v49
	global_store_dwordx4 v[44:45], v[40:43], off
	v_pk_fma_f32 v[12:13], v[32:33], v[12:13], v[172:173]
	v_lshlrev_b32_e32 v90, 16, v120
	v_pk_fma_f32 v[40:41], v[30:31], v[2:3], v[112:113]
	v_pk_fma_f32 v[30:31], v[28:29], v[0:1], v[170:171]
	v_cvt_pk_bf16_f32 v28, v36, v37
	v_lshl_add_u64 v[36:37], s[16:17], 0, v[84:85]
	v_and_b32_e32 v91, 0xffff0000, v120
	v_lshlrev_b32_e32 v120, 16, v121
	v_and_b32_e32 v121, 0xffff0000, v121
	v_pk_fma_f32 v[38:39], v[38:39], v[6:7], v[110:111]
	v_pk_fma_f32 v[14:15], v[34:35], v[14:15], v[114:115]
	v_cvt_pk_bf16_f32 v29, v38, v39
	v_cvt_pk_bf16_f32 v30, v30, v31
	v_cvt_pk_bf16_f32 v31, v40, v41
	global_store_dwordx4 v[36:37], v[28:31], off
	v_pk_fma_f32 v[26:27], v[26:27], v[10:11], v[116:117]
	v_pk_fma_f32 v[10:11], v[24:25], v[8:9], v[182:183]
	v_cvt_pk_bf16_f32 v8, v12, v13
	v_cvt_pk_bf16_f32 v9, v14, v15
	v_lshl_add_u64 v[12:13], s[16:17], 0, v[82:83]
	v_pk_fma_f32 v[4:5], v[20:21], v[4:5], v[184:185]
	v_lshlrev_b32_e32 v118, 16, v119
	v_and_b32_e32 v119, 0xffff0000, v119
	v_cvt_pk_bf16_f32 v10, v10, v11
	v_cvt_pk_bf16_f32 v11, v26, v27
	global_store_dwordx4 v[12:13], v[8:11], off
	v_pk_fma_f32 v[6:7], v[22:23], v[6:7], v[118:119]
	s_nop 0
	v_pk_fma_f32 v[8:9], v[18:19], v[2:3], v[120:121]
	v_pk_fma_f32 v[2:3], v[16:17], v[0:1], v[90:91]
	v_cvt_pk_bf16_f32 v0, v4, v5
	v_lshl_add_u64 v[4:5], s[16:17], 0, v[80:81]
	v_cvt_pk_bf16_f32 v1, v6, v7
	v_cvt_pk_bf16_f32 v2, v2, v3
	v_cvt_pk_bf16_f32 v3, v8, v9
	global_store_dwordx4 v[4:5], v[0:3], off
	s_mov_b64 s[16:17], s[12:13]
	s_cbranch_vccz .LBB0_2255
	s_waitcnt vmcnt(0)
	s_cmpk_gt_u32 s23, 0xff
	s_cbranch_scc1 .LBB0_2266
	s_barrier
